# early barrier invalidate + packed f32 ops split into scalar ops in the four router rowpasses
# baseline (speedup 1.0000x reference)
.LBB0_630:
	v_ashrrev_i32_e32 v23, 31, v16
	v_mov_b32_e32 v22, v16
	v_ashrrev_i32_e32 v21, 31, v17
	v_mov_b32_e32 v20, v17
	v_lshlrev_b64 v[22:23], 2, v[22:23]
	v_lshl_add_u64 v[24:25], s[36:37], 0, v[22:23]
	v_lshlrev_b64 v[20:21], 2, v[20:21]
	v_lshl_add_u64 v[26:27], s[36:37], 0, v[20:21]
	global_load_dword v24, v[24:25], off
	s_nop 0
	global_load_dword v25, v[26:27], off
	v_lshl_add_u64 v[26:27], s[64:65], 0, v[20:21]
	v_add_u32_e32 v18, -2, v18
	v_add_u32_e32 v90, 0x2000, v19
	s_add_i32 s63, s63, 4
	v_cmp_eq_u32_e32 vcc, 0, v18
	s_or_b64 s[40:41], vcc, s[40:41]
	s_waitcnt vmcnt(0)
	ds_write2st64_b32 v19, v24, v25 offset1:8
	v_lshl_add_u64 v[24:25], s[64:65], 0, v[22:23]
	global_load_dword v24, v[24:25], off
	s_nop 0
	global_load_dword v30, v[26:27], off
	v_lshl_add_u64 v[26:27], s[66:67], 0, v[20:21]
	s_waitcnt vmcnt(1)
	ds_write_b32 v19, v24 offset:4096
	v_lshl_add_u64 v[24:25], s[66:67], 0, v[22:23]
	global_load_dword v31, v[24:25], off
	global_load_dword v44, v[26:27], off
	v_lshl_add_u64 v[24:25], s[34:35], 0, v[22:23]
	v_lshl_add_u64 v[26:27], s[34:35], 0, v[20:21]
	v_lshl_add_u64 v[22:23], s[30:31], 0, v[22:23]
	v_lshl_add_u64 v[20:21], s[30:31], 0, v[20:21]
	global_load_dword v24, v[24:25], off
	s_nop 0
	global_load_dword v25, v[26:27], off
	global_load_dword v91, v[22:23], off
	global_load_dword v92, v[20:21], off
	v_add_u32_e32 v20, 0x400, v16
	v_add_u32_e32 v22, 0x400, v17
	v_ashrrev_i32_e32 v21, 31, v20
	v_ashrrev_i32_e32 v23, 31, v22
	v_lshlrev_b64 v[20:21], 2, v[20:21]
	v_lshl_add_u64 v[26:27], s[36:37], 0, v[20:21]
	v_lshlrev_b64 v[22:23], 2, v[22:23]
	v_lshl_add_u64 v[28:29], s[36:37], 0, v[22:23]
	global_load_dword v26, v[26:27], off
	s_nop 0
	global_load_dword v27, v[28:29], off
	v_lshl_add_u64 v[28:29], s[64:65], 0, v[22:23]
	v_add_u32_e32 v17, 0x800, v17
	v_add_u32_e32 v16, 0x800, v16
	s_waitcnt vmcnt(1)
	ds_write2st64_b32 v19, v26, v30 offset0:16 offset1:24
	s_waitcnt vmcnt(0)
	ds_write2st64_b32 v19, v27, v31 offset0:24 offset1:32
	v_lshl_add_u64 v[26:27], s[64:65], 0, v[20:21]
	global_load_dword v26, v[26:27], off
	s_nop 0
	global_load_dword v27, v[28:29], off
	v_add_f32_e32 v24, 1.0, v24
	v_add_f32_e32 v25, 1.0, v25
	v_lshl_add_u64 v[28:29], s[66:67], 0, v[22:23]
	s_waitcnt vmcnt(1)
	ds_write2st64_b32 v19, v26, v44 offset0:32 offset1:40
	s_waitcnt vmcnt(0)
	ds_write2st64_b32 v19, v27, v24 offset0:40 offset1:48
	v_lshl_add_u64 v[26:27], s[66:67], 0, v[20:21]
	global_load_dword v24, v[26:27], off
	s_nop 0
	global_load_dword v26, v[28:29], off
	s_waitcnt vmcnt(1)
	ds_write2st64_b32 v19, v24, v25 offset0:48 offset1:56
	s_waitcnt vmcnt(0)
	ds_write2st64_b32 v19, v26, v91 offset0:56 offset1:64
	v_lshl_add_u64 v[24:25], s[34:35], 0, v[20:21]
	v_lshl_add_u64 v[26:27], s[34:35], 0, v[22:23]
	global_load_dword v24, v[24:25], off
	s_nop 0
	global_load_dword v25, v[26:27], off
	v_lshl_add_u64 v[20:21], s[30:31], 0, v[20:21]
	v_lshl_add_u64 v[22:23], s[30:31], 0, v[22:23]
	s_waitcnt vmcnt(0)
	v_add_f32_e32 v24, 1.0, v24
	v_add_f32_e32 v25, 1.0, v25
	ds_write2st64_b32 v19, v24, v92 offset0:64 offset1:72
	global_load_dword v20, v[20:21], off
	s_nop 0
	global_load_dword v21, v[22:23], off
	s_waitcnt vmcnt(1)
	ds_write2st64_b32 v19, v25, v20 offset0:72 offset1:80
	s_waitcnt vmcnt(0)
	ds_write_b32 v19, v21 offset:22528
	v_mov_b32_e32 v20, s63
	v_mov_b32_e32 v19, v90
	s_andn2_b64 exec, exec, s[40:41]
	s_cbranch_execnz .LBB0_630
	s_or_b64 exec, exec, s[40:41]
	v_lshlrev_b32_e32 v18, 9, v20
	s_or_b64 exec, exec, s[38:39]
	s_and_saveexec_b64 s[38:39], s[12:13]
	s_cbranch_execz .LBB0_634
	s_branch .LBB0_633

.LBB0_633:
	v_ashrrev_i32_e32 v21, 31, v17
	v_mov_b32_e32 v20, v17
	v_ashrrev_i32_e32 v17, 31, v16
	v_lshlrev_b64 v[16:17], 2, v[16:17]
	v_lshl_add_u64 v[22:23], s[36:37], 0, v[16:17]
	v_lshlrev_b64 v[20:21], 2, v[20:21]
	v_lshl_add_u64 v[24:25], s[36:37], 0, v[20:21]
	global_load_dword v19, v[22:23], off
	s_nop 0
	global_load_dword v22, v[24:25], off
	v_readlane_b32 s64, v253, 27
	v_readlane_b32 s65, v253, 28
	v_readlane_b32 s66, v253, 29
	v_readlane_b32 s67, v253, 30
	v_readlane_b32 s72, v253, 35
	v_readlane_b32 s73, v253, 36
	v_lshl_add_u32 v24, v18, 2, v103
	v_readlane_b32 s74, v253, 37
	v_readlane_b32 s75, v253, 38
	s_mov_b64 s[64:65], s[72:73]
	s_mov_b64 s[66:67], s[74:75]
	v_readlane_b32 s68, v253, 31
	v_readlane_b32 s69, v253, 32
	v_readlane_b32 s70, v253, 33
	v_readlane_b32 s71, v253, 34
	v_readlane_b32 s76, v253, 39
	v_readlane_b32 s77, v253, 40
	v_readlane_b32 s78, v253, 41
	v_readlane_b32 s79, v253, 42
	s_waitcnt vmcnt(0)
	ds_write2st64_b32 v24, v19, v22 offset1:8
	v_lshl_add_u64 v[18:19], s[64:65], 0, v[16:17]
	v_lshl_add_u64 v[22:23], s[64:65], 0, v[20:21]
	global_load_dword v18, v[18:19], off
	s_nop 0
	global_load_dword v19, v[22:23], off
	v_lshl_add_u64 v[22:23], s[66:67], 0, v[20:21]
	s_waitcnt vmcnt(0)
	ds_write2st64_b32 v24, v18, v19 offset0:16 offset1:24
	v_lshl_add_u64 v[18:19], s[66:67], 0, v[16:17]
	global_load_dword v18, v[18:19], off
	s_nop 0
	global_load_dword v19, v[22:23], off
	v_lshl_add_u64 v[22:23], s[34:35], 0, v[20:21]
	s_waitcnt vmcnt(0)
	ds_write2st64_b32 v24, v18, v19 offset0:32 offset1:40
	v_lshl_add_u64 v[18:19], s[34:35], 0, v[16:17]
	global_load_dword v18, v[18:19], off
	s_nop 0
	global_load_dword v19, v[22:23], off
	v_lshl_add_u64 v[16:17], s[30:31], 0, v[16:17]
	s_waitcnt vmcnt(0)
	v_add_f32_e32 v18, 1.0, v18
	v_add_f32_e32 v19, 1.0, v19
	ds_write2st64_b32 v24, v18, v19 offset0:48 offset1:56
	v_lshl_add_u64 v[18:19], s[30:31], 0, v[20:21]
	global_load_dword v16, v[16:17], off
	s_nop 0
	global_load_dword v17, v[18:19], off
	s_waitcnt vmcnt(0)
	ds_write2st64_b32 v24, v16, v17 offset0:64 offset1:72

.LBB0_641:
	s_or_b64 exec, exec, s[16:17]
	ds_read_b128 v[94:97], v119 offset:12288
	ds_read_b128 v[98:101], v119 offset:16384
	v_mul_f32_e32 v30, v30, v44
	v_mul_f32_e32 v31, v31, v44
	v_mul_f32_e32 v28, v28, v44
	v_mul_f32_e32 v29, v29, v44
	s_lshl_b64 s[16:17], s[28:29], 10
	v_mul_f32_e32 v26, v26, v44
	v_mul_f32_e32 v27, v27, v44
	s_waitcnt lgkmcnt(0)
	v_fma_f32 v30, v30, v94, v98
	v_fma_f32 v31, v31, v95, v99
	v_fma_f32 v28, v28, v96, v100
	v_fma_f32 v29, v29, v97, v101
	v_cvt_pk_bf16_f32 v94, v30, v31
	v_mul_f32_e32 v30, 0x41800000, v30
	v_mul_f32_e32 v31, 0x41800000, v31
	v_med3_f32 v30, v30, s54, v120
	v_med3_f32 v31, v31, s54, v120
	v_mov_b32_e32 v100, 0
	v_cvt_pk_fp8_f32 v100, v30, v31
	v_cvt_pk_bf16_f32 v94, v28, v29
	v_mul_f32_e32 v28, 0x41800000, v28
	v_mul_f32_e32 v29, 0x41800000, v29
	v_med3_f32 v28, v28, s54, v120
	v_med3_f32 v29, v29, s54, v120
	v_cvt_pk_fp8_f32 v100, v28, v29 op_sel:[0,0,1]
	ds_read_b128 v[28:31], v119 offset:13312
	ds_read_b128 v[94:97], v119 offset:17408
	v_lshl_add_u64 v[98:99], v[88:89], 0, s[16:17]
	v_mul_f32_e32 v24, v24, v44
	v_mul_f32_e32 v25, v25, v44
	global_store_dword v[98:99], v100, off
	v_mul_f32_e32 v22, v22, v44
	v_mul_f32_e32 v23, v23, v44
	s_waitcnt lgkmcnt(0)
	v_fma_f32 v26, v26, v28, v94
	v_fma_f32 v27, v27, v29, v95
	v_mov_b32_e32 v94, 0
	v_cvt_pk_bf16_f32 v28, v26, v27
	v_mul_f32_e32 v26, 0x41800000, v26
	v_mul_f32_e32 v27, 0x41800000, v27
	v_med3_f32 v26, v26, s54, v120
	v_med3_f32 v27, v27, s54, v120
	v_cvt_pk_fp8_f32 v94, v26, v27
	v_fma_f32 v24, v24, v30, v96
	v_fma_f32 v25, v25, v31, v97
	v_mul_f32_e32 v20, v20, v44
	v_mul_f32_e32 v21, v21, v44
	v_cvt_pk_bf16_f32 v28, v24, v25
	v_mul_f32_e32 v24, 0x41800000, v24
	v_mul_f32_e32 v25, 0x41800000, v25
	v_med3_f32 v24, v24, s54, v120
	v_med3_f32 v25, v25, s54, v120
	v_cvt_pk_fp8_f32 v94, v24, v25 op_sel:[0,0,1]
	ds_read_b128 v[24:27], v119 offset:14336
	ds_read_b128 v[28:31], v119 offset:18432
	v_mul_f32_e32 v18, v18, v44
	v_mul_f32_e32 v19, v19, v44
	v_mul_f32_e32 v16, v16, v44
	v_mul_f32_e32 v17, v17, v44
	global_store_dword v[98:99], v94, off offset:256
	s_mov_b32 s33, 32
	s_waitcnt lgkmcnt(0)
	v_fma_f32 v22, v22, v24, v28
	v_fma_f32 v23, v23, v25, v29
	v_fma_f32 v20, v20, v26, v30
	v_fma_f32 v21, v21, v27, v31
	v_cvt_pk_bf16_f32 v24, v22, v23
	v_mul_f32_e32 v22, 0x41800000, v22
	v_mul_f32_e32 v23, 0x41800000, v23
	v_cvt_pk_bf16_f32 v24, v20, v21
	v_mul_f32_e32 v20, 0x41800000, v20
	v_mul_f32_e32 v28, 0x41800000, v21
	v_med3_f32 v21, v22, s54, v120
	v_med3_f32 v22, v23, s54, v120
	v_mov_b32_e32 v29, 0
	v_cvt_pk_fp8_f32 v29, v21, v22
	v_med3_f32 v30, v20, s54, v120
	ds_read_b128 v[20:23], v119 offset:15360
	ds_read_b128 v[24:27], v119 offset:19456
	v_med3_f32 v28, v28, s54, v120
	v_cvt_pk_fp8_f32 v29, v30, v28 op_sel:[0,0,1]
	s_mov_b64 s[16:17], 0
	s_mov_b64 s[28:29], -1
	s_waitcnt lgkmcnt(0)
	v_fma_f32 v18, v18, v20, v24
	v_fma_f32 v19, v19, v21, v25
	v_fma_f32 v16, v16, v22, v26
	v_fma_f32 v17, v17, v23, v27
	v_mul_f32_e32 v20, 0x41800000, v18
	v_mul_f32_e32 v21, 0x41800000, v19
	v_med3_f32 v20, v20, s54, v120
	v_med3_f32 v21, v21, s54, v120
	v_mov_b32_e32 v23, 0
	v_cvt_pk_fp8_f32 v23, v20, v21
	v_mul_f32_e32 v22, 0x41800000, v16
	v_mul_f32_e32 v20, 0x41800000, v17
	v_med3_f32 v21, v22, s54, v120
	v_med3_f32 v20, v20, s54, v120
	v_cvt_pk_fp8_f32 v23, v21, v20 op_sel:[0,0,1]
	s_and_b64 vcc, exec, s[18:19]
	global_store_dword v[98:99], v29, off offset:512
	v_cvt_pk_bf16_f32 v18, v18, v19
	v_cvt_pk_bf16_f32 v16, v16, v17
	global_store_dword v[98:99], v23, off offset:768
	s_cbranch_vccnz .LBB0_651

.LBB0_643:
	s_mov_b32 s34, s30
	s_add_i32 s30, s30, 1
	s_ashr_i32 s31, s30, 31
	s_lshl_b64 s[38:39], s[30:31], 12
	s_waitcnt vmcnt(14)
	v_mov_b64_e32 v[4:5], v[16:17]
	v_lshl_add_u64 v[32:33], v[82:83], 0, s[38:39]
	v_mov_b64_e32 v[6:7], v[18:19]
	global_load_dwordx4 v[20:23], v[32:33], off
	global_load_dwordx4 v[16:19], v[32:33], off offset:1024
	ds_read_b128 v[8:11], v119
	ds_read_b128 v[12:15], v119 offset:1024
	s_waitcnt vmcnt(13)
	v_lshlrev_b32_e32 v34, 16, v100
	v_and_b32_e32 v35, 0xffff0000, v100
	v_lshlrev_b32_e32 v36, 16, v101
	v_and_b32_e32 v37, 0xffff0000, v101
	s_waitcnt lgkmcnt(1)
	v_mul_f32_e32 v10, v10, v36
	v_mul_f32_e32 v11, v11, v37
	v_mul_f32_e32 v8, v8, v34
	v_mul_f32_e32 v9, v9, v35
	v_fmac_f32_e32 v10, s26, v2
	v_fmac_f32_e32 v11, s26, v3
	v_fmac_f32_e32 v8, s26, v0
	v_fmac_f32_e32 v9, s26, v1
	v_add_f32_e32 v1, v10, v11
	v_add_f32_e32 v0, v8, v9
	s_waitcnt vmcnt(12)
	v_lshlrev_b32_e32 v38, 16, v98
	v_and_b32_e32 v39, 0xffff0000, v98
	v_lshlrev_b32_e32 v98, 16, v99
	v_and_b32_e32 v99, 0xffff0000, v99
	v_add_f32_e32 v0, v0, v1
	v_add_f32_e32 v44, 0, v0
	s_waitcnt lgkmcnt(0)
	v_mul_f32_e32 v0, v14, v98
	v_mul_f32_e32 v1, v15, v99
	v_mul_f32_e32 v2, v12, v38
	v_mul_f32_e32 v3, v13, v39
	v_fma_f32 v34, v6, s26, v0
	v_fma_f32 v35, v7, s26, v1
	v_fma_f32 v36, v4, s26, v2
	v_fma_f32 v37, v5, s26, v3
	ds_read_b128 v[0:3], v119 offset:2048
	v_add_f32_e32 v4, v36, v37
	v_add_f32_e32 v5, v34, v35
	v_add_f32_e32 v4, v4, v5
	s_waitcnt vmcnt(11)
	v_lshlrev_b32_e32 v100, 16, v96
	v_and_b32_e32 v101, 0xffff0000, v96
	v_lshlrev_b32_e32 v96, 16, v97
	v_and_b32_e32 v97, 0xffff0000, v97
	v_add_f32_e32 v12, v44, v4
	ds_read_b128 v[4:7], v119 offset:3072
	s_waitcnt lgkmcnt(1)
	v_mul_f32_e32 v2, v2, v96
	v_mul_f32_e32 v3, v3, v97
	v_mul_f32_e32 v0, v0, v100
	v_mul_f32_e32 v1, v1, v101
	v_fma_f32 v38, v30, s26, v2
	v_fma_f32 v39, v31, s26, v3
	v_fma_f32 v124, v28, s26, v0
	v_fma_f32 v125, v29, s26, v1
	v_add_f32_e32 v1, v38, v39
	v_add_f32_e32 v0, v124, v125
	s_waitcnt vmcnt(10)
	v_lshlrev_b32_e32 v122, 16, v94
	v_and_b32_e32 v123, 0xffff0000, v94
	v_lshlrev_b32_e32 v94, 16, v95
	v_and_b32_e32 v95, 0xffff0000, v95
	v_add_f32_e32 v0, v0, v1
	v_add_f32_e32 v12, v12, v0
	s_waitcnt lgkmcnt(0)
	v_mul_f32_e32 v0, v6, v94
	v_mul_f32_e32 v1, v7, v95
	v_mul_f32_e32 v2, v4, v122
	v_mul_f32_e32 v3, v5, v123
	v_fma_f32 v122, v26, s26, v0
	v_fma_f32 v123, v27, s26, v1
	v_fma_f32 v126, v24, s26, v2
	v_fma_f32 v127, v25, s26, v3
	v_add_f32_e32 v1, v122, v123
	v_add_f32_e32 v0, v126, v127
	v_add_f32_e32 v0, v0, v1
	v_add_f32_e32 v0, v12, v0
	s_lshl_b64 s[16:17], s[30:31], 11
	global_load_dwordx4 v[28:31], v[32:33], off offset:2048
	global_load_dwordx4 v[24:27], v[32:33], off offset:3072
	v_add_f32_dpp v0, v0, v0 quad_perm:[1,0,3,2] row_mask:0xf bank_mask:0xf bound_ctrl:1
	s_ashr_i32 s35, s34, 31
	s_nop 0
	v_add_f32_dpp v0, v0, v0 quad_perm:[2,3,0,1] row_mask:0xf bank_mask:0xf bound_ctrl:1
	s_nop 1
	v_add_f32_dpp v0, v0, v0 row_half_mirror row_mask:0xf bank_mask:0xf bound_ctrl:1
	s_nop 1
	v_add_f32_dpp v0, v0, v0 row_mirror row_mask:0xf bank_mask:0xf bound_ctrl:1
	v_mov_b32_e32 v1, v0
	s_nop 1
	v_permlane16_swap_b32_e32 v0, v1
	v_add_f32_e32 v0, v0, v1
	v_mov_b32_e32 v1, v0
	s_nop 1
	v_permlane32_swap_b32_e32 v0, v1
	v_add_f32_e32 v0, v0, v1
	v_fmac_f32_e32 v11, 0xba800000, v0
	v_fmac_f32_e32 v9, 0xba800000, v0
	v_fmamk_f32 v10, v0, 0xba800000, v10
	v_fmamk_f32 v8, v0, 0xba800000, v8
	v_mul_f32_e32 v1, v9, v9
	v_mul_f32_e32 v2, v11, v11
	v_fmac_f32_e32 v1, v8, v8
	v_fmac_f32_e32 v2, v10, v10
	v_fmac_f32_e32 v35, 0xba800000, v0
	v_fmac_f32_e32 v37, 0xba800000, v0
	v_add_f32_e32 v1, v1, v2
	v_fmamk_f32 v34, v0, 0xba800000, v34
	v_fmamk_f32 v36, v0, 0xba800000, v36
	v_mul_f32_e32 v2, v37, v37
	v_mul_f32_e32 v3, v35, v35
	v_fmac_f32_e32 v2, v36, v36
	v_fmac_f32_e32 v3, v34, v34
	v_add_f32_e32 v2, v2, v3
	v_fmac_f32_e32 v39, 0xba800000, v0
	v_fmac_f32_e32 v125, 0xba800000, v0
	v_add_f32_e32 v1, v1, v2
	v_fmamk_f32 v38, v0, 0xba800000, v38
	v_fmamk_f32 v124, v0, 0xba800000, v124
	v_mul_f32_e32 v2, v125, v125
	v_mul_f32_e32 v3, v39, v39
	v_fmac_f32_e32 v2, v124, v124
	v_fmac_f32_e32 v3, v38, v38
	v_add_f32_e32 v2, v2, v3
	v_fmac_f32_e32 v123, 0xba800000, v0
	v_fmac_f32_e32 v127, 0xba800000, v0
	v_add_f32_e32 v1, v2, v1
	v_fmamk_f32 v122, v0, 0xba800000, v122
	v_fmamk_f32 v126, v0, 0xba800000, v126
	v_mul_f32_e32 v0, v127, v127
	v_mul_f32_e32 v2, v123, v123
	v_fmac_f32_e32 v0, v126, v126
	v_fmac_f32_e32 v2, v122, v122
	v_add_f32_e32 v0, v0, v2
	v_add_f32_e32 v0, v0, v1
	s_nop 1
	v_add_f32_dpp v0, v0, v0 quad_perm:[1,0,3,2] row_mask:0xf bank_mask:0xf bound_ctrl:1
	s_nop 1
	v_add_f32_dpp v0, v0, v0 quad_perm:[2,3,0,1] row_mask:0xf bank_mask:0xf bound_ctrl:1
	s_nop 1
	v_add_f32_dpp v0, v0, v0 row_half_mirror row_mask:0xf bank_mask:0xf bound_ctrl:1
	s_nop 1
	v_add_f32_dpp v0, v0, v0 row_mirror row_mask:0xf bank_mask:0xf bound_ctrl:1
	v_mov_b32_e32 v1, v0
	s_nop 1
	v_permlane16_swap_b32_e32 v0, v1
	v_add_f32_e32 v0, v0, v1
	v_mov_b32_e32 v1, v0
	s_nop 1
	v_permlane32_swap_b32_e32 v0, v1
	v_add_f32_e32 v0, v0, v1
	v_fmamk_f32 v0, v0, 0x3a800000, v113
	v_mul_f32_e32 v1, 0x4f800000, v0
	v_cmp_gt_f32_e32 vcc, s53, v0
	s_nop 1
	v_cndmask_b32_e32 v2, v0, v1, vcc
	v_sqrt_f32_e32 v3, v2
	v_lshl_add_u64 v[0:1], v[84:85], 0, s[16:17]
	global_load_dwordx2 v[100:101], v[0:1], off
	global_load_dwordx2 v[98:99], v[0:1], off offset:512
	global_load_dwordx2 v[96:97], v[0:1], off offset:1024
	global_load_dwordx2 v[94:95], v[0:1], off offset:1536
	v_add_u32_e32 v4, -1, v3
	v_fma_f32 v5, -v4, v3, v2
	v_cmp_ge_f32_e64 s[16:17], 0, v5
	v_add_u32_e32 v5, 1, v3
	s_nop 0
	v_cndmask_b32_e64 v4, v3, v4, s[16:17]
	v_fma_f32 v3, -v5, v3, v2
	v_cmp_lt_f32_e64 s[16:17], 0, v3
	s_nop 1
	v_cndmask_b32_e64 v3, v4, v5, s[16:17]
	v_mul_f32_e32 v4, 0x37800000, v3
	v_cndmask_b32_e32 v3, v3, v4, vcc
	v_cmp_class_f32_e32 vcc, v2, v114
	s_nop 1
	v_cndmask_b32_e32 v2, v3, v2, vcc
	v_div_scale_f32 v3, s[16:17], v2, v2, 1.0
	v_rcp_f32_e32 v4, v3
	s_lshl_b64 s[16:17], s[34:35], 11
	v_fma_f32 v0, -v3, v4, 1.0
	v_fmac_f32_e32 v4, v0, v4
	v_div_scale_f32 v0, vcc, 1.0, v2, 1.0
	v_mul_f32_e32 v1, v0, v4
	v_fma_f32 v5, -v3, v1, v0
	v_fmac_f32_e32 v1, v5, v4
	v_fma_f32 v0, -v3, v1, v0
	v_div_fmas_f32 v0, v0, v4, v1
	v_div_fixup_f32 v32, v0, v2, 1.0
	ds_read_b128 v[0:3], v119 offset:4096
	ds_read_b128 v[4:7], v119 offset:8192
	v_mul_f32_e32 v128, v10, v32
	v_mul_f32_e32 v129, v11, v32
	v_mul_f32_e32 v130, v8, v32
	v_mul_f32_e32 v131, v9, v32
	ds_read_b128 v[8:11], v119 offset:5120
	ds_read_b128 v[12:15], v119 offset:9216
	s_waitcnt lgkmcnt(2)
	v_fma_f32 v2, v2, v128, v6
	v_fma_f32 v3, v3, v129, v7
	s_nop 0
	v_cvt_pk_f16_f32 v129, v2, v3
	v_cvt_f32_f16_e32 v33, v129
	v_fma_f32 v0, v0, v130, v4
	v_fma_f32 v1, v1, v131, v5
	v_cvt_f32_f16_sdwa v44, v129 dst_sel:DWORD dst_unused:UNUSED_PAD src0_sel:WORD_1
	v_cvt_pk_f16_f32 v128, v0, v1
	v_mul_f32_e32 v0, v34, v32
	v_mul_f32_e32 v1, v35, v32
	v_mul_f32_e32 v2, v36, v32
	v_mul_f32_e32 v3, v37, v32
	s_waitcnt lgkmcnt(0)
	v_fma_f32 v0, v10, v0, v14
	v_fma_f32 v1, v11, v1, v15
	v_fma_f32 v2, v8, v2, v12
	v_fma_f32 v3, v9, v3, v13
	v_cvt_pk_f16_f32 v35, v0, v1
	v_cvt_pk_f16_f32 v34, v2, v3
	ds_read_b128 v[0:3], v119 offset:6144
	ds_read_b128 v[4:7], v119 offset:10240
	ds_read_b128 v[8:11], v119 offset:7168
	ds_read_b128 v[12:15], v119 offset:11264
	v_mul_f32_e32 v36, v124, v32
	v_mul_f32_e32 v37, v125, v32
	v_mul_f32_e32 v38, v38, v32
	v_mul_f32_e32 v39, v39, v32
	v_cvt_f32_f16_e32 v130, v128
	s_waitcnt lgkmcnt(2)
	v_fma_f32 v2, v2, v38, v6
	v_fma_f32 v3, v3, v39, v7
	v_fma_f32 v0, v0, v36, v4
	v_fma_f32 v1, v1, v37, v5
	v_cvt_f32_f16_sdwa v131, v128 dst_sel:DWORD dst_unused:UNUSED_PAD src0_sel:WORD_1
	v_cvt_pk_f16_f32 v36, v0, v1
	v_cvt_pk_f16_f32 v37, v2, v3
	v_mul_f32_e32 v0, v126, v32
	v_mul_f32_e32 v1, v127, v32
	v_mul_f32_e32 v2, v122, v32
	v_mul_f32_e32 v3, v123, v32
	v_cvt_f32_f16_e32 v132, v35
	v_cvt_f32_f16_sdwa v133, v35 dst_sel:DWORD dst_unused:UNUSED_PAD src0_sel:WORD_1
	v_cvt_f32_f16_e32 v134, v34
	v_cvt_f32_f16_sdwa v135, v34 dst_sel:DWORD dst_unused:UNUSED_PAD src0_sel:WORD_1
	s_waitcnt lgkmcnt(0)
	v_fma_f32 v2, v2, v10, v14
	v_fma_f32 v3, v3, v11, v15
	v_fma_f32 v0, v0, v8, v12
	v_fma_f32 v1, v1, v9, v13
	v_cvt_f32_f16_e32 v4, v37
	v_cvt_f32_f16_sdwa v5, v37 dst_sel:DWORD dst_unused:UNUSED_PAD src0_sel:WORD_1
	v_cvt_f32_f16_e32 v6, v36
	v_cvt_f32_f16_sdwa v7, v36 dst_sel:DWORD dst_unused:UNUSED_PAD src0_sel:WORD_1
	v_cvt_pk_f16_f32 v38, v0, v1
	v_cvt_pk_f16_f32 v39, v2, v3
	v_cvt_f32_f16_e32 v0, v39
	v_cvt_f32_f16_sdwa v1, v39 dst_sel:DWORD dst_unused:UNUSED_PAD src0_sel:WORD_1
	v_cvt_f32_f16_e32 v2, v38
	v_cvt_f32_f16_sdwa v3, v38 dst_sel:DWORD dst_unused:UNUSED_PAD src0_sel:WORD_1
	v_add_f32_e32 v8, v130, v131
	v_add_f32_e32 v9, v33, v44
	v_add_f32_e32 v8, v8, v9
	v_add_f32_e32 v9, v134, v135
	v_add_f32_e32 v10, v132, v133
	v_add_f32_e32 v8, 0, v8
	v_add_f32_e32 v9, v9, v10
	v_add_f32_e32 v6, v6, v7
	v_add_f32_e32 v4, v4, v5
	v_add_f32_e32 v8, v9, v8
	v_add_f32_e32 v4, v6, v4
	v_add_f32_e32 v2, v2, v3
	v_add_f32_e32 v0, v0, v1
	v_add_f32_e32 v4, v4, v8
	v_add_f32_e32 v0, v2, v0
	v_add_f32_e32 v0, v0, v4
	s_nop 1
	v_add_f32_dpp v0, v0, v0 quad_perm:[1,0,3,2] row_mask:0xf bank_mask:0xf bound_ctrl:1
	s_nop 1
	v_add_f32_dpp v0, v0, v0 quad_perm:[2,3,0,1] row_mask:0xf bank_mask:0xf bound_ctrl:1
	s_nop 1
	v_add_f32_dpp v0, v0, v0 row_half_mirror row_mask:0xf bank_mask:0xf bound_ctrl:1
	s_nop 1
	v_add_f32_dpp v0, v0, v0 row_mirror row_mask:0xf bank_mask:0xf bound_ctrl:1
	v_mov_b32_e32 v1, v0
	s_nop 1
	v_permlane16_swap_b32_e32 v0, v1
	v_add_f32_e32 v0, v0, v1
	v_mov_b32_e32 v1, v0
	s_nop 1
	v_permlane32_swap_b32_e32 v0, v1
	v_add_f32_e32 v13, v0, v1
	v_fma_mix_f32 v15, v13, s52, v129 op_sel:[0,0,1] op_sel_hi:[0,0,1]
	v_fma_mix_f32 v33, v13, s52, v128 op_sel:[0,0,1] op_sel_hi:[0,0,1]
	v_fma_mix_f32 v14, v13, s52, v129 op_sel_hi:[0,0,1]
	v_fma_mix_f32 v32, v13, s52, v128 op_sel_hi:[0,0,1]
	v_mul_f32_e32 v0, v33, v33
	v_mul_f32_e32 v1, v15, v15
	v_fmac_f32_e32 v0, v32, v32
	v_fmac_f32_e32 v1, v14, v14
	v_fma_mix_f32 v9, v13, s52, v35 op_sel:[0,0,1] op_sel_hi:[0,0,1]
	v_fma_mix_f32 v11, v13, s52, v34 op_sel:[0,0,1] op_sel_hi:[0,0,1]
	v_add_f32_e32 v0, v0, v1
	v_fma_mix_f32 v8, v13, s52, v35 op_sel_hi:[0,0,1]
	v_fma_mix_f32 v10, v13, s52, v34 op_sel_hi:[0,0,1]
	v_mul_f32_e32 v1, v11, v11
	v_mul_f32_e32 v2, v9, v9
	v_fmac_f32_e32 v1, v10, v10
	v_fmac_f32_e32 v2, v8, v8
	v_add_f32_e32 v1, v1, v2
	v_fma_mix_f32 v5, v13, s52, v37 op_sel:[0,0,1] op_sel_hi:[0,0,1]
	v_fma_mix_f32 v7, v13, s52, v36 op_sel:[0,0,1] op_sel_hi:[0,0,1]
	v_add_f32_e32 v0, v0, v1
	v_fma_mix_f32 v4, v13, s52, v37 op_sel_hi:[0,0,1]
	v_fma_mix_f32 v6, v13, s52, v36 op_sel_hi:[0,0,1]
	v_mul_f32_e32 v1, v7, v7
	v_mul_f32_e32 v2, v5, v5
	v_fmac_f32_e32 v1, v6, v6
	v_fmac_f32_e32 v2, v4, v4
	v_add_f32_e32 v1, v1, v2
	v_add_f32_e32 v12, v1, v0
	v_fma_mix_f32 v1, v13, s52, v39 op_sel:[0,0,1] op_sel_hi:[0,0,1]
	v_fma_mix_f32 v3, v13, s52, v38 op_sel:[0,0,1] op_sel_hi:[0,0,1]
	v_fma_mix_f32 v0, v13, s52, v39 op_sel_hi:[0,0,1]
	v_fma_mix_f32 v2, v13, s52, v38 op_sel_hi:[0,0,1]
	v_mul_f32_e32 v44, v3, v3
	v_mul_f32_e32 v122, v1, v1
	v_fmac_f32_e32 v44, v2, v2
	v_fmac_f32_e32 v122, v0, v0
	v_add_f32_e32 v44, v44, v122
	v_add_f32_e32 v12, v44, v12
	v_lshl_add_u64 v[122:123], v[86:87], 0, s[16:17]
	global_store_dwordx2 v[122:123], v[128:129], off
	v_add_f32_dpp v12, v12, v12 quad_perm:[1,0,3,2] row_mask:0xf bank_mask:0xf bound_ctrl:1
	global_store_dwordx2 v[122:123], v[34:35], off offset:512
	global_store_dwordx2 v[122:123], v[36:37], off offset:1024
	global_store_dwordx2 v[122:123], v[38:39], off offset:1536
	v_add_f32_dpp v12, v12, v12 quad_perm:[2,3,0,1] row_mask:0xf bank_mask:0xf bound_ctrl:1
	s_nop 1
	v_add_f32_dpp v12, v12, v12 row_half_mirror row_mask:0xf bank_mask:0xf bound_ctrl:1
	s_nop 1
	v_add_f32_dpp v12, v12, v12 row_mirror row_mask:0xf bank_mask:0xf bound_ctrl:1
	v_mov_b32_e32 v44, v12
	s_nop 1
	v_permlane16_swap_b32_e32 v12, v44
	v_add_f32_e32 v12, v12, v44
	v_mov_b32_e32 v44, v12
	s_nop 1
	v_permlane32_swap_b32_e32 v12, v44
	v_add_f32_e32 v12, v12, v44
	v_fmamk_f32 v12, v12, 0x3a800000, v113
	v_mul_f32_e32 v44, 0x4f800000, v12
	v_cmp_gt_f32_e32 vcc, s53, v12
	s_nop 1
	v_cndmask_b32_e32 v12, v12, v44, vcc
	v_sqrt_f32_e32 v44, v12
	s_nop 0
	v_add_u32_e32 v124, -1, v44
	v_fma_f32 v125, -v124, v44, v12
	v_cmp_ge_f32_e64 s[16:17], 0, v125
	v_add_u32_e32 v125, 1, v44
	s_nop 0
	v_cndmask_b32_e64 v124, v44, v124, s[16:17]
	v_fma_f32 v44, -v125, v44, v12
	v_cmp_lt_f32_e64 s[16:17], 0, v44
	s_nop 1
	v_cndmask_b32_e64 v44, v124, v125, s[16:17]
	v_mul_f32_e32 v124, 0x37800000, v44
	v_cndmask_b32_e32 v44, v44, v124, vcc
	v_cmp_class_f32_e32 vcc, v12, v114
	s_nop 1
	v_cndmask_b32_e32 v12, v44, v12, vcc
	v_div_scale_f32 v44, s[16:17], v12, v12, 1.0
	v_rcp_f32_e32 v124, v44
	s_nop 0
	v_fma_f32 v34, -v44, v124, 1.0
	v_fmac_f32_e32 v124, v34, v124
	v_div_scale_f32 v34, vcc, 1.0, v12, 1.0
	v_mul_f32_e32 v35, v34, v124
	v_fma_f32 v36, -v44, v35, v34
	v_fmac_f32_e32 v35, v36, v124
	v_fma_f32 v34, -v44, v35, v34
	v_div_fmas_f32 v34, v34, v124, v35
	v_div_fixup_f32 v12, v34, v12, 1.0
	s_and_saveexec_b64 s[16:17], s[2:3]
	s_add_i32 s31, s36, s37
	v_mul_f32_e32 v34, 0x3a800000, v13
	v_mov_b32_e32 v35, v12
	v_mov_b32_e32 v13, s31
	ds_write_b64 v13, v[34:35] offset:24
	s_or_b64 exec, exec, s[16:17]
	ds_read_b128 v[34:37], v119 offset:12288
	ds_read_b128 v[122:125], v119 offset:16384
	v_mul_f32_e32 v14, v14, v12
	v_mul_f32_e32 v15, v15, v12
	v_mul_f32_e32 v32, v32, v12
	v_mul_f32_e32 v33, v33, v12
	v_mov_b32_e32 v44, 0
	s_lshl_b64 s[16:17], s[34:35], 10
	s_waitcnt lgkmcnt(0)
	v_fma_f32 v14, v14, v36, v124
	v_fma_f32 v15, v15, v37, v125
	v_fma_f32 v32, v32, v34, v122
	v_fma_f32 v33, v33, v35, v123
	s_add_i32 s37, s37, 8
	v_cvt_pk_bf16_f32 v13, v32, v33
	s_cmp_eq_u32 s37, 0
	v_cvt_pk_bf16_f32 v13, v14, v15
	v_mul_f32_e32 v14, 0x41800000, v14
	v_mul_f32_e32 v13, 0x41800000, v32
	v_mul_f32_e32 v32, 0x41800000, v33
	v_med3_f32 v13, v13, s54, v120
	v_med3_f32 v32, v32, s54, v120
	v_cvt_pk_fp8_f32 v44, v13, v32
	v_mul_f32_e32 v13, 0x41800000, v15
	ds_read_b128 v[32:35], v119 offset:13312
	ds_read_b128 v[36:39], v119 offset:17408
	v_med3_f32 v14, v14, s54, v120
	v_med3_f32 v13, v13, s54, v120
	v_cvt_pk_fp8_f32 v44, v14, v13 op_sel:[0,0,1]
	v_mul_f32_e32 v10, v10, v12
	v_mul_f32_e32 v11, v11, v12
	v_lshl_add_u64 v[14:15], v[88:89], 0, s[16:17]
	v_mul_f32_e32 v8, v8, v12
	v_mul_f32_e32 v9, v9, v12
	s_waitcnt lgkmcnt(0)
	v_fma_f32 v10, v10, v32, v36
	v_fma_f32 v11, v11, v33, v37
	global_store_dword v[14:15], v44, off
	v_fma_f32 v8, v8, v34, v38
	v_fma_f32 v9, v9, v35, v39
	v_cvt_pk_bf16_f32 v13, v10, v11
	v_mul_f32_e32 v10, 0x41800000, v10
	v_cvt_pk_bf16_f32 v13, v8, v9
	v_mul_f32_e32 v11, 0x41800000, v11
	v_med3_f32 v10, v10, s54, v120
	v_med3_f32 v11, v11, s54, v120
	v_mov_b32_e32 v13, 0
	v_cvt_pk_fp8_f32 v13, v10, v11
	v_mul_f32_e32 v8, 0x41800000, v8
	v_mul_f32_e32 v9, 0x41800000, v9
	v_med3_f32 v8, v8, s54, v120
	v_med3_f32 v9, v9, s54, v120
	v_cvt_pk_fp8_f32 v13, v8, v9 op_sel:[0,0,1]
	ds_read_b128 v[8:11], v119 offset:14336
	ds_read_b128 v[32:35], v119 offset:18432
	v_mul_f32_e32 v6, v6, v12
	v_mul_f32_e32 v7, v7, v12
	global_store_dword v[14:15], v13, off offset:256
	s_waitcnt lgkmcnt(0)
	v_fma_f32 v6, v6, v8, v32
	v_fma_f32 v7, v7, v9, v33
	v_mul_f32_e32 v4, v4, v12
	v_mul_f32_e32 v5, v5, v12
	v_cvt_pk_bf16_f32 v8, v6, v7
	v_mul_f32_e32 v6, 0x41800000, v6
	v_mul_f32_e32 v7, 0x41800000, v7
	v_med3_f32 v6, v6, s54, v120
	v_med3_f32 v7, v7, s54, v120
	v_mov_b32_e32 v13, 0
	v_cvt_pk_fp8_f32 v13, v6, v7
	v_fma_f32 v4, v4, v10, v34
	v_fma_f32 v5, v5, v11, v35
	s_nop 0
	v_cvt_pk_bf16_f32 v8, v4, v5
	v_mul_f32_e32 v4, 0x41800000, v4
	v_mul_f32_e32 v5, 0x41800000, v5
	v_med3_f32 v4, v4, s54, v120
	v_med3_f32 v5, v5, s54, v120
	v_cvt_pk_fp8_f32 v13, v4, v5 op_sel:[0,0,1]
	ds_read_b128 v[4:7], v119 offset:15360
	ds_read_b128 v[8:11], v119 offset:19456
	v_mul_f32_e32 v2, v2, v12
	v_mul_f32_e32 v3, v3, v12
	global_store_dword v[14:15], v13, off offset:512
	s_waitcnt lgkmcnt(0)
	v_fma_f32 v2, v2, v4, v8
	v_fma_f32 v3, v3, v5, v9
	v_mov_b32_e32 v5, 0
	v_cvt_pk_bf16_f32 v4, v2, v3
	v_mul_f32_e32 v2, 0x41800000, v2
	v_mul_f32_e32 v3, 0x41800000, v3
	v_med3_f32 v2, v2, s54, v120
	v_med3_f32 v3, v3, s54, v120
	v_mul_f32_e32 v0, v0, v12
	v_mul_f32_e32 v1, v1, v12
	v_cvt_pk_fp8_f32 v5, v2, v3
	v_fma_f32 v0, v0, v6, v10
	v_fma_f32 v1, v1, v7, v11
	s_nop 0
	v_mul_f32_e32 v4, 0x41800000, v0
	v_mul_f32_e32 v2, 0x41800000, v1
	v_med3_f32 v3, v4, s54, v120
	v_med3_f32 v2, v2, s54, v120
	v_cvt_pk_fp8_f32 v5, v3, v2 op_sel:[0,0,1]
	v_cvt_pk_bf16_f32 v0, v0, v1
	global_store_dword v[14:15], v5, off offset:768
	s_cbranch_scc1 .LBB0_647
	s_waitcnt vmcnt(15)
	v_mov_b64_e32 v[0:1], v[20:21]
	v_mov_b64_e32 v[2:3], v[22:23]
	s_branch .LBB0_643

.LBB0_649:
	v_lshlrev_b32_e32 v128, 16, v98
	v_and_b32_e32 v129, 0xffff0000, v98
	v_lshlrev_b32_e32 v130, 16, v99
	v_and_b32_e32 v131, 0xffff0000, v99
	v_lshlrev_b32_e32 v132, 16, v96
	v_and_b32_e32 v133, 0xffff0000, v96
	v_lshlrev_b32_e32 v134, 16, v97
	v_and_b32_e32 v135, 0xffff0000, v97
	ds_read_b128 v[96:99], v119
	ds_read_b128 v[122:125], v119 offset:1024
	v_lshlrev_b32_e32 v126, 16, v100
	v_and_b32_e32 v127, 0xffff0000, v100
	v_lshlrev_b32_e32 v100, 16, v101
	v_and_b32_e32 v101, 0xffff0000, v101
	v_lshlrev_b32_e32 v136, 16, v94
	v_and_b32_e32 v137, 0xffff0000, v94
	v_lshlrev_b32_e32 v138, 16, v95
	v_and_b32_e32 v139, 0xffff0000, v95
	s_waitcnt lgkmcnt(1)
	v_mul_f32_e32 v94, v98, v100
	v_mul_f32_e32 v95, v99, v101
	v_mul_f32_e32 v98, v96, v126
	v_mul_f32_e32 v99, v97, v127
	v_fma_f32 v96, v22, s26, v94
	v_fma_f32 v97, v23, s26, v95
	v_fma_f32 v94, v20, s26, v98
	v_fma_f32 v95, v21, s26, v99
	v_add_f32_e32 v21, v96, v97
	v_add_f32_e32 v20, v94, v95
	v_add_f32_e32 v20, v20, v21
	v_add_f32_e32 v44, 0, v20
	s_waitcnt lgkmcnt(0)
	v_mul_f32_e32 v20, v124, v130
	v_mul_f32_e32 v21, v125, v131
	v_mul_f32_e32 v22, v122, v128
	v_mul_f32_e32 v23, v123, v129
	v_fma_f32 v18, v18, s26, v20
	v_fma_f32 v19, v19, s26, v21
	v_fma_f32 v16, v16, s26, v22
	v_fma_f32 v17, v17, s26, v23
	ds_read_b128 v[20:23], v119 offset:2048
	v_add_f32_e32 v98, v16, v17
	v_add_f32_e32 v99, v18, v19
	v_add_f32_e32 v98, v98, v99
	v_add_f32_e32 v44, v44, v98
	ds_read_b128 v[98:101], v119 offset:3072
	s_waitcnt lgkmcnt(1)
	v_mul_f32_e32 v22, v22, v134
	v_mul_f32_e32 v23, v23, v135
	v_mul_f32_e32 v20, v20, v132
	v_mul_f32_e32 v21, v21, v133
	v_fma_f32 v30, v30, s26, v22
	v_fma_f32 v31, v31, s26, v23
	v_fma_f32 v28, v28, s26, v20
	v_fma_f32 v29, v29, s26, v21
	v_add_f32_e32 v21, v30, v31
	v_add_f32_e32 v20, v28, v29
	v_add_f32_e32 v20, v20, v21
	v_add_f32_e32 v44, v44, v20
	s_waitcnt lgkmcnt(0)
	v_mul_f32_e32 v20, v100, v138
	v_mul_f32_e32 v21, v101, v139
	v_mul_f32_e32 v98, v98, v136
	v_mul_f32_e32 v99, v99, v137
	v_fma_f32 v22, v26, s26, v20
	v_fma_f32 v23, v27, s26, v21
	v_fma_f32 v20, v24, s26, v98
	v_fma_f32 v21, v25, s26, v99
	v_add_f32_e32 v25, v22, v23
	v_add_f32_e32 v24, v20, v21
	v_add_f32_e32 v24, v24, v25
	v_add_f32_e32 v24, v44, v24
	s_add_i32 s30, s33, s47
	s_add_i32 s28, s30, s62
	v_add_f32_dpp v24, v24, v24 quad_perm:[1,0,3,2] row_mask:0xf bank_mask:0xf bound_ctrl:1
	s_ashr_i32 s29, s28, 31
	s_nop 0
	v_add_f32_dpp v24, v24, v24 quad_perm:[2,3,0,1] row_mask:0xf bank_mask:0xf bound_ctrl:1
	s_nop 1
	v_add_f32_dpp v24, v24, v24 row_half_mirror row_mask:0xf bank_mask:0xf bound_ctrl:1
	s_nop 1
	v_add_f32_dpp v24, v24, v24 row_mirror row_mask:0xf bank_mask:0xf bound_ctrl:1
	v_mov_b32_e32 v25, v24
	s_nop 1
	v_permlane16_swap_b32_e32 v24, v25
	v_add_f32_e32 v24, v24, v25
	v_mov_b32_e32 v25, v24
	s_nop 1
	v_permlane32_swap_b32_e32 v24, v25
	v_add_f32_e32 v24, v24, v25
	v_fmac_f32_e32 v97, 0xba800000, v24
	v_fmac_f32_e32 v95, 0xba800000, v24
	v_fmamk_f32 v96, v24, 0xba800000, v96
	v_fmamk_f32 v94, v24, 0xba800000, v94
	v_mul_f32_e32 v25, v95, v95
	v_mul_f32_e32 v26, v97, v97
	v_fmac_f32_e32 v25, v94, v94
	v_fmac_f32_e32 v26, v96, v96
	v_fmac_f32_e32 v19, 0xba800000, v24
	v_fmac_f32_e32 v17, 0xba800000, v24
	v_add_f32_e32 v25, v25, v26
	v_fmamk_f32 v18, v24, 0xba800000, v18
	v_fmamk_f32 v16, v24, 0xba800000, v16
	v_mul_f32_e32 v26, v17, v17
	v_mul_f32_e32 v27, v19, v19
	v_fmac_f32_e32 v26, v16, v16
	v_fmac_f32_e32 v27, v18, v18
	v_add_f32_e32 v26, v26, v27
	v_fmac_f32_e32 v31, 0xba800000, v24
	v_fmac_f32_e32 v29, 0xba800000, v24
	v_add_f32_e32 v25, v25, v26
	v_fmamk_f32 v30, v24, 0xba800000, v30
	v_fmamk_f32 v28, v24, 0xba800000, v28
	v_mul_f32_e32 v26, v29, v29
	v_mul_f32_e32 v27, v31, v31
	v_fmac_f32_e32 v26, v28, v28
	v_fmac_f32_e32 v27, v30, v30
	v_add_f32_e32 v26, v26, v27
	v_fmac_f32_e32 v23, 0xba800000, v24
	v_fmac_f32_e32 v21, 0xba800000, v24
	v_add_f32_e32 v25, v26, v25
	v_fmamk_f32 v22, v24, 0xba800000, v22
	v_fmamk_f32 v20, v24, 0xba800000, v20
	v_mul_f32_e32 v24, v21, v21
	v_mul_f32_e32 v26, v23, v23
	v_fmac_f32_e32 v24, v20, v20
	v_fmac_f32_e32 v26, v22, v22
	v_add_f32_e32 v24, v24, v26
	v_add_f32_e32 v24, v24, v25
	s_nop 1
	v_add_f32_dpp v24, v24, v24 quad_perm:[1,0,3,2] row_mask:0xf bank_mask:0xf bound_ctrl:1
	s_nop 1
	v_add_f32_dpp v24, v24, v24 quad_perm:[2,3,0,1] row_mask:0xf bank_mask:0xf bound_ctrl:1
	s_nop 1
	v_add_f32_dpp v24, v24, v24 row_half_mirror row_mask:0xf bank_mask:0xf bound_ctrl:1
	s_nop 1
	v_add_f32_dpp v24, v24, v24 row_mirror row_mask:0xf bank_mask:0xf bound_ctrl:1
	v_mov_b32_e32 v25, v24
	s_nop 1
	v_permlane16_swap_b32_e32 v24, v25
	v_add_f32_e32 v24, v24, v25
	v_mov_b32_e32 v25, v24
	s_nop 1
	v_permlane32_swap_b32_e32 v24, v25
	v_add_f32_e32 v24, v24, v25
	v_fmamk_f32 v24, v24, 0x3a800000, v113
	v_mul_f32_e32 v25, 0x4f800000, v24
	v_cmp_gt_f32_e32 vcc, s53, v24
	s_nop 1
	v_cndmask_b32_e32 v24, v24, v25, vcc
	v_sqrt_f32_e32 v25, v24
	s_nop 0
	v_add_u32_e32 v26, -1, v25
	v_fma_f32 v27, -v26, v25, v24
	v_cmp_ge_f32_e64 s[16:17], 0, v27
	v_add_u32_e32 v27, 1, v25
	s_nop 0
	v_cndmask_b32_e64 v26, v25, v26, s[16:17]
	v_fma_f32 v25, -v27, v25, v24
	v_cmp_lt_f32_e64 s[16:17], 0, v25
	s_nop 1
	v_cndmask_b32_e64 v25, v26, v27, s[16:17]
	v_mul_f32_e32 v26, 0x37800000, v25
	v_cndmask_b32_e32 v25, v25, v26, vcc
	v_cmp_class_f32_e32 vcc, v24, v114
	s_nop 1
	v_cndmask_b32_e32 v24, v25, v24, vcc
	v_div_scale_f32 v25, s[16:17], v24, v24, 1.0
	v_rcp_f32_e32 v26, v25
	s_lshl_b64 s[16:17], s[28:29], 11
	v_fma_f32 v27, -v25, v26, 1.0
	v_fmac_f32_e32 v26, v27, v26
	v_div_scale_f32 v27, vcc, 1.0, v24, 1.0
	v_mul_f32_e32 v44, v27, v26
	v_fma_f32 v98, -v25, v44, v27
	v_fmac_f32_e32 v44, v98, v26
	v_fma_f32 v25, -v25, v44, v27
	v_div_fmas_f32 v25, v25, v26, v44
	v_div_fixup_f32 v44, v25, v24, 1.0
	ds_read_b128 v[24:27], v119 offset:4096
	ds_read_b128 v[98:101], v119 offset:8192
	v_mul_f32_e32 v126, v96, v44
	v_mul_f32_e32 v127, v97, v44
	v_mul_f32_e32 v128, v94, v44
	v_mul_f32_e32 v129, v95, v44
	ds_read_b128 v[94:97], v119 offset:5120
	ds_read_b128 v[122:125], v119 offset:9216
	v_mul_f32_e32 v18, v18, v44
	v_mul_f32_e32 v19, v19, v44
	v_mul_f32_e32 v16, v16, v44
	v_mul_f32_e32 v17, v17, v44
	s_waitcnt lgkmcnt(2)
	v_fma_f32 v24, v24, v128, v98
	v_fma_f32 v25, v25, v129, v99
	v_fma_f32 v26, v26, v126, v100
	v_fma_f32 v27, v27, v127, v101
	s_waitcnt lgkmcnt(0)
	v_fma_f32 v16, v94, v16, v122
	v_fma_f32 v17, v95, v17, v123
	v_fma_f32 v18, v96, v18, v124
	v_fma_f32 v19, v97, v19, v125
	v_cvt_pk_f16_f32 v99, v26, v27
	v_cvt_pk_f16_f32 v98, v24, v25
	v_cvt_pk_f16_f32 v101, v18, v19
	v_cvt_pk_f16_f32 v100, v16, v17
	ds_read_b128 v[16:19], v119 offset:6144
	ds_read_b128 v[24:27], v119 offset:10240
	v_mul_f32_e32 v122, v30, v44
	v_mul_f32_e32 v123, v31, v44
	v_mul_f32_e32 v124, v28, v44
	v_mul_f32_e32 v125, v29, v44
	ds_read_b128 v[28:31], v119 offset:7168
	ds_read_b128 v[94:97], v119 offset:11264
	v_cvt_f32_f16_e32 v126, v99
	v_cvt_f32_f16_sdwa v127, v99 dst_sel:DWORD dst_unused:UNUSED_PAD src0_sel:WORD_1
	v_cvt_f32_f16_e32 v128, v98
	v_cvt_f32_f16_sdwa v129, v98 dst_sel:DWORD dst_unused:UNUSED_PAD src0_sel:WORD_1
	s_waitcnt lgkmcnt(2)
	v_fma_f32 v16, v16, v124, v24
	v_fma_f32 v17, v17, v125, v25
	v_fma_f32 v18, v18, v122, v26
	v_fma_f32 v19, v19, v123, v27
	v_cvt_f32_f16_e32 v130, v101
	v_cvt_f32_f16_sdwa v131, v101 dst_sel:DWORD dst_unused:UNUSED_PAD src0_sel:WORD_1
	v_cvt_f32_f16_e32 v132, v100
	v_cvt_f32_f16_sdwa v133, v100 dst_sel:DWORD dst_unused:UNUSED_PAD src0_sel:WORD_1
	v_cvt_pk_f16_f32 v123, v18, v19
	v_cvt_pk_f16_f32 v122, v16, v17
	v_mul_f32_e32 v16, v22, v44
	v_mul_f32_e32 v17, v23, v44
	v_mul_f32_e32 v18, v20, v44
	v_mul_f32_e32 v19, v21, v44
	s_waitcnt lgkmcnt(0)
	v_fma_f32 v16, v16, v30, v96
	v_fma_f32 v17, v17, v31, v97
	v_fma_f32 v18, v18, v28, v94
	v_fma_f32 v19, v19, v29, v95
	v_cvt_f32_f16_e32 v24, v123
	v_cvt_f32_f16_sdwa v25, v123 dst_sel:DWORD dst_unused:UNUSED_PAD src0_sel:WORD_1
	v_cvt_f32_f16_e32 v26, v122
	v_cvt_f32_f16_sdwa v27, v122 dst_sel:DWORD dst_unused:UNUSED_PAD src0_sel:WORD_1
	v_cvt_pk_f16_f32 v97, v16, v17
	v_cvt_pk_f16_f32 v96, v18, v19
	v_cvt_f32_f16_e32 v16, v97
	v_cvt_f32_f16_sdwa v17, v97 dst_sel:DWORD dst_unused:UNUSED_PAD src0_sel:WORD_1
	v_cvt_f32_f16_e32 v18, v96
	v_cvt_f32_f16_sdwa v19, v96 dst_sel:DWORD dst_unused:UNUSED_PAD src0_sel:WORD_1
	v_add_f32_e32 v20, v128, v129
	v_add_f32_e32 v21, v126, v127
	v_add_f32_e32 v20, v20, v21
	v_add_f32_e32 v21, v132, v133
	v_add_f32_e32 v22, v130, v131
	v_add_f32_e32 v20, 0, v20
	v_add_f32_e32 v21, v21, v22
	v_add_f32_e32 v20, v21, v20
	v_add_f32_e32 v21, v26, v27
	v_add_f32_e32 v22, v24, v25
	v_add_f32_e32 v21, v21, v22
	v_add_f32_e32 v18, v18, v19
	v_add_f32_e32 v16, v16, v17
	v_add_f32_e32 v20, v21, v20
	v_add_f32_e32 v16, v18, v16
	v_add_f32_e32 v16, v16, v20
	s_nop 1
	v_add_f32_dpp v16, v16, v16 quad_perm:[1,0,3,2] row_mask:0xf bank_mask:0xf bound_ctrl:1
	s_nop 1
	v_add_f32_dpp v16, v16, v16 quad_perm:[2,3,0,1] row_mask:0xf bank_mask:0xf bound_ctrl:1
	s_nop 1
	v_add_f32_dpp v16, v16, v16 row_half_mirror row_mask:0xf bank_mask:0xf bound_ctrl:1
	s_nop 1
	v_add_f32_dpp v16, v16, v16 row_mirror row_mask:0xf bank_mask:0xf bound_ctrl:1
	v_mov_b32_e32 v17, v16
	s_nop 1
	v_permlane16_swap_b32_e32 v16, v17
	v_add_f32_e32 v16, v16, v17
	v_mov_b32_e32 v17, v16
	s_nop 1
	v_permlane32_swap_b32_e32 v16, v17
	v_add_f32_e32 v94, v16, v17
	v_fma_mix_f32 v29, v94, s52, v99 op_sel:[0,0,1] op_sel_hi:[0,0,1]
	v_fma_mix_f32 v31, v94, s52, v98 op_sel:[0,0,1] op_sel_hi:[0,0,1]
	v_fma_mix_f32 v28, v94, s52, v99 op_sel_hi:[0,0,1]
	v_fma_mix_f32 v30, v94, s52, v98 op_sel_hi:[0,0,1]
	v_mul_f32_e32 v16, v31, v31
	v_mul_f32_e32 v17, v29, v29
	v_fmac_f32_e32 v16, v30, v30
	v_fmac_f32_e32 v17, v28, v28
	v_fma_mix_f32 v25, v94, s52, v101 op_sel:[0,0,1] op_sel_hi:[0,0,1]
	v_fma_mix_f32 v27, v94, s52, v100 op_sel:[0,0,1] op_sel_hi:[0,0,1]
	v_add_f32_e32 v16, v16, v17
	v_fma_mix_f32 v24, v94, s52, v101 op_sel_hi:[0,0,1]
	v_fma_mix_f32 v26, v94, s52, v100 op_sel_hi:[0,0,1]
	v_mul_f32_e32 v17, v27, v27
	v_mul_f32_e32 v18, v25, v25
	v_fmac_f32_e32 v17, v26, v26
	v_fmac_f32_e32 v18, v24, v24
	v_add_f32_e32 v17, v17, v18
	v_fma_mix_f32 v21, v94, s52, v123 op_sel:[0,0,1] op_sel_hi:[0,0,1]
	v_fma_mix_f32 v23, v94, s52, v122 op_sel:[0,0,1] op_sel_hi:[0,0,1]
	v_add_f32_e32 v16, v16, v17
	v_fma_mix_f32 v20, v94, s52, v123 op_sel_hi:[0,0,1]
	v_fma_mix_f32 v22, v94, s52, v122 op_sel_hi:[0,0,1]
	v_mul_f32_e32 v17, v23, v23
	v_mul_f32_e32 v18, v21, v21
	v_fmac_f32_e32 v17, v22, v22
	v_fmac_f32_e32 v18, v20, v20
	v_add_f32_e32 v17, v17, v18
	v_add_f32_e32 v44, v17, v16
	v_fma_mix_f32 v17, v94, s52, v97 op_sel:[0,0,1] op_sel_hi:[0,0,1]
	v_fma_mix_f32 v19, v94, s52, v96 op_sel:[0,0,1] op_sel_hi:[0,0,1]
	v_fma_mix_f32 v16, v94, s52, v97 op_sel_hi:[0,0,1]
	v_fma_mix_f32 v18, v94, s52, v96 op_sel_hi:[0,0,1]
	v_mul_f32_e32 v95, v19, v19
	v_mul_f32_e32 v124, v17, v17
	v_fmac_f32_e32 v95, v18, v18
	v_fmac_f32_e32 v124, v16, v16
	v_add_f32_e32 v95, v95, v124
	v_add_f32_e32 v44, v95, v44
	v_lshl_add_u64 v[124:125], v[86:87], 0, s[16:17]
	global_store_dwordx2 v[124:125], v[98:99], off
	v_add_f32_dpp v44, v44, v44 quad_perm:[1,0,3,2] row_mask:0xf bank_mask:0xf bound_ctrl:1
	global_store_dwordx2 v[124:125], v[100:101], off offset:512
	global_store_dwordx2 v[124:125], v[122:123], off offset:1024
	global_store_dwordx2 v[124:125], v[96:97], off offset:1536
	v_add_f32_dpp v44, v44, v44 quad_perm:[2,3,0,1] row_mask:0xf bank_mask:0xf bound_ctrl:1
	s_nop 1
	v_add_f32_dpp v44, v44, v44 row_half_mirror row_mask:0xf bank_mask:0xf bound_ctrl:1
	s_nop 1
	v_add_f32_dpp v44, v44, v44 row_mirror row_mask:0xf bank_mask:0xf bound_ctrl:1
	v_mov_b32_e32 v95, v44
	s_nop 1
	v_permlane16_swap_b32_e32 v44, v95
	v_add_f32_e32 v44, v44, v95
	v_mov_b32_e32 v95, v44
	s_nop 1
	v_permlane32_swap_b32_e32 v44, v95
	v_add_f32_e32 v44, v44, v95
	v_fmamk_f32 v44, v44, 0x3a800000, v113
	v_mul_f32_e32 v95, 0x4f800000, v44
	v_cmp_gt_f32_e32 vcc, s53, v44
	s_nop 1
	v_cndmask_b32_e32 v44, v44, v95, vcc
	v_sqrt_f32_e32 v95, v44
	s_nop 0
	v_add_u32_e32 v98, -1, v95
	v_fma_f32 v99, -v98, v95, v44
	v_cmp_ge_f32_e64 s[16:17], 0, v99
	v_add_u32_e32 v99, 1, v95
	s_nop 0
	v_cndmask_b32_e64 v98, v95, v98, s[16:17]
	v_fma_f32 v95, -v99, v95, v44
	v_cmp_lt_f32_e64 s[16:17], 0, v95
	s_nop 1
	v_cndmask_b32_e64 v95, v98, v99, s[16:17]
	v_mul_f32_e32 v98, 0x37800000, v95
	v_cndmask_b32_e32 v95, v95, v98, vcc
	v_cmp_class_f32_e32 vcc, v44, v114
	s_nop 1
	v_cndmask_b32_e32 v44, v95, v44, vcc
	v_div_scale_f32 v95, s[16:17], v44, v44, 1.0
	v_rcp_f32_e32 v98, v95
	s_nop 0
	v_fma_f32 v96, -v95, v98, 1.0
	v_fmac_f32_e32 v98, v96, v98
	v_div_scale_f32 v96, vcc, 1.0, v44, 1.0
	v_mul_f32_e32 v97, v96, v98
	v_fma_f32 v99, -v95, v97, v96
	v_fmac_f32_e32 v97, v99, v98
	v_fma_f32 v95, -v95, v97, v96
	v_div_fmas_f32 v95, v95, v98, v97
	v_div_fixup_f32 v44, v95, v44, 1.0
	s_and_saveexec_b64 s[16:17], s[2:3]
	s_cbranch_execz .LBB0_641
	s_lshl_b32 s30, s30, 3
	s_add_i32 s30, s30, 0
	v_mul_f32_e32 v94, 0x3a800000, v94
	v_mov_b32_e32 v95, v44
	v_mov_b32_e32 v96, s30
	ds_write_b64 v96, v[94:95] offset:20480
	s_branch .LBB0_641
.LBB0_651:
	s_waitcnt vmcnt(0)
	s_barrier
	s_waitcnt vmcnt(0)
	buffer_inv sc1
	s_waitcnt vmcnt(0)
	s_and_saveexec_b64 s[16:17], s[4:5]
	ds_write_b32 v103, v45 offset:58624
	s_or_b64 exec, exec, s[16:17]
	v_add_u32_e32 v0, s62, v42
	v_ashrrev_i32_e32 v1, 31, v0
	v_lshlrev_b64 v[0:1], 11, v[0:1]
	v_lshl_add_u64 v[94:95], v[46:47], 0, v[0:1]
	global_load_dwordx4 v[30:33], v[94:95], off
	global_load_dwordx4 v[34:37], v[48:49], off
	global_load_dwordx4 v[20:23], v[52:53], off
	global_load_dwordx4 v[24:27], v[94:95], off offset:128
	ds_read_b64 v[38:39], v115 offset:20480
	ds_read_b128 v[98:101], v43 offset:12288
	ds_read_b128 v[122:125], v43 offset:12304
	ds_read_b128 v[126:129], v43 offset:16384
	ds_read_b128 v[130:133], v43 offset:16400
	v_add_u32_e32 v96, 0x6000, v105
	v_mov_b32_e32 v4, 0
	s_waitcnt lgkmcnt(4)
	v_mov_b32_e32 v0, v38
	v_mov_b32_e32 v1, v38
	v_mov_b32_e32 v2, v38
	v_mov_b32_e32 v3, v38
	v_mov_b32_e32 v90, v39
	v_mov_b32_e32 v91, v39
	v_mov_b32_e32 v92, v39
	v_mov_b32_e32 v93, v39
	v_add_u32_e32 v44, 0x6400, v105
	s_mov_b32 s16, 0
	v_mov_b32_e32 v28, v112
	v_mov_b32_e32 v5, v4
	v_mov_b32_e32 v6, v4
	v_mov_b32_e32 v7, v4
	v_mov_b32_e32 v8, v4
	v_mov_b32_e32 v9, v4
	v_mov_b32_e32 v10, v4
	v_mov_b32_e32 v11, v4
	v_mov_b32_e32 v12, v4
	v_mov_b32_e32 v13, v4
	v_mov_b32_e32 v14, v4
	v_mov_b32_e32 v15, v4
	v_mov_b32_e32 v16, v4
	v_mov_b32_e32 v17, v4
	v_mov_b32_e32 v18, v4
	s_waitcnt vmcnt(3)
	v_cvt_f32_f16_sdwa v19, v31 dst_sel:DWORD dst_unused:UNUSED_PAD src0_sel:WORD_1
	v_cvt_f32_f16_e32 v29, v31
	v_cvt_f32_f16_sdwa v31, v30 dst_sel:DWORD dst_unused:UNUSED_PAD src0_sel:WORD_1
	v_cvt_f32_f16_e32 v30, v30
	v_cvt_f32_f16_sdwa v97, v33 dst_sel:DWORD dst_unused:UNUSED_PAD src0_sel:WORD_1
	v_cvt_f32_f16_e32 v136, v33
	v_cvt_f32_f16_sdwa v135, v32 dst_sel:DWORD dst_unused:UNUSED_PAD src0_sel:WORD_1
	v_cvt_f32_f16_e32 v134, v32
	v_sub_f32_e32 v30, v30, v38
	v_sub_f32_e32 v31, v31, v38
	v_sub_f32_e32 v32, v29, v38
	v_sub_f32_e32 v33, v19, v38
	v_sub_f32_e32 v134, v134, v38
	v_sub_f32_e32 v135, v135, v38
	v_sub_f32_e32 v136, v136, v38
	v_sub_f32_e32 v137, v97, v38
	v_mul_f32_e32 v30, v39, v30
	v_mul_f32_e32 v31, v39, v31
	v_mul_f32_e32 v32, v39, v32
	v_mul_f32_e32 v33, v39, v33
	v_mul_f32_e32 v136, v39, v136
	v_mul_f32_e32 v137, v39, v137
	v_mul_f32_e32 v38, v39, v134
	v_mul_f32_e32 v39, v39, v135
	s_waitcnt lgkmcnt(1)
	v_fma_f32 v19, v98, v30, v126
	v_fma_f32 v30, v99, v31, v127
	s_waitcnt lgkmcnt(0)
	v_fma_f32 v29, v122, v38, v130
	v_fma_f32 v31, v123, v39, v131
	v_fma_f32 v32, v100, v32, v128
	v_fma_f32 v38, v124, v136, v132
	v_fmac_f32_e32 v129, v101, v33
	v_fmac_f32_e32 v133, v125, v137
	ds_write2_b32 v96, v19, v30 offset1:68
	ds_write2_b32 v44, v29, v31 offset0:16 offset1:84
	ds_write2_b32 v96, v32, v129 offset0:136 offset1:204
	ds_write2_b32 v44, v38, v133 offset0:152 offset1:220
	s_waitcnt vmcnt(2)
	ds_write_b128 v104, v[34:37] offset:41984
	v_mov_b32_e32 v19, v4
	s_waitcnt lgkmcnt(0)
	s_barrier
.LBB0_654:
	v_add_u32_e32 v29, s16, v111
	ds_read_b128 v[30:33], v28
	ds_read_b128 v[34:37], v28 offset:272
	ds_read_b128 v[98:101], v28 offset:544
	ds_read_b128 v[122:125], v28 offset:816
	ds_read_b128 v[126:129], v29
	ds_read_b128 v[130:133], v29 offset:128
	ds_read_b128 v[134:137], v29 offset:256
	ds_read_b128 v[138:141], v29 offset:384
	s_waitcnt lgkmcnt(7)
	v_mov_b32_e32 v38, v33
	s_waitcnt lgkmcnt(6)
	v_mov_b32_e32 v142, v37
	s_waitcnt lgkmcnt(3)
	v_fmac_f32_e32 v16, v126, v30
	v_fmac_f32_e32 v17, v127, v30
	v_fmac_f32_e32 v18, v128, v30
	v_fmac_f32_e32 v19, v129, v30
	v_fmac_f32_e32 v12, v126, v31
	v_fmac_f32_e32 v13, v127, v31
	v_fmac_f32_e32 v14, v128, v31
	v_fmac_f32_e32 v15, v129, v31
	v_fmac_f32_e32 v8, v126, v32
	v_fmac_f32_e32 v9, v127, v32
	v_fmac_f32_e32 v10, v128, v32
	v_fmac_f32_e32 v11, v129, v32
	v_fmac_f32_e32 v4, v126, v38
	v_fmac_f32_e32 v5, v127, v38
	v_fmac_f32_e32 v6, v128, v38
	v_fmac_f32_e32 v7, v129, v38
	v_mov_b32_e32 v144, v101
	s_waitcnt lgkmcnt(2)
	v_fmac_f32_e32 v18, v132, v34
	v_fmac_f32_e32 v19, v133, v34
	v_fmac_f32_e32 v16, v130, v34
	v_fmac_f32_e32 v17, v131, v34
	v_fmac_f32_e32 v14, v132, v35
	v_fmac_f32_e32 v15, v133, v35
	v_fmac_f32_e32 v12, v130, v35
	v_fmac_f32_e32 v13, v131, v35
	v_fmac_f32_e32 v10, v132, v36
	v_fmac_f32_e32 v11, v133, v36
	v_fmac_f32_e32 v8, v130, v36
	v_fmac_f32_e32 v9, v131, v36
	v_fmac_f32_e32 v6, v132, v142
	v_fmac_f32_e32 v7, v133, v142
	v_fmac_f32_e32 v4, v130, v142
	v_fmac_f32_e32 v5, v131, v142
	s_addk_i32 s16, 0x200
	v_mov_b32_e32 v146, v125
	s_waitcnt lgkmcnt(1)
	v_fmac_f32_e32 v18, v136, v98
	v_fmac_f32_e32 v19, v137, v98
	v_fmac_f32_e32 v16, v134, v98
	v_fmac_f32_e32 v17, v135, v98
	v_fmac_f32_e32 v14, v136, v99
	v_fmac_f32_e32 v15, v137, v99
	v_fmac_f32_e32 v12, v134, v99
	v_fmac_f32_e32 v13, v135, v99
	v_fmac_f32_e32 v8, v134, v100
	v_fmac_f32_e32 v9, v135, v100
	v_fmac_f32_e32 v10, v136, v100
	v_fmac_f32_e32 v11, v137, v100
	v_fmac_f32_e32 v4, v134, v144
	v_fmac_f32_e32 v5, v135, v144
	v_fmac_f32_e32 v6, v136, v144
	v_fmac_f32_e32 v7, v137, v144
	v_add_u32_e32 v28, 0x440, v28
	s_cmpk_eq_i32 s16, 0x800
	s_waitcnt lgkmcnt(0)
	v_fmac_f32_e32 v18, v140, v122
	v_fmac_f32_e32 v19, v141, v122
	v_fmac_f32_e32 v16, v138, v122
	v_fmac_f32_e32 v17, v139, v122
	v_fmac_f32_e32 v14, v140, v123
	v_fmac_f32_e32 v15, v141, v123
	v_fmac_f32_e32 v12, v138, v123
	v_fmac_f32_e32 v13, v139, v123
	v_fmac_f32_e32 v10, v140, v124
	v_fmac_f32_e32 v11, v141, v124
	v_fmac_f32_e32 v8, v138, v124
	v_fmac_f32_e32 v9, v139, v124
	v_fmac_f32_e32 v6, v140, v146
	v_fmac_f32_e32 v7, v141, v146
	v_fmac_f32_e32 v4, v138, v146
	v_fmac_f32_e32 v5, v139, v146
	s_cbranch_scc0 .LBB0_654
	s_barrier
	global_load_dwordx4 v[32:35], v[94:95], off offset:256
	global_load_dwordx4 v[28:31], v[54:55], off
	s_waitcnt vmcnt(2)
	v_cvt_f32_f16_sdwa v130, v24 dst_sel:DWORD dst_unused:UNUSED_PAD src0_sel:WORD_1
	v_cvt_f32_f16_e32 v24, v24
	v_cvt_f32_f16_e32 v131, v25
	v_cvt_f32_f16_sdwa v132, v26 dst_sel:DWORD dst_unused:UNUSED_PAD src0_sel:WORD_1
	v_cvt_f32_f16_e32 v135, v26
	ds_read_b128 v[36:39], v43 offset:12544
	ds_read_b128 v[98:101], v43 offset:12560
	ds_read_b128 v[122:125], v43 offset:16640
	ds_read_b128 v[126:129], v43 offset:16656
	v_cvt_f32_f16_sdwa v97, v25 dst_sel:DWORD dst_unused:UNUSED_PAD src0_sel:WORD_1
	v_cvt_f32_f16_sdwa v133, v27 dst_sel:DWORD dst_unused:UNUSED_PAD src0_sel:WORD_1
	v_cvt_f32_f16_e32 v134, v27
	v_sub_f32_e32 v24, v24, v0
	v_sub_f32_e32 v25, v130, v1
	v_sub_f32_e32 v26, v131, v2
	v_mul_f32_e32 v24, v90, v24
	v_mul_f32_e32 v25, v91, v25
	v_sub_f32_e32 v130, v135, v0
	v_sub_f32_e32 v131, v132, v1
	v_sub_f32_e32 v27, v97, v3
	v_sub_f32_e32 v132, v134, v2
	v_sub_f32_e32 v133, v133, v3
	v_mul_f32_e32 v130, v90, v130
	v_mul_f32_e32 v131, v91, v131
	s_waitcnt lgkmcnt(1)
	v_fma_f32 v24, v36, v24, v122
	v_fma_f32 v25, v37, v25, v123
	v_mul_f32_e32 v26, v92, v26
	v_mul_f32_e32 v27, v93, v27
	v_mul_f32_e32 v132, v92, v132
	v_mul_f32_e32 v133, v93, v133
	s_waitcnt lgkmcnt(0)
	v_fma_f32 v36, v98, v130, v126
	ds_write2_b32 v96, v24, v25 offset1:68
	v_fma_f32 v24, v99, v131, v127
	ds_write2_b32 v44, v36, v24 offset0:16 offset1:84
	v_fma_f32 v24, v38, v26, v124
	v_fma_f32 v25, v100, v132, v128
	v_fmac_f32_e32 v125, v39, v27
	v_fmac_f32_e32 v129, v101, v133
	ds_write2_b32 v96, v24, v125 offset0:136 offset1:204
	ds_write2_b32 v44, v25, v129 offset0:152 offset1:220
	ds_write_b128 v104, v[20:23] offset:41984
	s_mov_b32 s16, 0
	v_mov_b32_e32 v20, v112
	s_waitcnt lgkmcnt(0)
	s_barrier
.LBB0_656:
	v_add_u32_e32 v21, s16, v111
	ds_read_b128 v[22:25], v20
	ds_read_b128 v[36:39], v20 offset:272
	ds_read_b128 v[98:101], v20 offset:544
	ds_read_b128 v[122:125], v20 offset:816
	ds_read_b128 v[126:129], v21
	ds_read_b128 v[130:133], v21 offset:128
	ds_read_b128 v[134:137], v21 offset:256
	ds_read_b128 v[138:141], v21 offset:384
	s_waitcnt lgkmcnt(7)
	v_mov_b32_e32 v26, v25
	s_waitcnt lgkmcnt(6)
	v_mov_b32_e32 v142, v39
	s_waitcnt lgkmcnt(3)
	v_fmac_f32_e32 v18, v128, v22
	v_fmac_f32_e32 v19, v129, v22
	v_fmac_f32_e32 v16, v126, v22
	v_fmac_f32_e32 v17, v127, v22
	v_fmac_f32_e32 v14, v128, v23
	v_fmac_f32_e32 v15, v129, v23
	v_fmac_f32_e32 v12, v126, v23
	v_fmac_f32_e32 v13, v127, v23
	v_fmac_f32_e32 v8, v126, v24
	v_fmac_f32_e32 v9, v127, v24
	v_fmac_f32_e32 v10, v128, v24
	v_fmac_f32_e32 v11, v129, v24
	v_fmac_f32_e32 v4, v126, v26
	v_fmac_f32_e32 v5, v127, v26
	v_fmac_f32_e32 v6, v128, v26
	v_fmac_f32_e32 v7, v129, v26
	v_mov_b32_e32 v144, v101
	s_waitcnt lgkmcnt(2)
	v_fmac_f32_e32 v18, v132, v36
	v_fmac_f32_e32 v19, v133, v36
	v_fmac_f32_e32 v16, v130, v36
	v_fmac_f32_e32 v17, v131, v36
	v_fmac_f32_e32 v14, v132, v37
	v_fmac_f32_e32 v15, v133, v37
	v_fmac_f32_e32 v12, v130, v37
	v_fmac_f32_e32 v13, v131, v37
	v_fmac_f32_e32 v10, v132, v38
	v_fmac_f32_e32 v11, v133, v38
	v_fmac_f32_e32 v8, v130, v38
	v_fmac_f32_e32 v9, v131, v38
	v_fmac_f32_e32 v6, v132, v142
	v_fmac_f32_e32 v7, v133, v142
	v_fmac_f32_e32 v4, v130, v142
	v_fmac_f32_e32 v5, v131, v142
	s_addk_i32 s16, 0x200
	v_mov_b32_e32 v146, v125
	s_waitcnt lgkmcnt(1)
	v_fmac_f32_e32 v18, v136, v98
	v_fmac_f32_e32 v19, v137, v98
	v_fmac_f32_e32 v16, v134, v98
	v_fmac_f32_e32 v17, v135, v98
	v_fmac_f32_e32 v14, v136, v99
	v_fmac_f32_e32 v15, v137, v99
	v_fmac_f32_e32 v12, v134, v99
	v_fmac_f32_e32 v13, v135, v99
	v_fmac_f32_e32 v10, v136, v100
	v_fmac_f32_e32 v11, v137, v100
	v_fmac_f32_e32 v8, v134, v100
	v_fmac_f32_e32 v9, v135, v100
	v_fmac_f32_e32 v6, v136, v144
	v_fmac_f32_e32 v7, v137, v144
	v_fmac_f32_e32 v4, v134, v144
	v_fmac_f32_e32 v5, v135, v144
	v_add_u32_e32 v20, 0x440, v20
	s_cmpk_lg_i32 s16, 0x800
	s_waitcnt lgkmcnt(0)
	v_fmac_f32_e32 v18, v140, v122
	v_fmac_f32_e32 v19, v141, v122
	v_fmac_f32_e32 v16, v138, v122
	v_fmac_f32_e32 v17, v139, v122
	v_fmac_f32_e32 v14, v140, v123
	v_fmac_f32_e32 v15, v141, v123
	v_fmac_f32_e32 v12, v138, v123
	v_fmac_f32_e32 v13, v139, v123
	v_fmac_f32_e32 v10, v140, v124
	v_fmac_f32_e32 v11, v141, v124
	v_fmac_f32_e32 v8, v138, v124
	v_fmac_f32_e32 v9, v139, v124
	v_fmac_f32_e32 v6, v140, v146
	v_fmac_f32_e32 v7, v141, v146
	v_fmac_f32_e32 v4, v138, v146
	v_fmac_f32_e32 v5, v139, v146
	s_cbranch_scc1 .LBB0_656
	s_barrier
	global_load_dwordx4 v[36:39], v[94:95], off offset:384
	global_load_dwordx4 v[20:23], v[56:57], off
	s_waitcnt vmcnt(3)
	v_cvt_f32_f16_sdwa v130, v32 dst_sel:DWORD dst_unused:UNUSED_PAD src0_sel:WORD_1
	v_cvt_f32_f16_e32 v32, v32
	v_cvt_f32_f16_e32 v131, v33
	v_cvt_f32_f16_sdwa v132, v34 dst_sel:DWORD dst_unused:UNUSED_PAD src0_sel:WORD_1
	v_cvt_f32_f16_e32 v135, v34
	ds_read_b128 v[24:27], v43 offset:12800
	ds_read_b128 v[98:101], v43 offset:12816
	ds_read_b128 v[122:125], v43 offset:16896
	ds_read_b128 v[126:129], v43 offset:16912
	v_cvt_f32_f16_sdwa v97, v33 dst_sel:DWORD dst_unused:UNUSED_PAD src0_sel:WORD_1
	v_cvt_f32_f16_sdwa v133, v35 dst_sel:DWORD dst_unused:UNUSED_PAD src0_sel:WORD_1
	v_cvt_f32_f16_e32 v134, v35
	v_sub_f32_e32 v32, v32, v0
	v_sub_f32_e32 v33, v130, v1
	v_sub_f32_e32 v34, v131, v2
	v_mul_f32_e32 v32, v90, v32
	v_mul_f32_e32 v33, v91, v33
	v_sub_f32_e32 v130, v135, v0
	v_sub_f32_e32 v131, v132, v1
	v_sub_f32_e32 v35, v97, v3
	v_mul_f32_e32 v130, v90, v130
	v_mul_f32_e32 v131, v91, v131
	s_waitcnt lgkmcnt(1)
	v_fma_f32 v24, v24, v32, v122
	v_fma_f32 v25, v25, v33, v123
	v_mul_f32_e32 v34, v92, v34
	v_mul_f32_e32 v35, v93, v35
	v_sub_f32_e32 v132, v134, v2
	v_sub_f32_e32 v133, v133, v3
	s_waitcnt lgkmcnt(0)
	v_fma_f32 v32, v98, v130, v126
	ds_write2_b32 v96, v24, v25 offset1:68
	v_fma_f32 v24, v99, v131, v127
	v_mul_f32_e32 v132, v92, v132
	v_mul_f32_e32 v133, v93, v133
	ds_write2_b32 v44, v32, v24 offset0:16 offset1:84
	v_fma_f32 v24, v26, v34, v124
	v_fmac_f32_e32 v125, v27, v35
	v_fma_f32 v25, v100, v132, v128
	ds_write2_b32 v96, v24, v125 offset0:136 offset1:204
	v_fmac_f32_e32 v129, v101, v133
	s_mov_b32 s16, 0
	v_mov_b32_e32 v24, v112
	ds_write2_b32 v44, v25, v129 offset0:152 offset1:220
	s_waitcnt vmcnt(2)
	ds_write_b128 v104, v[28:31] offset:41984
	s_waitcnt lgkmcnt(0)
	s_barrier
.LBB0_658:
	v_add_u32_e32 v25, s16, v111
	ds_read_b128 v[26:29], v24
	ds_read_b128 v[30:33], v24 offset:272
	ds_read_b128 v[98:101], v24 offset:544
	ds_read_b128 v[122:125], v24 offset:816
	ds_read_b128 v[126:129], v25
	ds_read_b128 v[130:133], v25 offset:128
	ds_read_b128 v[134:137], v25 offset:256
	ds_read_b128 v[138:141], v25 offset:384
	s_waitcnt lgkmcnt(7)
	v_mov_b32_e32 v34, v29
	s_waitcnt lgkmcnt(6)
	v_mov_b32_e32 v142, v33
	s_waitcnt lgkmcnt(3)
	v_fmac_f32_e32 v18, v128, v26
	v_fmac_f32_e32 v19, v129, v26
	v_fmac_f32_e32 v16, v126, v26
	v_fmac_f32_e32 v17, v127, v26
	v_fmac_f32_e32 v14, v128, v27
	v_fmac_f32_e32 v15, v129, v27
	v_fmac_f32_e32 v12, v126, v27
	v_fmac_f32_e32 v13, v127, v27
	v_fmac_f32_e32 v8, v126, v28
	v_fmac_f32_e32 v9, v127, v28
	v_fmac_f32_e32 v10, v128, v28
	v_fmac_f32_e32 v11, v129, v28
	v_fmac_f32_e32 v4, v126, v34
	v_fmac_f32_e32 v5, v127, v34
	v_fmac_f32_e32 v6, v128, v34
	v_fmac_f32_e32 v7, v129, v34
	v_mov_b32_e32 v144, v101
	s_waitcnt lgkmcnt(2)
	v_fmac_f32_e32 v18, v132, v30
	v_fmac_f32_e32 v19, v133, v30
	v_fmac_f32_e32 v16, v130, v30
	v_fmac_f32_e32 v17, v131, v30
	v_fmac_f32_e32 v14, v132, v31
	v_fmac_f32_e32 v15, v133, v31
	v_fmac_f32_e32 v12, v130, v31
	v_fmac_f32_e32 v13, v131, v31
	v_fmac_f32_e32 v10, v132, v32
	v_fmac_f32_e32 v11, v133, v32
	v_fmac_f32_e32 v8, v130, v32
	v_fmac_f32_e32 v9, v131, v32
	v_fmac_f32_e32 v6, v132, v142
	v_fmac_f32_e32 v7, v133, v142
	v_fmac_f32_e32 v4, v130, v142
	v_fmac_f32_e32 v5, v131, v142
	s_addk_i32 s16, 0x200
	v_mov_b32_e32 v146, v125
	s_waitcnt lgkmcnt(1)
	v_fmac_f32_e32 v18, v136, v98
	v_fmac_f32_e32 v19, v137, v98
	v_fmac_f32_e32 v16, v134, v98
	v_fmac_f32_e32 v17, v135, v98
	v_fmac_f32_e32 v14, v136, v99
	v_fmac_f32_e32 v15, v137, v99
	v_fmac_f32_e32 v12, v134, v99
	v_fmac_f32_e32 v13, v135, v99
	v_fmac_f32_e32 v10, v136, v100
	v_fmac_f32_e32 v11, v137, v100
	v_fmac_f32_e32 v8, v134, v100
	v_fmac_f32_e32 v9, v135, v100
	v_fmac_f32_e32 v6, v136, v144
	v_fmac_f32_e32 v7, v137, v144
	v_fmac_f32_e32 v4, v134, v144
	v_fmac_f32_e32 v5, v135, v144
	v_add_u32_e32 v24, 0x440, v24
	s_cmpk_lg_i32 s16, 0x800
	s_waitcnt lgkmcnt(0)
	v_fmac_f32_e32 v18, v140, v122
	v_fmac_f32_e32 v19, v141, v122
	v_fmac_f32_e32 v16, v138, v122
	v_fmac_f32_e32 v17, v139, v122
	v_fmac_f32_e32 v14, v140, v123
	v_fmac_f32_e32 v15, v141, v123
	v_fmac_f32_e32 v12, v138, v123
	v_fmac_f32_e32 v13, v139, v123
	v_fmac_f32_e32 v10, v140, v124
	v_fmac_f32_e32 v11, v141, v124
	v_fmac_f32_e32 v8, v138, v124
	v_fmac_f32_e32 v9, v139, v124
	v_fmac_f32_e32 v6, v140, v146
	v_fmac_f32_e32 v7, v141, v146
	v_fmac_f32_e32 v4, v138, v146
	v_fmac_f32_e32 v5, v139, v146
	s_cbranch_scc1 .LBB0_658
	s_barrier
	global_load_dwordx4 v[28:31], v[94:95], off offset:512
	global_load_dwordx4 v[24:27], v[58:59], off
	s_waitcnt vmcnt(3)
	v_cvt_f32_f16_sdwa v130, v36 dst_sel:DWORD dst_unused:UNUSED_PAD src0_sel:WORD_1
	v_cvt_f32_f16_e32 v36, v36
	v_cvt_f32_f16_e32 v131, v37
	v_cvt_f32_f16_sdwa v132, v38 dst_sel:DWORD dst_unused:UNUSED_PAD src0_sel:WORD_1
	v_cvt_f32_f16_e32 v135, v38
	ds_read_b128 v[32:35], v43 offset:13056
	ds_read_b128 v[98:101], v43 offset:13072
	ds_read_b128 v[122:125], v43 offset:17152
	ds_read_b128 v[126:129], v43 offset:17168
	v_cvt_f32_f16_sdwa v97, v37 dst_sel:DWORD dst_unused:UNUSED_PAD src0_sel:WORD_1
	v_cvt_f32_f16_sdwa v133, v39 dst_sel:DWORD dst_unused:UNUSED_PAD src0_sel:WORD_1
	v_cvt_f32_f16_e32 v134, v39
	v_sub_f32_e32 v36, v36, v0
	v_sub_f32_e32 v37, v130, v1
	v_sub_f32_e32 v38, v131, v2
	v_mul_f32_e32 v36, v90, v36
	v_mul_f32_e32 v37, v91, v37
	v_sub_f32_e32 v130, v135, v0
	v_sub_f32_e32 v131, v132, v1
	v_sub_f32_e32 v39, v97, v3
	v_sub_f32_e32 v132, v134, v2
	v_sub_f32_e32 v133, v133, v3
	v_mul_f32_e32 v130, v90, v130
	v_mul_f32_e32 v131, v91, v131
	s_waitcnt lgkmcnt(1)
	v_fma_f32 v32, v32, v36, v122
	v_fma_f32 v33, v33, v37, v123
	v_mul_f32_e32 v38, v92, v38
	v_mul_f32_e32 v39, v93, v39
	v_mul_f32_e32 v132, v92, v132
	v_mul_f32_e32 v133, v93, v133
	s_waitcnt lgkmcnt(0)
	v_fma_f32 v36, v98, v130, v126
	ds_write2_b32 v96, v32, v33 offset1:68
	v_fma_f32 v32, v99, v131, v127
	ds_write2_b32 v44, v36, v32 offset0:16 offset1:84
	v_fma_f32 v32, v34, v38, v124
	v_fma_f32 v33, v100, v132, v128
	v_fmac_f32_e32 v125, v35, v39
	v_fmac_f32_e32 v129, v101, v133
	ds_write2_b32 v96, v32, v125 offset0:136 offset1:204
	ds_write2_b32 v44, v33, v129 offset0:152 offset1:220
	s_waitcnt vmcnt(2)
	ds_write_b128 v104, v[20:23] offset:41984
	s_mov_b32 s16, 0
	v_mov_b32_e32 v20, v112
	s_waitcnt lgkmcnt(0)
	s_barrier
.LBB0_660:
	v_add_u32_e32 v21, s16, v111
	ds_read_b128 v[32:35], v20
	ds_read_b128 v[36:39], v20 offset:272
	ds_read_b128 v[98:101], v20 offset:544
	ds_read_b128 v[122:125], v20 offset:816
	ds_read_b128 v[126:129], v21
	ds_read_b128 v[130:133], v21 offset:128
	ds_read_b128 v[134:137], v21 offset:256
	ds_read_b128 v[138:141], v21 offset:384
	s_waitcnt lgkmcnt(7)
	v_mov_b32_e32 v22, v35
	s_waitcnt lgkmcnt(6)
	v_mov_b32_e32 v142, v39
	s_waitcnt lgkmcnt(3)
	v_fmac_f32_e32 v18, v128, v32
	v_fmac_f32_e32 v19, v129, v32
	v_fmac_f32_e32 v16, v126, v32
	v_fmac_f32_e32 v17, v127, v32
	v_fmac_f32_e32 v14, v128, v33
	v_fmac_f32_e32 v15, v129, v33
	v_fmac_f32_e32 v12, v126, v33
	v_fmac_f32_e32 v13, v127, v33
	v_fmac_f32_e32 v8, v126, v34
	v_fmac_f32_e32 v9, v127, v34
	v_fmac_f32_e32 v10, v128, v34
	v_fmac_f32_e32 v11, v129, v34
	v_fmac_f32_e32 v4, v126, v22
	v_fmac_f32_e32 v5, v127, v22
	v_fmac_f32_e32 v6, v128, v22
	v_fmac_f32_e32 v7, v129, v22
	v_mov_b32_e32 v144, v101
	s_waitcnt lgkmcnt(2)
	v_fmac_f32_e32 v18, v132, v36
	v_fmac_f32_e32 v19, v133, v36
	v_fmac_f32_e32 v16, v130, v36
	v_fmac_f32_e32 v17, v131, v36
	v_fmac_f32_e32 v14, v132, v37
	v_fmac_f32_e32 v15, v133, v37
	v_fmac_f32_e32 v12, v130, v37
	v_fmac_f32_e32 v13, v131, v37
	v_fmac_f32_e32 v10, v132, v38
	v_fmac_f32_e32 v11, v133, v38
	v_fmac_f32_e32 v8, v130, v38
	v_fmac_f32_e32 v9, v131, v38
	v_fmac_f32_e32 v6, v132, v142
	v_fmac_f32_e32 v7, v133, v142
	v_fmac_f32_e32 v4, v130, v142
	v_fmac_f32_e32 v5, v131, v142
	s_addk_i32 s16, 0x200
	v_mov_b32_e32 v146, v125
	s_waitcnt lgkmcnt(1)
	v_fmac_f32_e32 v18, v136, v98
	v_fmac_f32_e32 v19, v137, v98
	v_fmac_f32_e32 v16, v134, v98
	v_fmac_f32_e32 v17, v135, v98
	v_fmac_f32_e32 v14, v136, v99
	v_fmac_f32_e32 v15, v137, v99
	v_fmac_f32_e32 v12, v134, v99
	v_fmac_f32_e32 v13, v135, v99
	v_fmac_f32_e32 v10, v136, v100
	v_fmac_f32_e32 v11, v137, v100
	v_fmac_f32_e32 v8, v134, v100
	v_fmac_f32_e32 v9, v135, v100
	v_fmac_f32_e32 v6, v136, v144
	v_fmac_f32_e32 v7, v137, v144
	v_fmac_f32_e32 v4, v134, v144
	v_fmac_f32_e32 v5, v135, v144
	v_add_u32_e32 v20, 0x440, v20
	s_cmpk_lg_i32 s16, 0x800
	s_waitcnt lgkmcnt(0)
	v_fmac_f32_e32 v18, v140, v122
	v_fmac_f32_e32 v19, v141, v122
	v_fmac_f32_e32 v16, v138, v122
	v_fmac_f32_e32 v17, v139, v122
	v_fmac_f32_e32 v14, v140, v123
	v_fmac_f32_e32 v15, v141, v123
	v_fmac_f32_e32 v12, v138, v123
	v_fmac_f32_e32 v13, v139, v123
	v_fmac_f32_e32 v10, v140, v124
	v_fmac_f32_e32 v11, v141, v124
	v_fmac_f32_e32 v8, v138, v124
	v_fmac_f32_e32 v9, v139, v124
	v_fmac_f32_e32 v6, v140, v146
	v_fmac_f32_e32 v7, v141, v146
	v_fmac_f32_e32 v4, v138, v146
	v_fmac_f32_e32 v5, v139, v146
	s_cbranch_scc1 .LBB0_660
	s_barrier
	global_load_dwordx4 v[32:35], v[94:95], off offset:640
	global_load_dwordx4 v[20:23], v[60:61], off
	s_waitcnt vmcnt(3)
	v_cvt_f32_f16_sdwa v130, v28 dst_sel:DWORD dst_unused:UNUSED_PAD src0_sel:WORD_1
	v_cvt_f32_f16_e32 v28, v28
	v_cvt_f32_f16_e32 v131, v29
	v_cvt_f32_f16_sdwa v132, v30 dst_sel:DWORD dst_unused:UNUSED_PAD src0_sel:WORD_1
	v_cvt_f32_f16_e32 v135, v30
	ds_read_b128 v[36:39], v43 offset:13312
	ds_read_b128 v[98:101], v43 offset:13328
	ds_read_b128 v[122:125], v43 offset:17408
	ds_read_b128 v[126:129], v43 offset:17424
	v_cvt_f32_f16_sdwa v97, v29 dst_sel:DWORD dst_unused:UNUSED_PAD src0_sel:WORD_1
	v_cvt_f32_f16_sdwa v133, v31 dst_sel:DWORD dst_unused:UNUSED_PAD src0_sel:WORD_1
	v_cvt_f32_f16_e32 v134, v31
	v_sub_f32_e32 v28, v28, v0
	v_sub_f32_e32 v29, v130, v1
	v_sub_f32_e32 v30, v131, v2
	v_mul_f32_e32 v28, v90, v28
	v_mul_f32_e32 v29, v91, v29
	v_sub_f32_e32 v130, v135, v0
	v_sub_f32_e32 v131, v132, v1
	v_sub_f32_e32 v31, v97, v3
	v_sub_f32_e32 v132, v134, v2
	v_sub_f32_e32 v133, v133, v3
	v_mul_f32_e32 v130, v90, v130
	v_mul_f32_e32 v131, v91, v131
	s_waitcnt lgkmcnt(1)
	v_fma_f32 v28, v36, v28, v122
	v_fma_f32 v29, v37, v29, v123
	v_mul_f32_e32 v30, v92, v30
	v_mul_f32_e32 v31, v93, v31
	v_mul_f32_e32 v132, v92, v132
	v_mul_f32_e32 v133, v93, v133
	s_waitcnt lgkmcnt(0)
	v_fma_f32 v36, v98, v130, v126
	ds_write2_b32 v96, v28, v29 offset1:68
	v_fma_f32 v28, v99, v131, v127
	ds_write2_b32 v44, v36, v28 offset0:16 offset1:84
	v_fma_f32 v28, v38, v30, v124
	v_fma_f32 v29, v100, v132, v128
	v_fmac_f32_e32 v125, v39, v31
	v_fmac_f32_e32 v129, v101, v133
	ds_write2_b32 v96, v28, v125 offset0:136 offset1:204
	ds_write2_b32 v44, v29, v129 offset0:152 offset1:220
	s_waitcnt vmcnt(2)
	ds_write_b128 v104, v[24:27] offset:41984
	s_mov_b32 s16, 0
	v_mov_b32_e32 v24, v112
	s_waitcnt lgkmcnt(0)
	s_barrier
.LBB0_662:
	v_add_u32_e32 v25, s16, v111
	ds_read_b128 v[26:29], v24
	ds_read_b128 v[36:39], v24 offset:272
	ds_read_b128 v[98:101], v24 offset:544
	ds_read_b128 v[122:125], v24 offset:816
	ds_read_b128 v[126:129], v25
	ds_read_b128 v[130:133], v25 offset:128
	ds_read_b128 v[134:137], v25 offset:256
	ds_read_b128 v[138:141], v25 offset:384
	s_waitcnt lgkmcnt(7)
	v_mov_b32_e32 v30, v29
	s_waitcnt lgkmcnt(6)
	v_mov_b32_e32 v142, v39
	s_waitcnt lgkmcnt(3)
	v_fmac_f32_e32 v18, v128, v26
	v_fmac_f32_e32 v19, v129, v26
	v_fmac_f32_e32 v16, v126, v26
	v_fmac_f32_e32 v17, v127, v26
	v_fmac_f32_e32 v14, v128, v27
	v_fmac_f32_e32 v15, v129, v27
	v_fmac_f32_e32 v12, v126, v27
	v_fmac_f32_e32 v13, v127, v27
	v_fmac_f32_e32 v8, v126, v28
	v_fmac_f32_e32 v9, v127, v28
	v_fmac_f32_e32 v10, v128, v28
	v_fmac_f32_e32 v11, v129, v28
	v_fmac_f32_e32 v4, v126, v30
	v_fmac_f32_e32 v5, v127, v30
	v_fmac_f32_e32 v6, v128, v30
	v_fmac_f32_e32 v7, v129, v30
	v_mov_b32_e32 v144, v101
	s_waitcnt lgkmcnt(2)
	v_fmac_f32_e32 v18, v132, v36
	v_fmac_f32_e32 v19, v133, v36
	v_fmac_f32_e32 v16, v130, v36
	v_fmac_f32_e32 v17, v131, v36
	v_fmac_f32_e32 v14, v132, v37
	v_fmac_f32_e32 v15, v133, v37
	v_fmac_f32_e32 v12, v130, v37
	v_fmac_f32_e32 v13, v131, v37
	v_fmac_f32_e32 v10, v132, v38
	v_fmac_f32_e32 v11, v133, v38
	v_fmac_f32_e32 v8, v130, v38
	v_fmac_f32_e32 v9, v131, v38
	v_fmac_f32_e32 v6, v132, v142
	v_fmac_f32_e32 v7, v133, v142
	v_fmac_f32_e32 v4, v130, v142
	v_fmac_f32_e32 v5, v131, v142
	s_addk_i32 s16, 0x200
	v_mov_b32_e32 v146, v125
	s_waitcnt lgkmcnt(1)
	v_fmac_f32_e32 v18, v136, v98
	v_fmac_f32_e32 v19, v137, v98
	v_fmac_f32_e32 v16, v134, v98
	v_fmac_f32_e32 v17, v135, v98
	v_fmac_f32_e32 v14, v136, v99
	v_fmac_f32_e32 v15, v137, v99
	v_fmac_f32_e32 v12, v134, v99
	v_fmac_f32_e32 v13, v135, v99
	v_fmac_f32_e32 v10, v136, v100
	v_fmac_f32_e32 v11, v137, v100
	v_fmac_f32_e32 v8, v134, v100
	v_fmac_f32_e32 v9, v135, v100
	v_fmac_f32_e32 v6, v136, v144
	v_fmac_f32_e32 v7, v137, v144
	v_fmac_f32_e32 v4, v134, v144
	v_fmac_f32_e32 v5, v135, v144
	v_add_u32_e32 v24, 0x440, v24
	s_cmpk_lg_i32 s16, 0x800
	s_waitcnt lgkmcnt(0)
	v_fmac_f32_e32 v18, v140, v122
	v_fmac_f32_e32 v19, v141, v122
	v_fmac_f32_e32 v16, v138, v122
	v_fmac_f32_e32 v17, v139, v122
	v_fmac_f32_e32 v14, v140, v123
	v_fmac_f32_e32 v15, v141, v123
	v_fmac_f32_e32 v12, v138, v123
	v_fmac_f32_e32 v13, v139, v123
	v_fmac_f32_e32 v10, v140, v124
	v_fmac_f32_e32 v11, v141, v124
	v_fmac_f32_e32 v8, v138, v124
	v_fmac_f32_e32 v9, v139, v124
	v_fmac_f32_e32 v6, v140, v146
	v_fmac_f32_e32 v7, v141, v146
	v_fmac_f32_e32 v4, v138, v146
	v_fmac_f32_e32 v5, v139, v146
	s_cbranch_scc1 .LBB0_662
	s_barrier
	global_load_dwordx4 v[28:31], v[94:95], off offset:768
	global_load_dwordx4 v[24:27], v[62:63], off
	s_waitcnt vmcnt(3)
	v_cvt_f32_f16_sdwa v130, v32 dst_sel:DWORD dst_unused:UNUSED_PAD src0_sel:WORD_1
	v_cvt_f32_f16_e32 v32, v32
	v_cvt_f32_f16_e32 v131, v33
	v_cvt_f32_f16_sdwa v132, v34 dst_sel:DWORD dst_unused:UNUSED_PAD src0_sel:WORD_1
	v_cvt_f32_f16_e32 v135, v34
	ds_read_b128 v[36:39], v43 offset:13568
	ds_read_b128 v[98:101], v43 offset:13584
	ds_read_b128 v[122:125], v43 offset:17664
	ds_read_b128 v[126:129], v43 offset:17680
	v_cvt_f32_f16_sdwa v97, v33 dst_sel:DWORD dst_unused:UNUSED_PAD src0_sel:WORD_1
	v_cvt_f32_f16_sdwa v133, v35 dst_sel:DWORD dst_unused:UNUSED_PAD src0_sel:WORD_1
	v_cvt_f32_f16_e32 v134, v35
	v_sub_f32_e32 v32, v32, v0
	v_sub_f32_e32 v33, v130, v1
	v_sub_f32_e32 v34, v131, v2
	v_mul_f32_e32 v32, v90, v32
	v_mul_f32_e32 v33, v91, v33
	v_sub_f32_e32 v130, v135, v0
	v_sub_f32_e32 v131, v132, v1
	v_sub_f32_e32 v35, v97, v3
	v_sub_f32_e32 v132, v134, v2
	v_sub_f32_e32 v133, v133, v3
	v_mul_f32_e32 v130, v90, v130
	v_mul_f32_e32 v131, v91, v131
	s_waitcnt lgkmcnt(1)
	v_fma_f32 v32, v36, v32, v122
	v_fma_f32 v33, v37, v33, v123
	v_mul_f32_e32 v34, v92, v34
	v_mul_f32_e32 v35, v93, v35
	v_mul_f32_e32 v132, v92, v132
	v_mul_f32_e32 v133, v93, v133
	s_waitcnt lgkmcnt(0)
	v_fma_f32 v36, v98, v130, v126
	ds_write2_b32 v96, v32, v33 offset1:68
	v_fma_f32 v32, v99, v131, v127
	ds_write2_b32 v44, v36, v32 offset0:16 offset1:84
	v_fma_f32 v32, v38, v34, v124
	v_fma_f32 v33, v100, v132, v128
	v_fmac_f32_e32 v125, v39, v35
	v_fmac_f32_e32 v129, v101, v133
	ds_write2_b32 v96, v32, v125 offset0:136 offset1:204
	ds_write2_b32 v44, v33, v129 offset0:152 offset1:220
	s_waitcnt vmcnt(2)
	ds_write_b128 v104, v[20:23] offset:41984
	s_mov_b32 s16, 0
	v_mov_b32_e32 v20, v112
	s_waitcnt lgkmcnt(0)
	s_barrier
.LBB0_664:
	v_add_u32_e32 v21, s16, v111
	ds_read_b128 v[32:35], v20
	ds_read_b128 v[36:39], v20 offset:272
	ds_read_b128 v[98:101], v20 offset:544
	ds_read_b128 v[122:125], v20 offset:816
	ds_read_b128 v[126:129], v21
	ds_read_b128 v[130:133], v21 offset:128
	ds_read_b128 v[134:137], v21 offset:256
	ds_read_b128 v[138:141], v21 offset:384
	s_waitcnt lgkmcnt(7)
	v_mov_b32_e32 v22, v35
	s_waitcnt lgkmcnt(6)
	v_mov_b32_e32 v142, v39
	s_waitcnt lgkmcnt(3)
	v_fmac_f32_e32 v18, v128, v32
	v_fmac_f32_e32 v19, v129, v32
	v_fmac_f32_e32 v16, v126, v32
	v_fmac_f32_e32 v17, v127, v32
	v_fmac_f32_e32 v14, v128, v33
	v_fmac_f32_e32 v15, v129, v33
	v_fmac_f32_e32 v12, v126, v33
	v_fmac_f32_e32 v13, v127, v33
	v_fmac_f32_e32 v8, v126, v34
	v_fmac_f32_e32 v9, v127, v34
	v_fmac_f32_e32 v10, v128, v34
	v_fmac_f32_e32 v11, v129, v34
	v_fmac_f32_e32 v4, v126, v22
	v_fmac_f32_e32 v5, v127, v22
	v_fmac_f32_e32 v6, v128, v22
	v_fmac_f32_e32 v7, v129, v22
	v_mov_b32_e32 v144, v101
	s_waitcnt lgkmcnt(2)
	v_fmac_f32_e32 v18, v132, v36
	v_fmac_f32_e32 v19, v133, v36
	v_fmac_f32_e32 v16, v130, v36
	v_fmac_f32_e32 v17, v131, v36
	v_fmac_f32_e32 v14, v132, v37
	v_fmac_f32_e32 v15, v133, v37
	v_fmac_f32_e32 v12, v130, v37
	v_fmac_f32_e32 v13, v131, v37
	v_fmac_f32_e32 v10, v132, v38
	v_fmac_f32_e32 v11, v133, v38
	v_fmac_f32_e32 v8, v130, v38
	v_fmac_f32_e32 v9, v131, v38
	v_fmac_f32_e32 v6, v132, v142
	v_fmac_f32_e32 v7, v133, v142
	v_fmac_f32_e32 v4, v130, v142
	v_fmac_f32_e32 v5, v131, v142
	s_addk_i32 s16, 0x200
	v_mov_b32_e32 v146, v125
	s_waitcnt lgkmcnt(1)
	v_fmac_f32_e32 v18, v136, v98
	v_fmac_f32_e32 v19, v137, v98
	v_fmac_f32_e32 v16, v134, v98
	v_fmac_f32_e32 v17, v135, v98
	v_fmac_f32_e32 v14, v136, v99
	v_fmac_f32_e32 v15, v137, v99
	v_fmac_f32_e32 v12, v134, v99
	v_fmac_f32_e32 v13, v135, v99
	v_fmac_f32_e32 v10, v136, v100
	v_fmac_f32_e32 v11, v137, v100
	v_fmac_f32_e32 v8, v134, v100
	v_fmac_f32_e32 v9, v135, v100
	v_fmac_f32_e32 v6, v136, v144
	v_fmac_f32_e32 v7, v137, v144
	v_fmac_f32_e32 v4, v134, v144
	v_fmac_f32_e32 v5, v135, v144
	v_add_u32_e32 v20, 0x440, v20
	s_cmpk_lg_i32 s16, 0x800
	s_waitcnt lgkmcnt(0)
	v_fmac_f32_e32 v18, v140, v122
	v_fmac_f32_e32 v19, v141, v122
	v_fmac_f32_e32 v16, v138, v122
	v_fmac_f32_e32 v17, v139, v122
	v_fmac_f32_e32 v14, v140, v123
	v_fmac_f32_e32 v15, v141, v123
	v_fmac_f32_e32 v12, v138, v123
	v_fmac_f32_e32 v13, v139, v123
	v_fmac_f32_e32 v10, v140, v124
	v_fmac_f32_e32 v11, v141, v124
	v_fmac_f32_e32 v8, v138, v124
	v_fmac_f32_e32 v9, v139, v124
	v_fmac_f32_e32 v6, v140, v146
	v_fmac_f32_e32 v7, v141, v146
	v_fmac_f32_e32 v4, v138, v146
	v_fmac_f32_e32 v5, v139, v146
	s_cbranch_scc1 .LBB0_664
	s_barrier
	global_load_dwordx4 v[32:35], v[94:95], off offset:896
	global_load_dwordx4 v[20:23], v[64:65], off
	s_waitcnt vmcnt(3)
	v_cvt_f32_f16_sdwa v130, v28 dst_sel:DWORD dst_unused:UNUSED_PAD src0_sel:WORD_1
	v_cvt_f32_f16_e32 v28, v28
	v_cvt_f32_f16_e32 v131, v29
	v_cvt_f32_f16_sdwa v132, v30 dst_sel:DWORD dst_unused:UNUSED_PAD src0_sel:WORD_1
	v_cvt_f32_f16_e32 v135, v30
	ds_read_b128 v[36:39], v43 offset:13824
	ds_read_b128 v[98:101], v43 offset:13840
	ds_read_b128 v[122:125], v43 offset:17920
	ds_read_b128 v[126:129], v43 offset:17936
	v_cvt_f32_f16_sdwa v97, v29 dst_sel:DWORD dst_unused:UNUSED_PAD src0_sel:WORD_1
	v_cvt_f32_f16_sdwa v133, v31 dst_sel:DWORD dst_unused:UNUSED_PAD src0_sel:WORD_1
	v_cvt_f32_f16_e32 v134, v31
	v_sub_f32_e32 v28, v28, v0
	v_sub_f32_e32 v29, v130, v1
	v_sub_f32_e32 v30, v131, v2
	v_mul_f32_e32 v28, v90, v28
	v_mul_f32_e32 v29, v91, v29
	v_sub_f32_e32 v130, v135, v0
	v_sub_f32_e32 v131, v132, v1
	v_sub_f32_e32 v31, v97, v3
	v_sub_f32_e32 v132, v134, v2
	v_sub_f32_e32 v133, v133, v3
	v_mul_f32_e32 v130, v90, v130
	v_mul_f32_e32 v131, v91, v131
	s_waitcnt lgkmcnt(1)
	v_fma_f32 v28, v36, v28, v122
	v_fma_f32 v29, v37, v29, v123
	v_mul_f32_e32 v30, v92, v30
	v_mul_f32_e32 v31, v93, v31
	v_mul_f32_e32 v132, v92, v132
	v_mul_f32_e32 v133, v93, v133
	s_waitcnt lgkmcnt(0)
	v_fma_f32 v36, v98, v130, v126
	ds_write2_b32 v96, v28, v29 offset1:68
	v_fma_f32 v28, v99, v131, v127
	ds_write2_b32 v44, v36, v28 offset0:16 offset1:84
	v_fma_f32 v28, v38, v30, v124
	v_fma_f32 v29, v100, v132, v128
	v_fmac_f32_e32 v125, v39, v31
	v_fmac_f32_e32 v129, v101, v133
	ds_write2_b32 v96, v28, v125 offset0:136 offset1:204
	ds_write2_b32 v44, v29, v129 offset0:152 offset1:220
	s_waitcnt vmcnt(2)
	ds_write_b128 v104, v[24:27] offset:41984
	s_mov_b32 s16, 0
	v_mov_b32_e32 v24, v112
	s_waitcnt lgkmcnt(0)
	s_barrier
.LBB0_666:
	v_add_u32_e32 v25, s16, v111
	ds_read_b128 v[26:29], v24
	ds_read_b128 v[36:39], v24 offset:272
	ds_read_b128 v[98:101], v24 offset:544
	ds_read_b128 v[122:125], v24 offset:816
	ds_read_b128 v[126:129], v25
	ds_read_b128 v[130:133], v25 offset:128
	ds_read_b128 v[134:137], v25 offset:256
	ds_read_b128 v[138:141], v25 offset:384
	s_waitcnt lgkmcnt(7)
	v_mov_b32_e32 v30, v29
	s_waitcnt lgkmcnt(6)
	v_mov_b32_e32 v142, v39
	s_waitcnt lgkmcnt(3)
	v_fmac_f32_e32 v18, v128, v26
	v_fmac_f32_e32 v19, v129, v26
	v_fmac_f32_e32 v16, v126, v26
	v_fmac_f32_e32 v17, v127, v26
	v_fmac_f32_e32 v14, v128, v27
	v_fmac_f32_e32 v15, v129, v27
	v_fmac_f32_e32 v12, v126, v27
	v_fmac_f32_e32 v13, v127, v27
	v_fmac_f32_e32 v8, v126, v28
	v_fmac_f32_e32 v9, v127, v28
	v_fmac_f32_e32 v10, v128, v28
	v_fmac_f32_e32 v11, v129, v28
	v_fmac_f32_e32 v4, v126, v30
	v_fmac_f32_e32 v5, v127, v30
	v_fmac_f32_e32 v6, v128, v30
	v_fmac_f32_e32 v7, v129, v30
	v_mov_b32_e32 v144, v101
	s_waitcnt lgkmcnt(2)
	v_fmac_f32_e32 v18, v132, v36
	v_fmac_f32_e32 v19, v133, v36
	v_fmac_f32_e32 v16, v130, v36
	v_fmac_f32_e32 v17, v131, v36
	v_fmac_f32_e32 v14, v132, v37
	v_fmac_f32_e32 v15, v133, v37
	v_fmac_f32_e32 v12, v130, v37
	v_fmac_f32_e32 v13, v131, v37
	v_fmac_f32_e32 v10, v132, v38
	v_fmac_f32_e32 v11, v133, v38
	v_fmac_f32_e32 v8, v130, v38
	v_fmac_f32_e32 v9, v131, v38
	v_fmac_f32_e32 v6, v132, v142
	v_fmac_f32_e32 v7, v133, v142
	v_fmac_f32_e32 v4, v130, v142
	v_fmac_f32_e32 v5, v131, v142
	s_addk_i32 s16, 0x200
	v_mov_b32_e32 v146, v125
	s_waitcnt lgkmcnt(1)
	v_fmac_f32_e32 v18, v136, v98
	v_fmac_f32_e32 v19, v137, v98
	v_fmac_f32_e32 v16, v134, v98
	v_fmac_f32_e32 v17, v135, v98
	v_fmac_f32_e32 v14, v136, v99
	v_fmac_f32_e32 v15, v137, v99
	v_fmac_f32_e32 v12, v134, v99
	v_fmac_f32_e32 v13, v135, v99
	v_fmac_f32_e32 v10, v136, v100
	v_fmac_f32_e32 v11, v137, v100
	v_fmac_f32_e32 v8, v134, v100
	v_fmac_f32_e32 v9, v135, v100
	v_fmac_f32_e32 v6, v136, v144
	v_fmac_f32_e32 v7, v137, v144
	v_fmac_f32_e32 v4, v134, v144
	v_fmac_f32_e32 v5, v135, v144
	v_add_u32_e32 v24, 0x440, v24
	s_cmpk_lg_i32 s16, 0x800
	s_waitcnt lgkmcnt(0)
	v_fmac_f32_e32 v18, v140, v122
	v_fmac_f32_e32 v19, v141, v122
	v_fmac_f32_e32 v16, v138, v122
	v_fmac_f32_e32 v17, v139, v122
	v_fmac_f32_e32 v14, v140, v123
	v_fmac_f32_e32 v15, v141, v123
	v_fmac_f32_e32 v12, v138, v123
	v_fmac_f32_e32 v13, v139, v123
	v_fmac_f32_e32 v10, v140, v124
	v_fmac_f32_e32 v11, v141, v124
	v_fmac_f32_e32 v8, v138, v124
	v_fmac_f32_e32 v9, v139, v124
	v_fmac_f32_e32 v6, v140, v146
	v_fmac_f32_e32 v7, v141, v146
	v_fmac_f32_e32 v4, v138, v146
	v_fmac_f32_e32 v5, v139, v146
	s_cbranch_scc1 .LBB0_666
	s_barrier
	global_load_dwordx4 v[28:31], v[94:95], off offset:1024
	global_load_dwordx4 v[24:27], v[66:67], off
	s_waitcnt vmcnt(3)
	v_cvt_f32_f16_sdwa v130, v32 dst_sel:DWORD dst_unused:UNUSED_PAD src0_sel:WORD_1
	v_cvt_f32_f16_e32 v32, v32
	v_cvt_f32_f16_e32 v131, v33
	v_cvt_f32_f16_sdwa v132, v34 dst_sel:DWORD dst_unused:UNUSED_PAD src0_sel:WORD_1
	v_cvt_f32_f16_e32 v135, v34
	ds_read_b128 v[36:39], v43 offset:14080
	ds_read_b128 v[98:101], v43 offset:14096
	ds_read_b128 v[122:125], v43 offset:18176
	ds_read_b128 v[126:129], v43 offset:18192
	v_cvt_f32_f16_sdwa v97, v33 dst_sel:DWORD dst_unused:UNUSED_PAD src0_sel:WORD_1
	v_cvt_f32_f16_sdwa v133, v35 dst_sel:DWORD dst_unused:UNUSED_PAD src0_sel:WORD_1
	v_cvt_f32_f16_e32 v134, v35
	v_sub_f32_e32 v32, v32, v0
	v_sub_f32_e32 v33, v130, v1
	v_sub_f32_e32 v34, v131, v2
	v_mul_f32_e32 v32, v90, v32
	v_mul_f32_e32 v33, v91, v33
	v_sub_f32_e32 v130, v135, v0
	v_sub_f32_e32 v131, v132, v1
	v_sub_f32_e32 v35, v97, v3
	v_sub_f32_e32 v132, v134, v2
	v_sub_f32_e32 v133, v133, v3
	v_mul_f32_e32 v130, v90, v130
	v_mul_f32_e32 v131, v91, v131
	s_waitcnt lgkmcnt(1)
	v_fma_f32 v32, v36, v32, v122
	v_fma_f32 v33, v37, v33, v123
	v_mul_f32_e32 v34, v92, v34
	v_mul_f32_e32 v35, v93, v35
	v_mul_f32_e32 v132, v92, v132
	v_mul_f32_e32 v133, v93, v133
	s_waitcnt lgkmcnt(0)
	v_fma_f32 v36, v98, v130, v126
	ds_write2_b32 v96, v32, v33 offset1:68
	v_fma_f32 v32, v99, v131, v127
	ds_write2_b32 v44, v36, v32 offset0:16 offset1:84
	v_fma_f32 v32, v38, v34, v124
	v_fma_f32 v33, v100, v132, v128
	v_fmac_f32_e32 v125, v39, v35
	v_fmac_f32_e32 v129, v101, v133
	ds_write2_b32 v96, v32, v125 offset0:136 offset1:204
	ds_write2_b32 v44, v33, v129 offset0:152 offset1:220
	s_waitcnt vmcnt(2)
	ds_write_b128 v104, v[20:23] offset:41984
	s_mov_b32 s16, 0
	v_mov_b32_e32 v20, v112
	s_waitcnt lgkmcnt(0)
	s_barrier
.LBB0_668:
	v_add_u32_e32 v21, s16, v111
	ds_read_b128 v[32:35], v20
	ds_read_b128 v[36:39], v20 offset:272
	ds_read_b128 v[98:101], v20 offset:544
	ds_read_b128 v[122:125], v20 offset:816
	ds_read_b128 v[126:129], v21
	ds_read_b128 v[130:133], v21 offset:128
	ds_read_b128 v[134:137], v21 offset:256
	ds_read_b128 v[138:141], v21 offset:384
	s_waitcnt lgkmcnt(7)
	v_mov_b32_e32 v22, v35
	s_waitcnt lgkmcnt(6)
	v_mov_b32_e32 v142, v39
	s_waitcnt lgkmcnt(3)
	v_fmac_f32_e32 v18, v128, v32
	v_fmac_f32_e32 v19, v129, v32
	v_fmac_f32_e32 v16, v126, v32
	v_fmac_f32_e32 v17, v127, v32
	v_fmac_f32_e32 v14, v128, v33
	v_fmac_f32_e32 v15, v129, v33
	v_fmac_f32_e32 v12, v126, v33
	v_fmac_f32_e32 v13, v127, v33
	v_fmac_f32_e32 v8, v126, v34
	v_fmac_f32_e32 v9, v127, v34
	v_fmac_f32_e32 v10, v128, v34
	v_fmac_f32_e32 v11, v129, v34
	v_fmac_f32_e32 v4, v126, v22
	v_fmac_f32_e32 v5, v127, v22
	v_fmac_f32_e32 v6, v128, v22
	v_fmac_f32_e32 v7, v129, v22
	v_mov_b32_e32 v144, v101
	s_waitcnt lgkmcnt(2)
	v_fmac_f32_e32 v18, v132, v36
	v_fmac_f32_e32 v19, v133, v36
	v_fmac_f32_e32 v16, v130, v36
	v_fmac_f32_e32 v17, v131, v36
	v_fmac_f32_e32 v14, v132, v37
	v_fmac_f32_e32 v15, v133, v37
	v_fmac_f32_e32 v12, v130, v37
	v_fmac_f32_e32 v13, v131, v37
	v_fmac_f32_e32 v10, v132, v38
	v_fmac_f32_e32 v11, v133, v38
	v_fmac_f32_e32 v8, v130, v38
	v_fmac_f32_e32 v9, v131, v38
	v_fmac_f32_e32 v6, v132, v142
	v_fmac_f32_e32 v7, v133, v142
	v_fmac_f32_e32 v4, v130, v142
	v_fmac_f32_e32 v5, v131, v142
	s_addk_i32 s16, 0x200
	v_mov_b32_e32 v146, v125
	s_waitcnt lgkmcnt(1)
	v_fmac_f32_e32 v18, v136, v98
	v_fmac_f32_e32 v19, v137, v98
	v_fmac_f32_e32 v16, v134, v98
	v_fmac_f32_e32 v17, v135, v98
	v_fmac_f32_e32 v14, v136, v99
	v_fmac_f32_e32 v15, v137, v99
	v_fmac_f32_e32 v12, v134, v99
	v_fmac_f32_e32 v13, v135, v99
	v_fmac_f32_e32 v10, v136, v100
	v_fmac_f32_e32 v11, v137, v100
	v_fmac_f32_e32 v8, v134, v100
	v_fmac_f32_e32 v9, v135, v100
	v_fmac_f32_e32 v6, v136, v144
	v_fmac_f32_e32 v7, v137, v144
	v_fmac_f32_e32 v4, v134, v144
	v_fmac_f32_e32 v5, v135, v144
	v_add_u32_e32 v20, 0x440, v20
	s_cmpk_lg_i32 s16, 0x800
	s_waitcnt lgkmcnt(0)
	v_fmac_f32_e32 v18, v140, v122
	v_fmac_f32_e32 v19, v141, v122
	v_fmac_f32_e32 v16, v138, v122
	v_fmac_f32_e32 v17, v139, v122
	v_fmac_f32_e32 v14, v140, v123
	v_fmac_f32_e32 v15, v141, v123
	v_fmac_f32_e32 v12, v138, v123
	v_fmac_f32_e32 v13, v139, v123
	v_fmac_f32_e32 v10, v140, v124
	v_fmac_f32_e32 v11, v141, v124
	v_fmac_f32_e32 v8, v138, v124
	v_fmac_f32_e32 v9, v139, v124
	v_fmac_f32_e32 v6, v140, v146
	v_fmac_f32_e32 v7, v141, v146
	v_fmac_f32_e32 v4, v138, v146
	v_fmac_f32_e32 v5, v139, v146
	s_cbranch_scc1 .LBB0_668
	s_barrier
	global_load_dwordx4 v[32:35], v[94:95], off offset:1152
	global_load_dwordx4 v[20:23], v[68:69], off
	s_waitcnt vmcnt(3)
	v_cvt_f32_f16_sdwa v130, v28 dst_sel:DWORD dst_unused:UNUSED_PAD src0_sel:WORD_1
	v_cvt_f32_f16_e32 v28, v28
	v_cvt_f32_f16_e32 v131, v29
	v_cvt_f32_f16_sdwa v132, v30 dst_sel:DWORD dst_unused:UNUSED_PAD src0_sel:WORD_1
	v_cvt_f32_f16_e32 v135, v30
	ds_read_b128 v[36:39], v43 offset:14336
	ds_read_b128 v[98:101], v43 offset:14352
	ds_read_b128 v[122:125], v43 offset:18432
	ds_read_b128 v[126:129], v43 offset:18448
	v_cvt_f32_f16_sdwa v97, v29 dst_sel:DWORD dst_unused:UNUSED_PAD src0_sel:WORD_1
	v_cvt_f32_f16_sdwa v133, v31 dst_sel:DWORD dst_unused:UNUSED_PAD src0_sel:WORD_1
	v_cvt_f32_f16_e32 v134, v31
	v_sub_f32_e32 v28, v28, v0
	v_sub_f32_e32 v29, v130, v1
	v_sub_f32_e32 v30, v131, v2
	v_mul_f32_e32 v28, v90, v28
	v_mul_f32_e32 v29, v91, v29
	v_sub_f32_e32 v130, v135, v0
	v_sub_f32_e32 v131, v132, v1
	v_sub_f32_e32 v31, v97, v3
	v_sub_f32_e32 v132, v134, v2
	v_sub_f32_e32 v133, v133, v3
	v_mul_f32_e32 v130, v90, v130
	v_mul_f32_e32 v131, v91, v131
	s_waitcnt lgkmcnt(1)
	v_fma_f32 v28, v36, v28, v122
	v_fma_f32 v29, v37, v29, v123
	v_mul_f32_e32 v30, v92, v30
	v_mul_f32_e32 v31, v93, v31
	v_mul_f32_e32 v132, v92, v132
	v_mul_f32_e32 v133, v93, v133
	s_waitcnt lgkmcnt(0)
	v_fma_f32 v36, v98, v130, v126
	ds_write2_b32 v96, v28, v29 offset1:68
	v_fma_f32 v28, v99, v131, v127
	ds_write2_b32 v44, v36, v28 offset0:16 offset1:84
	v_fma_f32 v28, v38, v30, v124
	v_fma_f32 v29, v100, v132, v128
	v_fmac_f32_e32 v125, v39, v31
	v_fmac_f32_e32 v129, v101, v133
	ds_write2_b32 v96, v28, v125 offset0:136 offset1:204
	ds_write2_b32 v44, v29, v129 offset0:152 offset1:220
	s_waitcnt vmcnt(2)
	ds_write_b128 v104, v[24:27] offset:41984
	s_mov_b32 s16, 0
	v_mov_b32_e32 v24, v112
	s_waitcnt lgkmcnt(0)
	s_barrier
.LBB0_670:
	v_add_u32_e32 v25, s16, v111
	ds_read_b128 v[26:29], v24
	ds_read_b128 v[36:39], v24 offset:272
	ds_read_b128 v[98:101], v24 offset:544
	ds_read_b128 v[122:125], v24 offset:816
	ds_read_b128 v[126:129], v25
	ds_read_b128 v[130:133], v25 offset:128
	ds_read_b128 v[134:137], v25 offset:256
	ds_read_b128 v[138:141], v25 offset:384
	s_waitcnt lgkmcnt(7)
	v_mov_b32_e32 v30, v29
	s_waitcnt lgkmcnt(6)
	v_mov_b32_e32 v142, v39
	s_waitcnt lgkmcnt(3)
	v_fmac_f32_e32 v18, v128, v26
	v_fmac_f32_e32 v19, v129, v26
	v_fmac_f32_e32 v16, v126, v26
	v_fmac_f32_e32 v17, v127, v26
	v_fmac_f32_e32 v14, v128, v27
	v_fmac_f32_e32 v15, v129, v27
	v_fmac_f32_e32 v12, v126, v27
	v_fmac_f32_e32 v13, v127, v27
	v_fmac_f32_e32 v8, v126, v28
	v_fmac_f32_e32 v9, v127, v28
	v_fmac_f32_e32 v10, v128, v28
	v_fmac_f32_e32 v11, v129, v28
	v_fmac_f32_e32 v4, v126, v30
	v_fmac_f32_e32 v5, v127, v30
	v_fmac_f32_e32 v6, v128, v30
	v_fmac_f32_e32 v7, v129, v30
	v_mov_b32_e32 v144, v101
	s_waitcnt lgkmcnt(2)
	v_fmac_f32_e32 v18, v132, v36
	v_fmac_f32_e32 v19, v133, v36
	v_fmac_f32_e32 v16, v130, v36
	v_fmac_f32_e32 v17, v131, v36
	v_fmac_f32_e32 v14, v132, v37
	v_fmac_f32_e32 v15, v133, v37
	v_fmac_f32_e32 v12, v130, v37
	v_fmac_f32_e32 v13, v131, v37
	v_fmac_f32_e32 v10, v132, v38
	v_fmac_f32_e32 v11, v133, v38
	v_fmac_f32_e32 v8, v130, v38
	v_fmac_f32_e32 v9, v131, v38
	v_fmac_f32_e32 v6, v132, v142
	v_fmac_f32_e32 v7, v133, v142
	v_fmac_f32_e32 v4, v130, v142
	v_fmac_f32_e32 v5, v131, v142
	s_addk_i32 s16, 0x200
	v_mov_b32_e32 v146, v125
	s_waitcnt lgkmcnt(1)
	v_fmac_f32_e32 v18, v136, v98
	v_fmac_f32_e32 v19, v137, v98
	v_fmac_f32_e32 v16, v134, v98
	v_fmac_f32_e32 v17, v135, v98
	v_fmac_f32_e32 v14, v136, v99
	v_fmac_f32_e32 v15, v137, v99
	v_fmac_f32_e32 v12, v134, v99
	v_fmac_f32_e32 v13, v135, v99
	v_fmac_f32_e32 v10, v136, v100
	v_fmac_f32_e32 v11, v137, v100
	v_fmac_f32_e32 v8, v134, v100
	v_fmac_f32_e32 v9, v135, v100
	v_fmac_f32_e32 v6, v136, v144
	v_fmac_f32_e32 v7, v137, v144
	v_fmac_f32_e32 v4, v134, v144
	v_fmac_f32_e32 v5, v135, v144
	v_add_u32_e32 v24, 0x440, v24
	s_cmpk_lg_i32 s16, 0x800
	s_waitcnt lgkmcnt(0)
	v_fmac_f32_e32 v18, v140, v122
	v_fmac_f32_e32 v19, v141, v122
	v_fmac_f32_e32 v16, v138, v122
	v_fmac_f32_e32 v17, v139, v122
	v_fmac_f32_e32 v14, v140, v123
	v_fmac_f32_e32 v15, v141, v123
	v_fmac_f32_e32 v12, v138, v123
	v_fmac_f32_e32 v13, v139, v123
	v_fmac_f32_e32 v10, v140, v124
	v_fmac_f32_e32 v11, v141, v124
	v_fmac_f32_e32 v8, v138, v124
	v_fmac_f32_e32 v9, v139, v124
	v_fmac_f32_e32 v6, v140, v146
	v_fmac_f32_e32 v7, v141, v146
	v_fmac_f32_e32 v4, v138, v146
	v_fmac_f32_e32 v5, v139, v146
	s_cbranch_scc1 .LBB0_670
	s_barrier
	global_load_dwordx4 v[28:31], v[94:95], off offset:1280
	global_load_dwordx4 v[24:27], v[70:71], off
	s_waitcnt vmcnt(3)
	v_cvt_f32_f16_sdwa v130, v32 dst_sel:DWORD dst_unused:UNUSED_PAD src0_sel:WORD_1
	v_cvt_f32_f16_e32 v32, v32
	v_cvt_f32_f16_e32 v131, v33
	v_cvt_f32_f16_sdwa v132, v34 dst_sel:DWORD dst_unused:UNUSED_PAD src0_sel:WORD_1
	v_cvt_f32_f16_e32 v135, v34
	ds_read_b128 v[36:39], v43 offset:14592
	ds_read_b128 v[98:101], v43 offset:14608
	ds_read_b128 v[122:125], v43 offset:18688
	ds_read_b128 v[126:129], v43 offset:18704
	v_cvt_f32_f16_sdwa v97, v33 dst_sel:DWORD dst_unused:UNUSED_PAD src0_sel:WORD_1
	v_cvt_f32_f16_sdwa v133, v35 dst_sel:DWORD dst_unused:UNUSED_PAD src0_sel:WORD_1
	v_cvt_f32_f16_e32 v134, v35
	v_sub_f32_e32 v32, v32, v0
	v_sub_f32_e32 v33, v130, v1
	v_sub_f32_e32 v34, v131, v2
	v_mul_f32_e32 v32, v90, v32
	v_mul_f32_e32 v33, v91, v33
	v_sub_f32_e32 v130, v135, v0
	v_sub_f32_e32 v131, v132, v1
	v_sub_f32_e32 v35, v97, v3
	v_sub_f32_e32 v132, v134, v2
	v_sub_f32_e32 v133, v133, v3
	v_mul_f32_e32 v130, v90, v130
	v_mul_f32_e32 v131, v91, v131
	s_waitcnt lgkmcnt(1)
	v_fma_f32 v32, v36, v32, v122
	v_fma_f32 v33, v37, v33, v123
	v_mul_f32_e32 v34, v92, v34
	v_mul_f32_e32 v35, v93, v35
	v_mul_f32_e32 v132, v92, v132
	v_mul_f32_e32 v133, v93, v133
	s_waitcnt lgkmcnt(0)
	v_fma_f32 v36, v98, v130, v126
	ds_write2_b32 v96, v32, v33 offset1:68
	v_fma_f32 v32, v99, v131, v127
	ds_write2_b32 v44, v36, v32 offset0:16 offset1:84
	v_fma_f32 v32, v38, v34, v124
	v_fma_f32 v33, v100, v132, v128
	v_fmac_f32_e32 v125, v39, v35
	v_fmac_f32_e32 v129, v101, v133
	ds_write2_b32 v96, v32, v125 offset0:136 offset1:204
	ds_write2_b32 v44, v33, v129 offset0:152 offset1:220
	s_waitcnt vmcnt(2)
	ds_write_b128 v104, v[20:23] offset:41984
	s_mov_b32 s16, 0
	v_mov_b32_e32 v20, v112
	s_waitcnt lgkmcnt(0)
	s_barrier
.LBB0_672:
	v_add_u32_e32 v21, s16, v111
	ds_read_b128 v[32:35], v20
	ds_read_b128 v[36:39], v20 offset:272
	ds_read_b128 v[98:101], v20 offset:544
	ds_read_b128 v[122:125], v20 offset:816
	ds_read_b128 v[126:129], v21
	ds_read_b128 v[130:133], v21 offset:128
	ds_read_b128 v[134:137], v21 offset:256
	ds_read_b128 v[138:141], v21 offset:384
	s_waitcnt lgkmcnt(7)
	v_mov_b32_e32 v22, v35
	s_waitcnt lgkmcnt(6)
	v_mov_b32_e32 v142, v39
	s_waitcnt lgkmcnt(3)
	v_fmac_f32_e32 v18, v128, v32
	v_fmac_f32_e32 v19, v129, v32
	v_fmac_f32_e32 v16, v126, v32
	v_fmac_f32_e32 v17, v127, v32
	v_fmac_f32_e32 v14, v128, v33
	v_fmac_f32_e32 v15, v129, v33
	v_fmac_f32_e32 v12, v126, v33
	v_fmac_f32_e32 v13, v127, v33
	v_fmac_f32_e32 v8, v126, v34
	v_fmac_f32_e32 v9, v127, v34
	v_fmac_f32_e32 v10, v128, v34
	v_fmac_f32_e32 v11, v129, v34
	v_fmac_f32_e32 v4, v126, v22
	v_fmac_f32_e32 v5, v127, v22
	v_fmac_f32_e32 v6, v128, v22
	v_fmac_f32_e32 v7, v129, v22
	v_mov_b32_e32 v144, v101
	s_waitcnt lgkmcnt(2)
	v_fmac_f32_e32 v18, v132, v36
	v_fmac_f32_e32 v19, v133, v36
	v_fmac_f32_e32 v16, v130, v36
	v_fmac_f32_e32 v17, v131, v36
	v_fmac_f32_e32 v14, v132, v37
	v_fmac_f32_e32 v15, v133, v37
	v_fmac_f32_e32 v12, v130, v37
	v_fmac_f32_e32 v13, v131, v37
	v_fmac_f32_e32 v10, v132, v38
	v_fmac_f32_e32 v11, v133, v38
	v_fmac_f32_e32 v8, v130, v38
	v_fmac_f32_e32 v9, v131, v38
	v_fmac_f32_e32 v6, v132, v142
	v_fmac_f32_e32 v7, v133, v142
	v_fmac_f32_e32 v4, v130, v142
	v_fmac_f32_e32 v5, v131, v142
	s_addk_i32 s16, 0x200
	v_mov_b32_e32 v146, v125
	s_waitcnt lgkmcnt(1)
	v_fmac_f32_e32 v18, v136, v98
	v_fmac_f32_e32 v19, v137, v98
	v_fmac_f32_e32 v16, v134, v98
	v_fmac_f32_e32 v17, v135, v98
	v_fmac_f32_e32 v14, v136, v99
	v_fmac_f32_e32 v15, v137, v99
	v_fmac_f32_e32 v12, v134, v99
	v_fmac_f32_e32 v13, v135, v99
	v_fmac_f32_e32 v10, v136, v100
	v_fmac_f32_e32 v11, v137, v100
	v_fmac_f32_e32 v8, v134, v100
	v_fmac_f32_e32 v9, v135, v100
	v_fmac_f32_e32 v6, v136, v144
	v_fmac_f32_e32 v7, v137, v144
	v_fmac_f32_e32 v4, v134, v144
	v_fmac_f32_e32 v5, v135, v144
	v_add_u32_e32 v20, 0x440, v20
	s_cmpk_lg_i32 s16, 0x800
	s_waitcnt lgkmcnt(0)
	v_fmac_f32_e32 v18, v140, v122
	v_fmac_f32_e32 v19, v141, v122
	v_fmac_f32_e32 v16, v138, v122
	v_fmac_f32_e32 v17, v139, v122
	v_fmac_f32_e32 v14, v140, v123
	v_fmac_f32_e32 v15, v141, v123
	v_fmac_f32_e32 v12, v138, v123
	v_fmac_f32_e32 v13, v139, v123
	v_fmac_f32_e32 v10, v140, v124
	v_fmac_f32_e32 v11, v141, v124
	v_fmac_f32_e32 v8, v138, v124
	v_fmac_f32_e32 v9, v139, v124
	v_fmac_f32_e32 v6, v140, v146
	v_fmac_f32_e32 v7, v141, v146
	v_fmac_f32_e32 v4, v138, v146
	v_fmac_f32_e32 v5, v139, v146
	s_cbranch_scc1 .LBB0_672
	s_barrier
	global_load_dwordx4 v[32:35], v[94:95], off offset:1408
	global_load_dwordx4 v[20:23], v[72:73], off
	s_waitcnt vmcnt(3)
	v_cvt_f32_f16_sdwa v130, v28 dst_sel:DWORD dst_unused:UNUSED_PAD src0_sel:WORD_1
	v_cvt_f32_f16_e32 v28, v28
	v_cvt_f32_f16_e32 v131, v29
	v_cvt_f32_f16_sdwa v132, v30 dst_sel:DWORD dst_unused:UNUSED_PAD src0_sel:WORD_1
	v_cvt_f32_f16_e32 v135, v30
	ds_read_b128 v[36:39], v43 offset:14848
	ds_read_b128 v[98:101], v43 offset:14864
	ds_read_b128 v[122:125], v43 offset:18944
	ds_read_b128 v[126:129], v43 offset:18960
	v_cvt_f32_f16_sdwa v97, v29 dst_sel:DWORD dst_unused:UNUSED_PAD src0_sel:WORD_1
	v_cvt_f32_f16_sdwa v133, v31 dst_sel:DWORD dst_unused:UNUSED_PAD src0_sel:WORD_1
	v_cvt_f32_f16_e32 v134, v31
	v_sub_f32_e32 v28, v28, v0
	v_sub_f32_e32 v29, v130, v1
	v_sub_f32_e32 v30, v131, v2
	v_mul_f32_e32 v28, v90, v28
	v_mul_f32_e32 v29, v91, v29
	v_sub_f32_e32 v130, v135, v0
	v_sub_f32_e32 v131, v132, v1
	v_sub_f32_e32 v31, v97, v3
	v_sub_f32_e32 v132, v134, v2
	v_sub_f32_e32 v133, v133, v3
	v_mul_f32_e32 v130, v90, v130
	v_mul_f32_e32 v131, v91, v131
	s_waitcnt lgkmcnt(1)
	v_fma_f32 v28, v36, v28, v122
	v_fma_f32 v29, v37, v29, v123
	v_mul_f32_e32 v30, v92, v30
	v_mul_f32_e32 v31, v93, v31
	v_mul_f32_e32 v132, v92, v132
	v_mul_f32_e32 v133, v93, v133
	s_waitcnt lgkmcnt(0)
	v_fma_f32 v36, v98, v130, v126
	ds_write2_b32 v96, v28, v29 offset1:68
	v_fma_f32 v28, v99, v131, v127
	ds_write2_b32 v44, v36, v28 offset0:16 offset1:84
	v_fma_f32 v28, v38, v30, v124
	v_fma_f32 v29, v100, v132, v128
	v_fmac_f32_e32 v125, v39, v31
	v_fmac_f32_e32 v129, v101, v133
	ds_write2_b32 v96, v28, v125 offset0:136 offset1:204
	ds_write2_b32 v44, v29, v129 offset0:152 offset1:220
	s_waitcnt vmcnt(2)
	ds_write_b128 v104, v[24:27] offset:41984
	s_mov_b32 s16, 0
	v_mov_b32_e32 v24, v112
	s_waitcnt lgkmcnt(0)
	s_barrier
.LBB0_674:
	v_add_u32_e32 v25, s16, v111
	ds_read_b128 v[26:29], v24
	ds_read_b128 v[36:39], v24 offset:272
	ds_read_b128 v[98:101], v24 offset:544
	ds_read_b128 v[122:125], v24 offset:816
	ds_read_b128 v[126:129], v25
	ds_read_b128 v[130:133], v25 offset:128
	ds_read_b128 v[134:137], v25 offset:256
	ds_read_b128 v[138:141], v25 offset:384
	s_waitcnt lgkmcnt(7)
	v_mov_b32_e32 v30, v29
	s_waitcnt lgkmcnt(6)
	v_mov_b32_e32 v142, v39
	s_waitcnt lgkmcnt(3)
	v_fmac_f32_e32 v18, v128, v26
	v_fmac_f32_e32 v19, v129, v26
	v_fmac_f32_e32 v16, v126, v26
	v_fmac_f32_e32 v17, v127, v26
	v_fmac_f32_e32 v14, v128, v27
	v_fmac_f32_e32 v15, v129, v27
	v_fmac_f32_e32 v12, v126, v27
	v_fmac_f32_e32 v13, v127, v27
	v_fmac_f32_e32 v8, v126, v28
	v_fmac_f32_e32 v9, v127, v28
	v_fmac_f32_e32 v10, v128, v28
	v_fmac_f32_e32 v11, v129, v28
	v_fmac_f32_e32 v4, v126, v30
	v_fmac_f32_e32 v5, v127, v30
	v_fmac_f32_e32 v6, v128, v30
	v_fmac_f32_e32 v7, v129, v30
	v_mov_b32_e32 v144, v101
	s_waitcnt lgkmcnt(2)
	v_fmac_f32_e32 v18, v132, v36
	v_fmac_f32_e32 v19, v133, v36
	v_fmac_f32_e32 v16, v130, v36
	v_fmac_f32_e32 v17, v131, v36
	v_fmac_f32_e32 v14, v132, v37
	v_fmac_f32_e32 v15, v133, v37
	v_fmac_f32_e32 v12, v130, v37
	v_fmac_f32_e32 v13, v131, v37
	v_fmac_f32_e32 v10, v132, v38
	v_fmac_f32_e32 v11, v133, v38
	v_fmac_f32_e32 v8, v130, v38
	v_fmac_f32_e32 v9, v131, v38
	v_fmac_f32_e32 v6, v132, v142
	v_fmac_f32_e32 v7, v133, v142
	v_fmac_f32_e32 v4, v130, v142
	v_fmac_f32_e32 v5, v131, v142
	s_addk_i32 s16, 0x200
	v_mov_b32_e32 v146, v125
	s_waitcnt lgkmcnt(1)
	v_fmac_f32_e32 v18, v136, v98
	v_fmac_f32_e32 v19, v137, v98
	v_fmac_f32_e32 v16, v134, v98
	v_fmac_f32_e32 v17, v135, v98
	v_fmac_f32_e32 v14, v136, v99
	v_fmac_f32_e32 v15, v137, v99
	v_fmac_f32_e32 v12, v134, v99
	v_fmac_f32_e32 v13, v135, v99
	v_fmac_f32_e32 v10, v136, v100
	v_fmac_f32_e32 v11, v137, v100
	v_fmac_f32_e32 v8, v134, v100
	v_fmac_f32_e32 v9, v135, v100
	v_fmac_f32_e32 v6, v136, v144
	v_fmac_f32_e32 v7, v137, v144
	v_fmac_f32_e32 v4, v134, v144
	v_fmac_f32_e32 v5, v135, v144
	v_add_u32_e32 v24, 0x440, v24
	s_cmpk_lg_i32 s16, 0x800
	s_waitcnt lgkmcnt(0)
	v_fmac_f32_e32 v18, v140, v122
	v_fmac_f32_e32 v19, v141, v122
	v_fmac_f32_e32 v16, v138, v122
	v_fmac_f32_e32 v17, v139, v122
	v_fmac_f32_e32 v14, v140, v123
	v_fmac_f32_e32 v15, v141, v123
	v_fmac_f32_e32 v12, v138, v123
	v_fmac_f32_e32 v13, v139, v123
	v_fmac_f32_e32 v10, v140, v124
	v_fmac_f32_e32 v11, v141, v124
	v_fmac_f32_e32 v8, v138, v124
	v_fmac_f32_e32 v9, v139, v124
	v_fmac_f32_e32 v6, v140, v146
	v_fmac_f32_e32 v7, v141, v146
	v_fmac_f32_e32 v4, v138, v146
	v_fmac_f32_e32 v5, v139, v146
	s_cbranch_scc1 .LBB0_674
	s_barrier
	global_load_dwordx4 v[28:31], v[94:95], off offset:1536
	global_load_dwordx4 v[24:27], v[74:75], off
	s_waitcnt vmcnt(3)
	v_cvt_f32_f16_sdwa v130, v32 dst_sel:DWORD dst_unused:UNUSED_PAD src0_sel:WORD_1
	v_cvt_f32_f16_e32 v32, v32
	v_cvt_f32_f16_e32 v131, v33
	v_cvt_f32_f16_sdwa v132, v34 dst_sel:DWORD dst_unused:UNUSED_PAD src0_sel:WORD_1
	v_cvt_f32_f16_e32 v135, v34
	ds_read_b128 v[36:39], v43 offset:15104
	ds_read_b128 v[98:101], v43 offset:15120
	ds_read_b128 v[122:125], v43 offset:19200
	ds_read_b128 v[126:129], v43 offset:19216
	v_cvt_f32_f16_sdwa v97, v33 dst_sel:DWORD dst_unused:UNUSED_PAD src0_sel:WORD_1
	v_cvt_f32_f16_sdwa v133, v35 dst_sel:DWORD dst_unused:UNUSED_PAD src0_sel:WORD_1
	v_cvt_f32_f16_e32 v134, v35
	v_sub_f32_e32 v32, v32, v0
	v_sub_f32_e32 v33, v130, v1
	v_sub_f32_e32 v34, v131, v2
	v_mul_f32_e32 v32, v90, v32
	v_mul_f32_e32 v33, v91, v33
	v_sub_f32_e32 v130, v135, v0
	v_sub_f32_e32 v131, v132, v1
	v_sub_f32_e32 v35, v97, v3
	v_sub_f32_e32 v132, v134, v2
	v_sub_f32_e32 v133, v133, v3
	v_mul_f32_e32 v130, v90, v130
	v_mul_f32_e32 v131, v91, v131
	s_waitcnt lgkmcnt(1)
	v_fma_f32 v32, v36, v32, v122
	v_fma_f32 v33, v37, v33, v123
	v_mul_f32_e32 v34, v92, v34
	v_mul_f32_e32 v35, v93, v35
	v_mul_f32_e32 v132, v92, v132
	v_mul_f32_e32 v133, v93, v133
	s_waitcnt lgkmcnt(0)
	v_fma_f32 v36, v98, v130, v126
	ds_write2_b32 v96, v32, v33 offset1:68
	v_fma_f32 v32, v99, v131, v127
	ds_write2_b32 v44, v36, v32 offset0:16 offset1:84
	v_fma_f32 v32, v38, v34, v124
	v_fma_f32 v33, v100, v132, v128
	v_fmac_f32_e32 v125, v39, v35
	v_fmac_f32_e32 v129, v101, v133
	ds_write2_b32 v96, v32, v125 offset0:136 offset1:204
	ds_write2_b32 v44, v33, v129 offset0:152 offset1:220
	s_waitcnt vmcnt(2)
	ds_write_b128 v104, v[20:23] offset:41984
	s_mov_b32 s16, 0
	v_mov_b32_e32 v20, v112
	s_waitcnt lgkmcnt(0)
	s_barrier
.LBB0_676:
	v_add_u32_e32 v21, s16, v111
	ds_read_b128 v[32:35], v20
	ds_read_b128 v[36:39], v20 offset:272
	ds_read_b128 v[98:101], v20 offset:544
	ds_read_b128 v[122:125], v20 offset:816
	ds_read_b128 v[126:129], v21
	ds_read_b128 v[130:133], v21 offset:128
	ds_read_b128 v[134:137], v21 offset:256
	ds_read_b128 v[138:141], v21 offset:384
	s_waitcnt lgkmcnt(7)
	v_mov_b32_e32 v22, v35
	s_waitcnt lgkmcnt(6)
	v_mov_b32_e32 v142, v39
	s_waitcnt lgkmcnt(3)
	v_fmac_f32_e32 v18, v128, v32
	v_fmac_f32_e32 v19, v129, v32
	v_fmac_f32_e32 v16, v126, v32
	v_fmac_f32_e32 v17, v127, v32
	v_fmac_f32_e32 v14, v128, v33
	v_fmac_f32_e32 v15, v129, v33
	v_fmac_f32_e32 v12, v126, v33
	v_fmac_f32_e32 v13, v127, v33
	v_fmac_f32_e32 v8, v126, v34
	v_fmac_f32_e32 v9, v127, v34
	v_fmac_f32_e32 v10, v128, v34
	v_fmac_f32_e32 v11, v129, v34
	v_fmac_f32_e32 v4, v126, v22
	v_fmac_f32_e32 v5, v127, v22
	v_fmac_f32_e32 v6, v128, v22
	v_fmac_f32_e32 v7, v129, v22
	v_mov_b32_e32 v144, v101
	s_waitcnt lgkmcnt(2)
	v_fmac_f32_e32 v18, v132, v36
	v_fmac_f32_e32 v19, v133, v36
	v_fmac_f32_e32 v16, v130, v36
	v_fmac_f32_e32 v17, v131, v36
	v_fmac_f32_e32 v14, v132, v37
	v_fmac_f32_e32 v15, v133, v37
	v_fmac_f32_e32 v12, v130, v37
	v_fmac_f32_e32 v13, v131, v37
	v_fmac_f32_e32 v10, v132, v38
	v_fmac_f32_e32 v11, v133, v38
	v_fmac_f32_e32 v8, v130, v38
	v_fmac_f32_e32 v9, v131, v38
	v_fmac_f32_e32 v6, v132, v142
	v_fmac_f32_e32 v7, v133, v142
	v_fmac_f32_e32 v4, v130, v142
	v_fmac_f32_e32 v5, v131, v142
	s_addk_i32 s16, 0x200
	v_mov_b32_e32 v146, v125
	s_waitcnt lgkmcnt(1)
	v_fmac_f32_e32 v18, v136, v98
	v_fmac_f32_e32 v19, v137, v98
	v_fmac_f32_e32 v16, v134, v98
	v_fmac_f32_e32 v17, v135, v98
	v_fmac_f32_e32 v14, v136, v99
	v_fmac_f32_e32 v15, v137, v99
	v_fmac_f32_e32 v12, v134, v99
	v_fmac_f32_e32 v13, v135, v99
	v_fmac_f32_e32 v10, v136, v100
	v_fmac_f32_e32 v11, v137, v100
	v_fmac_f32_e32 v8, v134, v100
	v_fmac_f32_e32 v9, v135, v100
	v_fmac_f32_e32 v6, v136, v144
	v_fmac_f32_e32 v7, v137, v144
	v_fmac_f32_e32 v4, v134, v144
	v_fmac_f32_e32 v5, v135, v144
	v_add_u32_e32 v20, 0x440, v20
	s_cmpk_lg_i32 s16, 0x800
	s_waitcnt lgkmcnt(0)
	v_fmac_f32_e32 v18, v140, v122
	v_fmac_f32_e32 v19, v141, v122
	v_fmac_f32_e32 v16, v138, v122
	v_fmac_f32_e32 v17, v139, v122
	v_fmac_f32_e32 v14, v140, v123
	v_fmac_f32_e32 v15, v141, v123
	v_fmac_f32_e32 v12, v138, v123
	v_fmac_f32_e32 v13, v139, v123
	v_fmac_f32_e32 v10, v140, v124
	v_fmac_f32_e32 v11, v141, v124
	v_fmac_f32_e32 v8, v138, v124
	v_fmac_f32_e32 v9, v139, v124
	v_fmac_f32_e32 v6, v140, v146
	v_fmac_f32_e32 v7, v141, v146
	v_fmac_f32_e32 v4, v138, v146
	v_fmac_f32_e32 v5, v139, v146
	s_cbranch_scc1 .LBB0_676
	s_barrier
	global_load_dwordx4 v[32:35], v[94:95], off offset:1664
	global_load_dwordx4 v[20:23], v[76:77], off
	s_waitcnt vmcnt(3)
	v_cvt_f32_f16_sdwa v130, v28 dst_sel:DWORD dst_unused:UNUSED_PAD src0_sel:WORD_1
	v_cvt_f32_f16_e32 v28, v28
	v_cvt_f32_f16_e32 v131, v29
	v_cvt_f32_f16_sdwa v132, v30 dst_sel:DWORD dst_unused:UNUSED_PAD src0_sel:WORD_1
	v_cvt_f32_f16_e32 v135, v30
	ds_read_b128 v[36:39], v43 offset:15360
	ds_read_b128 v[98:101], v43 offset:15376
	ds_read_b128 v[122:125], v43 offset:19456
	ds_read_b128 v[126:129], v43 offset:19472
	v_cvt_f32_f16_sdwa v97, v29 dst_sel:DWORD dst_unused:UNUSED_PAD src0_sel:WORD_1
	v_cvt_f32_f16_sdwa v133, v31 dst_sel:DWORD dst_unused:UNUSED_PAD src0_sel:WORD_1
	v_cvt_f32_f16_e32 v134, v31
	v_sub_f32_e32 v28, v28, v0
	v_sub_f32_e32 v29, v130, v1
	v_sub_f32_e32 v30, v131, v2
	v_mul_f32_e32 v28, v90, v28
	v_mul_f32_e32 v29, v91, v29
	v_sub_f32_e32 v130, v135, v0
	v_sub_f32_e32 v131, v132, v1
	v_sub_f32_e32 v31, v97, v3
	v_sub_f32_e32 v132, v134, v2
	v_sub_f32_e32 v133, v133, v3
	v_mul_f32_e32 v130, v90, v130
	v_mul_f32_e32 v131, v91, v131
	s_waitcnt lgkmcnt(1)
	v_fma_f32 v28, v36, v28, v122
	v_fma_f32 v29, v37, v29, v123
	v_mul_f32_e32 v30, v92, v30
	v_mul_f32_e32 v31, v93, v31
	v_mul_f32_e32 v132, v92, v132
	v_mul_f32_e32 v133, v93, v133
	s_waitcnt lgkmcnt(0)
	v_fma_f32 v36, v98, v130, v126
	ds_write2_b32 v96, v28, v29 offset1:68
	v_fma_f32 v28, v99, v131, v127
	ds_write2_b32 v44, v36, v28 offset0:16 offset1:84
	v_fma_f32 v28, v38, v30, v124
	v_fma_f32 v29, v100, v132, v128
	v_fmac_f32_e32 v125, v39, v31
	v_fmac_f32_e32 v129, v101, v133
	ds_write2_b32 v96, v28, v125 offset0:136 offset1:204
	ds_write2_b32 v44, v29, v129 offset0:152 offset1:220
	s_waitcnt vmcnt(2)
	ds_write_b128 v104, v[24:27] offset:41984
	s_mov_b32 s16, 0
	v_mov_b32_e32 v24, v112
	s_waitcnt lgkmcnt(0)
	s_barrier
.LBB0_678:
	v_add_u32_e32 v25, s16, v111
	ds_read_b128 v[26:29], v24
	ds_read_b128 v[36:39], v24 offset:272
	ds_read_b128 v[98:101], v24 offset:544
	ds_read_b128 v[122:125], v24 offset:816
	ds_read_b128 v[126:129], v25
	ds_read_b128 v[130:133], v25 offset:128
	ds_read_b128 v[134:137], v25 offset:256
	ds_read_b128 v[138:141], v25 offset:384
	s_waitcnt lgkmcnt(7)
	v_mov_b32_e32 v30, v29
	s_waitcnt lgkmcnt(6)
	v_mov_b32_e32 v142, v39
	s_waitcnt lgkmcnt(3)
	v_fmac_f32_e32 v18, v128, v26
	v_fmac_f32_e32 v19, v129, v26
	v_fmac_f32_e32 v16, v126, v26
	v_fmac_f32_e32 v17, v127, v26
	v_fmac_f32_e32 v14, v128, v27
	v_fmac_f32_e32 v15, v129, v27
	v_fmac_f32_e32 v12, v126, v27
	v_fmac_f32_e32 v13, v127, v27
	v_fmac_f32_e32 v8, v126, v28
	v_fmac_f32_e32 v9, v127, v28
	v_fmac_f32_e32 v10, v128, v28
	v_fmac_f32_e32 v11, v129, v28
	v_fmac_f32_e32 v4, v126, v30
	v_fmac_f32_e32 v5, v127, v30
	v_fmac_f32_e32 v6, v128, v30
	v_fmac_f32_e32 v7, v129, v30
	v_mov_b32_e32 v144, v101
	s_waitcnt lgkmcnt(2)
	v_fmac_f32_e32 v18, v132, v36
	v_fmac_f32_e32 v19, v133, v36
	v_fmac_f32_e32 v16, v130, v36
	v_fmac_f32_e32 v17, v131, v36
	v_fmac_f32_e32 v14, v132, v37
	v_fmac_f32_e32 v15, v133, v37
	v_fmac_f32_e32 v12, v130, v37
	v_fmac_f32_e32 v13, v131, v37
	v_fmac_f32_e32 v10, v132, v38
	v_fmac_f32_e32 v11, v133, v38
	v_fmac_f32_e32 v8, v130, v38
	v_fmac_f32_e32 v9, v131, v38
	v_fmac_f32_e32 v6, v132, v142
	v_fmac_f32_e32 v7, v133, v142
	v_fmac_f32_e32 v4, v130, v142
	v_fmac_f32_e32 v5, v131, v142
	s_addk_i32 s16, 0x200
	v_mov_b32_e32 v146, v125
	s_waitcnt lgkmcnt(1)
	v_fmac_f32_e32 v18, v136, v98
	v_fmac_f32_e32 v19, v137, v98
	v_fmac_f32_e32 v16, v134, v98
	v_fmac_f32_e32 v17, v135, v98
	v_fmac_f32_e32 v14, v136, v99
	v_fmac_f32_e32 v15, v137, v99
	v_fmac_f32_e32 v12, v134, v99
	v_fmac_f32_e32 v13, v135, v99
	v_fmac_f32_e32 v10, v136, v100
	v_fmac_f32_e32 v11, v137, v100
	v_fmac_f32_e32 v8, v134, v100
	v_fmac_f32_e32 v9, v135, v100
	v_fmac_f32_e32 v6, v136, v144
	v_fmac_f32_e32 v7, v137, v144
	v_fmac_f32_e32 v4, v134, v144
	v_fmac_f32_e32 v5, v135, v144
	v_add_u32_e32 v24, 0x440, v24
	s_cmpk_lg_i32 s16, 0x800
	s_waitcnt lgkmcnt(0)
	v_fmac_f32_e32 v18, v140, v122
	v_fmac_f32_e32 v19, v141, v122
	v_fmac_f32_e32 v16, v138, v122
	v_fmac_f32_e32 v17, v139, v122
	v_fmac_f32_e32 v14, v140, v123
	v_fmac_f32_e32 v15, v141, v123
	v_fmac_f32_e32 v12, v138, v123
	v_fmac_f32_e32 v13, v139, v123
	v_fmac_f32_e32 v10, v140, v124
	v_fmac_f32_e32 v11, v141, v124
	v_fmac_f32_e32 v8, v138, v124
	v_fmac_f32_e32 v9, v139, v124
	v_fmac_f32_e32 v6, v140, v146
	v_fmac_f32_e32 v7, v141, v146
	v_fmac_f32_e32 v4, v138, v146
	v_fmac_f32_e32 v5, v139, v146
	s_cbranch_scc1 .LBB0_678
	s_barrier
	global_load_dwordx4 v[28:31], v[94:95], off offset:1792
	global_load_dwordx4 v[24:27], v[78:79], off
	s_waitcnt vmcnt(3)
	v_cvt_f32_f16_sdwa v130, v32 dst_sel:DWORD dst_unused:UNUSED_PAD src0_sel:WORD_1
	v_cvt_f32_f16_e32 v32, v32
	v_cvt_f32_f16_e32 v131, v33
	v_cvt_f32_f16_sdwa v132, v34 dst_sel:DWORD dst_unused:UNUSED_PAD src0_sel:WORD_1
	v_cvt_f32_f16_e32 v135, v34
	ds_read_b128 v[36:39], v43 offset:15616
	ds_read_b128 v[98:101], v43 offset:15632
	ds_read_b128 v[122:125], v43 offset:19712
	ds_read_b128 v[126:129], v43 offset:19728
	v_cvt_f32_f16_sdwa v97, v33 dst_sel:DWORD dst_unused:UNUSED_PAD src0_sel:WORD_1
	v_cvt_f32_f16_sdwa v133, v35 dst_sel:DWORD dst_unused:UNUSED_PAD src0_sel:WORD_1
	v_cvt_f32_f16_e32 v134, v35
	v_sub_f32_e32 v32, v32, v0
	v_sub_f32_e32 v33, v130, v1
	v_sub_f32_e32 v34, v131, v2
	v_mul_f32_e32 v32, v90, v32
	v_mul_f32_e32 v33, v91, v33
	v_sub_f32_e32 v130, v135, v0
	v_sub_f32_e32 v131, v132, v1
	v_sub_f32_e32 v35, v97, v3
	v_sub_f32_e32 v132, v134, v2
	v_sub_f32_e32 v133, v133, v3
	v_mul_f32_e32 v130, v90, v130
	v_mul_f32_e32 v131, v91, v131
	s_waitcnt lgkmcnt(1)
	v_fma_f32 v32, v36, v32, v122
	v_fma_f32 v33, v37, v33, v123
	v_mul_f32_e32 v34, v92, v34
	v_mul_f32_e32 v35, v93, v35
	v_mul_f32_e32 v132, v92, v132
	v_mul_f32_e32 v133, v93, v133
	s_waitcnt lgkmcnt(0)
	v_fma_f32 v36, v98, v130, v126
	ds_write2_b32 v96, v32, v33 offset1:68
	v_fma_f32 v32, v99, v131, v127
	ds_write2_b32 v44, v36, v32 offset0:16 offset1:84
	v_fma_f32 v32, v38, v34, v124
	v_fma_f32 v33, v100, v132, v128
	v_fmac_f32_e32 v125, v39, v35
	v_fmac_f32_e32 v129, v101, v133
	ds_write2_b32 v96, v32, v125 offset0:136 offset1:204
	ds_write2_b32 v44, v33, v129 offset0:152 offset1:220
	s_waitcnt vmcnt(2)
	ds_write_b128 v104, v[20:23] offset:41984
	s_mov_b32 s16, 0
	v_mov_b32_e32 v20, v112
	s_waitcnt lgkmcnt(0)
	s_barrier
.LBB0_680:
	v_add_u32_e32 v21, s16, v111
	ds_read_b128 v[32:35], v20
	ds_read_b128 v[36:39], v20 offset:272
	ds_read_b128 v[98:101], v20 offset:544
	ds_read_b128 v[122:125], v20 offset:816
	ds_read_b128 v[126:129], v21
	ds_read_b128 v[130:133], v21 offset:128
	ds_read_b128 v[134:137], v21 offset:256
	ds_read_b128 v[138:141], v21 offset:384
	s_waitcnt lgkmcnt(7)
	v_mov_b32_e32 v22, v35
	s_waitcnt lgkmcnt(6)
	v_mov_b32_e32 v142, v39
	s_waitcnt lgkmcnt(3)
	v_fmac_f32_e32 v18, v128, v32
	v_fmac_f32_e32 v19, v129, v32
	v_fmac_f32_e32 v16, v126, v32
	v_fmac_f32_e32 v17, v127, v32
	v_fmac_f32_e32 v14, v128, v33
	v_fmac_f32_e32 v15, v129, v33
	v_fmac_f32_e32 v12, v126, v33
	v_fmac_f32_e32 v13, v127, v33
	v_fmac_f32_e32 v8, v126, v34
	v_fmac_f32_e32 v9, v127, v34
	v_fmac_f32_e32 v10, v128, v34
	v_fmac_f32_e32 v11, v129, v34
	v_fmac_f32_e32 v4, v126, v22
	v_fmac_f32_e32 v5, v127, v22
	v_fmac_f32_e32 v6, v128, v22
	v_fmac_f32_e32 v7, v129, v22
	v_mov_b32_e32 v144, v101
	s_waitcnt lgkmcnt(2)
	v_fmac_f32_e32 v18, v132, v36
	v_fmac_f32_e32 v19, v133, v36
	v_fmac_f32_e32 v16, v130, v36
	v_fmac_f32_e32 v17, v131, v36
	v_fmac_f32_e32 v14, v132, v37
	v_fmac_f32_e32 v15, v133, v37
	v_fmac_f32_e32 v12, v130, v37
	v_fmac_f32_e32 v13, v131, v37
	v_fmac_f32_e32 v10, v132, v38
	v_fmac_f32_e32 v11, v133, v38
	v_fmac_f32_e32 v8, v130, v38
	v_fmac_f32_e32 v9, v131, v38
	v_fmac_f32_e32 v6, v132, v142
	v_fmac_f32_e32 v7, v133, v142
	v_fmac_f32_e32 v4, v130, v142
	v_fmac_f32_e32 v5, v131, v142
	s_addk_i32 s16, 0x200
	v_mov_b32_e32 v146, v125
	s_waitcnt lgkmcnt(1)
	v_fmac_f32_e32 v18, v136, v98
	v_fmac_f32_e32 v19, v137, v98
	v_fmac_f32_e32 v16, v134, v98
	v_fmac_f32_e32 v17, v135, v98
	v_fmac_f32_e32 v14, v136, v99
	v_fmac_f32_e32 v15, v137, v99
	v_fmac_f32_e32 v12, v134, v99
	v_fmac_f32_e32 v13, v135, v99
	v_fmac_f32_e32 v10, v136, v100
	v_fmac_f32_e32 v11, v137, v100
	v_fmac_f32_e32 v8, v134, v100
	v_fmac_f32_e32 v9, v135, v100
	v_fmac_f32_e32 v6, v136, v144
	v_fmac_f32_e32 v7, v137, v144
	v_fmac_f32_e32 v4, v134, v144
	v_fmac_f32_e32 v5, v135, v144
	v_add_u32_e32 v20, 0x440, v20
	s_cmpk_lg_i32 s16, 0x800
	s_waitcnt lgkmcnt(0)
	v_fmac_f32_e32 v18, v140, v122
	v_fmac_f32_e32 v19, v141, v122
	v_fmac_f32_e32 v16, v138, v122
	v_fmac_f32_e32 v17, v139, v122
	v_fmac_f32_e32 v14, v140, v123
	v_fmac_f32_e32 v15, v141, v123
	v_fmac_f32_e32 v12, v138, v123
	v_fmac_f32_e32 v13, v139, v123
	v_fmac_f32_e32 v10, v140, v124
	v_fmac_f32_e32 v11, v141, v124
	v_fmac_f32_e32 v8, v138, v124
	v_fmac_f32_e32 v9, v139, v124
	v_fmac_f32_e32 v6, v140, v146
	v_fmac_f32_e32 v7, v141, v146
	v_fmac_f32_e32 v4, v138, v146
	v_fmac_f32_e32 v5, v139, v146
	s_cbranch_scc1 .LBB0_680
	s_barrier
	global_load_dwordx4 v[32:35], v[94:95], off offset:1920
	global_load_dwordx4 v[20:23], v[80:81], off
	s_waitcnt vmcnt(3)
	v_cvt_f32_f16_sdwa v95, v28 dst_sel:DWORD dst_unused:UNUSED_PAD src0_sel:WORD_1
	v_cvt_f32_f16_e32 v28, v28
	v_cvt_f32_f16_sdwa v94, v29 dst_sel:DWORD dst_unused:UNUSED_PAD src0_sel:WORD_1
	v_cvt_f32_f16_sdwa v130, v30 dst_sel:DWORD dst_unused:UNUSED_PAD src0_sel:WORD_1
	v_cvt_f32_f16_e32 v133, v30
	ds_read_b128 v[36:39], v43 offset:15872
	ds_read_b128 v[98:101], v43 offset:15888
	ds_read_b128 v[122:125], v43 offset:19968
	ds_read_b128 v[126:129], v43 offset:19984
	v_cvt_f32_f16_e32 v97, v29
	v_cvt_f32_f16_sdwa v131, v31 dst_sel:DWORD dst_unused:UNUSED_PAD src0_sel:WORD_1
	v_cvt_f32_f16_e32 v132, v31
	v_sub_f32_e32 v28, v28, v0
	v_sub_f32_e32 v29, v95, v1
	v_sub_f32_e32 v31, v94, v3
	v_mul_f32_e32 v28, v90, v28
	v_mul_f32_e32 v29, v91, v29
	v_sub_f32_e32 v94, v133, v0
	v_sub_f32_e32 v95, v130, v1
	v_sub_f32_e32 v30, v97, v2
	v_sub_f32_e32 v130, v132, v2
	v_sub_f32_e32 v131, v131, v3
	v_mul_f32_e32 v94, v90, v94
	v_mul_f32_e32 v95, v91, v95
	s_waitcnt lgkmcnt(1)
	v_fma_f32 v28, v36, v28, v122
	v_fma_f32 v29, v37, v29, v123
	v_mul_f32_e32 v30, v92, v30
	v_mul_f32_e32 v31, v93, v31
	v_mul_f32_e32 v130, v92, v130
	v_mul_f32_e32 v131, v93, v131
	s_waitcnt lgkmcnt(0)
	v_fma_f32 v36, v98, v94, v126
	ds_write2_b32 v96, v28, v29 offset1:68
	v_fma_f32 v28, v99, v95, v127
	ds_write2_b32 v44, v36, v28 offset0:16 offset1:84
	v_fma_f32 v28, v38, v30, v124
	v_fma_f32 v29, v100, v130, v128
	v_fmac_f32_e32 v125, v39, v31
	v_fmac_f32_e32 v129, v101, v131
	ds_write2_b32 v96, v28, v125 offset0:136 offset1:204
	ds_write2_b32 v44, v29, v129 offset0:152 offset1:220
	s_waitcnt vmcnt(2)
	ds_write_b128 v104, v[24:27] offset:41984
	s_mov_b32 s16, 0
	v_mov_b32_e32 v24, v112
	s_waitcnt lgkmcnt(0)
	s_barrier
.LBB0_682:
	v_add_u32_e32 v25, s16, v111
	ds_read_b128 v[26:29], v24
	ds_read_b128 v[36:39], v24 offset:272
	ds_read_b128 v[98:101], v24 offset:544
	ds_read_b128 v[122:125], v24 offset:816
	ds_read_b128 v[126:129], v25
	ds_read_b128 v[130:133], v25 offset:128
	ds_read_b128 v[134:137], v25 offset:256
	ds_read_b128 v[138:141], v25 offset:384
	s_waitcnt lgkmcnt(7)
	v_mov_b32_e32 v30, v29
	s_waitcnt lgkmcnt(6)
	v_mov_b32_e32 v94, v39
	s_waitcnt lgkmcnt(3)
	v_fmac_f32_e32 v18, v128, v26
	v_fmac_f32_e32 v19, v129, v26
	v_fmac_f32_e32 v16, v126, v26
	v_fmac_f32_e32 v17, v127, v26
	v_fmac_f32_e32 v14, v128, v27
	v_fmac_f32_e32 v15, v129, v27
	v_fmac_f32_e32 v12, v126, v27
	v_fmac_f32_e32 v13, v127, v27
	v_fmac_f32_e32 v8, v126, v28
	v_fmac_f32_e32 v9, v127, v28
	v_fmac_f32_e32 v10, v128, v28
	v_fmac_f32_e32 v11, v129, v28
	v_fmac_f32_e32 v4, v126, v30
	v_fmac_f32_e32 v5, v127, v30
	v_fmac_f32_e32 v6, v128, v30
	v_fmac_f32_e32 v7, v129, v30
	v_mov_b32_e32 v142, v101
	s_waitcnt lgkmcnt(2)
	v_fmac_f32_e32 v18, v132, v36
	v_fmac_f32_e32 v19, v133, v36
	v_fmac_f32_e32 v16, v130, v36
	v_fmac_f32_e32 v17, v131, v36
	v_fmac_f32_e32 v14, v132, v37
	v_fmac_f32_e32 v15, v133, v37
	v_fmac_f32_e32 v12, v130, v37
	v_fmac_f32_e32 v13, v131, v37
	v_fmac_f32_e32 v10, v132, v38
	v_fmac_f32_e32 v11, v133, v38
	v_fmac_f32_e32 v8, v130, v38
	v_fmac_f32_e32 v9, v131, v38
	v_fmac_f32_e32 v6, v132, v94
	v_fmac_f32_e32 v7, v133, v94
	v_fmac_f32_e32 v4, v130, v94
	v_fmac_f32_e32 v5, v131, v94
	s_addk_i32 s16, 0x200
	v_mov_b32_e32 v144, v125
	s_waitcnt lgkmcnt(1)
	v_fmac_f32_e32 v18, v136, v98
	v_fmac_f32_e32 v19, v137, v98
	v_fmac_f32_e32 v16, v134, v98
	v_fmac_f32_e32 v17, v135, v98
	v_fmac_f32_e32 v14, v136, v99
	v_fmac_f32_e32 v15, v137, v99
	v_fmac_f32_e32 v12, v134, v99
	v_fmac_f32_e32 v13, v135, v99
	v_fmac_f32_e32 v10, v136, v100
	v_fmac_f32_e32 v11, v137, v100
	v_fmac_f32_e32 v8, v134, v100
	v_fmac_f32_e32 v9, v135, v100
	v_fmac_f32_e32 v6, v136, v142
	v_fmac_f32_e32 v7, v137, v142
	v_fmac_f32_e32 v4, v134, v142
	v_fmac_f32_e32 v5, v135, v142
	v_add_u32_e32 v24, 0x440, v24
	s_cmpk_lg_i32 s16, 0x800
	s_waitcnt lgkmcnt(0)
	v_fmac_f32_e32 v18, v140, v122
	v_fmac_f32_e32 v19, v141, v122
	v_fmac_f32_e32 v16, v138, v122
	v_fmac_f32_e32 v17, v139, v122
	v_fmac_f32_e32 v14, v140, v123
	v_fmac_f32_e32 v15, v141, v123
	v_fmac_f32_e32 v12, v138, v123
	v_fmac_f32_e32 v13, v139, v123
	v_fmac_f32_e32 v10, v140, v124
	v_fmac_f32_e32 v11, v141, v124
	v_fmac_f32_e32 v8, v138, v124
	v_fmac_f32_e32 v9, v139, v124
	v_fmac_f32_e32 v6, v140, v144
	v_fmac_f32_e32 v7, v141, v144
	v_fmac_f32_e32 v4, v138, v144
	v_fmac_f32_e32 v5, v139, v144
	s_cbranch_scc1 .LBB0_682
	s_waitcnt vmcnt(1)
	v_cvt_f32_f16_sdwa v95, v32 dst_sel:DWORD dst_unused:UNUSED_PAD src0_sel:WORD_1
	v_cvt_f32_f16_e32 v32, v32
	v_cvt_f32_f16_sdwa v123, v34 dst_sel:DWORD dst_unused:UNUSED_PAD src0_sel:WORD_1
	v_cvt_f32_f16_e32 v125, v34
	s_barrier
	ds_read_b128 v[24:27], v43 offset:16128
	ds_read_b128 v[28:31], v43 offset:16144
	ds_read_b128 v[36:39], v43 offset:20224
	ds_read_b128 v[98:101], v43 offset:20240
	v_cvt_f32_f16_sdwa v94, v33 dst_sel:DWORD dst_unused:UNUSED_PAD src0_sel:WORD_1
	v_cvt_f32_f16_e32 v97, v33
	v_cvt_f32_f16_sdwa v122, v35 dst_sel:DWORD dst_unused:UNUSED_PAD src0_sel:WORD_1
	v_cvt_f32_f16_e32 v124, v35
	v_sub_f32_e32 v32, v32, v0
	v_sub_f32_e32 v33, v95, v1
	v_sub_f32_e32 v0, v125, v0
	v_sub_f32_e32 v1, v123, v1
	v_sub_f32_e32 v34, v97, v2
	v_sub_f32_e32 v35, v94, v3
	v_mul_f32_e32 v0, v90, v0
	v_mul_f32_e32 v1, v91, v1
	v_mul_f32_e32 v34, v92, v34
	v_mul_f32_e32 v35, v93, v35
	v_sub_f32_e32 v2, v124, v2
	v_sub_f32_e32 v3, v122, v3
	s_waitcnt lgkmcnt(0)
	v_fma_f32 v0, v28, v0, v98
	v_fma_f32 v1, v29, v1, v99
	v_mul_f32_e32 v32, v90, v32
	v_mul_f32_e32 v33, v91, v33
	v_mul_f32_e32 v2, v92, v2
	v_mul_f32_e32 v3, v93, v3
	ds_write2_b32 v44, v0, v1 offset0:16 offset1:84
	v_fma_f32 v0, v26, v34, v38
	v_fmac_f32_e32 v39, v27, v35
	v_fma_f32 v24, v24, v32, v36
	v_fma_f32 v25, v25, v33, v37
	v_fma_f32 v1, v30, v2, v100
	ds_write2_b32 v96, v0, v39 offset0:136 offset1:204
	v_fmac_f32_e32 v101, v31, v3
	s_mov_b32 s16, 0
	v_mov_b32_e32 v0, v112
	ds_write2_b32 v96, v24, v25 offset1:68
	ds_write2_b32 v44, v1, v101 offset0:152 offset1:220
	s_waitcnt vmcnt(0)
	ds_write_b128 v104, v[20:23] offset:41984
	s_waitcnt lgkmcnt(0)
	s_barrier
.LBB0_684:
	v_add_u32_e32 v1, s16, v111
	ds_read_b128 v[20:23], v0
	ds_read_b128 v[24:27], v0 offset:272
	ds_read_b128 v[28:31], v0 offset:544
	ds_read_b128 v[32:35], v0 offset:816
	ds_read_b128 v[36:39], v1
	ds_read_b128 v[90:93], v1 offset:128
	ds_read_b128 v[94:97], v1 offset:256
	ds_read_b128 v[98:101], v1 offset:384
	s_waitcnt lgkmcnt(7)
	v_mov_b32_e32 v2, v23
	s_waitcnt lgkmcnt(6)
	v_mov_b32_e32 v44, v27
	s_waitcnt lgkmcnt(3)
	v_fmac_f32_e32 v18, v38, v20
	v_fmac_f32_e32 v19, v39, v20
	v_fmac_f32_e32 v16, v36, v20
	v_fmac_f32_e32 v17, v37, v20
	v_fmac_f32_e32 v14, v38, v21
	v_fmac_f32_e32 v15, v39, v21
	v_fmac_f32_e32 v12, v36, v21
	v_fmac_f32_e32 v13, v37, v21
	v_fmac_f32_e32 v8, v36, v22
	v_fmac_f32_e32 v9, v37, v22
	v_fmac_f32_e32 v10, v38, v22
	v_fmac_f32_e32 v11, v39, v22
	v_fmac_f32_e32 v4, v36, v2
	v_fmac_f32_e32 v5, v37, v2
	v_fma_f32 v3, v39, v2, v7
	v_fma_f32 v2, v38, v2, v6
	v_mov_b32_e32 v122, v31
	s_waitcnt lgkmcnt(2)
	v_fma_f32 v6, v92, v24, v18
	v_fma_f32 v7, v93, v24, v19
	v_fmac_f32_e32 v16, v90, v24
	v_fmac_f32_e32 v17, v91, v24
	v_fmac_f32_e32 v14, v92, v25
	v_fmac_f32_e32 v15, v93, v25
	v_fmac_f32_e32 v12, v90, v25
	v_fmac_f32_e32 v13, v91, v25
	v_fmac_f32_e32 v10, v92, v26
	v_fmac_f32_e32 v11, v93, v26
	v_fmac_f32_e32 v8, v90, v26
	v_fmac_f32_e32 v9, v91, v26
	v_fmac_f32_e32 v2, v92, v44
	v_fmac_f32_e32 v3, v93, v44
	v_fmac_f32_e32 v4, v90, v44
	v_fmac_f32_e32 v5, v91, v44
	s_addk_i32 s16, 0x200
	v_mov_b32_e32 v124, v35
	s_waitcnt lgkmcnt(1)
	v_fmac_f32_e32 v6, v96, v28
	v_fmac_f32_e32 v7, v97, v28
	v_fmac_f32_e32 v16, v94, v28
	v_fmac_f32_e32 v17, v95, v28
	v_fmac_f32_e32 v14, v96, v29
	v_fmac_f32_e32 v15, v97, v29
	v_fmac_f32_e32 v12, v94, v29
	v_fmac_f32_e32 v13, v95, v29
	v_fmac_f32_e32 v10, v96, v30
	v_fmac_f32_e32 v11, v97, v30
	v_fmac_f32_e32 v8, v94, v30
	v_fmac_f32_e32 v9, v95, v30
	v_fmac_f32_e32 v2, v96, v122
	v_fmac_f32_e32 v3, v97, v122
	v_fmac_f32_e32 v4, v94, v122
	v_fmac_f32_e32 v5, v95, v122
	v_add_u32_e32 v0, 0x440, v0
	s_cmpk_lg_i32 s16, 0x800
	s_waitcnt lgkmcnt(0)
	v_fma_f32 v18, v100, v32, v6
	v_fma_f32 v19, v101, v32, v7
	v_fmac_f32_e32 v16, v98, v32
	v_fmac_f32_e32 v17, v99, v32
	v_fmac_f32_e32 v14, v100, v33
	v_fmac_f32_e32 v15, v101, v33
	v_fmac_f32_e32 v12, v98, v33
	v_fmac_f32_e32 v13, v99, v33
	v_fmac_f32_e32 v10, v100, v34
	v_fmac_f32_e32 v11, v101, v34
	v_fmac_f32_e32 v8, v98, v34
	v_fmac_f32_e32 v9, v99, v34
	v_fma_f32 v6, v100, v124, v2
	v_fma_f32 v7, v101, v124, v3
	v_fmac_f32_e32 v4, v98, v124
	v_fmac_f32_e32 v5, v99, v124
	s_cbranch_scc1 .LBB0_684
	s_barrier
	ds_write_b128 v116, v[16:19] offset:58752
	ds_write_b128 v116, v[12:15] offset:58880
	ds_write_b128 v116, v[8:11] offset:59008
	ds_write_b128 v116, v[4:7] offset:59136
	s_waitcnt lgkmcnt(0)
	s_barrier
	global_load_dwordx4 v[0:3], v[50:51], off
	ds_read_b128 v[4:7], v106 offset:58752
	ds_read_b128 v[8:11], v107 offset:8192
	ds_read_b128 v[12:15], v107 offset:16384
	ds_read_b128 v[16:19], v107 offset:24576
	v_add_u32_e32 v20, 0xc400, v108
	v_add_u32_e32 v21, 0xc408, v108
	s_waitcnt lgkmcnt(2)
	v_add_f32_e32 v4, v4, v8
	v_add_f32_e32 v5, v5, v9
	v_add_f32_e32 v6, v6, v10
	v_add_f32_e32 v7, v7, v11
	s_waitcnt lgkmcnt(1)
	v_add_f32_e32 v4, v12, v4
	v_add_f32_e32 v5, v13, v5
	v_add_f32_e32 v6, v14, v6
	v_add_f32_e32 v7, v15, v7
	s_waitcnt lgkmcnt(0)
	v_add_f32_e32 v4, v16, v4
	v_add_f32_e32 v5, v17, v5
	v_add_f32_e32 v6, v18, v6
	v_add_f32_e32 v7, v19, v7
	s_waitcnt vmcnt(0)
	v_add_f32_e32 v0, v0, v4
	v_add_f32_e32 v1, v1, v5
	v_add_f32_e32 v2, v6, v2
	v_add_f32_e32 v3, v7, v3
	ds_write2_b32 v20, v0, v1 offset1:1
	ds_write2_b32 v21, v2, v3 offset1:1
	s_waitcnt lgkmcnt(0)
	s_barrier
	s_and_saveexec_b64 s[28:29], s[6:7]
	s_cbranch_execz .LBB0_687
	v_add_u32_e32 v0, 0xc400, v117
	v_add_u32_e32 v1, 0xc408, v117
	v_add_u32_e32 v2, 0xc410, v117
	v_add_u32_e32 v3, 0xc418, v117
	ds_read2_b32 v[34:35], v0 offset1:1
	ds_read2_b32 v[30:31], v1 offset1:1
	ds_read2_b32 v[22:23], v2 offset1:1
	ds_read2_b32 v[10:11], v3 offset1:1
	s_mov_b32 s16, 0xff61b1e6
	s_waitcnt lgkmcnt(3)
	v_max_f32_e32 v0, v34, v34
	v_max_f32_e32 v0, 0xff61b1e6, v0
	v_cmp_lt_f32_e32 vcc, s16, v34
	v_cmp_gt_f32_e64 s[16:17], v35, v0
	v_add_u32_e32 v2, 0xc420, v117
	ds_read2_b32 v[24:25], v2 offset1:1
	v_cndmask_b32_e64 v0, v0, v35, s[16:17]
	v_cndmask_b32_e64 v1, 0, 1, s[16:17]
	s_waitcnt lgkmcnt(3)
	v_cmp_gt_f32_e64 s[16:17], v30, v0
	v_add_u32_e32 v2, 0xc428, v117
	v_add_u32_e32 v3, 0xc430, v117
	v_cndmask_b32_e64 v0, v0, v30, s[16:17]
	v_cndmask_b32_e64 v1, v1, 2, s[16:17]
	v_cmp_gt_f32_e64 s[16:17], v31, v0
	v_add_u32_e32 v4, 0xc438, v117
	ds_read2_b32 v[32:33], v2 offset1:1
	ds_read2_b32 v[20:21], v3 offset1:1
	ds_read2_b32 v[6:7], v4 offset1:1
	v_cndmask_b32_e64 v0, v0, v31, s[16:17]
	v_cndmask_b32_e64 v1, v1, 3, s[16:17]
	s_waitcnt lgkmcnt(5)
	v_cmp_gt_f32_e64 s[16:17], v22, v0
	v_add_u32_e32 v2, 0xc440, v117
	ds_read2_b32 v[18:19], v2 offset1:1
	v_cndmask_b32_e64 v0, v0, v22, s[16:17]
	v_cndmask_b32_e64 v1, v1, 4, s[16:17]
	v_cmp_gt_f32_e64 s[16:17], v23, v0
	v_add_u32_e32 v2, 0xc448, v117
	v_add_u32_e32 v4, 0xc458, v117
	v_cndmask_b32_e64 v0, v0, v23, s[16:17]
	v_cndmask_b32_e64 v1, v1, 5, s[16:17]
	s_waitcnt lgkmcnt(5)
	v_cmp_gt_f32_e64 s[16:17], v10, v0
	v_add_u32_e32 v3, 0xc450, v117
	ds_read2_b32 v[26:27], v2 offset1:1
	ds_read2_b32 v[12:13], v3 offset1:1
	ds_read2_b32 v[4:5], v4 offset1:1
	v_cndmask_b32_e64 v0, v0, v10, s[16:17]
	v_cndmask_b32_e64 v1, v1, 6, s[16:17]
	v_cmp_gt_f32_e64 s[16:17], v11, v0
	v_add_u32_e32 v2, 0xc460, v117
	ds_read2_b32 v[14:15], v2 offset1:1
	v_cndmask_b32_e64 v0, v0, v11, s[16:17]
	v_cndmask_b32_e64 v1, v1, 7, s[16:17]
	s_waitcnt lgkmcnt(8)
	v_cmp_gt_f32_e64 s[16:17], v24, v0
	v_add_u32_e32 v2, 0xc468, v117
	v_add_u32_e32 v8, 0xc478, v117
	v_cndmask_b32_e64 v0, v0, v24, s[16:17]
	v_cndmask_b32_e64 v1, v1, 8, s[16:17]
	v_cmp_gt_f32_e64 s[16:17], v25, v0
	v_add_u32_e32 v3, 0xc470, v117
	ds_read2_b32 v[28:29], v2 offset1:1
	ds_read2_b32 v[16:17], v3 offset1:1
	ds_read2_b32 v[8:9], v8 offset1:1
	v_cndmask_b32_e64 v0, v0, v25, s[16:17]
	v_cndmask_b32_e64 v1, v1, 9, s[16:17]
	s_waitcnt lgkmcnt(10)
	v_cmp_gt_f32_e64 s[16:17], v32, v0
	s_nop 1
	v_cndmask_b32_e64 v0, v0, v32, s[16:17]
	v_cndmask_b32_e64 v1, v1, 10, s[16:17]
	v_cmp_gt_f32_e64 s[16:17], v33, v0
	s_nop 1
	v_cndmask_b32_e64 v0, v0, v33, s[16:17]
	v_cndmask_b32_e64 v1, v1, 11, s[16:17]
	s_waitcnt lgkmcnt(9)
	v_cmp_gt_f32_e64 s[16:17], v20, v0
	s_nop 1
	v_cndmask_b32_e64 v0, v0, v20, s[16:17]
	v_cndmask_b32_e64 v1, v1, 12, s[16:17]
	v_cmp_gt_f32_e64 s[16:17], v21, v0
	s_nop 1
	v_cndmask_b32_e64 v0, v0, v21, s[16:17]
	v_cndmask_b32_e64 v1, v1, 13, s[16:17]
	s_waitcnt lgkmcnt(8)
	v_cmp_gt_f32_e64 s[16:17], v6, v0
	s_nop 1
	v_cndmask_b32_e64 v0, v0, v6, s[16:17]
	v_cndmask_b32_e64 v1, v1, 14, s[16:17]
	v_cmp_gt_f32_e64 s[16:17], v7, v0
	s_nop 1
	v_cndmask_b32_e64 v0, v0, v7, s[16:17]
	v_cndmask_b32_e64 v1, v1, 15, s[16:17]
	s_waitcnt lgkmcnt(7)
	v_cmp_gt_f32_e64 s[16:17], v18, v0
	s_nop 1
	v_cndmask_b32_e64 v0, v0, v18, s[16:17]
	v_cndmask_b32_e64 v1, v1, 16, s[16:17]
	v_cmp_gt_f32_e64 s[16:17], v19, v0
	s_nop 1
	v_cndmask_b32_e64 v0, v0, v19, s[16:17]
	v_cndmask_b32_e64 v1, v1, 17, s[16:17]
	s_waitcnt lgkmcnt(6)
	v_cmp_gt_f32_e64 s[16:17], v26, v0
	s_nop 1
	v_cndmask_b32_e64 v0, v0, v26, s[16:17]
	v_cndmask_b32_e64 v1, v1, 18, s[16:17]
	v_cmp_gt_f32_e64 s[16:17], v27, v0
	s_nop 1
	v_cndmask_b32_e64 v0, v0, v27, s[16:17]
	v_cndmask_b32_e64 v1, v1, 19, s[16:17]
	s_waitcnt lgkmcnt(5)
	v_cmp_gt_f32_e64 s[16:17], v12, v0
	s_nop 1
	v_cndmask_b32_e64 v0, v0, v12, s[16:17]
	v_cndmask_b32_e64 v1, v1, 20, s[16:17]
	v_cmp_gt_f32_e64 s[16:17], v13, v0
	s_nop 1
	v_cndmask_b32_e64 v0, v0, v13, s[16:17]
	v_cndmask_b32_e64 v1, v1, 21, s[16:17]
	s_waitcnt lgkmcnt(4)
	v_cmp_gt_f32_e64 s[16:17], v4, v0
	s_nop 1
	v_cndmask_b32_e64 v0, v0, v4, s[16:17]
	v_cndmask_b32_e64 v1, v1, 22, s[16:17]
	v_cmp_gt_f32_e64 s[16:17], v5, v0
	s_nop 1
	v_cndmask_b32_e64 v0, v0, v5, s[16:17]
	v_cndmask_b32_e64 v1, v1, 23, s[16:17]
	s_waitcnt lgkmcnt(3)
	v_cmp_gt_f32_e64 s[16:17], v14, v0
	s_nop 1
	v_cndmask_b32_e64 v0, v0, v14, s[16:17]
	v_cndmask_b32_e64 v1, v1, 24, s[16:17]
	v_cmp_gt_f32_e64 s[16:17], v15, v0
	s_nop 1
	v_cndmask_b32_e64 v0, v0, v15, s[16:17]
	v_cndmask_b32_e64 v1, v1, 25, s[16:17]
	s_waitcnt lgkmcnt(2)
	v_cmp_gt_f32_e64 s[16:17], v28, v0
	s_nop 1
	v_cndmask_b32_e64 v0, v0, v28, s[16:17]
	v_cndmask_b32_e64 v1, v1, 26, s[16:17]
	v_cmp_gt_f32_e64 s[16:17], v29, v0
	s_nop 1
	v_cndmask_b32_e64 v0, v0, v29, s[16:17]
	v_cndmask_b32_e64 v1, v1, 27, s[16:17]
	s_waitcnt lgkmcnt(1)
	v_cmp_gt_f32_e64 s[16:17], v16, v0
	s_nop 1
	v_cndmask_b32_e64 v0, v0, v16, s[16:17]
	v_cndmask_b32_e64 v1, v1, 28, s[16:17]
	v_cmp_gt_f32_e64 s[16:17], v17, v0
	s_nop 1
	v_cndmask_b32_e64 v0, v0, v17, s[16:17]
	v_cndmask_b32_e64 v1, v1, 29, s[16:17]
	s_waitcnt lgkmcnt(0)
	v_cmp_gt_f32_e64 s[16:17], v8, v0
	s_nop 1
	v_cndmask_b32_e64 v0, v0, v8, s[16:17]
	v_cndmask_b32_e64 v1, v1, 30, s[16:17]
	v_cmp_gt_f32_e64 s[16:17], v9, v0
	s_nop 1
	v_cndmask_b32_e64 v36, v0, v9, s[16:17]
	v_cndmask_b32_e64 v0, v1, 31, s[16:17]
	v_cmp_ne_u32_e64 s[16:17], 0, v0
	v_lshlrev_b32_e64 v2, v0, 1
	s_and_b64 s[16:17], s[16:17], vcc
	v_cndmask_b32_e64 v1, v121, v34, s[16:17]
	v_and_b32_e32 v3, 2, v2
	v_cmp_eq_u32_e64 s[16:17], 0, v3
	v_cmp_gt_f32_e64 s[18:19], v35, v1
	s_and_b64 s[16:17], s[16:17], s[18:19]
	v_cndmask_b32_e64 v1, v1, v35, s[16:17]
	v_and_b32_e32 v37, 4, v2
	v_cndmask_b32_e64 v3, 0, 1, s[16:17]
	v_cmp_eq_u32_e64 s[16:17], 0, v37
	v_cmp_gt_f32_e64 s[18:19], v30, v1
	s_and_b64 s[16:17], s[16:17], s[18:19]
	v_cndmask_b32_e64 v1, v1, v30, s[16:17]
	v_and_b32_e32 v37, 8, v2
	v_cndmask_b32_e64 v3, v3, 2, s[16:17]
	v_cmp_eq_u32_e64 s[16:17], 0, v37
	v_cmp_gt_f32_e64 s[18:19], v31, v1
	s_and_b64 s[16:17], s[16:17], s[18:19]
	v_cndmask_b32_e64 v1, v1, v31, s[16:17]
	v_and_b32_e32 v37, 16, v2
	v_cndmask_b32_e64 v3, v3, 3, s[16:17]
	v_cmp_eq_u32_e64 s[16:17], 0, v37
	v_cmp_gt_f32_e64 s[18:19], v22, v1
	s_and_b64 s[16:17], s[16:17], s[18:19]
	v_cndmask_b32_e64 v1, v1, v22, s[16:17]
	v_and_b32_e32 v37, 32, v2
	v_cndmask_b32_e64 v3, v3, 4, s[16:17]
	v_cmp_eq_u32_e64 s[16:17], 0, v37
	v_cmp_gt_f32_e64 s[18:19], v23, v1
	s_and_b64 s[16:17], s[16:17], s[18:19]
	v_cndmask_b32_e64 v1, v1, v23, s[16:17]
	v_and_b32_e32 v37, 64, v2
	v_cndmask_b32_e64 v3, v3, 5, s[16:17]
	v_cmp_eq_u32_e64 s[16:17], 0, v37
	v_cmp_gt_f32_e64 s[18:19], v10, v1
	s_and_b64 s[16:17], s[16:17], s[18:19]
	v_cndmask_b32_e64 v1, v1, v10, s[16:17]
	v_and_b32_e32 v37, 0x80, v2
	v_cndmask_b32_e64 v3, v3, 6, s[16:17]
	v_cmp_eq_u32_e64 s[16:17], 0, v37
	v_cmp_gt_f32_e64 s[18:19], v11, v1
	s_and_b64 s[16:17], s[16:17], s[18:19]
	v_cndmask_b32_e64 v1, v1, v11, s[16:17]
	v_and_b32_e32 v37, 0x100, v2
	v_cndmask_b32_e64 v3, v3, 7, s[16:17]
	v_cmp_eq_u32_e64 s[16:17], 0, v37
	v_cmp_gt_f32_e64 s[18:19], v24, v1
	s_and_b64 s[16:17], s[16:17], s[18:19]
	v_cndmask_b32_e64 v1, v1, v24, s[16:17]
	v_and_b32_e32 v37, 0x200, v2
	v_cndmask_b32_e64 v3, v3, 8, s[16:17]
	v_cmp_eq_u32_e64 s[16:17], 0, v37
	v_cmp_gt_f32_e64 s[18:19], v25, v1
	s_and_b64 s[16:17], s[16:17], s[18:19]
	v_cndmask_b32_e64 v1, v1, v25, s[16:17]
	v_and_b32_e32 v37, 0x400, v2
	v_cndmask_b32_e64 v3, v3, 9, s[16:17]
	v_cmp_eq_u32_e64 s[16:17], 0, v37
	v_cmp_gt_f32_e64 s[18:19], v32, v1
	s_and_b64 s[16:17], s[16:17], s[18:19]
	v_cndmask_b32_e64 v1, v1, v32, s[16:17]
	v_and_b32_e32 v37, 0x800, v2
	v_cndmask_b32_e64 v3, v3, 10, s[16:17]
	v_cmp_eq_u32_e64 s[16:17], 0, v37
	v_cmp_gt_f32_e64 s[18:19], v33, v1
	s_and_b64 s[16:17], s[16:17], s[18:19]
	v_cndmask_b32_e64 v1, v1, v33, s[16:17]
	v_and_b32_e32 v37, 0x1000, v2
	v_cndmask_b32_e64 v3, v3, 11, s[16:17]
	v_cmp_eq_u32_e64 s[16:17], 0, v37
	v_cmp_gt_f32_e64 s[18:19], v20, v1
	s_and_b64 s[16:17], s[16:17], s[18:19]
	v_cndmask_b32_e64 v1, v1, v20, s[16:17]
	v_and_b32_e32 v37, 0x2000, v2
	v_cndmask_b32_e64 v3, v3, 12, s[16:17]
	v_cmp_eq_u32_e64 s[16:17], 0, v37
	v_cmp_gt_f32_e64 s[18:19], v21, v1
	s_and_b64 s[16:17], s[16:17], s[18:19]
	v_cndmask_b32_e64 v1, v1, v21, s[16:17]
	v_and_b32_e32 v37, 0x4000, v2
	v_cndmask_b32_e64 v3, v3, 13, s[16:17]
	v_cmp_eq_u32_e64 s[16:17], 0, v37
	v_cmp_gt_f32_e64 s[18:19], v6, v1
	s_and_b64 s[16:17], s[16:17], s[18:19]
	v_cndmask_b32_e64 v1, v1, v6, s[16:17]
	v_and_b32_e32 v37, 0x8000, v2
	v_cndmask_b32_e64 v3, v3, 14, s[16:17]
	v_cmp_eq_u32_e64 s[16:17], 0, v37
	v_cmp_gt_f32_e64 s[18:19], v7, v1
	s_and_b64 s[16:17], s[16:17], s[18:19]
	v_cndmask_b32_e64 v1, v1, v7, s[16:17]
	v_and_b32_e32 v37, 0x10000, v2
	v_cndmask_b32_e64 v3, v3, 15, s[16:17]
	v_cmp_eq_u32_e64 s[16:17], 0, v37
	v_cmp_gt_f32_e64 s[18:19], v18, v1
	s_and_b64 s[16:17], s[16:17], s[18:19]
	v_cndmask_b32_e64 v1, v1, v18, s[16:17]
	v_and_b32_e32 v37, 0x20000, v2
	v_cndmask_b32_e64 v3, v3, 16, s[16:17]
	v_cmp_eq_u32_e64 s[16:17], 0, v37
	v_cmp_gt_f32_e64 s[18:19], v19, v1
	s_and_b64 s[16:17], s[16:17], s[18:19]
	v_cndmask_b32_e64 v1, v1, v19, s[16:17]
	v_and_b32_e32 v37, 0x40000, v2
	v_cndmask_b32_e64 v3, v3, 17, s[16:17]
	v_cmp_eq_u32_e64 s[16:17], 0, v37
	v_cmp_gt_f32_e64 s[18:19], v26, v1
	s_and_b64 s[16:17], s[16:17], s[18:19]
	v_cndmask_b32_e64 v1, v1, v26, s[16:17]
	v_and_b32_e32 v37, 0x80000, v2
	v_cndmask_b32_e64 v3, v3, 18, s[16:17]
	v_cmp_eq_u32_e64 s[16:17], 0, v37
	v_cmp_gt_f32_e64 s[18:19], v27, v1
	s_and_b64 s[16:17], s[16:17], s[18:19]
	v_cndmask_b32_e64 v1, v1, v27, s[16:17]
	v_and_b32_e32 v37, 0x100000, v2
	v_cndmask_b32_e64 v3, v3, 19, s[16:17]
	v_cmp_eq_u32_e64 s[16:17], 0, v37
	v_cmp_gt_f32_e64 s[18:19], v12, v1
	s_and_b64 s[16:17], s[16:17], s[18:19]
	v_cndmask_b32_e64 v1, v1, v12, s[16:17]
	v_and_b32_e32 v37, 0x200000, v2
	v_cndmask_b32_e64 v3, v3, 20, s[16:17]
	v_cmp_eq_u32_e64 s[16:17], 0, v37
	v_cmp_gt_f32_e64 s[18:19], v13, v1
	s_and_b64 s[16:17], s[16:17], s[18:19]
	v_cndmask_b32_e64 v1, v1, v13, s[16:17]
	v_and_b32_e32 v37, 0x400000, v2
	v_cndmask_b32_e64 v3, v3, 21, s[16:17]
	v_cmp_eq_u32_e64 s[16:17], 0, v37
	v_cmp_gt_f32_e64 s[18:19], v4, v1
	s_and_b64 s[16:17], s[16:17], s[18:19]
	v_cndmask_b32_e64 v1, v1, v4, s[16:17]
	v_and_b32_e32 v37, 0x800000, v2
	v_cndmask_b32_e64 v3, v3, 22, s[16:17]
	v_cmp_eq_u32_e64 s[16:17], 0, v37
	v_cmp_gt_f32_e64 s[18:19], v5, v1
	s_and_b64 s[16:17], s[16:17], s[18:19]
	v_cndmask_b32_e64 v1, v1, v5, s[16:17]
	v_and_b32_e32 v37, 0x1000000, v2
	v_cndmask_b32_e64 v3, v3, 23, s[16:17]
	v_cmp_eq_u32_e64 s[16:17], 0, v37
	v_cmp_gt_f32_e64 s[18:19], v14, v1
	s_and_b64 s[16:17], s[16:17], s[18:19]
	v_cndmask_b32_e64 v1, v1, v14, s[16:17]
	v_and_b32_e32 v37, 0x2000000, v2
	v_cndmask_b32_e64 v3, v3, 24, s[16:17]
	v_cmp_eq_u32_e64 s[16:17], 0, v37
	v_cmp_gt_f32_e64 s[18:19], v15, v1
	s_and_b64 s[16:17], s[16:17], s[18:19]
	v_cndmask_b32_e64 v1, v1, v15, s[16:17]
	v_and_b32_e32 v37, 0x4000000, v2
	v_cndmask_b32_e64 v3, v3, 25, s[16:17]
	v_cmp_eq_u32_e64 s[16:17], 0, v37
	v_cmp_gt_f32_e64 s[18:19], v28, v1
	s_and_b64 s[16:17], s[16:17], s[18:19]
	v_cndmask_b32_e64 v1, v1, v28, s[16:17]
	v_and_b32_e32 v37, 0x8000000, v2
	v_cndmask_b32_e64 v3, v3, 26, s[16:17]
	v_cmp_eq_u32_e64 s[16:17], 0, v37
	v_cmp_gt_f32_e64 s[18:19], v29, v1
	s_and_b64 s[16:17], s[16:17], s[18:19]
	v_cndmask_b32_e64 v1, v1, v29, s[16:17]
	v_and_b32_e32 v37, 0x10000000, v2
	v_cndmask_b32_e64 v3, v3, 27, s[16:17]
	v_cmp_eq_u32_e64 s[16:17], 0, v37
	v_cmp_gt_f32_e64 s[18:19], v16, v1
	s_and_b64 s[16:17], s[16:17], s[18:19]
	v_cndmask_b32_e64 v1, v1, v16, s[16:17]
	v_and_b32_e32 v37, 0x20000000, v2
	v_cndmask_b32_e64 v3, v3, 28, s[16:17]
	v_cmp_eq_u32_e64 s[16:17], 0, v37
	v_cmp_gt_f32_e64 s[18:19], v17, v1
	s_and_b64 s[16:17], s[16:17], s[18:19]
	v_cndmask_b32_e64 v1, v1, v17, s[16:17]
	v_and_b32_e32 v37, 2.0, v2
	v_cndmask_b32_e64 v3, v3, 29, s[16:17]
	v_cmp_eq_u32_e64 s[16:17], 0, v37
	v_cmp_gt_f32_e64 s[18:19], v8, v1
	s_and_b64 s[16:17], s[16:17], s[18:19]
	v_cndmask_b32_e64 v1, v1, v8, s[16:17]
	v_cndmask_b32_e64 v3, v3, 30, s[16:17]
	v_cmp_ne_u32_e64 s[16:17], 31, v0
	v_cmp_gt_f32_e64 s[18:19], v9, v1
	s_and_b64 s[16:17], s[16:17], s[18:19]
	v_cndmask_b32_e64 v37, v1, v9, s[16:17]
	v_cndmask_b32_e64 v1, v3, 31, s[16:17]
	v_lshl_or_b32 v3, 1, v1, v2
	v_and_b32_e32 v2, 1, v3
	v_cmp_eq_u32_e64 s[16:17], 0, v2
	s_and_b64 s[16:17], s[16:17], vcc
	v_and_b32_e32 v38, 2, v3
	v_cndmask_b32_e64 v2, v121, v34, s[16:17]
	v_cmp_eq_u32_e64 s[16:17], 0, v38
	v_cmp_gt_f32_e64 s[18:19], v35, v2
	s_and_b64 s[16:17], s[16:17], s[18:19]
	v_cndmask_b32_e64 v2, v2, v35, s[16:17]
	v_and_b32_e32 v39, 4, v3
	v_cndmask_b32_e64 v38, 0, 1, s[16:17]
	v_cmp_eq_u32_e64 s[16:17], 0, v39
	v_cmp_gt_f32_e64 s[18:19], v30, v2
	s_and_b64 s[16:17], s[16:17], s[18:19]
	v_cndmask_b32_e64 v2, v2, v30, s[16:17]
	v_and_b32_e32 v39, 8, v3
	v_cndmask_b32_e64 v38, v38, 2, s[16:17]
	v_cmp_eq_u32_e64 s[16:17], 0, v39
	v_cmp_gt_f32_e64 s[18:19], v31, v2
	s_and_b64 s[16:17], s[16:17], s[18:19]
	v_cndmask_b32_e64 v2, v2, v31, s[16:17]
	v_and_b32_e32 v39, 16, v3
	v_cndmask_b32_e64 v38, v38, 3, s[16:17]
	v_cmp_eq_u32_e64 s[16:17], 0, v39
	v_cmp_gt_f32_e64 s[18:19], v22, v2
	s_and_b64 s[16:17], s[16:17], s[18:19]
	v_cndmask_b32_e64 v2, v2, v22, s[16:17]
	v_and_b32_e32 v39, 32, v3
	v_cndmask_b32_e64 v38, v38, 4, s[16:17]
	v_cmp_eq_u32_e64 s[16:17], 0, v39
	v_cmp_gt_f32_e64 s[18:19], v23, v2
	s_and_b64 s[16:17], s[16:17], s[18:19]
	v_cndmask_b32_e64 v2, v2, v23, s[16:17]
	v_and_b32_e32 v39, 64, v3
	v_cndmask_b32_e64 v38, v38, 5, s[16:17]
	v_cmp_eq_u32_e64 s[16:17], 0, v39
	v_cmp_gt_f32_e64 s[18:19], v10, v2
	s_and_b64 s[16:17], s[16:17], s[18:19]
	v_cndmask_b32_e64 v2, v2, v10, s[16:17]
	v_and_b32_e32 v39, 0x80, v3
	v_cndmask_b32_e64 v38, v38, 6, s[16:17]
	v_cmp_eq_u32_e64 s[16:17], 0, v39
	v_cmp_gt_f32_e64 s[18:19], v11, v2
	s_and_b64 s[16:17], s[16:17], s[18:19]
	v_cndmask_b32_e64 v2, v2, v11, s[16:17]
	v_and_b32_e32 v39, 0x100, v3
	v_cndmask_b32_e64 v38, v38, 7, s[16:17]
	v_cmp_eq_u32_e64 s[16:17], 0, v39
	v_cmp_gt_f32_e64 s[18:19], v24, v2
	s_and_b64 s[16:17], s[16:17], s[18:19]
	v_cndmask_b32_e64 v2, v2, v24, s[16:17]
	v_and_b32_e32 v39, 0x200, v3
	v_cndmask_b32_e64 v38, v38, 8, s[16:17]
	v_cmp_eq_u32_e64 s[16:17], 0, v39
	v_cmp_gt_f32_e64 s[18:19], v25, v2
	s_and_b64 s[16:17], s[16:17], s[18:19]
	v_cndmask_b32_e64 v2, v2, v25, s[16:17]
	v_and_b32_e32 v39, 0x400, v3
	v_cndmask_b32_e64 v38, v38, 9, s[16:17]
	v_cmp_eq_u32_e64 s[16:17], 0, v39
	v_cmp_gt_f32_e64 s[18:19], v32, v2
	s_and_b64 s[16:17], s[16:17], s[18:19]
	v_cndmask_b32_e64 v2, v2, v32, s[16:17]
	v_and_b32_e32 v39, 0x800, v3
	v_cndmask_b32_e64 v38, v38, 10, s[16:17]
	v_cmp_eq_u32_e64 s[16:17], 0, v39
	v_cmp_gt_f32_e64 s[18:19], v33, v2
	s_and_b64 s[16:17], s[16:17], s[18:19]
	v_cndmask_b32_e64 v2, v2, v33, s[16:17]
	v_and_b32_e32 v39, 0x1000, v3
	v_cndmask_b32_e64 v38, v38, 11, s[16:17]
	v_cmp_eq_u32_e64 s[16:17], 0, v39
	v_cmp_gt_f32_e64 s[18:19], v20, v2
	s_and_b64 s[16:17], s[16:17], s[18:19]
	v_cndmask_b32_e64 v2, v2, v20, s[16:17]
	v_and_b32_e32 v39, 0x2000, v3
	v_cndmask_b32_e64 v38, v38, 12, s[16:17]
	v_cmp_eq_u32_e64 s[16:17], 0, v39
	v_cmp_gt_f32_e64 s[18:19], v21, v2
	s_and_b64 s[16:17], s[16:17], s[18:19]
	v_cndmask_b32_e64 v2, v2, v21, s[16:17]
	v_and_b32_e32 v39, 0x4000, v3
	v_cndmask_b32_e64 v38, v38, 13, s[16:17]
	v_cmp_eq_u32_e64 s[16:17], 0, v39
	v_cmp_gt_f32_e64 s[18:19], v6, v2
	s_and_b64 s[16:17], s[16:17], s[18:19]
	v_cndmask_b32_e64 v2, v2, v6, s[16:17]
	v_and_b32_e32 v39, 0x8000, v3
	v_cndmask_b32_e64 v38, v38, 14, s[16:17]
	v_cmp_eq_u32_e64 s[16:17], 0, v39
	v_cmp_gt_f32_e64 s[18:19], v7, v2
	s_and_b64 s[16:17], s[16:17], s[18:19]
	v_cndmask_b32_e64 v2, v2, v7, s[16:17]
	v_and_b32_e32 v39, 0x10000, v3
	v_cndmask_b32_e64 v38, v38, 15, s[16:17]
	v_cmp_eq_u32_e64 s[16:17], 0, v39
	v_cmp_gt_f32_e64 s[18:19], v18, v2
	s_and_b64 s[16:17], s[16:17], s[18:19]
	v_cndmask_b32_e64 v2, v2, v18, s[16:17]
	v_and_b32_e32 v39, 0x20000, v3
	v_cndmask_b32_e64 v38, v38, 16, s[16:17]
	v_cmp_eq_u32_e64 s[16:17], 0, v39
	v_cmp_gt_f32_e64 s[18:19], v19, v2
	s_and_b64 s[16:17], s[16:17], s[18:19]
	v_cndmask_b32_e64 v2, v2, v19, s[16:17]
	v_and_b32_e32 v39, 0x40000, v3
	v_cndmask_b32_e64 v38, v38, 17, s[16:17]
	v_cmp_eq_u32_e64 s[16:17], 0, v39
	v_cmp_gt_f32_e64 s[18:19], v26, v2
	s_and_b64 s[16:17], s[16:17], s[18:19]
	v_cndmask_b32_e64 v2, v2, v26, s[16:17]
	v_and_b32_e32 v39, 0x80000, v3
	v_cndmask_b32_e64 v38, v38, 18, s[16:17]
	v_cmp_eq_u32_e64 s[16:17], 0, v39
	v_cmp_gt_f32_e64 s[18:19], v27, v2
	s_and_b64 s[16:17], s[16:17], s[18:19]
	v_cndmask_b32_e64 v2, v2, v27, s[16:17]
	v_and_b32_e32 v39, 0x100000, v3
	v_cndmask_b32_e64 v38, v38, 19, s[16:17]
	v_cmp_eq_u32_e64 s[16:17], 0, v39
	v_cmp_gt_f32_e64 s[18:19], v12, v2
	s_and_b64 s[16:17], s[16:17], s[18:19]
	v_cndmask_b32_e64 v2, v2, v12, s[16:17]
	v_and_b32_e32 v39, 0x200000, v3
	v_cndmask_b32_e64 v38, v38, 20, s[16:17]
	v_cmp_eq_u32_e64 s[16:17], 0, v39
	v_cmp_gt_f32_e64 s[18:19], v13, v2
	s_and_b64 s[16:17], s[16:17], s[18:19]
	v_cndmask_b32_e64 v2, v2, v13, s[16:17]
	v_and_b32_e32 v39, 0x400000, v3
	v_cndmask_b32_e64 v38, v38, 21, s[16:17]
	v_cmp_eq_u32_e64 s[16:17], 0, v39
	v_cmp_gt_f32_e64 s[18:19], v4, v2
	s_and_b64 s[16:17], s[16:17], s[18:19]
	v_cndmask_b32_e64 v2, v2, v4, s[16:17]
	v_and_b32_e32 v39, 0x800000, v3
	v_cndmask_b32_e64 v38, v38, 22, s[16:17]
	v_cmp_eq_u32_e64 s[16:17], 0, v39
	v_cmp_gt_f32_e64 s[18:19], v5, v2
	s_and_b64 s[16:17], s[16:17], s[18:19]
	v_cndmask_b32_e64 v2, v2, v5, s[16:17]
	v_and_b32_e32 v39, 0x1000000, v3
	v_cndmask_b32_e64 v38, v38, 23, s[16:17]
	v_cmp_eq_u32_e64 s[16:17], 0, v39
	v_cmp_gt_f32_e64 s[18:19], v14, v2
	s_and_b64 s[16:17], s[16:17], s[18:19]
	v_cndmask_b32_e64 v2, v2, v14, s[16:17]
	v_and_b32_e32 v39, 0x2000000, v3
	v_cndmask_b32_e64 v38, v38, 24, s[16:17]
	v_cmp_eq_u32_e64 s[16:17], 0, v39
	v_cmp_gt_f32_e64 s[18:19], v15, v2
	s_and_b64 s[16:17], s[16:17], s[18:19]
	v_cndmask_b32_e64 v2, v2, v15, s[16:17]
	v_and_b32_e32 v39, 0x4000000, v3
	v_cndmask_b32_e64 v38, v38, 25, s[16:17]
	v_cmp_eq_u32_e64 s[16:17], 0, v39
	v_cmp_gt_f32_e64 s[18:19], v28, v2
	s_and_b64 s[16:17], s[16:17], s[18:19]
	v_cndmask_b32_e64 v2, v2, v28, s[16:17]
	v_and_b32_e32 v39, 0x8000000, v3
	v_cndmask_b32_e64 v38, v38, 26, s[16:17]
	v_cmp_eq_u32_e64 s[16:17], 0, v39
	v_cmp_gt_f32_e64 s[18:19], v29, v2
	s_and_b64 s[16:17], s[16:17], s[18:19]
	v_cndmask_b32_e64 v2, v2, v29, s[16:17]
	v_and_b32_e32 v39, 0x10000000, v3
	v_cndmask_b32_e64 v38, v38, 27, s[16:17]
	v_cmp_eq_u32_e64 s[16:17], 0, v39
	v_cmp_gt_f32_e64 s[18:19], v16, v2
	s_and_b64 s[16:17], s[16:17], s[18:19]
	v_cndmask_b32_e64 v2, v2, v16, s[16:17]
	v_and_b32_e32 v39, 0x20000000, v3
	v_cndmask_b32_e64 v38, v38, 28, s[16:17]
	v_cmp_eq_u32_e64 s[16:17], 0, v39
	v_cmp_gt_f32_e64 s[18:19], v17, v2
	s_and_b64 s[16:17], s[16:17], s[18:19]
	v_cndmask_b32_e64 v2, v2, v17, s[16:17]
	v_and_b32_e32 v39, 2.0, v3
	v_cndmask_b32_e64 v38, v38, 29, s[16:17]
	v_cmp_eq_u32_e64 s[16:17], 0, v39
	v_cmp_gt_f32_e64 s[18:19], v8, v2
	s_and_b64 s[16:17], s[16:17], s[18:19]
	v_cndmask_b32_e64 v2, v2, v8, s[16:17]
	v_cndmask_b32_e64 v38, v38, 30, s[16:17]
	v_cmp_lt_i32_e64 s[16:17], -1, v3
	v_cmp_gt_f32_e64 s[18:19], v9, v2
	s_and_b64 s[16:17], s[16:17], s[18:19]
	v_cndmask_b32_e64 v39, v2, v9, s[16:17]
	v_cndmask_b32_e64 v2, v38, 31, s[16:17]
	v_lshlrev_b32_e64 v38, v2, 1
	v_bitop3_b32 v90, v38, 1, v3 bitop3:0xc8
	v_cmp_eq_u32_e64 s[16:17], 0, v90
	s_and_b64 vcc, s[16:17], vcc
	v_cndmask_b32_e32 v34, v121, v34, vcc
	v_bitop3_b32 v90, v38, 2, v3 bitop3:0xc8
	v_cmp_eq_u32_e32 vcc, 0, v90
	v_cmp_gt_f32_e64 s[16:17], v35, v34
	s_and_b64 vcc, vcc, s[16:17]
	v_cndmask_b32_e32 v34, v34, v35, vcc
	v_bitop3_b32 v90, v38, 4, v3 bitop3:0xc8
	v_cndmask_b32_e64 v35, 0, 1, vcc
	v_cmp_eq_u32_e32 vcc, 0, v90
	v_cmp_gt_f32_e64 s[16:17], v30, v34
	s_and_b64 vcc, vcc, s[16:17]
	v_cndmask_b32_e32 v30, v34, v30, vcc
	v_cndmask_b32_e64 v34, v35, 2, vcc
	v_bitop3_b32 v35, v38, 8, v3 bitop3:0xc8
	v_cmp_eq_u32_e32 vcc, 0, v35
	v_cmp_gt_f32_e64 s[16:17], v31, v30
	s_and_b64 vcc, vcc, s[16:17]
	v_cndmask_b32_e32 v30, v30, v31, vcc
	v_cndmask_b32_e64 v31, v34, 3, vcc
	v_bitop3_b32 v34, v38, 16, v3 bitop3:0xc8
	v_cmp_eq_u32_e32 vcc, 0, v34
	v_cmp_gt_f32_e64 s[16:17], v22, v30
	s_and_b64 vcc, vcc, s[16:17]
	v_cndmask_b32_e32 v22, v30, v22, vcc
	v_cndmask_b32_e64 v30, v31, 4, vcc
	v_bitop3_b32 v31, v38, 32, v3 bitop3:0xc8
	v_cmp_eq_u32_e32 vcc, 0, v31
	v_cmp_gt_f32_e64 s[16:17], v23, v22
	s_and_b64 vcc, vcc, s[16:17]
	v_cndmask_b32_e32 v22, v22, v23, vcc
	v_cndmask_b32_e64 v23, v30, 5, vcc
	v_bitop3_b32 v30, v38, 64, v3 bitop3:0xc8
	v_cmp_eq_u32_e32 vcc, 0, v30
	v_cmp_gt_f32_e64 s[16:17], v10, v22
	s_and_b64 vcc, vcc, s[16:17]
	s_movk_i32 s16, 0x80
	v_cndmask_b32_e32 v10, v22, v10, vcc
	v_cndmask_b32_e64 v22, v23, 6, vcc
	v_bitop3_b32 v23, v38, s16, v3 bitop3:0xc8
	v_cmp_eq_u32_e32 vcc, 0, v23
	v_cmp_gt_f32_e64 s[16:17], v11, v10
	s_and_b64 vcc, vcc, s[16:17]
	s_movk_i32 s16, 0x100
	v_cndmask_b32_e32 v10, v10, v11, vcc
	v_cndmask_b32_e64 v11, v22, 7, vcc
	v_bitop3_b32 v22, v38, s16, v3 bitop3:0xc8
	v_cmp_eq_u32_e32 vcc, 0, v22
	v_cmp_gt_f32_e64 s[16:17], v24, v10
	s_and_b64 vcc, vcc, s[16:17]
	s_movk_i32 s16, 0x200
	v_cndmask_b32_e32 v10, v10, v24, vcc
	v_bitop3_b32 v22, v38, s16, v3 bitop3:0xc8
	v_cndmask_b32_e64 v11, v11, 8, vcc
	v_cmp_eq_u32_e32 vcc, 0, v22
	v_cmp_gt_f32_e64 s[16:17], v25, v10
	s_and_b64 vcc, vcc, s[16:17]
	v_cndmask_b32_e32 v10, v10, v25, vcc
	v_bitop3_b32 v22, v38, s46, v3 bitop3:0xc8
	v_cndmask_b32_e64 v11, v11, 9, vcc
	v_cmp_eq_u32_e32 vcc, 0, v22
	v_cmp_gt_f32_e64 s[16:17], v32, v10
	s_and_b64 vcc, vcc, s[16:17]
	s_movk_i32 s16, 0x800
	v_cndmask_b32_e32 v10, v10, v32, vcc
	v_bitop3_b32 v22, v38, s16, v3 bitop3:0xc8
	v_cndmask_b32_e64 v11, v11, 10, vcc
	v_cmp_eq_u32_e32 vcc, 0, v22
	v_cmp_gt_f32_e64 s[16:17], v33, v10
	s_and_b64 vcc, vcc, s[16:17]
	s_movk_i32 s16, 0x1000
	v_cndmask_b32_e32 v10, v10, v33, vcc
	v_bitop3_b32 v22, v38, s16, v3 bitop3:0xc8
	v_cndmask_b32_e64 v11, v11, 11, vcc
	v_cmp_eq_u32_e32 vcc, 0, v22
	v_cmp_gt_f32_e64 s[16:17], v20, v10
	s_and_b64 vcc, vcc, s[16:17]
	s_movk_i32 s16, 0x2000
	v_cndmask_b32_e32 v10, v10, v20, vcc
	v_bitop3_b32 v20, v38, s16, v3 bitop3:0xc8
	v_cndmask_b32_e64 v11, v11, 12, vcc
	v_cmp_eq_u32_e32 vcc, 0, v20
	v_cmp_gt_f32_e64 s[16:17], v21, v10
	s_and_b64 vcc, vcc, s[16:17]
	s_movk_i32 s16, 0x4000
	v_cndmask_b32_e32 v10, v10, v21, vcc
	v_bitop3_b32 v20, v38, s16, v3 bitop3:0xc8
	v_cndmask_b32_e64 v11, v11, 13, vcc
	v_cmp_eq_u32_e32 vcc, 0, v20
	v_cmp_gt_f32_e64 s[16:17], v6, v10
	s_and_b64 vcc, vcc, s[16:17]
	s_mov_b32 s16, 0x8000
	v_cndmask_b32_e32 v6, v10, v6, vcc
	v_cndmask_b32_e64 v10, v11, 14, vcc
	v_bitop3_b32 v11, v38, s16, v3 bitop3:0xc8
	v_cmp_eq_u32_e32 vcc, 0, v11
	v_cmp_gt_f32_e64 s[16:17], v7, v6
	s_and_b64 vcc, vcc, s[16:17]
	s_mov_b32 s16, 0x10000
	v_cndmask_b32_e32 v6, v6, v7, vcc
	v_cndmask_b32_e64 v7, v10, 15, vcc
	v_bitop3_b32 v10, v38, s16, v3 bitop3:0xc8
	v_cmp_eq_u32_e32 vcc, 0, v10
	v_cmp_gt_f32_e64 s[16:17], v18, v6
	s_and_b64 vcc, vcc, s[16:17]
	s_mov_b32 s16, 0x20000
	v_cndmask_b32_e32 v6, v6, v18, vcc
	v_bitop3_b32 v10, v38, s16, v3 bitop3:0xc8
	v_cndmask_b32_e64 v7, v7, 16, vcc
	v_cmp_eq_u32_e32 vcc, 0, v10
	v_cmp_gt_f32_e64 s[16:17], v19, v6
	s_and_b64 vcc, vcc, s[16:17]
	s_mov_b32 s16, 0x40000
	v_cndmask_b32_e32 v6, v6, v19, vcc
	v_bitop3_b32 v10, v38, s16, v3 bitop3:0xc8
	v_cndmask_b32_e64 v7, v7, 17, vcc
	v_cmp_eq_u32_e32 vcc, 0, v10
	v_cmp_gt_f32_e64 s[16:17], v26, v6
	s_and_b64 vcc, vcc, s[16:17]
	s_mov_b32 s16, 0x80000
	v_cndmask_b32_e32 v6, v6, v26, vcc
	v_bitop3_b32 v10, v38, s16, v3 bitop3:0xc8
	v_cndmask_b32_e64 v7, v7, 18, vcc
	v_cmp_eq_u32_e32 vcc, 0, v10
	v_cmp_gt_f32_e64 s[16:17], v27, v6
	s_and_b64 vcc, vcc, s[16:17]
	s_mov_b32 s16, 0x100000
	v_cndmask_b32_e32 v6, v6, v27, vcc
	v_bitop3_b32 v10, v38, s16, v3 bitop3:0xc8
	v_cndmask_b32_e64 v7, v7, 19, vcc
	v_cmp_eq_u32_e32 vcc, 0, v10
	v_cmp_gt_f32_e64 s[16:17], v12, v6
	s_and_b64 vcc, vcc, s[16:17]
	s_mov_b32 s16, 0x200000
	v_cndmask_b32_e32 v6, v6, v12, vcc
	v_bitop3_b32 v10, v38, s16, v3 bitop3:0xc8
	v_cndmask_b32_e64 v7, v7, 20, vcc
	v_cmp_eq_u32_e32 vcc, 0, v10
	v_cmp_gt_f32_e64 s[16:17], v13, v6
	s_and_b64 vcc, vcc, s[16:17]
	s_mov_b32 s16, 0x400000
	v_cndmask_b32_e32 v6, v6, v13, vcc
	v_bitop3_b32 v10, v38, s16, v3 bitop3:0xc8
	v_cndmask_b32_e64 v7, v7, 21, vcc
	v_cmp_eq_u32_e32 vcc, 0, v10
	v_cmp_gt_f32_e64 s[16:17], v4, v6
	s_and_b64 vcc, vcc, s[16:17]
	s_mov_b32 s16, 0x800000
	v_cndmask_b32_e32 v4, v6, v4, vcc
	v_cndmask_b32_e64 v6, v7, 22, vcc
	v_bitop3_b32 v7, v38, s16, v3 bitop3:0xc8
	v_cmp_eq_u32_e32 vcc, 0, v7
	v_cmp_gt_f32_e64 s[16:17], v5, v4
	s_and_b64 vcc, vcc, s[16:17]
	v_cndmask_b32_e32 v4, v4, v5, vcc
	v_cndmask_b32_e64 v5, v6, 23, vcc
	v_bitop3_b32 v6, v38, s55, v3 bitop3:0xc8
	v_cmp_eq_u32_e32 vcc, 0, v6
	v_cmp_gt_f32_e64 s[16:17], v14, v4
	s_and_b64 vcc, vcc, s[16:17]
	v_cndmask_b32_e32 v4, v4, v14, vcc
	v_bitop3_b32 v6, v38, s56, v3 bitop3:0xc8
	v_cndmask_b32_e64 v5, v5, 24, vcc
	v_cmp_eq_u32_e32 vcc, 0, v6
	v_cmp_gt_f32_e64 s[16:17], v15, v4
	s_and_b64 vcc, vcc, s[16:17]
	v_cndmask_b32_e32 v4, v4, v15, vcc
	v_bitop3_b32 v6, v38, s57, v3 bitop3:0xc8
	v_cndmask_b32_e64 v5, v5, 25, vcc
	v_cmp_eq_u32_e32 vcc, 0, v6
	v_cmp_gt_f32_e64 s[16:17], v28, v4
	s_and_b64 vcc, vcc, s[16:17]
	v_cndmask_b32_e32 v4, v4, v28, vcc
	v_bitop3_b32 v6, v38, s58, v3 bitop3:0xc8
	v_cndmask_b32_e64 v5, v5, 26, vcc
	v_cmp_eq_u32_e32 vcc, 0, v6
	v_cmp_gt_f32_e64 s[16:17], v29, v4
	s_and_b64 vcc, vcc, s[16:17]
	v_cndmask_b32_e32 v4, v4, v29, vcc
	v_bitop3_b32 v6, v38, s59, v3 bitop3:0xc8
	v_cndmask_b32_e64 v5, v5, 27, vcc
	v_cmp_eq_u32_e32 vcc, 0, v6
	v_cmp_gt_f32_e64 s[16:17], v16, v4
	s_and_b64 vcc, vcc, s[16:17]
	v_cndmask_b32_e32 v4, v4, v16, vcc
	v_bitop3_b32 v6, v38, s60, v3 bitop3:0xc8
	v_cndmask_b32_e64 v5, v5, 28, vcc
	v_cmp_eq_u32_e32 vcc, 0, v6
	v_cmp_gt_f32_e64 s[16:17], v17, v4
	s_and_b64 vcc, vcc, s[16:17]
	v_or_b32_e32 v44, v38, v3
	v_cndmask_b32_e32 v4, v4, v17, vcc
	v_bitop3_b32 v3, v38, 2.0, v3 bitop3:0xc8
	v_cndmask_b32_e64 v5, v5, 29, vcc
	v_cmp_eq_u32_e32 vcc, 0, v3
	v_cmp_gt_f32_e64 s[16:17], v8, v4
	s_and_b64 vcc, vcc, s[16:17]
	v_cndmask_b32_e32 v3, v4, v8, vcc
	v_cndmask_b32_e64 v4, v5, 30, vcc
	v_cmp_lt_i32_e32 vcc, -1, v44
	v_cmp_gt_f32_e64 s[16:17], v9, v3
	s_and_b64 vcc, vcc, s[16:17]
	v_cndmask_b32_e32 v5, v3, v9, vcc
	v_cndmask_b32_e64 v3, v4, 31, vcc
	v_sub_f32_e32 v4, v36, v36
	v_mul_f32_e32 v4, 0x3fb8aa3b, v4
	v_exp_f32_e32 v10, v4
	v_sub_f32_e32 v4, v37, v36
	v_mul_f32_e32 v4, 0x3fb8aa3b, v4
	v_exp_f32_e32 v11, v4
	v_sub_f32_e32 v4, v39, v36
	v_mul_f32_e32 v4, 0x3fb8aa3b, v4
	v_exp_f32_e32 v12, v4
	v_sub_f32_e32 v4, v5, v36
	v_mul_f32_e32 v4, 0x3fb8aa3b, v4
	v_exp_f32_e32 v13, v4
	v_add_f32_e32 v4, 0, v10
	v_add_f32_e32 v4, v4, v11
	v_add_f32_e32 v4, v4, v12
	v_add_f32_e32 v14, v4, v13
	v_div_scale_f32 v15, s[16:17], v14, v14, v10
	v_rcp_f32_e32 v16, v15
	v_lshl_add_u32 v4, s61, 8, v102
	v_ashrrev_i32_e32 v5, 31, v4
	v_lshlrev_b64 v[6:7], 2, v[4:5]
	v_fma_f32 v5, -v15, v16, 1.0
	v_fmac_f32_e32 v16, v5, v16
	v_div_scale_f32 v5, vcc, v10, v14, v10
	v_mul_f32_e32 v17, v5, v16
	v_fma_f32 v18, -v15, v17, v5
	v_fmac_f32_e32 v17, v18, v16
	v_fma_f32 v5, -v15, v17, v5
	v_div_fmas_f32 v5, v5, v16, v17
	v_div_fixup_f32 v5, v5, v14, v10
	v_div_scale_f32 v10, s[16:17], v14, v14, v11
	v_rcp_f32_e32 v15, v10
	v_lshl_add_u64 v[8:9], s[20:21], 0, v[6:7]
	v_lshl_add_u64 v[6:7], s[22:23], 0, v[6:7]
	global_store_dword v[6:7], v5, off
	v_or_b32_e32 v6, 1, v4
	v_fma_f32 v4, -v10, v15, 1.0
	v_lshl_add_u32 v5, v0, 2, 0
	v_fmac_f32_e32 v15, v4, v15
	v_div_scale_f32 v4, vcc, v11, v14, v11
	ds_add_u32 v5, v118 offset:58624
	v_mul_f32_e32 v5, v4, v15
	v_fma_f32 v16, -v10, v5, v4
	v_fmac_f32_e32 v5, v16, v15
	v_fma_f32 v4, -v10, v5, v4
	v_div_fmas_f32 v4, v4, v15, v5
	v_div_scale_f32 v5, s[16:17], v14, v14, v12
	v_rcp_f32_e32 v15, v5
	v_ashrrev_i32_e32 v7, 31, v6
	v_div_fixup_f32 v4, v4, v14, v11
	v_lshl_add_u64 v[10:11], v[6:7], 2, s[22:23]
	v_lshl_add_u32 v6, v1, 2, 0
	ds_add_u32 v6, v118 offset:58624
	v_fma_f32 v6, -v5, v15, 1.0
	v_fmac_f32_e32 v15, v6, v15
	v_div_scale_f32 v6, vcc, v12, v14, v12
	v_mul_f32_e32 v7, v6, v15
	v_fma_f32 v16, -v5, v7, v6
	v_fmac_f32_e32 v7, v16, v15
	v_fma_f32 v5, -v5, v7, v6
	v_div_scale_f32 v6, s[16:17], v14, v14, v13
	v_div_fmas_f32 v5, v5, v15, v7
	v_rcp_f32_e32 v7, v6
	v_div_fixup_f32 v5, v5, v14, v12
	v_lshl_add_u32 v12, v2, 2, 0
	ds_add_u32 v12, v118 offset:58624
	global_store_dwordx4 v[8:9], v[0:3], off
	s_nop 1
	v_fma_f32 v0, -v6, v7, 1.0
	v_fmac_f32_e32 v7, v0, v7
	v_div_scale_f32 v0, vcc, v13, v14, v13
	v_mul_f32_e32 v1, v0, v7
	v_fma_f32 v2, -v6, v1, v0
	v_fmac_f32_e32 v1, v2, v7
	v_fma_f32 v0, -v6, v1, v0
	v_div_fmas_f32 v0, v0, v7, v1
	v_div_fixup_f32 v6, v0, v14, v13
	global_store_dwordx3 v[10:11], v[4:6], off
	v_lshl_add_u32 v0, v3, 2, 0
	ds_add_u32 v0, v118 offset:58624

.LBB0_1453:
	v_ashrrev_i32_e32 v17, 31, v21
	v_mov_b32_e32 v16, v21
	v_ashrrev_i32_e32 v19, 31, v20
	v_mov_b32_e32 v18, v20
	v_lshlrev_b64 v[22:23], 2, v[18:19]
	v_lshlrev_b64 v[24:25], 2, v[16:17]
	v_lshl_add_u64 v[18:19], s[42:43], 0, v[22:23]
	v_lshl_add_u64 v[16:17], s[42:43], 0, v[24:25]
	global_load_dword v18, v[18:19], off
	s_nop 0
	global_load_dword v16, v[16:17], off
	v_add_u32_e32 v17, 0x800, v21
	v_ashrrev_i32_e32 v19, 31, v17
	v_add_u32_e32 v26, -2, v26
	v_add_u32_e32 v35, 0x2000, v27
	s_add_i32 s33, s33, 4
	v_cmp_eq_u32_e32 vcc, 0, v26
	s_or_b64 s[46:47], vcc, s[46:47]
	s_waitcnt vmcnt(0)
	ds_write2st64_b32 v27, v18, v16 offset1:8
	v_add_u32_e32 v16, 0x800, v20
	v_mov_b32_e32 v18, v17
	v_ashrrev_i32_e32 v29, 31, v16
	v_mov_b32_e32 v28, v16
	v_lshlrev_b64 v[28:29], 2, v[28:29]
	v_lshlrev_b64 v[18:19], 2, v[18:19]
	v_lshl_add_u64 v[30:31], s[68:69], 0, v[28:29]
	v_lshl_add_u64 v[32:33], s[68:69], 0, v[18:19]
	global_load_dword v30, v[30:31], off
	s_nop 0
	global_load_dword v32, v[32:33], off
	v_lshl_add_u64 v[28:29], s[70:71], 0, v[28:29]
	v_lshl_add_u64 v[18:19], s[70:71], 0, v[18:19]
	s_waitcnt vmcnt(1)
	ds_write_b32 v27, v30 offset:4096
	global_load_dword v33, v[28:29], off
	global_load_dword v34, v[18:19], off
	v_lshl_add_u64 v[18:19], s[40:41], 0, v[22:23]
	v_lshl_add_u64 v[22:23], s[38:39], 0, v[22:23]
	v_lshl_add_u64 v[28:29], s[40:41], 0, v[24:25]
	global_load_dword v18, v[18:19], off
	s_nop 0
	global_load_dword v19, v[28:29], off
	v_lshl_add_u64 v[24:25], s[38:39], 0, v[24:25]
	global_load_dword v36, v[22:23], off
	global_load_dword v37, v[24:25], off
	v_add_u32_e32 v22, 0x400, v20
	v_add_u32_e32 v24, 0x400, v21
	v_ashrrev_i32_e32 v23, 31, v22
	v_ashrrev_i32_e32 v25, 31, v24
	v_lshlrev_b64 v[22:23], 2, v[22:23]
	v_lshl_add_u64 v[28:29], s[42:43], 0, v[22:23]
	v_lshlrev_b64 v[24:25], 2, v[24:25]
	v_lshl_add_u64 v[30:31], s[42:43], 0, v[24:25]
	global_load_dword v28, v[28:29], off
	s_nop 0
	global_load_dword v29, v[30:31], off
	v_add_u32_e32 v20, 0xc00, v20
	s_waitcnt vmcnt(1)
	ds_write2st64_b32 v27, v28, v32 offset0:16 offset1:24
	s_waitcnt vmcnt(0)
	ds_write2st64_b32 v27, v29, v33 offset0:24 offset1:32
	v_add_u32_e32 v28, 0xc00, v21
	v_ashrrev_i32_e32 v21, 31, v20
	v_ashrrev_i32_e32 v29, 31, v28
	v_lshlrev_b64 v[20:21], 2, v[20:21]
	v_lshl_add_u64 v[30:31], s[68:69], 0, v[20:21]
	v_lshlrev_b64 v[28:29], 2, v[28:29]
	v_lshl_add_u64 v[32:33], s[68:69], 0, v[28:29]
	global_load_dword v30, v[30:31], off
	s_nop 0
	global_load_dword v31, v[32:33], off
	v_add_f32_e32 v18, 1.0, v18
	v_add_f32_e32 v19, 1.0, v19
	v_lshl_add_u64 v[20:21], s[70:71], 0, v[20:21]
	v_lshl_add_u64 v[28:29], s[70:71], 0, v[28:29]
	s_waitcnt vmcnt(1)
	ds_write2st64_b32 v27, v30, v34 offset0:32 offset1:40
	s_waitcnt vmcnt(0)
	ds_write2st64_b32 v27, v31, v18 offset0:40 offset1:48
	global_load_dword v18, v[20:21], off
	s_nop 0
	global_load_dword v20, v[28:29], off
	s_waitcnt vmcnt(1)
	ds_write2st64_b32 v27, v18, v19 offset0:48 offset1:56
	s_waitcnt vmcnt(0)
	ds_write2st64_b32 v27, v20, v36 offset0:56 offset1:64
	v_lshl_add_u64 v[18:19], s[40:41], 0, v[22:23]
	v_lshl_add_u64 v[20:21], s[40:41], 0, v[24:25]
	global_load_dword v18, v[18:19], off
	s_nop 0
	global_load_dword v19, v[20:21], off
	v_lshl_add_u64 v[20:21], s[38:39], 0, v[22:23]
	v_lshl_add_u64 v[22:23], s[38:39], 0, v[24:25]
	s_waitcnt vmcnt(0)
	v_add_f32_e32 v18, 1.0, v18
	v_add_f32_e32 v19, 1.0, v19
	ds_write2st64_b32 v27, v18, v37 offset0:64 offset1:72
	global_load_dword v18, v[20:21], off
	s_nop 0
	global_load_dword v20, v[22:23], off
	s_waitcnt vmcnt(1)
	ds_write2st64_b32 v27, v19, v18 offset0:72 offset1:80
	s_waitcnt vmcnt(0)
	ds_write_b32 v27, v20 offset:22528
	v_mov_b32_e32 v18, s33
	v_mov_b32_e32 v27, v35
	v_mov_b64_e32 v[20:21], v[16:17]
	s_andn2_b64 exec, exec, s[46:47]
	s_cbranch_execnz .LBB0_1453
	s_or_b64 exec, exec, s[46:47]
	v_lshlrev_b32_e32 v18, 9, v18
	s_or_b64 exec, exec, s[44:45]
	s_and_saveexec_b64 s[44:45], s[12:13]
	s_cbranch_execz .LBB0_1457
	s_branch .LBB0_1456

.LBB0_1456:
	v_ashrrev_i32_e32 v21, 31, v17
	v_mov_b32_e32 v20, v17
	v_ashrrev_i32_e32 v17, 31, v16
	v_lshlrev_b64 v[16:17], 2, v[16:17]
	v_lshl_add_u64 v[22:23], s[42:43], 0, v[16:17]
	v_lshlrev_b64 v[20:21], 2, v[20:21]
	v_lshl_add_u64 v[24:25], s[42:43], 0, v[20:21]
	global_load_dword v19, v[22:23], off
	s_nop 0
	global_load_dword v22, v[24:25], off
	v_readlane_b32 s68, v253, 27
	v_lshl_add_u32 v28, v18, 2, v95
	v_readlane_b32 s69, v253, 28
	v_readlane_b32 s70, v253, 29
	v_readlane_b32 s71, v253, 30
	v_readlane_b32 s76, v253, 35
	v_readlane_b32 s77, v253, 36
	v_readlane_b32 s78, v253, 37
	v_readlane_b32 s79, v253, 38
	s_mov_b64 s[68:69], s[76:77]
	s_mov_b64 s[70:71], s[78:79]
	v_readlane_b32 s72, v253, 31
	v_readlane_b32 s73, v253, 32
	v_readlane_b32 s74, v253, 33
	v_readlane_b32 s75, v253, 34
	v_readlane_b32 s80, v253, 39
	v_readlane_b32 s81, v253, 40
	v_readlane_b32 s82, v253, 41
	v_readlane_b32 s83, v253, 42
	s_waitcnt vmcnt(0)
	ds_write2st64_b32 v28, v19, v22 offset1:8
	v_lshl_add_u64 v[22:23], v[16:17], 0, s[30:31]
	v_lshl_add_u64 v[18:19], v[20:21], 0, s[30:31]
	v_lshl_add_u64 v[24:25], s[68:69], 0, v[22:23]
	v_lshl_add_u64 v[26:27], s[68:69], 0, v[18:19]
	global_load_dword v24, v[24:25], off
	s_nop 0
	global_load_dword v25, v[26:27], off
	v_lshl_add_u64 v[22:23], s[70:71], 0, v[22:23]
	v_lshl_add_u64 v[18:19], s[70:71], 0, v[18:19]
	s_waitcnt vmcnt(0)
	ds_write2st64_b32 v28, v24, v25 offset0:16 offset1:24
	global_load_dword v22, v[22:23], off
	s_nop 0
	global_load_dword v18, v[18:19], off
	s_waitcnt vmcnt(0)
	ds_write2st64_b32 v28, v22, v18 offset0:32 offset1:40
	v_lshl_add_u64 v[18:19], s[40:41], 0, v[16:17]
	v_lshl_add_u64 v[22:23], s[40:41], 0, v[20:21]
	global_load_dword v18, v[18:19], off
	s_nop 0
	global_load_dword v19, v[22:23], off
	v_lshl_add_u64 v[16:17], s[38:39], 0, v[16:17]
	s_waitcnt vmcnt(0)
	v_add_f32_e32 v18, 1.0, v18
	v_add_f32_e32 v19, 1.0, v19
	ds_write2st64_b32 v28, v18, v19 offset0:48 offset1:56
	v_lshl_add_u64 v[18:19], s[38:39], 0, v[20:21]
	global_load_dword v16, v[16:17], off
	s_nop 0
	global_load_dword v17, v[18:19], off
	s_waitcnt vmcnt(0)
	ds_write2st64_b32 v28, v16, v17 offset0:64 offset1:72

.LBB0_1464:
	s_or_b64 exec, exec, s[16:17]
	ds_read_b128 v[88:91], v110 offset:12288
	ds_read_b128 v[114:117], v110 offset:16384
	v_mul_f32_e32 v34, v34, v36
	v_mul_f32_e32 v35, v35, v36
	v_mul_f32_e32 v32, v32, v36
	v_mul_f32_e32 v33, v33, v36
	s_lshl_b64 s[16:17], s[36:37], 10
	v_lshl_add_u64 v[38:39], v[86:87], 0, s[16:17]
	s_waitcnt lgkmcnt(0)
	v_fma_f32 v34, v34, v88, v114
	v_fma_f32 v35, v35, v89, v115
	v_fma_f32 v32, v32, v90, v116
	v_fma_f32 v33, v33, v91, v117
	v_cvt_pk_bf16_f32 v37, v34, v35
	v_mul_f32_e32 v34, 0x41800000, v34
	v_cvt_pk_bf16_f32 v37, v32, v33
	v_mul_f32_e32 v35, 0x41800000, v35
	v_med3_f32 v34, v34, s60, v111
	v_med3_f32 v35, v35, s60, v111
	v_mov_b32_e32 v37, 0
	v_cvt_pk_fp8_f32 v37, v34, v35
	v_mul_f32_e32 v32, 0x41800000, v32
	v_mul_f32_e32 v33, 0x41800000, v33
	v_med3_f32 v32, v32, s60, v111
	v_med3_f32 v33, v33, s60, v111
	v_cvt_pk_fp8_f32 v37, v32, v33 op_sel:[0,0,1]
	ds_read_b128 v[32:35], v110 offset:13312
	ds_read_b128 v[88:91], v110 offset:17408
	s_mov_b32 s33, 32
	s_mov_b64 s[16:17], 0
	v_mul_f32_e32 v30, v30, v36
	v_mul_f32_e32 v31, v31, v36
	global_store_dword v[38:39], v37, off
	s_waitcnt lgkmcnt(0)
	v_fma_f32 v30, v30, v32, v88
	v_fma_f32 v31, v31, v33, v89
	v_mul_f32_e32 v28, v28, v36
	v_mul_f32_e32 v29, v29, v36
	v_cvt_pk_bf16_f32 v32, v30, v31
	v_mul_f32_e32 v30, 0x41800000, v30
	v_mul_f32_e32 v31, 0x41800000, v31
	v_med3_f32 v30, v30, s60, v111
	v_med3_f32 v31, v31, s60, v111
	v_mov_b32_e32 v37, 0
	v_cvt_pk_fp8_f32 v37, v30, v31
	v_fma_f32 v28, v28, v34, v90
	v_fma_f32 v29, v29, v35, v91
	s_mov_b64 s[36:37], -1
	v_cvt_pk_bf16_f32 v32, v28, v29
	v_mul_f32_e32 v28, 0x41800000, v28
	v_mul_f32_e32 v29, 0x41800000, v29
	v_med3_f32 v28, v28, s60, v111
	v_med3_f32 v29, v29, s60, v111
	v_cvt_pk_fp8_f32 v37, v28, v29 op_sel:[0,0,1]
	ds_read_b128 v[28:31], v110 offset:14336
	ds_read_b128 v[32:35], v110 offset:18432
	s_and_b64 vcc, exec, s[18:19]
	v_mul_f32_e32 v26, v26, v36
	v_mul_f32_e32 v27, v27, v36
	v_mul_f32_e32 v24, v24, v36
	v_mul_f32_e32 v25, v25, v36
	s_waitcnt lgkmcnt(0)
	v_fma_f32 v26, v26, v28, v32
	v_fma_f32 v27, v27, v29, v33
	global_store_dword v[38:39], v37, off offset:256
	v_fma_f32 v24, v24, v30, v34
	v_fma_f32 v25, v25, v31, v35
	v_cvt_pk_bf16_f32 v28, v26, v27
	v_mul_f32_e32 v26, 0x41800000, v26
	v_mul_f32_e32 v27, 0x41800000, v27
	v_cvt_pk_bf16_f32 v28, v24, v25
	v_mul_f32_e32 v24, 0x41800000, v24
	v_mul_f32_e32 v32, 0x41800000, v25
	v_med3_f32 v25, v26, s60, v111
	v_med3_f32 v26, v27, s60, v111
	v_mov_b32_e32 v33, 0
	v_cvt_pk_fp8_f32 v33, v25, v26
	v_med3_f32 v34, v24, s60, v111
	ds_read_b128 v[24:27], v110 offset:15360
	ds_read_b128 v[28:31], v110 offset:19456
	v_mul_f32_e32 v22, v22, v36
	v_mul_f32_e32 v23, v23, v36
	v_mul_f32_e32 v20, v20, v36
	v_mul_f32_e32 v21, v21, v36
	v_med3_f32 v32, v32, s60, v111
	v_cvt_pk_fp8_f32 v33, v34, v32 op_sel:[0,0,1]
	s_waitcnt lgkmcnt(0)
	v_fma_f32 v22, v22, v24, v28
	v_fma_f32 v23, v23, v25, v29
	v_fma_f32 v20, v20, v26, v30
	v_fma_f32 v21, v21, v27, v31
	v_mul_f32_e32 v24, 0x41800000, v22
	v_mul_f32_e32 v25, 0x41800000, v23
	v_med3_f32 v24, v24, s60, v111
	v_med3_f32 v25, v25, s60, v111
	v_mov_b32_e32 v27, 0
	v_cvt_pk_fp8_f32 v27, v24, v25
	v_mul_f32_e32 v26, 0x41800000, v20
	v_mul_f32_e32 v24, 0x41800000, v21
	v_med3_f32 v25, v26, s60, v111
	v_med3_f32 v24, v24, s60, v111
	v_cvt_pk_fp8_f32 v27, v25, v24 op_sel:[0,0,1]
	global_store_dword v[38:39], v33, off offset:512
	v_cvt_pk_bf16_f32 v22, v22, v23
	v_cvt_pk_bf16_f32 v20, v20, v21
	global_store_dword v[38:39], v27, off offset:768
	s_cbranch_vccnz .LBB0_1474

.LBB0_1466:
	v_cvt_f32_f16_sdwa v11, v0 dst_sel:DWORD dst_unused:UNUSED_PAD src0_sel:WORD_1
	v_cvt_f32_f16_sdwa v13, v1 dst_sel:DWORD dst_unused:UNUSED_PAD src0_sel:WORD_1
	v_cvt_f32_f16_e32 v10, v0
	v_cvt_f32_f16_e32 v12, v1
	ds_read_b128 v[0:3], v110
	ds_read_b128 v[4:7], v110 offset:1024
	s_waitcnt vmcnt(14)
	v_cvt_f32_f16_sdwa v15, v32 dst_sel:DWORD dst_unused:UNUSED_PAD src0_sel:WORD_1
	v_cvt_f32_f16_sdwa v35, v33 dst_sel:DWORD dst_unused:UNUSED_PAD src0_sel:WORD_1
	v_cvt_f32_f16_e32 v14, v32
	v_cvt_f32_f16_e32 v34, v33
	s_waitcnt vmcnt(13)
	v_cvt_f32_f16_sdwa v33, v28 dst_sel:DWORD dst_unused:UNUSED_PAD src0_sel:WORD_1
	v_cvt_f32_f16_sdwa v37, v29 dst_sel:DWORD dst_unused:UNUSED_PAD src0_sel:WORD_1
	v_cvt_f32_f16_e32 v32, v28
	v_cvt_f32_f16_e32 v36, v29
	s_waitcnt vmcnt(12)
	v_cvt_f32_f16_sdwa v29, v24 dst_sel:DWORD dst_unused:UNUSED_PAD src0_sel:WORD_1
	v_cvt_f32_f16_sdwa v39, v25 dst_sel:DWORD dst_unused:UNUSED_PAD src0_sel:WORD_1
	v_cvt_f32_f16_e32 v28, v24
	v_cvt_f32_f16_e32 v38, v25
	s_waitcnt vmcnt(11)
	v_lshlrev_b32_e32 v24, 16, v30
	v_and_b32_e32 v25, 0xffff0000, v30
	v_lshlrev_b32_e32 v30, 16, v31
	v_and_b32_e32 v31, 0xffff0000, v31
	s_waitcnt lgkmcnt(1)
	v_mul_f32_e32 v2, v2, v30
	v_mul_f32_e32 v3, v3, v31
	v_mul_f32_e32 v0, v0, v24
	v_mul_f32_e32 v1, v1, v25
	v_fma_f32 v12, v12, s34, v2
	v_fma_f32 v13, v13, s34, v3
	v_fma_f32 v10, v10, s34, v0
	v_fma_f32 v11, v11, s34, v1
	v_add_f32_e32 v1, v12, v13
	v_add_f32_e32 v0, v10, v11
	s_waitcnt vmcnt(10)
	v_lshlrev_b32_e32 v88, 16, v26
	v_and_b32_e32 v89, 0xffff0000, v26
	v_lshlrev_b32_e32 v26, 16, v27
	v_and_b32_e32 v27, 0xffff0000, v27
	v_add_f32_e32 v0, v0, v1
	v_add_f32_e32 v24, 0, v0
	s_waitcnt lgkmcnt(0)
	v_mul_f32_e32 v0, v6, v26
	v_mul_f32_e32 v1, v7, v27
	v_mul_f32_e32 v2, v4, v88
	v_mul_f32_e32 v3, v5, v89
	v_fma_f32 v88, v34, s34, v0
	v_fma_f32 v89, v35, s34, v1
	v_fma_f32 v114, v14, s34, v2
	v_fma_f32 v115, v15, s34, v3
	ds_read_b128 v[0:3], v110 offset:2048
	v_add_f32_e32 v4, v114, v115
	v_add_f32_e32 v5, v88, v89
	v_add_f32_e32 v4, v4, v5
	s_waitcnt vmcnt(9)
	v_lshlrev_b32_e32 v90, 16, v22
	v_and_b32_e32 v91, 0xffff0000, v22
	v_lshlrev_b32_e32 v22, 16, v23
	v_and_b32_e32 v23, 0xffff0000, v23
	v_add_f32_e32 v14, v24, v4
	ds_read_b128 v[4:7], v110 offset:3072
	s_waitcnt lgkmcnt(1)
	v_mul_f32_e32 v2, v2, v22
	v_mul_f32_e32 v3, v3, v23
	v_mul_f32_e32 v0, v0, v90
	v_mul_f32_e32 v1, v1, v91
	v_fma_f32 v36, v36, s34, v2
	v_fma_f32 v37, v37, s34, v3
	v_fma_f32 v90, v32, s34, v0
	v_fma_f32 v91, v33, s34, v1
	v_add_f32_e32 v1, v36, v37
	v_add_f32_e32 v0, v90, v91
	s_waitcnt vmcnt(8)
	v_lshlrev_b32_e32 v92, 16, v20
	v_and_b32_e32 v93, 0xffff0000, v20
	v_lshlrev_b32_e32 v20, 16, v21
	v_and_b32_e32 v21, 0xffff0000, v21
	v_add_f32_e32 v0, v0, v1
	v_add_f32_e32 v14, v14, v0
	s_waitcnt lgkmcnt(0)
	v_mul_f32_e32 v0, v6, v20
	v_mul_f32_e32 v1, v7, v21
	v_mul_f32_e32 v2, v4, v92
	v_mul_f32_e32 v3, v5, v93
	v_fma_f32 v38, v38, s34, v0
	v_fma_f32 v39, v39, s34, v1
	v_fma_f32 v92, v28, s34, v2
	v_fma_f32 v93, v29, s34, v3
	v_add_f32_e32 v1, v38, v39
	v_add_f32_e32 v0, v92, v93
	v_add_f32_e32 v0, v0, v1
	v_add_f32_e32 v0, v14, v0
	s_mov_b32 s40, s38
	s_add_i32 s38, s38, 1
	v_add_f32_dpp v0, v0, v0 quad_perm:[1,0,3,2] row_mask:0xf bank_mask:0xf bound_ctrl:1
	s_ashr_i32 s39, s38, 31
	s_lshl_b64 s[16:17], s[38:39], 11
	v_add_f32_dpp v0, v0, v0 quad_perm:[2,3,0,1] row_mask:0xf bank_mask:0xf bound_ctrl:1
	v_lshl_add_u64 v[8:9], v[82:83], 0, s[16:17]
	global_load_dwordx2 v[34:35], v[8:9], off
	global_load_dwordx2 v[32:33], v[8:9], off offset:512
	global_load_dwordx2 v[28:29], v[8:9], off offset:1024
	global_load_dwordx2 v[24:25], v[8:9], off offset:1536
	v_add_f32_dpp v0, v0, v0 row_half_mirror row_mask:0xf bank_mask:0xf bound_ctrl:1
	s_ashr_i32 s41, s40, 31
	s_nop 0
	v_add_f32_dpp v0, v0, v0 row_mirror row_mask:0xf bank_mask:0xf bound_ctrl:1
	v_mov_b32_e32 v1, v0
	s_nop 1
	v_permlane16_swap_b32_e32 v0, v1
	v_add_f32_e32 v0, v0, v1
	v_mov_b32_e32 v1, v0
	s_nop 1
	v_permlane32_swap_b32_e32 v0, v1
	v_add_f32_e32 v0, v0, v1
	v_fmac_f32_e32 v13, 0xba800000, v0
	v_fmac_f32_e32 v11, 0xba800000, v0
	v_fmamk_f32 v12, v0, 0xba800000, v12
	v_fmamk_f32 v10, v0, 0xba800000, v10
	v_mul_f32_e32 v1, v11, v11
	v_mul_f32_e32 v2, v13, v13
	v_fmac_f32_e32 v1, v10, v10
	v_fmac_f32_e32 v2, v12, v12
	v_fmac_f32_e32 v89, 0xba800000, v0
	v_fmac_f32_e32 v115, 0xba800000, v0
	v_add_f32_e32 v1, v1, v2
	v_fmamk_f32 v88, v0, 0xba800000, v88
	v_fmamk_f32 v114, v0, 0xba800000, v114
	v_mul_f32_e32 v2, v115, v115
	v_mul_f32_e32 v3, v89, v89
	v_fmac_f32_e32 v2, v114, v114
	v_fmac_f32_e32 v3, v88, v88
	v_add_f32_e32 v2, v2, v3
	v_fmac_f32_e32 v37, 0xba800000, v0
	v_fmac_f32_e32 v91, 0xba800000, v0
	v_add_f32_e32 v1, v1, v2
	v_fmamk_f32 v36, v0, 0xba800000, v36
	v_fmamk_f32 v90, v0, 0xba800000, v90
	v_mul_f32_e32 v2, v91, v91
	v_mul_f32_e32 v3, v37, v37
	v_fmac_f32_e32 v2, v90, v90
	v_fmac_f32_e32 v3, v36, v36
	v_add_f32_e32 v2, v2, v3
	v_fmac_f32_e32 v39, 0xba800000, v0
	v_fmac_f32_e32 v93, 0xba800000, v0
	v_add_f32_e32 v1, v2, v1
	v_fmamk_f32 v38, v0, 0xba800000, v38
	v_fmamk_f32 v92, v0, 0xba800000, v92
	v_mul_f32_e32 v0, v93, v93
	v_mul_f32_e32 v2, v39, v39
	v_fmac_f32_e32 v0, v92, v92
	v_fmac_f32_e32 v2, v38, v38
	v_add_f32_e32 v0, v0, v2
	v_add_f32_e32 v0, v0, v1
	s_nop 1
	v_add_f32_dpp v0, v0, v0 quad_perm:[1,0,3,2] row_mask:0xf bank_mask:0xf bound_ctrl:1
	s_nop 1
	v_add_f32_dpp v0, v0, v0 quad_perm:[2,3,0,1] row_mask:0xf bank_mask:0xf bound_ctrl:1
	s_nop 1
	v_add_f32_dpp v0, v0, v0 row_half_mirror row_mask:0xf bank_mask:0xf bound_ctrl:1
	s_nop 1
	v_add_f32_dpp v0, v0, v0 row_mirror row_mask:0xf bank_mask:0xf bound_ctrl:1
	v_mov_b32_e32 v1, v0
	s_nop 1
	v_permlane16_swap_b32_e32 v0, v1
	v_add_f32_e32 v0, v0, v1
	v_mov_b32_e32 v1, v0
	s_nop 1
	v_permlane32_swap_b32_e32 v0, v1
	v_add_f32_e32 v0, v0, v1
	v_fmamk_f32 v0, v0, 0x3a800000, v104
	v_mul_f32_e32 v1, 0x4f800000, v0
	v_cmp_gt_f32_e32 vcc, s59, v0
	s_nop 1
	v_cndmask_b32_e32 v2, v0, v1, vcc
	v_sqrt_f32_e32 v3, v2
	v_lshl_add_u64 v[0:1], v[84:85], 0, s[16:17]
	global_load_dwordx2 v[30:31], v[0:1], off
	global_load_dwordx2 v[26:27], v[0:1], off offset:512
	global_load_dwordx2 v[22:23], v[0:1], off offset:1024
	global_load_dwordx2 v[20:21], v[0:1], off offset:1536
	v_add_u32_e32 v4, -1, v3
	v_fma_f32 v5, -v4, v3, v2
	v_cmp_ge_f32_e64 s[16:17], 0, v5
	v_add_u32_e32 v5, 1, v3
	s_nop 0
	v_cndmask_b32_e64 v4, v3, v4, s[16:17]
	v_fma_f32 v3, -v5, v3, v2
	v_cmp_lt_f32_e64 s[16:17], 0, v3
	s_nop 1
	v_cndmask_b32_e64 v3, v4, v5, s[16:17]
	v_mul_f32_e32 v4, 0x37800000, v3
	v_cndmask_b32_e32 v3, v3, v4, vcc
	v_cmp_class_f32_e32 vcc, v2, v105
	s_nop 1
	v_cndmask_b32_e32 v2, v3, v2, vcc
	v_div_scale_f32 v3, s[16:17], v2, v2, 1.0
	v_rcp_f32_e32 v4, v3
	s_lshl_b64 s[16:17], s[40:41], 11
	v_fma_f32 v0, -v3, v4, 1.0
	v_fmac_f32_e32 v4, v0, v4
	v_div_scale_f32 v0, vcc, 1.0, v2, 1.0
	v_mul_f32_e32 v1, v0, v4
	v_fma_f32 v5, -v3, v1, v0
	v_fmac_f32_e32 v1, v5, v4
	v_fma_f32 v0, -v3, v1, v0
	v_div_fmas_f32 v0, v0, v4, v1
	v_div_fixup_f32 v116, v0, v2, 1.0
	ds_read_b128 v[0:3], v110 offset:4096
	ds_read_b128 v[4:7], v110 offset:8192
	v_mul_f32_e32 v118, v12, v116
	v_mul_f32_e32 v119, v13, v116
	v_mul_f32_e32 v120, v10, v116
	v_mul_f32_e32 v121, v11, v116
	ds_read_b128 v[8:11], v110 offset:5120
	ds_read_b128 v[12:15], v110 offset:9216
	s_waitcnt lgkmcnt(2)
	v_fma_f32 v2, v2, v118, v6
	v_fma_f32 v3, v3, v119, v7
	s_nop 0
	v_cvt_pk_f16_f32 v119, v2, v3
	v_cvt_f32_f16_sdwa v117, v119 dst_sel:DWORD dst_unused:UNUSED_PAD src0_sel:WORD_1
	v_fma_f32 v0, v0, v120, v4
	v_fma_f32 v1, v1, v121, v5
	v_cvt_f32_f16_e32 v113, v119
	v_cvt_pk_f16_f32 v118, v0, v1
	v_mul_f32_e32 v0, v88, v116
	v_mul_f32_e32 v1, v89, v116
	v_mul_f32_e32 v2, v114, v116
	v_mul_f32_e32 v3, v115, v116
	s_waitcnt lgkmcnt(0)
	v_fma_f32 v0, v10, v0, v14
	v_fma_f32 v1, v11, v1, v15
	v_fma_f32 v2, v8, v2, v12
	v_fma_f32 v3, v9, v3, v13
	v_cvt_pk_f16_f32 v89, v0, v1
	v_cvt_pk_f16_f32 v88, v2, v3
	ds_read_b128 v[0:3], v110 offset:6144
	ds_read_b128 v[4:7], v110 offset:10240
	ds_read_b128 v[8:11], v110 offset:7168
	ds_read_b128 v[12:15], v110 offset:11264
	v_mul_f32_e32 v90, v90, v116
	v_mul_f32_e32 v91, v91, v116
	v_mul_f32_e32 v36, v36, v116
	v_mul_f32_e32 v37, v37, v116
	v_cvt_f32_f16_e32 v120, v118
	s_waitcnt lgkmcnt(2)
	v_fma_f32 v2, v2, v36, v6
	v_fma_f32 v3, v3, v37, v7
	v_fma_f32 v0, v0, v90, v4
	v_fma_f32 v1, v1, v91, v5
	v_cvt_f32_f16_sdwa v121, v118 dst_sel:DWORD dst_unused:UNUSED_PAD src0_sel:WORD_1
	v_cvt_pk_f16_f32 v90, v0, v1
	v_cvt_pk_f16_f32 v91, v2, v3
	v_mul_f32_e32 v0, v92, v116
	v_mul_f32_e32 v1, v93, v116
	v_mul_f32_e32 v2, v38, v116
	v_mul_f32_e32 v3, v39, v116
	v_cvt_f32_f16_e32 v114, v89
	v_cvt_f32_f16_sdwa v115, v89 dst_sel:DWORD dst_unused:UNUSED_PAD src0_sel:WORD_1
	v_cvt_f32_f16_e32 v122, v88
	v_cvt_f32_f16_sdwa v123, v88 dst_sel:DWORD dst_unused:UNUSED_PAD src0_sel:WORD_1
	s_waitcnt lgkmcnt(0)
	v_fma_f32 v2, v2, v10, v14
	v_fma_f32 v3, v3, v11, v15
	v_fma_f32 v0, v0, v8, v12
	v_fma_f32 v1, v1, v9, v13
	v_cvt_f32_f16_e32 v4, v91
	v_cvt_f32_f16_sdwa v5, v91 dst_sel:DWORD dst_unused:UNUSED_PAD src0_sel:WORD_1
	v_cvt_f32_f16_e32 v6, v90
	v_cvt_f32_f16_sdwa v7, v90 dst_sel:DWORD dst_unused:UNUSED_PAD src0_sel:WORD_1
	v_cvt_pk_f16_f32 v38, v0, v1
	v_cvt_pk_f16_f32 v39, v2, v3
	v_cvt_f32_f16_e32 v0, v39
	v_cvt_f32_f16_sdwa v1, v39 dst_sel:DWORD dst_unused:UNUSED_PAD src0_sel:WORD_1
	v_cvt_f32_f16_e32 v2, v38
	v_cvt_f32_f16_sdwa v3, v38 dst_sel:DWORD dst_unused:UNUSED_PAD src0_sel:WORD_1
	v_add_f32_e32 v8, v120, v121
	v_add_f32_e32 v9, v113, v117
	v_add_f32_e32 v8, v8, v9
	v_add_f32_e32 v9, v122, v123
	v_add_f32_e32 v10, v114, v115
	v_add_f32_e32 v8, 0, v8
	v_add_f32_e32 v9, v9, v10
	v_add_f32_e32 v6, v6, v7
	v_add_f32_e32 v4, v4, v5
	v_add_f32_e32 v8, v9, v8
	v_add_f32_e32 v4, v6, v4
	v_add_f32_e32 v2, v2, v3
	v_add_f32_e32 v0, v0, v1
	v_add_f32_e32 v4, v4, v8
	v_add_f32_e32 v0, v2, v0
	v_add_f32_e32 v0, v0, v4
	s_nop 1
	v_add_f32_dpp v0, v0, v0 quad_perm:[1,0,3,2] row_mask:0xf bank_mask:0xf bound_ctrl:1
	s_nop 1
	v_add_f32_dpp v0, v0, v0 quad_perm:[2,3,0,1] row_mask:0xf bank_mask:0xf bound_ctrl:1
	s_nop 1
	v_add_f32_dpp v0, v0, v0 row_half_mirror row_mask:0xf bank_mask:0xf bound_ctrl:1
	s_nop 1
	v_add_f32_dpp v0, v0, v0 row_mirror row_mask:0xf bank_mask:0xf bound_ctrl:1
	v_mov_b32_e32 v1, v0
	s_nop 1
	v_permlane16_swap_b32_e32 v0, v1
	v_add_f32_e32 v0, v0, v1
	v_mov_b32_e32 v1, v0
	s_nop 1
	v_permlane32_swap_b32_e32 v0, v1
	v_add_f32_e32 v13, v0, v1
	v_fma_mix_f32 v15, v13, s58, v119 op_sel:[0,0,1] op_sel_hi:[0,0,1]
	v_fma_mix_f32 v37, v13, s58, v118 op_sel:[0,0,1] op_sel_hi:[0,0,1]
	v_fma_mix_f32 v14, v13, s58, v119 op_sel_hi:[0,0,1]
	v_fma_mix_f32 v36, v13, s58, v118 op_sel_hi:[0,0,1]
	v_mul_f32_e32 v0, v37, v37
	v_mul_f32_e32 v1, v15, v15
	v_fmac_f32_e32 v0, v36, v36
	v_fmac_f32_e32 v1, v14, v14
	v_fma_mix_f32 v9, v13, s58, v89 op_sel:[0,0,1] op_sel_hi:[0,0,1]
	v_fma_mix_f32 v11, v13, s58, v88 op_sel:[0,0,1] op_sel_hi:[0,0,1]
	v_add_f32_e32 v0, v0, v1
	v_fma_mix_f32 v8, v13, s58, v89 op_sel_hi:[0,0,1]
	v_fma_mix_f32 v10, v13, s58, v88 op_sel_hi:[0,0,1]
	v_mul_f32_e32 v1, v11, v11
	v_mul_f32_e32 v2, v9, v9
	v_fmac_f32_e32 v1, v10, v10
	v_fmac_f32_e32 v2, v8, v8
	v_add_f32_e32 v1, v1, v2
	v_fma_mix_f32 v5, v13, s58, v91 op_sel:[0,0,1] op_sel_hi:[0,0,1]
	v_fma_mix_f32 v7, v13, s58, v90 op_sel:[0,0,1] op_sel_hi:[0,0,1]
	v_add_f32_e32 v0, v0, v1
	v_fma_mix_f32 v4, v13, s58, v91 op_sel_hi:[0,0,1]
	v_fma_mix_f32 v6, v13, s58, v90 op_sel_hi:[0,0,1]
	v_mul_f32_e32 v1, v7, v7
	v_mul_f32_e32 v2, v5, v5
	v_fmac_f32_e32 v1, v6, v6
	v_fmac_f32_e32 v2, v4, v4
	v_add_f32_e32 v1, v1, v2
	v_add_f32_e32 v12, v1, v0
	v_fma_mix_f32 v1, v13, s58, v39 op_sel:[0,0,1] op_sel_hi:[0,0,1]
	v_fma_mix_f32 v3, v13, s58, v38 op_sel:[0,0,1] op_sel_hi:[0,0,1]
	v_fma_mix_f32 v0, v13, s58, v39 op_sel_hi:[0,0,1]
	v_fma_mix_f32 v2, v13, s58, v38 op_sel_hi:[0,0,1]
	v_mul_f32_e32 v92, v3, v3
	v_mul_f32_e32 v93, v1, v1
	v_fmac_f32_e32 v92, v2, v2
	v_fmac_f32_e32 v93, v0, v0
	v_add_f32_e32 v92, v92, v93
	v_add_f32_e32 v12, v92, v12
	s_nop 1
	v_add_f32_dpp v12, v12, v12 quad_perm:[1,0,3,2] row_mask:0xf bank_mask:0xf bound_ctrl:1
	s_nop 1
	v_add_f32_dpp v12, v12, v12 quad_perm:[2,3,0,1] row_mask:0xf bank_mask:0xf bound_ctrl:1
	s_nop 1
	v_add_f32_dpp v12, v12, v12 row_half_mirror row_mask:0xf bank_mask:0xf bound_ctrl:1
	s_nop 1
	v_add_f32_dpp v12, v12, v12 row_mirror row_mask:0xf bank_mask:0xf bound_ctrl:1
	v_mov_b32_e32 v92, v12
	s_nop 1
	v_permlane16_swap_b32_e32 v12, v92
	v_add_f32_e32 v12, v12, v92
	v_mov_b32_e32 v92, v12
	s_nop 1
	v_permlane32_swap_b32_e32 v12, v92
	v_add_f32_e32 v12, v12, v92
	v_fmamk_f32 v12, v12, 0x3a800000, v104
	v_mul_f32_e32 v92, 0x4f800000, v12
	v_cmp_gt_f32_e32 vcc, s59, v12
	s_nop 1
	v_cndmask_b32_e32 v12, v12, v92, vcc
	v_sqrt_f32_e32 v113, v12
	v_lshl_add_u64 v[92:93], v[82:83], 0, s[16:17]
	global_store_dwordx2 v[92:93], v[118:119], off
	global_store_dwordx2 v[92:93], v[88:89], off offset:512
	global_store_dwordx2 v[92:93], v[90:91], off offset:1024
	global_store_dwordx2 v[92:93], v[38:39], off offset:1536
	v_add_u32_e32 v114, -1, v113
	v_fma_f32 v115, -v114, v113, v12
	v_cmp_ge_f32_e64 s[16:17], 0, v115
	v_add_u32_e32 v115, 1, v113
	s_nop 0
	v_cndmask_b32_e64 v114, v113, v114, s[16:17]
	v_fma_f32 v113, -v115, v113, v12
	v_cmp_lt_f32_e64 s[16:17], 0, v113
	s_nop 1
	v_cndmask_b32_e64 v113, v114, v115, s[16:17]
	v_mul_f32_e32 v114, 0x37800000, v113
	v_cndmask_b32_e32 v113, v113, v114, vcc
	v_cmp_class_f32_e32 vcc, v12, v105
	s_nop 1
	v_cndmask_b32_e32 v12, v113, v12, vcc
	v_div_scale_f32 v113, s[16:17], v12, v12, 1.0
	v_rcp_f32_e32 v114, v113
	s_nop 0
	v_fma_f32 v38, -v113, v114, 1.0
	v_fmac_f32_e32 v114, v38, v114
	v_div_scale_f32 v38, vcc, 1.0, v12, 1.0
	v_mul_f32_e32 v39, v38, v114
	v_fma_f32 v88, -v113, v39, v38
	v_fmac_f32_e32 v39, v88, v114
	v_fma_f32 v38, -v113, v39, v38
	v_div_fmas_f32 v38, v38, v114, v39
	v_div_fixup_f32 v12, v38, v12, 1.0
	s_and_saveexec_b64 s[16:17], s[2:3]
	s_add_i32 s39, s42, s43
	v_mul_f32_e32 v38, 0x3a800000, v13
	v_mov_b32_e32 v39, v12
	v_mov_b32_e32 v13, s39
	ds_write_b64 v13, v[38:39] offset:24
	s_or_b64 exec, exec, s[16:17]
	ds_read_b128 v[88:91], v110 offset:12288
	ds_read_b128 v[114:117], v110 offset:16384
	v_mul_f32_e32 v14, v14, v12
	v_mul_f32_e32 v15, v15, v12
	v_mul_f32_e32 v36, v36, v12
	v_mul_f32_e32 v37, v37, v12
	v_mov_b32_e32 v92, 0
	s_lshl_b64 s[16:17], s[40:41], 10
	s_waitcnt lgkmcnt(0)
	v_fma_f32 v14, v14, v90, v116
	v_fma_f32 v15, v15, v91, v117
	v_fma_f32 v36, v36, v88, v114
	v_fma_f32 v37, v37, v89, v115
	s_add_i32 s43, s43, 8
	v_cvt_pk_bf16_f32 v13, v36, v37
	s_cmp_eq_u32 s43, 0
	v_cvt_pk_bf16_f32 v13, v14, v15
	v_mul_f32_e32 v14, 0x41800000, v14
	v_mul_f32_e32 v13, 0x41800000, v36
	v_mul_f32_e32 v36, 0x41800000, v37
	v_med3_f32 v13, v13, s60, v111
	v_med3_f32 v36, v36, s60, v111
	v_cvt_pk_fp8_f32 v92, v13, v36
	v_mul_f32_e32 v13, 0x41800000, v15
	ds_read_b128 v[36:39], v110 offset:13312
	ds_read_b128 v[88:91], v110 offset:17408
	v_med3_f32 v14, v14, s60, v111
	v_med3_f32 v13, v13, s60, v111
	v_cvt_pk_fp8_f32 v92, v14, v13 op_sel:[0,0,1]
	v_mul_f32_e32 v10, v10, v12
	v_mul_f32_e32 v11, v11, v12
	v_lshl_add_u64 v[14:15], v[86:87], 0, s[16:17]
	v_mul_f32_e32 v8, v8, v12
	v_mul_f32_e32 v9, v9, v12
	s_waitcnt lgkmcnt(0)
	v_fma_f32 v10, v10, v36, v88
	v_fma_f32 v11, v11, v37, v89
	global_store_dword v[14:15], v92, off
	v_fma_f32 v8, v8, v38, v90
	v_fma_f32 v9, v9, v39, v91
	v_cvt_pk_bf16_f32 v13, v10, v11
	v_mul_f32_e32 v10, 0x41800000, v10
	v_cvt_pk_bf16_f32 v13, v8, v9
	v_mul_f32_e32 v11, 0x41800000, v11
	v_med3_f32 v10, v10, s60, v111
	v_med3_f32 v11, v11, s60, v111
	v_mov_b32_e32 v13, 0
	v_cvt_pk_fp8_f32 v13, v10, v11
	v_mul_f32_e32 v8, 0x41800000, v8
	v_mul_f32_e32 v9, 0x41800000, v9
	v_med3_f32 v8, v8, s60, v111
	v_med3_f32 v9, v9, s60, v111
	v_cvt_pk_fp8_f32 v13, v8, v9 op_sel:[0,0,1]
	ds_read_b128 v[8:11], v110 offset:14336
	ds_read_b128 v[36:39], v110 offset:18432
	v_mul_f32_e32 v6, v6, v12
	v_mul_f32_e32 v7, v7, v12
	global_store_dword v[14:15], v13, off offset:256
	s_waitcnt lgkmcnt(0)
	v_fma_f32 v6, v6, v8, v36
	v_fma_f32 v7, v7, v9, v37
	v_mul_f32_e32 v4, v4, v12
	v_mul_f32_e32 v5, v5, v12
	v_cvt_pk_bf16_f32 v8, v6, v7
	v_mul_f32_e32 v6, 0x41800000, v6
	v_mul_f32_e32 v7, 0x41800000, v7
	v_med3_f32 v6, v6, s60, v111
	v_med3_f32 v7, v7, s60, v111
	v_mov_b32_e32 v13, 0
	v_cvt_pk_fp8_f32 v13, v6, v7
	v_fma_f32 v4, v4, v10, v38
	v_fma_f32 v5, v5, v11, v39
	s_nop 0
	v_cvt_pk_bf16_f32 v8, v4, v5
	v_mul_f32_e32 v4, 0x41800000, v4
	v_mul_f32_e32 v5, 0x41800000, v5
	v_med3_f32 v4, v4, s60, v111
	v_med3_f32 v5, v5, s60, v111
	v_cvt_pk_fp8_f32 v13, v4, v5 op_sel:[0,0,1]
	ds_read_b128 v[4:7], v110 offset:15360
	ds_read_b128 v[8:11], v110 offset:19456
	v_mul_f32_e32 v2, v2, v12
	v_mul_f32_e32 v3, v3, v12
	global_store_dword v[14:15], v13, off offset:512
	s_waitcnt lgkmcnt(0)
	v_fma_f32 v2, v2, v4, v8
	v_fma_f32 v3, v3, v5, v9
	v_mov_b32_e32 v5, 0
	v_cvt_pk_bf16_f32 v4, v2, v3
	v_mul_f32_e32 v2, 0x41800000, v2
	v_mul_f32_e32 v3, 0x41800000, v3
	v_med3_f32 v2, v2, s60, v111
	v_med3_f32 v3, v3, s60, v111
	v_mul_f32_e32 v0, v0, v12
	v_mul_f32_e32 v1, v1, v12
	v_cvt_pk_fp8_f32 v5, v2, v3
	v_fma_f32 v0, v0, v6, v10
	v_fma_f32 v1, v1, v7, v11
	s_nop 0
	v_mul_f32_e32 v4, 0x41800000, v0
	v_mul_f32_e32 v2, 0x41800000, v1
	v_med3_f32 v3, v4, s60, v111
	v_med3_f32 v2, v2, s60, v111
	v_cvt_pk_fp8_f32 v5, v3, v2 op_sel:[0,0,1]
	v_cvt_pk_bf16_f32 v0, v0, v1
	global_store_dword v[14:15], v5, off offset:768
	s_cbranch_scc1 .LBB0_1470
	s_waitcnt vmcnt(15)
	v_mov_b64_e32 v[0:1], v[34:35]
	s_branch .LBB0_1466

.LBB0_1472:
	v_cvt_f32_f16_sdwa v117, v24 dst_sel:DWORD dst_unused:UNUSED_PAD src0_sel:WORD_1
	v_cvt_f32_f16_sdwa v119, v25 dst_sel:DWORD dst_unused:UNUSED_PAD src0_sel:WORD_1
	v_cvt_f32_f16_e32 v116, v24
	v_cvt_f32_f16_e32 v118, v25
	v_lshlrev_b32_e32 v122, 16, v22
	v_and_b32_e32 v123, 0xffff0000, v22
	v_lshlrev_b32_e32 v124, 16, v23
	v_and_b32_e32 v125, 0xffff0000, v23
	ds_read_b128 v[22:25], v110
	v_cvt_f32_f16_sdwa v37, v34 dst_sel:DWORD dst_unused:UNUSED_PAD src0_sel:WORD_1
	v_cvt_f32_f16_sdwa v39, v35 dst_sel:DWORD dst_unused:UNUSED_PAD src0_sel:WORD_1
	v_cvt_f32_f16_e32 v36, v34
	v_cvt_f32_f16_e32 v38, v35
	v_cvt_f32_f16_sdwa v89, v32 dst_sel:DWORD dst_unused:UNUSED_PAD src0_sel:WORD_1
	v_cvt_f32_f16_sdwa v91, v33 dst_sel:DWORD dst_unused:UNUSED_PAD src0_sel:WORD_1
	v_cvt_f32_f16_e32 v88, v32
	v_cvt_f32_f16_e32 v90, v33
	v_cvt_f32_f16_sdwa v93, v28 dst_sel:DWORD dst_unused:UNUSED_PAD src0_sel:WORD_1
	v_cvt_f32_f16_sdwa v115, v29 dst_sel:DWORD dst_unused:UNUSED_PAD src0_sel:WORD_1
	v_cvt_f32_f16_e32 v92, v28
	v_cvt_f32_f16_e32 v114, v29
	v_lshlrev_b32_e32 v28, 16, v30
	v_and_b32_e32 v29, 0xffff0000, v30
	v_lshlrev_b32_e32 v30, 16, v31
	v_and_b32_e32 v31, 0xffff0000, v31
	ds_read_b128 v[32:35], v110 offset:1024
	v_lshlrev_b32_e32 v126, 16, v20
	v_and_b32_e32 v127, 0xffff0000, v20
	v_lshlrev_b32_e32 v128, 16, v21
	v_and_b32_e32 v129, 0xffff0000, v21
	s_waitcnt lgkmcnt(1)
	v_mul_f32_e32 v20, v24, v30
	v_mul_f32_e32 v21, v25, v31
	v_mul_f32_e32 v22, v22, v28
	v_mul_f32_e32 v23, v23, v29
	v_fma_f32 v30, v38, s34, v20
	v_fma_f32 v31, v39, s34, v21
	v_fma_f32 v28, v36, s34, v22
	v_fma_f32 v29, v37, s34, v23
	v_add_f32_e32 v21, v30, v31
	v_add_f32_e32 v20, v28, v29
	v_lshlrev_b32_e32 v120, 16, v26
	v_and_b32_e32 v121, 0xffff0000, v26
	v_lshlrev_b32_e32 v26, 16, v27
	v_and_b32_e32 v27, 0xffff0000, v27
	v_add_f32_e32 v20, v20, v21
	v_add_f32_e32 v36, 0, v20
	s_waitcnt lgkmcnt(0)
	v_mul_f32_e32 v20, v34, v26
	v_mul_f32_e32 v21, v35, v27
	v_mul_f32_e32 v24, v32, v120
	v_mul_f32_e32 v25, v33, v121
	v_fma_f32 v22, v90, s34, v20
	v_fma_f32 v23, v91, s34, v21
	v_fma_f32 v20, v88, s34, v24
	v_fma_f32 v21, v89, s34, v25
	ds_read_b128 v[24:27], v110 offset:2048
	v_add_f32_e32 v32, v20, v21
	v_add_f32_e32 v33, v22, v23
	v_add_f32_e32 v32, v32, v33
	v_add_f32_e32 v88, v36, v32
	ds_read_b128 v[36:39], v110 offset:3072
	s_waitcnt lgkmcnt(1)
	v_mul_f32_e32 v26, v26, v124
	v_mul_f32_e32 v27, v27, v125
	v_mul_f32_e32 v24, v24, v122
	v_mul_f32_e32 v25, v25, v123
	v_fma_f32 v34, v114, s34, v26
	v_fma_f32 v35, v115, s34, v27
	v_fma_f32 v32, v92, s34, v24
	v_fma_f32 v33, v93, s34, v25
	v_add_f32_e32 v25, v34, v35
	v_add_f32_e32 v24, v32, v33
	v_add_f32_e32 v24, v24, v25
	v_add_f32_e32 v88, v88, v24
	s_waitcnt lgkmcnt(0)
	v_mul_f32_e32 v24, v38, v128
	v_mul_f32_e32 v25, v39, v129
	v_mul_f32_e32 v36, v36, v126
	v_mul_f32_e32 v37, v37, v127
	v_fma_f32 v26, v118, s34, v24
	v_fma_f32 v27, v119, s34, v25
	v_fma_f32 v24, v116, s34, v36
	v_fma_f32 v25, v117, s34, v37
	v_add_f32_e32 v37, v26, v27
	v_add_f32_e32 v36, v24, v25
	v_add_f32_e32 v36, v36, v37
	v_add_f32_e32 v36, v88, v36
	s_add_i32 s33, s33, s53
	s_add_i32 s36, s33, s67
	v_add_f32_dpp v36, v36, v36 quad_perm:[1,0,3,2] row_mask:0xf bank_mask:0xf bound_ctrl:1
	s_ashr_i32 s37, s36, 31
	s_nop 0
	v_add_f32_dpp v36, v36, v36 quad_perm:[2,3,0,1] row_mask:0xf bank_mask:0xf bound_ctrl:1
	s_nop 1
	v_add_f32_dpp v36, v36, v36 row_half_mirror row_mask:0xf bank_mask:0xf bound_ctrl:1
	s_nop 1
	v_add_f32_dpp v36, v36, v36 row_mirror row_mask:0xf bank_mask:0xf bound_ctrl:1
	v_mov_b32_e32 v37, v36
	s_nop 1
	v_permlane16_swap_b32_e32 v36, v37
	v_add_f32_e32 v36, v36, v37
	v_mov_b32_e32 v37, v36
	s_nop 1
	v_permlane32_swap_b32_e32 v36, v37
	v_add_f32_e32 v36, v36, v37
	v_fmac_f32_e32 v31, 0xba800000, v36
	v_fmac_f32_e32 v29, 0xba800000, v36
	v_fmamk_f32 v30, v36, 0xba800000, v30
	v_fmamk_f32 v28, v36, 0xba800000, v28
	v_mul_f32_e32 v37, v29, v29
	v_mul_f32_e32 v38, v31, v31
	v_fmac_f32_e32 v37, v28, v28
	v_fmac_f32_e32 v38, v30, v30
	v_fmac_f32_e32 v23, 0xba800000, v36
	v_fmac_f32_e32 v21, 0xba800000, v36
	v_add_f32_e32 v37, v37, v38
	v_fmamk_f32 v22, v36, 0xba800000, v22
	v_fmamk_f32 v20, v36, 0xba800000, v20
	v_mul_f32_e32 v38, v21, v21
	v_mul_f32_e32 v39, v23, v23
	v_fmac_f32_e32 v38, v20, v20
	v_fmac_f32_e32 v39, v22, v22
	v_add_f32_e32 v38, v38, v39
	v_fmac_f32_e32 v35, 0xba800000, v36
	v_fmac_f32_e32 v33, 0xba800000, v36
	v_add_f32_e32 v37, v37, v38
	v_fmamk_f32 v34, v36, 0xba800000, v34
	v_fmamk_f32 v32, v36, 0xba800000, v32
	v_mul_f32_e32 v38, v33, v33
	v_mul_f32_e32 v39, v35, v35
	v_fmac_f32_e32 v38, v32, v32
	v_fmac_f32_e32 v39, v34, v34
	v_add_f32_e32 v38, v38, v39
	v_fmac_f32_e32 v27, 0xba800000, v36
	v_fmac_f32_e32 v25, 0xba800000, v36
	v_add_f32_e32 v37, v38, v37
	v_fmamk_f32 v26, v36, 0xba800000, v26
	v_fmamk_f32 v24, v36, 0xba800000, v24
	v_mul_f32_e32 v36, v25, v25
	v_mul_f32_e32 v38, v27, v27
	v_fmac_f32_e32 v36, v24, v24
	v_fmac_f32_e32 v38, v26, v26
	v_add_f32_e32 v36, v36, v38
	v_add_f32_e32 v36, v36, v37
	s_nop 1
	v_add_f32_dpp v36, v36, v36 quad_perm:[1,0,3,2] row_mask:0xf bank_mask:0xf bound_ctrl:1
	s_nop 1
	v_add_f32_dpp v36, v36, v36 quad_perm:[2,3,0,1] row_mask:0xf bank_mask:0xf bound_ctrl:1
	s_nop 1
	v_add_f32_dpp v36, v36, v36 row_half_mirror row_mask:0xf bank_mask:0xf bound_ctrl:1
	s_nop 1
	v_add_f32_dpp v36, v36, v36 row_mirror row_mask:0xf bank_mask:0xf bound_ctrl:1
	v_mov_b32_e32 v37, v36
	s_nop 1
	v_permlane16_swap_b32_e32 v36, v37
	v_add_f32_e32 v36, v36, v37
	v_mov_b32_e32 v37, v36
	s_nop 1
	v_permlane32_swap_b32_e32 v36, v37
	v_add_f32_e32 v36, v36, v37
	v_fmamk_f32 v36, v36, 0x3a800000, v104
	v_mul_f32_e32 v37, 0x4f800000, v36
	v_cmp_gt_f32_e32 vcc, s59, v36
	s_nop 1
	v_cndmask_b32_e32 v36, v36, v37, vcc
	v_sqrt_f32_e32 v37, v36
	s_nop 0
	v_add_u32_e32 v38, -1, v37
	v_fma_f32 v39, -v38, v37, v36
	v_cmp_ge_f32_e64 s[16:17], 0, v39
	v_add_u32_e32 v39, 1, v37
	s_nop 0
	v_cndmask_b32_e64 v38, v37, v38, s[16:17]
	v_fma_f32 v37, -v39, v37, v36
	v_cmp_lt_f32_e64 s[16:17], 0, v37
	s_nop 1
	v_cndmask_b32_e64 v37, v38, v39, s[16:17]
	v_mul_f32_e32 v38, 0x37800000, v37
	v_cndmask_b32_e32 v37, v37, v38, vcc
	v_cmp_class_f32_e32 vcc, v36, v105
	s_nop 1
	v_cndmask_b32_e32 v36, v37, v36, vcc
	v_div_scale_f32 v37, s[16:17], v36, v36, 1.0
	v_rcp_f32_e32 v38, v37
	s_lshl_b64 s[16:17], s[36:37], 11
	v_fma_f32 v39, -v37, v38, 1.0
	v_fmac_f32_e32 v38, v39, v38
	v_div_scale_f32 v39, vcc, 1.0, v36, 1.0
	v_mul_f32_e32 v88, v39, v38
	v_fma_f32 v89, -v37, v88, v39
	v_fmac_f32_e32 v88, v89, v38
	v_fma_f32 v37, -v37, v88, v39
	v_div_fmas_f32 v37, v37, v38, v88
	v_div_fixup_f32 v92, v37, v36, 1.0
	ds_read_b128 v[36:39], v110 offset:4096
	ds_read_b128 v[88:91], v110 offset:8192
	v_mul_f32_e32 v118, v30, v92
	v_mul_f32_e32 v119, v31, v92
	v_mul_f32_e32 v120, v28, v92
	v_mul_f32_e32 v121, v29, v92
	ds_read_b128 v[28:31], v110 offset:5120
	ds_read_b128 v[114:117], v110 offset:9216
	s_waitcnt lgkmcnt(2)
	v_fma_f32 v38, v38, v118, v90
	v_fma_f32 v39, v39, v119, v91
	v_fma_f32 v36, v36, v120, v88
	v_fma_f32 v37, v37, v121, v89
	v_cvt_pk_f16_f32 v89, v38, v39
	v_cvt_f32_f16_e32 v93, v89
	v_cvt_pk_f16_f32 v88, v36, v37
	v_cvt_f32_f16_sdwa v113, v89 dst_sel:DWORD dst_unused:UNUSED_PAD src0_sel:WORD_1
	v_cvt_f32_f16_e32 v118, v88
	v_mul_f32_e32 v22, v22, v92
	v_mul_f32_e32 v23, v23, v92
	v_mul_f32_e32 v20, v20, v92
	v_mul_f32_e32 v21, v21, v92
	s_waitcnt lgkmcnt(0)
	v_fma_f32 v22, v30, v22, v116
	v_fma_f32 v23, v31, v23, v117
	v_fma_f32 v20, v28, v20, v114
	v_fma_f32 v21, v29, v21, v115
	v_cvt_pk_f16_f32 v91, v22, v23
	v_cvt_pk_f16_f32 v90, v20, v21
	ds_read_b128 v[20:23], v110 offset:6144
	ds_read_b128 v[28:31], v110 offset:10240
	v_mul_f32_e32 v114, v34, v92
	v_mul_f32_e32 v115, v35, v92
	v_mul_f32_e32 v116, v32, v92
	v_mul_f32_e32 v117, v33, v92
	ds_read_b128 v[32:35], v110 offset:7168
	ds_read_b128 v[36:39], v110 offset:11264
	v_cvt_f32_f16_sdwa v119, v88 dst_sel:DWORD dst_unused:UNUSED_PAD src0_sel:WORD_1
	s_waitcnt lgkmcnt(2)
	v_fma_f32 v20, v20, v116, v28
	v_fma_f32 v21, v21, v117, v29
	v_fma_f32 v22, v22, v114, v30
	v_fma_f32 v23, v23, v115, v31
	v_cvt_f32_f16_e32 v120, v91
	v_cvt_f32_f16_sdwa v121, v91 dst_sel:DWORD dst_unused:UNUSED_PAD src0_sel:WORD_1
	v_cvt_f32_f16_e32 v122, v90
	v_cvt_f32_f16_sdwa v123, v90 dst_sel:DWORD dst_unused:UNUSED_PAD src0_sel:WORD_1
	v_cvt_pk_f16_f32 v115, v22, v23
	v_cvt_pk_f16_f32 v114, v20, v21
	v_mul_f32_e32 v20, v26, v92
	v_mul_f32_e32 v21, v27, v92
	v_mul_f32_e32 v22, v24, v92
	v_mul_f32_e32 v23, v25, v92
	s_waitcnt lgkmcnt(0)
	v_fma_f32 v20, v20, v34, v38
	v_fma_f32 v21, v21, v35, v39
	v_fma_f32 v22, v22, v32, v36
	v_fma_f32 v23, v23, v33, v37
	v_cvt_f32_f16_e32 v28, v115
	v_cvt_f32_f16_sdwa v29, v115 dst_sel:DWORD dst_unused:UNUSED_PAD src0_sel:WORD_1
	v_cvt_f32_f16_e32 v30, v114
	v_cvt_f32_f16_sdwa v31, v114 dst_sel:DWORD dst_unused:UNUSED_PAD src0_sel:WORD_1
	v_cvt_pk_f16_f32 v39, v20, v21
	v_cvt_pk_f16_f32 v38, v22, v23
	v_cvt_f32_f16_e32 v20, v39
	v_cvt_f32_f16_sdwa v21, v39 dst_sel:DWORD dst_unused:UNUSED_PAD src0_sel:WORD_1
	v_cvt_f32_f16_e32 v22, v38
	v_cvt_f32_f16_sdwa v23, v38 dst_sel:DWORD dst_unused:UNUSED_PAD src0_sel:WORD_1
	v_add_f32_e32 v24, v118, v119
	v_add_f32_e32 v25, v93, v113
	v_add_f32_e32 v24, v24, v25
	v_add_f32_e32 v25, v122, v123
	v_add_f32_e32 v26, v120, v121
	v_add_f32_e32 v24, 0, v24
	v_add_f32_e32 v25, v25, v26
	v_add_f32_e32 v24, v25, v24
	v_add_f32_e32 v25, v30, v31
	v_add_f32_e32 v26, v28, v29
	v_add_f32_e32 v25, v25, v26
	v_add_f32_e32 v22, v22, v23
	v_add_f32_e32 v20, v20, v21
	v_add_f32_e32 v24, v25, v24
	v_add_f32_e32 v20, v22, v20
	v_add_f32_e32 v20, v20, v24
	s_nop 1
	v_add_f32_dpp v20, v20, v20 quad_perm:[1,0,3,2] row_mask:0xf bank_mask:0xf bound_ctrl:1
	s_nop 1
	v_add_f32_dpp v20, v20, v20 quad_perm:[2,3,0,1] row_mask:0xf bank_mask:0xf bound_ctrl:1
	s_nop 1
	v_add_f32_dpp v20, v20, v20 row_half_mirror row_mask:0xf bank_mask:0xf bound_ctrl:1
	s_nop 1
	v_add_f32_dpp v20, v20, v20 row_mirror row_mask:0xf bank_mask:0xf bound_ctrl:1
	v_mov_b32_e32 v21, v20
	s_nop 1
	v_permlane16_swap_b32_e32 v20, v21
	v_add_f32_e32 v20, v20, v21
	v_mov_b32_e32 v21, v20
	s_nop 1
	v_permlane32_swap_b32_e32 v20, v21
	v_add_f32_e32 v37, v20, v21
	v_fma_mix_f32 v33, v37, s58, v89 op_sel:[0,0,1] op_sel_hi:[0,0,1]
	v_fma_mix_f32 v35, v37, s58, v88 op_sel:[0,0,1] op_sel_hi:[0,0,1]
	v_fma_mix_f32 v32, v37, s58, v89 op_sel_hi:[0,0,1]
	v_fma_mix_f32 v34, v37, s58, v88 op_sel_hi:[0,0,1]
	v_mul_f32_e32 v20, v35, v35
	v_mul_f32_e32 v21, v33, v33
	v_fmac_f32_e32 v20, v34, v34
	v_fmac_f32_e32 v21, v32, v32
	v_fma_mix_f32 v29, v37, s58, v91 op_sel:[0,0,1] op_sel_hi:[0,0,1]
	v_fma_mix_f32 v31, v37, s58, v90 op_sel:[0,0,1] op_sel_hi:[0,0,1]
	v_add_f32_e32 v20, v20, v21
	v_fma_mix_f32 v28, v37, s58, v91 op_sel_hi:[0,0,1]
	v_fma_mix_f32 v30, v37, s58, v90 op_sel_hi:[0,0,1]
	v_mul_f32_e32 v21, v31, v31
	v_mul_f32_e32 v22, v29, v29
	v_fmac_f32_e32 v21, v30, v30
	v_fmac_f32_e32 v22, v28, v28
	v_add_f32_e32 v21, v21, v22
	v_fma_mix_f32 v25, v37, s58, v115 op_sel:[0,0,1] op_sel_hi:[0,0,1]
	v_fma_mix_f32 v27, v37, s58, v114 op_sel:[0,0,1] op_sel_hi:[0,0,1]
	v_add_f32_e32 v20, v20, v21
	v_fma_mix_f32 v24, v37, s58, v115 op_sel_hi:[0,0,1]
	v_fma_mix_f32 v26, v37, s58, v114 op_sel_hi:[0,0,1]
	v_mul_f32_e32 v21, v27, v27
	v_mul_f32_e32 v22, v25, v25
	v_fmac_f32_e32 v21, v26, v26
	v_fmac_f32_e32 v22, v24, v24
	v_add_f32_e32 v21, v21, v22
	v_add_f32_e32 v36, v21, v20
	v_fma_mix_f32 v21, v37, s58, v39 op_sel:[0,0,1] op_sel_hi:[0,0,1]
	v_fma_mix_f32 v23, v37, s58, v38 op_sel:[0,0,1] op_sel_hi:[0,0,1]
	v_fma_mix_f32 v20, v37, s58, v39 op_sel_hi:[0,0,1]
	v_fma_mix_f32 v22, v37, s58, v38 op_sel_hi:[0,0,1]
	v_mul_f32_e32 v92, v23, v23
	v_mul_f32_e32 v93, v21, v21
	v_fmac_f32_e32 v92, v22, v22
	v_fmac_f32_e32 v93, v20, v20
	v_add_f32_e32 v92, v92, v93
	v_add_f32_e32 v36, v92, v36
	s_nop 1
	v_add_f32_dpp v36, v36, v36 quad_perm:[1,0,3,2] row_mask:0xf bank_mask:0xf bound_ctrl:1
	s_nop 1
	v_add_f32_dpp v36, v36, v36 quad_perm:[2,3,0,1] row_mask:0xf bank_mask:0xf bound_ctrl:1
	s_nop 1
	v_add_f32_dpp v36, v36, v36 row_half_mirror row_mask:0xf bank_mask:0xf bound_ctrl:1
	s_nop 1
	v_add_f32_dpp v36, v36, v36 row_mirror row_mask:0xf bank_mask:0xf bound_ctrl:1
	v_mov_b32_e32 v92, v36
	s_nop 1
	v_permlane16_swap_b32_e32 v36, v92
	v_add_f32_e32 v36, v36, v92
	v_mov_b32_e32 v92, v36
	s_nop 1
	v_permlane32_swap_b32_e32 v36, v92
	v_add_f32_e32 v36, v36, v92
	v_fmamk_f32 v36, v36, 0x3a800000, v104
	v_mul_f32_e32 v92, 0x4f800000, v36
	v_cmp_gt_f32_e32 vcc, s59, v36
	s_nop 1
	v_cndmask_b32_e32 v36, v36, v92, vcc
	v_sqrt_f32_e32 v113, v36
	v_lshl_add_u64 v[92:93], v[82:83], 0, s[16:17]
	global_store_dwordx2 v[92:93], v[88:89], off
	global_store_dwordx2 v[92:93], v[90:91], off offset:512
	global_store_dwordx2 v[92:93], v[114:115], off offset:1024
	global_store_dwordx2 v[92:93], v[38:39], off offset:1536
	v_add_u32_e32 v88, -1, v113
	v_fma_f32 v89, -v88, v113, v36
	v_cmp_ge_f32_e64 s[16:17], 0, v89
	v_add_u32_e32 v89, 1, v113
	s_nop 0
	v_cndmask_b32_e64 v88, v113, v88, s[16:17]
	v_fma_f32 v113, -v89, v113, v36
	v_cmp_lt_f32_e64 s[16:17], 0, v113
	s_nop 1
	v_cndmask_b32_e64 v88, v88, v89, s[16:17]
	v_mul_f32_e32 v89, 0x37800000, v88
	v_cndmask_b32_e32 v88, v88, v89, vcc
	v_cmp_class_f32_e32 vcc, v36, v105
	s_nop 1
	v_cndmask_b32_e32 v36, v88, v36, vcc
	v_div_scale_f32 v88, s[16:17], v36, v36, 1.0
	v_rcp_f32_e32 v89, v88
	s_nop 0
	v_fma_f32 v38, -v88, v89, 1.0
	v_fmac_f32_e32 v89, v38, v89
	v_div_scale_f32 v38, vcc, 1.0, v36, 1.0
	v_mul_f32_e32 v39, v38, v89
	v_fma_f32 v90, -v88, v39, v38
	v_fmac_f32_e32 v39, v90, v89
	v_fma_f32 v38, -v88, v39, v38
	v_div_fmas_f32 v38, v38, v89, v39
	v_div_fixup_f32 v36, v38, v36, 1.0
	s_and_saveexec_b64 s[16:17], s[2:3]
	s_cbranch_execz .LBB0_1464
	s_lshl_b32 s33, s33, 3
	s_add_i32 s33, s33, 0
	v_mul_f32_e32 v38, 0x3a800000, v37
	v_mov_b32_e32 v39, v36
	v_mov_b32_e32 v37, s33
	ds_write_b64 v37, v[38:39] offset:20480
	s_branch .LBB0_1464
.LBB0_1474:
	s_waitcnt vmcnt(0)
	s_barrier
	s_waitcnt vmcnt(0)
	buffer_inv sc1
	s_waitcnt vmcnt(0)
	s_and_saveexec_b64 s[16:17], s[4:5]
	ds_write_b32 v95, v45 offset:58624
	s_or_b64 exec, exec, s[16:17]
	v_add_u32_e32 v0, s67, v42
	v_ashrrev_i32_e32 v1, 31, v0
	v_lshlrev_b64 v[0:1], 11, v[0:1]
	v_lshl_add_u64 v[92:93], v[46:47], 0, v[0:1]
	global_load_dwordx4 v[30:33], v[92:93], off
	global_load_dwordx4 v[34:37], v[48:49], off
	global_load_dwordx4 v[20:23], v[52:53], off
	global_load_dwordx4 v[24:27], v[92:93], off offset:128
	ds_read_b64 v[38:39], v106 offset:20480
	ds_read_b128 v[116:119], v43 offset:12288
	ds_read_b128 v[120:123], v43 offset:12304
	ds_read_b128 v[124:127], v43 offset:16384
	ds_read_b128 v[128:131], v43 offset:16400
	v_add_u32_e32 v114, 0x6000, v97
	v_mov_b32_e32 v4, 0
	s_waitcnt lgkmcnt(4)
	v_mov_b32_e32 v0, v38
	v_mov_b32_e32 v1, v38
	v_mov_b32_e32 v2, v38
	v_mov_b32_e32 v3, v38
	v_mov_b32_e32 v88, v39
	v_mov_b32_e32 v89, v39
	v_mov_b32_e32 v90, v39
	v_mov_b32_e32 v91, v39
	v_add_u32_e32 v113, 0x6400, v97
	s_mov_b32 s16, 0
	v_mov_b32_e32 v28, v103
	v_mov_b32_e32 v5, v4
	v_mov_b32_e32 v6, v4
	v_mov_b32_e32 v7, v4
	v_mov_b32_e32 v8, v4
	v_mov_b32_e32 v9, v4
	v_mov_b32_e32 v10, v4
	v_mov_b32_e32 v11, v4
	v_mov_b32_e32 v12, v4
	v_mov_b32_e32 v13, v4
	v_mov_b32_e32 v14, v4
	v_mov_b32_e32 v15, v4
	v_mov_b32_e32 v16, v4
	v_mov_b32_e32 v17, v4
	v_mov_b32_e32 v18, v4
	s_waitcnt vmcnt(3)
	v_cvt_f32_f16_sdwa v19, v31 dst_sel:DWORD dst_unused:UNUSED_PAD src0_sel:WORD_1
	v_cvt_f32_f16_e32 v29, v31
	v_cvt_f32_f16_sdwa v31, v30 dst_sel:DWORD dst_unused:UNUSED_PAD src0_sel:WORD_1
	v_cvt_f32_f16_e32 v30, v30
	v_cvt_f32_f16_sdwa v115, v33 dst_sel:DWORD dst_unused:UNUSED_PAD src0_sel:WORD_1
	v_cvt_f32_f16_e32 v134, v33
	v_cvt_f32_f16_sdwa v133, v32 dst_sel:DWORD dst_unused:UNUSED_PAD src0_sel:WORD_1
	v_cvt_f32_f16_e32 v132, v32
	v_sub_f32_e32 v30, v30, v38
	v_sub_f32_e32 v31, v31, v38
	v_sub_f32_e32 v32, v29, v38
	v_sub_f32_e32 v33, v19, v38
	v_sub_f32_e32 v132, v132, v38
	v_sub_f32_e32 v133, v133, v38
	v_sub_f32_e32 v134, v134, v38
	v_sub_f32_e32 v135, v115, v38
	v_mul_f32_e32 v30, v39, v30
	v_mul_f32_e32 v31, v39, v31
	v_mul_f32_e32 v32, v39, v32
	v_mul_f32_e32 v33, v39, v33
	v_mul_f32_e32 v134, v39, v134
	v_mul_f32_e32 v135, v39, v135
	v_mul_f32_e32 v38, v39, v132
	v_mul_f32_e32 v39, v39, v133
	s_waitcnt lgkmcnt(1)
	v_fma_f32 v19, v116, v30, v124
	v_fma_f32 v30, v117, v31, v125
	s_waitcnt lgkmcnt(0)
	v_fma_f32 v29, v120, v38, v128
	v_fma_f32 v31, v121, v39, v129
	v_fma_f32 v32, v118, v32, v126
	v_fma_f32 v38, v122, v134, v130
	v_fmac_f32_e32 v127, v119, v33
	v_fmac_f32_e32 v131, v123, v135
	ds_write2_b32 v114, v19, v30 offset1:68
	ds_write2_b32 v113, v29, v31 offset0:16 offset1:84
	ds_write2_b32 v114, v32, v127 offset0:136 offset1:204
	ds_write2_b32 v113, v38, v131 offset0:152 offset1:220
	s_waitcnt vmcnt(2)
	ds_write_b128 v96, v[34:37] offset:41984
	v_mov_b32_e32 v19, v4
	s_waitcnt lgkmcnt(0)
	s_barrier
.LBB0_1477:
	v_add_u32_e32 v29, s16, v44
	ds_read_b128 v[30:33], v28
	ds_read_b128 v[34:37], v28 offset:272
	ds_read_b128 v[116:119], v28 offset:544
	ds_read_b128 v[120:123], v28 offset:816
	ds_read_b128 v[124:127], v29
	ds_read_b128 v[128:131], v29 offset:128
	ds_read_b128 v[132:135], v29 offset:256
	ds_read_b128 v[136:139], v29 offset:384
	s_waitcnt lgkmcnt(7)
	v_mov_b32_e32 v38, v33
	s_waitcnt lgkmcnt(6)
	v_mov_b32_e32 v140, v37
	s_waitcnt lgkmcnt(3)
	v_fmac_f32_e32 v16, v124, v30
	v_fmac_f32_e32 v17, v125, v30
	v_fmac_f32_e32 v18, v126, v30
	v_fmac_f32_e32 v19, v127, v30
	v_fmac_f32_e32 v12, v124, v31
	v_fmac_f32_e32 v13, v125, v31
	v_fmac_f32_e32 v14, v126, v31
	v_fmac_f32_e32 v15, v127, v31
	v_fmac_f32_e32 v8, v124, v32
	v_fmac_f32_e32 v9, v125, v32
	v_fmac_f32_e32 v10, v126, v32
	v_fmac_f32_e32 v11, v127, v32
	v_fmac_f32_e32 v4, v124, v38
	v_fmac_f32_e32 v5, v125, v38
	v_fmac_f32_e32 v6, v126, v38
	v_fmac_f32_e32 v7, v127, v38
	v_mov_b32_e32 v142, v119
	s_waitcnt lgkmcnt(2)
	v_fmac_f32_e32 v18, v130, v34
	v_fmac_f32_e32 v19, v131, v34
	v_fmac_f32_e32 v16, v128, v34
	v_fmac_f32_e32 v17, v129, v34
	v_fmac_f32_e32 v14, v130, v35
	v_fmac_f32_e32 v15, v131, v35
	v_fmac_f32_e32 v12, v128, v35
	v_fmac_f32_e32 v13, v129, v35
	v_fmac_f32_e32 v10, v130, v36
	v_fmac_f32_e32 v11, v131, v36
	v_fmac_f32_e32 v8, v128, v36
	v_fmac_f32_e32 v9, v129, v36
	v_fmac_f32_e32 v6, v130, v140
	v_fmac_f32_e32 v7, v131, v140
	v_fmac_f32_e32 v4, v128, v140
	v_fmac_f32_e32 v5, v129, v140
	s_addk_i32 s16, 0x200
	v_mov_b32_e32 v144, v123
	s_waitcnt lgkmcnt(1)
	v_fmac_f32_e32 v18, v134, v116
	v_fmac_f32_e32 v19, v135, v116
	v_fmac_f32_e32 v16, v132, v116
	v_fmac_f32_e32 v17, v133, v116
	v_fmac_f32_e32 v14, v134, v117
	v_fmac_f32_e32 v15, v135, v117
	v_fmac_f32_e32 v12, v132, v117
	v_fmac_f32_e32 v13, v133, v117
	v_fmac_f32_e32 v8, v132, v118
	v_fmac_f32_e32 v9, v133, v118
	v_fmac_f32_e32 v10, v134, v118
	v_fmac_f32_e32 v11, v135, v118
	v_fmac_f32_e32 v4, v132, v142
	v_fmac_f32_e32 v5, v133, v142
	v_fmac_f32_e32 v6, v134, v142
	v_fmac_f32_e32 v7, v135, v142
	v_add_u32_e32 v28, 0x440, v28
	s_cmpk_eq_i32 s16, 0x800
	s_waitcnt lgkmcnt(0)
	v_fmac_f32_e32 v18, v138, v120
	v_fmac_f32_e32 v19, v139, v120
	v_fmac_f32_e32 v16, v136, v120
	v_fmac_f32_e32 v17, v137, v120
	v_fmac_f32_e32 v14, v138, v121
	v_fmac_f32_e32 v15, v139, v121
	v_fmac_f32_e32 v12, v136, v121
	v_fmac_f32_e32 v13, v137, v121
	v_fmac_f32_e32 v10, v138, v122
	v_fmac_f32_e32 v11, v139, v122
	v_fmac_f32_e32 v8, v136, v122
	v_fmac_f32_e32 v9, v137, v122
	v_fmac_f32_e32 v6, v138, v144
	v_fmac_f32_e32 v7, v139, v144
	v_fmac_f32_e32 v4, v136, v144
	v_fmac_f32_e32 v5, v137, v144
	s_cbranch_scc0 .LBB0_1477
	s_barrier
	global_load_dwordx4 v[32:35], v[92:93], off offset:256
	global_load_dwordx4 v[28:31], v[54:55], off
	s_waitcnt vmcnt(2)
	v_cvt_f32_f16_sdwa v128, v24 dst_sel:DWORD dst_unused:UNUSED_PAD src0_sel:WORD_1
	v_cvt_f32_f16_e32 v24, v24
	v_cvt_f32_f16_e32 v129, v25
	v_cvt_f32_f16_sdwa v130, v26 dst_sel:DWORD dst_unused:UNUSED_PAD src0_sel:WORD_1
	v_cvt_f32_f16_e32 v133, v26
	ds_read_b128 v[36:39], v43 offset:12544
	ds_read_b128 v[116:119], v43 offset:12560
	ds_read_b128 v[120:123], v43 offset:16640
	ds_read_b128 v[124:127], v43 offset:16656
	v_cvt_f32_f16_sdwa v115, v25 dst_sel:DWORD dst_unused:UNUSED_PAD src0_sel:WORD_1
	v_cvt_f32_f16_sdwa v131, v27 dst_sel:DWORD dst_unused:UNUSED_PAD src0_sel:WORD_1
	v_cvt_f32_f16_e32 v132, v27
	v_sub_f32_e32 v24, v24, v0
	v_sub_f32_e32 v25, v128, v1
	v_sub_f32_e32 v26, v129, v2
	v_mul_f32_e32 v24, v88, v24
	v_mul_f32_e32 v25, v89, v25
	v_sub_f32_e32 v128, v133, v0
	v_sub_f32_e32 v129, v130, v1
	v_sub_f32_e32 v27, v115, v3
	v_sub_f32_e32 v130, v132, v2
	v_sub_f32_e32 v131, v131, v3
	v_mul_f32_e32 v128, v88, v128
	v_mul_f32_e32 v129, v89, v129
	s_waitcnt lgkmcnt(1)
	v_fma_f32 v24, v36, v24, v120
	v_fma_f32 v25, v37, v25, v121
	v_mul_f32_e32 v26, v90, v26
	v_mul_f32_e32 v27, v91, v27
	v_mul_f32_e32 v130, v90, v130
	v_mul_f32_e32 v131, v91, v131
	s_waitcnt lgkmcnt(0)
	v_fma_f32 v36, v116, v128, v124
	ds_write2_b32 v114, v24, v25 offset1:68
	v_fma_f32 v24, v117, v129, v125
	ds_write2_b32 v113, v36, v24 offset0:16 offset1:84
	v_fma_f32 v24, v38, v26, v122
	v_fma_f32 v25, v118, v130, v126
	v_fmac_f32_e32 v123, v39, v27
	v_fmac_f32_e32 v127, v119, v131
	ds_write2_b32 v114, v24, v123 offset0:136 offset1:204
	ds_write2_b32 v113, v25, v127 offset0:152 offset1:220
	ds_write_b128 v96, v[20:23] offset:41984
	s_mov_b32 s16, 0
	v_mov_b32_e32 v20, v103
	s_waitcnt lgkmcnt(0)
	s_barrier
.LBB0_1479:
	v_add_u32_e32 v21, s16, v44
	ds_read_b128 v[22:25], v20
	ds_read_b128 v[36:39], v20 offset:272
	ds_read_b128 v[116:119], v20 offset:544
	ds_read_b128 v[120:123], v20 offset:816
	ds_read_b128 v[124:127], v21
	ds_read_b128 v[128:131], v21 offset:128
	ds_read_b128 v[132:135], v21 offset:256
	ds_read_b128 v[136:139], v21 offset:384
	s_waitcnt lgkmcnt(7)
	v_mov_b32_e32 v26, v25
	s_waitcnt lgkmcnt(6)
	v_mov_b32_e32 v140, v39
	s_waitcnt lgkmcnt(3)
	v_fmac_f32_e32 v18, v126, v22
	v_fmac_f32_e32 v19, v127, v22
	v_fmac_f32_e32 v16, v124, v22
	v_fmac_f32_e32 v17, v125, v22
	v_fmac_f32_e32 v14, v126, v23
	v_fmac_f32_e32 v15, v127, v23
	v_fmac_f32_e32 v12, v124, v23
	v_fmac_f32_e32 v13, v125, v23
	v_fmac_f32_e32 v8, v124, v24
	v_fmac_f32_e32 v9, v125, v24
	v_fmac_f32_e32 v10, v126, v24
	v_fmac_f32_e32 v11, v127, v24
	v_fmac_f32_e32 v4, v124, v26
	v_fmac_f32_e32 v5, v125, v26
	v_fmac_f32_e32 v6, v126, v26
	v_fmac_f32_e32 v7, v127, v26
	v_mov_b32_e32 v142, v119
	s_waitcnt lgkmcnt(2)
	v_fmac_f32_e32 v18, v130, v36
	v_fmac_f32_e32 v19, v131, v36
	v_fmac_f32_e32 v16, v128, v36
	v_fmac_f32_e32 v17, v129, v36
	v_fmac_f32_e32 v14, v130, v37
	v_fmac_f32_e32 v15, v131, v37
	v_fmac_f32_e32 v12, v128, v37
	v_fmac_f32_e32 v13, v129, v37
	v_fmac_f32_e32 v10, v130, v38
	v_fmac_f32_e32 v11, v131, v38
	v_fmac_f32_e32 v8, v128, v38
	v_fmac_f32_e32 v9, v129, v38
	v_fmac_f32_e32 v6, v130, v140
	v_fmac_f32_e32 v7, v131, v140
	v_fmac_f32_e32 v4, v128, v140
	v_fmac_f32_e32 v5, v129, v140
	s_addk_i32 s16, 0x200
	v_mov_b32_e32 v144, v123
	s_waitcnt lgkmcnt(1)
	v_fmac_f32_e32 v18, v134, v116
	v_fmac_f32_e32 v19, v135, v116
	v_fmac_f32_e32 v16, v132, v116
	v_fmac_f32_e32 v17, v133, v116
	v_fmac_f32_e32 v14, v134, v117
	v_fmac_f32_e32 v15, v135, v117
	v_fmac_f32_e32 v12, v132, v117
	v_fmac_f32_e32 v13, v133, v117
	v_fmac_f32_e32 v10, v134, v118
	v_fmac_f32_e32 v11, v135, v118
	v_fmac_f32_e32 v8, v132, v118
	v_fmac_f32_e32 v9, v133, v118
	v_fmac_f32_e32 v6, v134, v142
	v_fmac_f32_e32 v7, v135, v142
	v_fmac_f32_e32 v4, v132, v142
	v_fmac_f32_e32 v5, v133, v142
	v_add_u32_e32 v20, 0x440, v20
	s_cmpk_lg_i32 s16, 0x800
	s_waitcnt lgkmcnt(0)
	v_fmac_f32_e32 v18, v138, v120
	v_fmac_f32_e32 v19, v139, v120
	v_fmac_f32_e32 v16, v136, v120
	v_fmac_f32_e32 v17, v137, v120
	v_fmac_f32_e32 v14, v138, v121
	v_fmac_f32_e32 v15, v139, v121
	v_fmac_f32_e32 v12, v136, v121
	v_fmac_f32_e32 v13, v137, v121
	v_fmac_f32_e32 v10, v138, v122
	v_fmac_f32_e32 v11, v139, v122
	v_fmac_f32_e32 v8, v136, v122
	v_fmac_f32_e32 v9, v137, v122
	v_fmac_f32_e32 v6, v138, v144
	v_fmac_f32_e32 v7, v139, v144
	v_fmac_f32_e32 v4, v136, v144
	v_fmac_f32_e32 v5, v137, v144
	s_cbranch_scc1 .LBB0_1479
	s_barrier
	global_load_dwordx4 v[36:39], v[92:93], off offset:384
	global_load_dwordx4 v[20:23], v[56:57], off
	s_waitcnt vmcnt(3)
	v_cvt_f32_f16_sdwa v128, v32 dst_sel:DWORD dst_unused:UNUSED_PAD src0_sel:WORD_1
	v_cvt_f32_f16_e32 v32, v32
	v_cvt_f32_f16_e32 v129, v33
	v_cvt_f32_f16_sdwa v130, v34 dst_sel:DWORD dst_unused:UNUSED_PAD src0_sel:WORD_1
	v_cvt_f32_f16_e32 v133, v34
	ds_read_b128 v[24:27], v43 offset:12800
	ds_read_b128 v[116:119], v43 offset:12816
	ds_read_b128 v[120:123], v43 offset:16896
	ds_read_b128 v[124:127], v43 offset:16912
	v_cvt_f32_f16_sdwa v115, v33 dst_sel:DWORD dst_unused:UNUSED_PAD src0_sel:WORD_1
	v_cvt_f32_f16_sdwa v131, v35 dst_sel:DWORD dst_unused:UNUSED_PAD src0_sel:WORD_1
	v_cvt_f32_f16_e32 v132, v35
	v_sub_f32_e32 v32, v32, v0
	v_sub_f32_e32 v33, v128, v1
	v_sub_f32_e32 v34, v129, v2
	v_mul_f32_e32 v32, v88, v32
	v_mul_f32_e32 v33, v89, v33
	v_sub_f32_e32 v128, v133, v0
	v_sub_f32_e32 v129, v130, v1
	v_sub_f32_e32 v35, v115, v3
	v_mul_f32_e32 v128, v88, v128
	v_mul_f32_e32 v129, v89, v129
	s_waitcnt lgkmcnt(1)
	v_fma_f32 v24, v24, v32, v120
	v_fma_f32 v25, v25, v33, v121
	v_mul_f32_e32 v34, v90, v34
	v_mul_f32_e32 v35, v91, v35
	v_sub_f32_e32 v130, v132, v2
	v_sub_f32_e32 v131, v131, v3
	s_waitcnt lgkmcnt(0)
	v_fma_f32 v32, v116, v128, v124
	ds_write2_b32 v114, v24, v25 offset1:68
	v_fma_f32 v24, v117, v129, v125
	v_mul_f32_e32 v130, v90, v130
	v_mul_f32_e32 v131, v91, v131
	ds_write2_b32 v113, v32, v24 offset0:16 offset1:84
	v_fma_f32 v24, v26, v34, v122
	v_fmac_f32_e32 v123, v27, v35
	v_fma_f32 v25, v118, v130, v126
	ds_write2_b32 v114, v24, v123 offset0:136 offset1:204
	v_fmac_f32_e32 v127, v119, v131
	s_mov_b32 s16, 0
	v_mov_b32_e32 v24, v103
	ds_write2_b32 v113, v25, v127 offset0:152 offset1:220
	s_waitcnt vmcnt(2)
	ds_write_b128 v96, v[28:31] offset:41984
	s_waitcnt lgkmcnt(0)
	s_barrier
.LBB0_1481:
	v_add_u32_e32 v25, s16, v44
	ds_read_b128 v[26:29], v24
	ds_read_b128 v[30:33], v24 offset:272
	ds_read_b128 v[116:119], v24 offset:544
	ds_read_b128 v[120:123], v24 offset:816
	ds_read_b128 v[124:127], v25
	ds_read_b128 v[128:131], v25 offset:128
	ds_read_b128 v[132:135], v25 offset:256
	ds_read_b128 v[136:139], v25 offset:384
	s_waitcnt lgkmcnt(7)
	v_mov_b32_e32 v34, v29
	s_waitcnt lgkmcnt(6)
	v_mov_b32_e32 v140, v33
	s_waitcnt lgkmcnt(3)
	v_fmac_f32_e32 v18, v126, v26
	v_fmac_f32_e32 v19, v127, v26
	v_fmac_f32_e32 v16, v124, v26
	v_fmac_f32_e32 v17, v125, v26
	v_fmac_f32_e32 v14, v126, v27
	v_fmac_f32_e32 v15, v127, v27
	v_fmac_f32_e32 v12, v124, v27
	v_fmac_f32_e32 v13, v125, v27
	v_fmac_f32_e32 v8, v124, v28
	v_fmac_f32_e32 v9, v125, v28
	v_fmac_f32_e32 v10, v126, v28
	v_fmac_f32_e32 v11, v127, v28
	v_fmac_f32_e32 v4, v124, v34
	v_fmac_f32_e32 v5, v125, v34
	v_fmac_f32_e32 v6, v126, v34
	v_fmac_f32_e32 v7, v127, v34
	v_mov_b32_e32 v142, v119
	s_waitcnt lgkmcnt(2)
	v_fmac_f32_e32 v18, v130, v30
	v_fmac_f32_e32 v19, v131, v30
	v_fmac_f32_e32 v16, v128, v30
	v_fmac_f32_e32 v17, v129, v30
	v_fmac_f32_e32 v14, v130, v31
	v_fmac_f32_e32 v15, v131, v31
	v_fmac_f32_e32 v12, v128, v31
	v_fmac_f32_e32 v13, v129, v31
	v_fmac_f32_e32 v10, v130, v32
	v_fmac_f32_e32 v11, v131, v32
	v_fmac_f32_e32 v8, v128, v32
	v_fmac_f32_e32 v9, v129, v32
	v_fmac_f32_e32 v6, v130, v140
	v_fmac_f32_e32 v7, v131, v140
	v_fmac_f32_e32 v4, v128, v140
	v_fmac_f32_e32 v5, v129, v140
	s_addk_i32 s16, 0x200
	v_mov_b32_e32 v144, v123
	s_waitcnt lgkmcnt(1)
	v_fmac_f32_e32 v18, v134, v116
	v_fmac_f32_e32 v19, v135, v116
	v_fmac_f32_e32 v16, v132, v116
	v_fmac_f32_e32 v17, v133, v116
	v_fmac_f32_e32 v14, v134, v117
	v_fmac_f32_e32 v15, v135, v117
	v_fmac_f32_e32 v12, v132, v117
	v_fmac_f32_e32 v13, v133, v117
	v_fmac_f32_e32 v10, v134, v118
	v_fmac_f32_e32 v11, v135, v118
	v_fmac_f32_e32 v8, v132, v118
	v_fmac_f32_e32 v9, v133, v118
	v_fmac_f32_e32 v6, v134, v142
	v_fmac_f32_e32 v7, v135, v142
	v_fmac_f32_e32 v4, v132, v142
	v_fmac_f32_e32 v5, v133, v142
	v_add_u32_e32 v24, 0x440, v24
	s_cmpk_lg_i32 s16, 0x800
	s_waitcnt lgkmcnt(0)
	v_fmac_f32_e32 v18, v138, v120
	v_fmac_f32_e32 v19, v139, v120
	v_fmac_f32_e32 v16, v136, v120
	v_fmac_f32_e32 v17, v137, v120
	v_fmac_f32_e32 v14, v138, v121
	v_fmac_f32_e32 v15, v139, v121
	v_fmac_f32_e32 v12, v136, v121
	v_fmac_f32_e32 v13, v137, v121
	v_fmac_f32_e32 v10, v138, v122
	v_fmac_f32_e32 v11, v139, v122
	v_fmac_f32_e32 v8, v136, v122
	v_fmac_f32_e32 v9, v137, v122
	v_fmac_f32_e32 v6, v138, v144
	v_fmac_f32_e32 v7, v139, v144
	v_fmac_f32_e32 v4, v136, v144
	v_fmac_f32_e32 v5, v137, v144
	s_cbranch_scc1 .LBB0_1481
	s_barrier
	global_load_dwordx4 v[28:31], v[92:93], off offset:512
	global_load_dwordx4 v[24:27], v[58:59], off
	s_waitcnt vmcnt(3)
	v_cvt_f32_f16_sdwa v128, v36 dst_sel:DWORD dst_unused:UNUSED_PAD src0_sel:WORD_1
	v_cvt_f32_f16_e32 v36, v36
	v_cvt_f32_f16_e32 v129, v37
	v_cvt_f32_f16_sdwa v130, v38 dst_sel:DWORD dst_unused:UNUSED_PAD src0_sel:WORD_1
	v_cvt_f32_f16_e32 v133, v38
	ds_read_b128 v[32:35], v43 offset:13056
	ds_read_b128 v[116:119], v43 offset:13072
	ds_read_b128 v[120:123], v43 offset:17152
	ds_read_b128 v[124:127], v43 offset:17168
	v_cvt_f32_f16_sdwa v115, v37 dst_sel:DWORD dst_unused:UNUSED_PAD src0_sel:WORD_1
	v_cvt_f32_f16_sdwa v131, v39 dst_sel:DWORD dst_unused:UNUSED_PAD src0_sel:WORD_1
	v_cvt_f32_f16_e32 v132, v39
	v_sub_f32_e32 v36, v36, v0
	v_sub_f32_e32 v37, v128, v1
	v_sub_f32_e32 v38, v129, v2
	v_mul_f32_e32 v36, v88, v36
	v_mul_f32_e32 v37, v89, v37
	v_sub_f32_e32 v128, v133, v0
	v_sub_f32_e32 v129, v130, v1
	v_sub_f32_e32 v39, v115, v3
	v_sub_f32_e32 v130, v132, v2
	v_sub_f32_e32 v131, v131, v3
	v_mul_f32_e32 v128, v88, v128
	v_mul_f32_e32 v129, v89, v129
	s_waitcnt lgkmcnt(1)
	v_fma_f32 v32, v32, v36, v120
	v_fma_f32 v33, v33, v37, v121
	v_mul_f32_e32 v38, v90, v38
	v_mul_f32_e32 v39, v91, v39
	v_mul_f32_e32 v130, v90, v130
	v_mul_f32_e32 v131, v91, v131
	s_waitcnt lgkmcnt(0)
	v_fma_f32 v36, v116, v128, v124
	ds_write2_b32 v114, v32, v33 offset1:68
	v_fma_f32 v32, v117, v129, v125
	ds_write2_b32 v113, v36, v32 offset0:16 offset1:84
	v_fma_f32 v32, v34, v38, v122
	v_fma_f32 v33, v118, v130, v126
	v_fmac_f32_e32 v123, v35, v39
	v_fmac_f32_e32 v127, v119, v131
	ds_write2_b32 v114, v32, v123 offset0:136 offset1:204
	ds_write2_b32 v113, v33, v127 offset0:152 offset1:220
	s_waitcnt vmcnt(2)
	ds_write_b128 v96, v[20:23] offset:41984
	s_mov_b32 s16, 0
	v_mov_b32_e32 v20, v103
	s_waitcnt lgkmcnt(0)
	s_barrier
.LBB0_1483:
	v_add_u32_e32 v21, s16, v44
	ds_read_b128 v[32:35], v20
	ds_read_b128 v[36:39], v20 offset:272
	ds_read_b128 v[116:119], v20 offset:544
	ds_read_b128 v[120:123], v20 offset:816
	ds_read_b128 v[124:127], v21
	ds_read_b128 v[128:131], v21 offset:128
	ds_read_b128 v[132:135], v21 offset:256
	ds_read_b128 v[136:139], v21 offset:384
	s_waitcnt lgkmcnt(7)
	v_mov_b32_e32 v22, v35
	s_waitcnt lgkmcnt(6)
	v_mov_b32_e32 v140, v39
	s_waitcnt lgkmcnt(3)
	v_fmac_f32_e32 v18, v126, v32
	v_fmac_f32_e32 v19, v127, v32
	v_fmac_f32_e32 v16, v124, v32
	v_fmac_f32_e32 v17, v125, v32
	v_fmac_f32_e32 v14, v126, v33
	v_fmac_f32_e32 v15, v127, v33
	v_fmac_f32_e32 v12, v124, v33
	v_fmac_f32_e32 v13, v125, v33
	v_fmac_f32_e32 v8, v124, v34
	v_fmac_f32_e32 v9, v125, v34
	v_fmac_f32_e32 v10, v126, v34
	v_fmac_f32_e32 v11, v127, v34
	v_fmac_f32_e32 v4, v124, v22
	v_fmac_f32_e32 v5, v125, v22
	v_fmac_f32_e32 v6, v126, v22
	v_fmac_f32_e32 v7, v127, v22
	v_mov_b32_e32 v142, v119
	s_waitcnt lgkmcnt(2)
	v_fmac_f32_e32 v18, v130, v36
	v_fmac_f32_e32 v19, v131, v36
	v_fmac_f32_e32 v16, v128, v36
	v_fmac_f32_e32 v17, v129, v36
	v_fmac_f32_e32 v14, v130, v37
	v_fmac_f32_e32 v15, v131, v37
	v_fmac_f32_e32 v12, v128, v37
	v_fmac_f32_e32 v13, v129, v37
	v_fmac_f32_e32 v10, v130, v38
	v_fmac_f32_e32 v11, v131, v38
	v_fmac_f32_e32 v8, v128, v38
	v_fmac_f32_e32 v9, v129, v38
	v_fmac_f32_e32 v6, v130, v140
	v_fmac_f32_e32 v7, v131, v140
	v_fmac_f32_e32 v4, v128, v140
	v_fmac_f32_e32 v5, v129, v140
	s_addk_i32 s16, 0x200
	v_mov_b32_e32 v144, v123
	s_waitcnt lgkmcnt(1)
	v_fmac_f32_e32 v18, v134, v116
	v_fmac_f32_e32 v19, v135, v116
	v_fmac_f32_e32 v16, v132, v116
	v_fmac_f32_e32 v17, v133, v116
	v_fmac_f32_e32 v14, v134, v117
	v_fmac_f32_e32 v15, v135, v117
	v_fmac_f32_e32 v12, v132, v117
	v_fmac_f32_e32 v13, v133, v117
	v_fmac_f32_e32 v10, v134, v118
	v_fmac_f32_e32 v11, v135, v118
	v_fmac_f32_e32 v8, v132, v118
	v_fmac_f32_e32 v9, v133, v118
	v_fmac_f32_e32 v6, v134, v142
	v_fmac_f32_e32 v7, v135, v142
	v_fmac_f32_e32 v4, v132, v142
	v_fmac_f32_e32 v5, v133, v142
	v_add_u32_e32 v20, 0x440, v20
	s_cmpk_lg_i32 s16, 0x800
	s_waitcnt lgkmcnt(0)
	v_fmac_f32_e32 v18, v138, v120
	v_fmac_f32_e32 v19, v139, v120
	v_fmac_f32_e32 v16, v136, v120
	v_fmac_f32_e32 v17, v137, v120
	v_fmac_f32_e32 v14, v138, v121
	v_fmac_f32_e32 v15, v139, v121
	v_fmac_f32_e32 v12, v136, v121
	v_fmac_f32_e32 v13, v137, v121
	v_fmac_f32_e32 v10, v138, v122
	v_fmac_f32_e32 v11, v139, v122
	v_fmac_f32_e32 v8, v136, v122
	v_fmac_f32_e32 v9, v137, v122
	v_fmac_f32_e32 v6, v138, v144
	v_fmac_f32_e32 v7, v139, v144
	v_fmac_f32_e32 v4, v136, v144
	v_fmac_f32_e32 v5, v137, v144
	s_cbranch_scc1 .LBB0_1483
	s_barrier
	global_load_dwordx4 v[32:35], v[92:93], off offset:640
	global_load_dwordx4 v[20:23], v[60:61], off
	s_waitcnt vmcnt(3)
	v_cvt_f32_f16_sdwa v128, v28 dst_sel:DWORD dst_unused:UNUSED_PAD src0_sel:WORD_1
	v_cvt_f32_f16_e32 v28, v28
	v_cvt_f32_f16_e32 v129, v29
	v_cvt_f32_f16_sdwa v130, v30 dst_sel:DWORD dst_unused:UNUSED_PAD src0_sel:WORD_1
	v_cvt_f32_f16_e32 v133, v30
	ds_read_b128 v[36:39], v43 offset:13312
	ds_read_b128 v[116:119], v43 offset:13328
	ds_read_b128 v[120:123], v43 offset:17408
	ds_read_b128 v[124:127], v43 offset:17424
	v_cvt_f32_f16_sdwa v115, v29 dst_sel:DWORD dst_unused:UNUSED_PAD src0_sel:WORD_1
	v_cvt_f32_f16_sdwa v131, v31 dst_sel:DWORD dst_unused:UNUSED_PAD src0_sel:WORD_1
	v_cvt_f32_f16_e32 v132, v31
	v_sub_f32_e32 v28, v28, v0
	v_sub_f32_e32 v29, v128, v1
	v_sub_f32_e32 v30, v129, v2
	v_mul_f32_e32 v28, v88, v28
	v_mul_f32_e32 v29, v89, v29
	v_sub_f32_e32 v128, v133, v0
	v_sub_f32_e32 v129, v130, v1
	v_sub_f32_e32 v31, v115, v3
	v_sub_f32_e32 v130, v132, v2
	v_sub_f32_e32 v131, v131, v3
	v_mul_f32_e32 v128, v88, v128
	v_mul_f32_e32 v129, v89, v129
	s_waitcnt lgkmcnt(1)
	v_fma_f32 v28, v36, v28, v120
	v_fma_f32 v29, v37, v29, v121
	v_mul_f32_e32 v30, v90, v30
	v_mul_f32_e32 v31, v91, v31
	v_mul_f32_e32 v130, v90, v130
	v_mul_f32_e32 v131, v91, v131
	s_waitcnt lgkmcnt(0)
	v_fma_f32 v36, v116, v128, v124
	ds_write2_b32 v114, v28, v29 offset1:68
	v_fma_f32 v28, v117, v129, v125
	ds_write2_b32 v113, v36, v28 offset0:16 offset1:84
	v_fma_f32 v28, v38, v30, v122
	v_fma_f32 v29, v118, v130, v126
	v_fmac_f32_e32 v123, v39, v31
	v_fmac_f32_e32 v127, v119, v131
	ds_write2_b32 v114, v28, v123 offset0:136 offset1:204
	ds_write2_b32 v113, v29, v127 offset0:152 offset1:220
	s_waitcnt vmcnt(2)
	ds_write_b128 v96, v[24:27] offset:41984
	s_mov_b32 s16, 0
	v_mov_b32_e32 v24, v103
	s_waitcnt lgkmcnt(0)
	s_barrier
.LBB0_1485:
	v_add_u32_e32 v25, s16, v44
	ds_read_b128 v[26:29], v24
	ds_read_b128 v[36:39], v24 offset:272
	ds_read_b128 v[116:119], v24 offset:544
	ds_read_b128 v[120:123], v24 offset:816
	ds_read_b128 v[124:127], v25
	ds_read_b128 v[128:131], v25 offset:128
	ds_read_b128 v[132:135], v25 offset:256
	ds_read_b128 v[136:139], v25 offset:384
	s_waitcnt lgkmcnt(7)
	v_mov_b32_e32 v30, v29
	s_waitcnt lgkmcnt(6)
	v_mov_b32_e32 v140, v39
	s_waitcnt lgkmcnt(3)
	v_fmac_f32_e32 v18, v126, v26
	v_fmac_f32_e32 v19, v127, v26
	v_fmac_f32_e32 v16, v124, v26
	v_fmac_f32_e32 v17, v125, v26
	v_fmac_f32_e32 v14, v126, v27
	v_fmac_f32_e32 v15, v127, v27
	v_fmac_f32_e32 v12, v124, v27
	v_fmac_f32_e32 v13, v125, v27
	v_fmac_f32_e32 v8, v124, v28
	v_fmac_f32_e32 v9, v125, v28
	v_fmac_f32_e32 v10, v126, v28
	v_fmac_f32_e32 v11, v127, v28
	v_fmac_f32_e32 v4, v124, v30
	v_fmac_f32_e32 v5, v125, v30
	v_fmac_f32_e32 v6, v126, v30
	v_fmac_f32_e32 v7, v127, v30
	v_mov_b32_e32 v142, v119
	s_waitcnt lgkmcnt(2)
	v_fmac_f32_e32 v18, v130, v36
	v_fmac_f32_e32 v19, v131, v36
	v_fmac_f32_e32 v16, v128, v36
	v_fmac_f32_e32 v17, v129, v36
	v_fmac_f32_e32 v14, v130, v37
	v_fmac_f32_e32 v15, v131, v37
	v_fmac_f32_e32 v12, v128, v37
	v_fmac_f32_e32 v13, v129, v37
	v_fmac_f32_e32 v10, v130, v38
	v_fmac_f32_e32 v11, v131, v38
	v_fmac_f32_e32 v8, v128, v38
	v_fmac_f32_e32 v9, v129, v38
	v_fmac_f32_e32 v6, v130, v140
	v_fmac_f32_e32 v7, v131, v140
	v_fmac_f32_e32 v4, v128, v140
	v_fmac_f32_e32 v5, v129, v140
	s_addk_i32 s16, 0x200
	v_mov_b32_e32 v144, v123
	s_waitcnt lgkmcnt(1)
	v_fmac_f32_e32 v18, v134, v116
	v_fmac_f32_e32 v19, v135, v116
	v_fmac_f32_e32 v16, v132, v116
	v_fmac_f32_e32 v17, v133, v116
	v_fmac_f32_e32 v14, v134, v117
	v_fmac_f32_e32 v15, v135, v117
	v_fmac_f32_e32 v12, v132, v117
	v_fmac_f32_e32 v13, v133, v117
	v_fmac_f32_e32 v10, v134, v118
	v_fmac_f32_e32 v11, v135, v118
	v_fmac_f32_e32 v8, v132, v118
	v_fmac_f32_e32 v9, v133, v118
	v_fmac_f32_e32 v6, v134, v142
	v_fmac_f32_e32 v7, v135, v142
	v_fmac_f32_e32 v4, v132, v142
	v_fmac_f32_e32 v5, v133, v142
	v_add_u32_e32 v24, 0x440, v24
	s_cmpk_lg_i32 s16, 0x800
	s_waitcnt lgkmcnt(0)
	v_fmac_f32_e32 v18, v138, v120
	v_fmac_f32_e32 v19, v139, v120
	v_fmac_f32_e32 v16, v136, v120
	v_fmac_f32_e32 v17, v137, v120
	v_fmac_f32_e32 v14, v138, v121
	v_fmac_f32_e32 v15, v139, v121
	v_fmac_f32_e32 v12, v136, v121
	v_fmac_f32_e32 v13, v137, v121
	v_fmac_f32_e32 v10, v138, v122
	v_fmac_f32_e32 v11, v139, v122
	v_fmac_f32_e32 v8, v136, v122
	v_fmac_f32_e32 v9, v137, v122
	v_fmac_f32_e32 v6, v138, v144
	v_fmac_f32_e32 v7, v139, v144
	v_fmac_f32_e32 v4, v136, v144
	v_fmac_f32_e32 v5, v137, v144
	s_cbranch_scc1 .LBB0_1485
	s_barrier
	global_load_dwordx4 v[28:31], v[92:93], off offset:768
	global_load_dwordx4 v[24:27], v[62:63], off
	s_waitcnt vmcnt(3)
	v_cvt_f32_f16_sdwa v128, v32 dst_sel:DWORD dst_unused:UNUSED_PAD src0_sel:WORD_1
	v_cvt_f32_f16_e32 v32, v32
	v_cvt_f32_f16_e32 v129, v33
	v_cvt_f32_f16_sdwa v130, v34 dst_sel:DWORD dst_unused:UNUSED_PAD src0_sel:WORD_1
	v_cvt_f32_f16_e32 v133, v34
	ds_read_b128 v[36:39], v43 offset:13568
	ds_read_b128 v[116:119], v43 offset:13584
	ds_read_b128 v[120:123], v43 offset:17664
	ds_read_b128 v[124:127], v43 offset:17680
	v_cvt_f32_f16_sdwa v115, v33 dst_sel:DWORD dst_unused:UNUSED_PAD src0_sel:WORD_1
	v_cvt_f32_f16_sdwa v131, v35 dst_sel:DWORD dst_unused:UNUSED_PAD src0_sel:WORD_1
	v_cvt_f32_f16_e32 v132, v35
	v_sub_f32_e32 v32, v32, v0
	v_sub_f32_e32 v33, v128, v1
	v_sub_f32_e32 v34, v129, v2
	v_mul_f32_e32 v32, v88, v32
	v_mul_f32_e32 v33, v89, v33
	v_sub_f32_e32 v128, v133, v0
	v_sub_f32_e32 v129, v130, v1
	v_sub_f32_e32 v35, v115, v3
	v_sub_f32_e32 v130, v132, v2
	v_sub_f32_e32 v131, v131, v3
	v_mul_f32_e32 v128, v88, v128
	v_mul_f32_e32 v129, v89, v129
	s_waitcnt lgkmcnt(1)
	v_fma_f32 v32, v36, v32, v120
	v_fma_f32 v33, v37, v33, v121
	v_mul_f32_e32 v34, v90, v34
	v_mul_f32_e32 v35, v91, v35
	v_mul_f32_e32 v130, v90, v130
	v_mul_f32_e32 v131, v91, v131
	s_waitcnt lgkmcnt(0)
	v_fma_f32 v36, v116, v128, v124
	ds_write2_b32 v114, v32, v33 offset1:68
	v_fma_f32 v32, v117, v129, v125
	ds_write2_b32 v113, v36, v32 offset0:16 offset1:84
	v_fma_f32 v32, v38, v34, v122
	v_fma_f32 v33, v118, v130, v126
	v_fmac_f32_e32 v123, v39, v35
	v_fmac_f32_e32 v127, v119, v131
	ds_write2_b32 v114, v32, v123 offset0:136 offset1:204
	ds_write2_b32 v113, v33, v127 offset0:152 offset1:220
	s_waitcnt vmcnt(2)
	ds_write_b128 v96, v[20:23] offset:41984
	s_mov_b32 s16, 0
	v_mov_b32_e32 v20, v103
	s_waitcnt lgkmcnt(0)
	s_barrier
.LBB0_1487:
	v_add_u32_e32 v21, s16, v44
	ds_read_b128 v[32:35], v20
	ds_read_b128 v[36:39], v20 offset:272
	ds_read_b128 v[116:119], v20 offset:544
	ds_read_b128 v[120:123], v20 offset:816
	ds_read_b128 v[124:127], v21
	ds_read_b128 v[128:131], v21 offset:128
	ds_read_b128 v[132:135], v21 offset:256
	ds_read_b128 v[136:139], v21 offset:384
	s_waitcnt lgkmcnt(7)
	v_mov_b32_e32 v22, v35
	s_waitcnt lgkmcnt(6)
	v_mov_b32_e32 v140, v39
	s_waitcnt lgkmcnt(3)
	v_fmac_f32_e32 v18, v126, v32
	v_fmac_f32_e32 v19, v127, v32
	v_fmac_f32_e32 v16, v124, v32
	v_fmac_f32_e32 v17, v125, v32
	v_fmac_f32_e32 v14, v126, v33
	v_fmac_f32_e32 v15, v127, v33
	v_fmac_f32_e32 v12, v124, v33
	v_fmac_f32_e32 v13, v125, v33
	v_fmac_f32_e32 v8, v124, v34
	v_fmac_f32_e32 v9, v125, v34
	v_fmac_f32_e32 v10, v126, v34
	v_fmac_f32_e32 v11, v127, v34
	v_fmac_f32_e32 v4, v124, v22
	v_fmac_f32_e32 v5, v125, v22
	v_fmac_f32_e32 v6, v126, v22
	v_fmac_f32_e32 v7, v127, v22
	v_mov_b32_e32 v142, v119
	s_waitcnt lgkmcnt(2)
	v_fmac_f32_e32 v18, v130, v36
	v_fmac_f32_e32 v19, v131, v36
	v_fmac_f32_e32 v16, v128, v36
	v_fmac_f32_e32 v17, v129, v36
	v_fmac_f32_e32 v14, v130, v37
	v_fmac_f32_e32 v15, v131, v37
	v_fmac_f32_e32 v12, v128, v37
	v_fmac_f32_e32 v13, v129, v37
	v_fmac_f32_e32 v10, v130, v38
	v_fmac_f32_e32 v11, v131, v38
	v_fmac_f32_e32 v8, v128, v38
	v_fmac_f32_e32 v9, v129, v38
	v_fmac_f32_e32 v6, v130, v140
	v_fmac_f32_e32 v7, v131, v140
	v_fmac_f32_e32 v4, v128, v140
	v_fmac_f32_e32 v5, v129, v140
	s_addk_i32 s16, 0x200
	v_mov_b32_e32 v144, v123
	s_waitcnt lgkmcnt(1)
	v_fmac_f32_e32 v18, v134, v116
	v_fmac_f32_e32 v19, v135, v116
	v_fmac_f32_e32 v16, v132, v116
	v_fmac_f32_e32 v17, v133, v116
	v_fmac_f32_e32 v14, v134, v117
	v_fmac_f32_e32 v15, v135, v117
	v_fmac_f32_e32 v12, v132, v117
	v_fmac_f32_e32 v13, v133, v117
	v_fmac_f32_e32 v10, v134, v118
	v_fmac_f32_e32 v11, v135, v118
	v_fmac_f32_e32 v8, v132, v118
	v_fmac_f32_e32 v9, v133, v118
	v_fmac_f32_e32 v6, v134, v142
	v_fmac_f32_e32 v7, v135, v142
	v_fmac_f32_e32 v4, v132, v142
	v_fmac_f32_e32 v5, v133, v142
	v_add_u32_e32 v20, 0x440, v20
	s_cmpk_lg_i32 s16, 0x800
	s_waitcnt lgkmcnt(0)
	v_fmac_f32_e32 v18, v138, v120
	v_fmac_f32_e32 v19, v139, v120
	v_fmac_f32_e32 v16, v136, v120
	v_fmac_f32_e32 v17, v137, v120
	v_fmac_f32_e32 v14, v138, v121
	v_fmac_f32_e32 v15, v139, v121
	v_fmac_f32_e32 v12, v136, v121
	v_fmac_f32_e32 v13, v137, v121
	v_fmac_f32_e32 v10, v138, v122
	v_fmac_f32_e32 v11, v139, v122
	v_fmac_f32_e32 v8, v136, v122
	v_fmac_f32_e32 v9, v137, v122
	v_fmac_f32_e32 v6, v138, v144
	v_fmac_f32_e32 v7, v139, v144
	v_fmac_f32_e32 v4, v136, v144
	v_fmac_f32_e32 v5, v137, v144
	s_cbranch_scc1 .LBB0_1487
	s_barrier
	global_load_dwordx4 v[32:35], v[92:93], off offset:896
	global_load_dwordx4 v[20:23], v[64:65], off
	s_waitcnt vmcnt(3)
	v_cvt_f32_f16_sdwa v128, v28 dst_sel:DWORD dst_unused:UNUSED_PAD src0_sel:WORD_1
	v_cvt_f32_f16_e32 v28, v28
	v_cvt_f32_f16_e32 v129, v29
	v_cvt_f32_f16_sdwa v130, v30 dst_sel:DWORD dst_unused:UNUSED_PAD src0_sel:WORD_1
	v_cvt_f32_f16_e32 v133, v30
	ds_read_b128 v[36:39], v43 offset:13824
	ds_read_b128 v[116:119], v43 offset:13840
	ds_read_b128 v[120:123], v43 offset:17920
	ds_read_b128 v[124:127], v43 offset:17936
	v_cvt_f32_f16_sdwa v115, v29 dst_sel:DWORD dst_unused:UNUSED_PAD src0_sel:WORD_1
	v_cvt_f32_f16_sdwa v131, v31 dst_sel:DWORD dst_unused:UNUSED_PAD src0_sel:WORD_1
	v_cvt_f32_f16_e32 v132, v31
	v_sub_f32_e32 v28, v28, v0
	v_sub_f32_e32 v29, v128, v1
	v_sub_f32_e32 v30, v129, v2
	v_mul_f32_e32 v28, v88, v28
	v_mul_f32_e32 v29, v89, v29
	v_sub_f32_e32 v128, v133, v0
	v_sub_f32_e32 v129, v130, v1
	v_sub_f32_e32 v31, v115, v3
	v_sub_f32_e32 v130, v132, v2
	v_sub_f32_e32 v131, v131, v3
	v_mul_f32_e32 v128, v88, v128
	v_mul_f32_e32 v129, v89, v129
	s_waitcnt lgkmcnt(1)
	v_fma_f32 v28, v36, v28, v120
	v_fma_f32 v29, v37, v29, v121
	v_mul_f32_e32 v30, v90, v30
	v_mul_f32_e32 v31, v91, v31
	v_mul_f32_e32 v130, v90, v130
	v_mul_f32_e32 v131, v91, v131
	s_waitcnt lgkmcnt(0)
	v_fma_f32 v36, v116, v128, v124
	ds_write2_b32 v114, v28, v29 offset1:68
	v_fma_f32 v28, v117, v129, v125
	ds_write2_b32 v113, v36, v28 offset0:16 offset1:84
	v_fma_f32 v28, v38, v30, v122
	v_fma_f32 v29, v118, v130, v126
	v_fmac_f32_e32 v123, v39, v31
	v_fmac_f32_e32 v127, v119, v131
	ds_write2_b32 v114, v28, v123 offset0:136 offset1:204
	ds_write2_b32 v113, v29, v127 offset0:152 offset1:220
	s_waitcnt vmcnt(2)
	ds_write_b128 v96, v[24:27] offset:41984
	s_mov_b32 s16, 0
	v_mov_b32_e32 v24, v103
	s_waitcnt lgkmcnt(0)
	s_barrier
.LBB0_1489:
	v_add_u32_e32 v25, s16, v44
	ds_read_b128 v[26:29], v24
	ds_read_b128 v[36:39], v24 offset:272
	ds_read_b128 v[116:119], v24 offset:544
	ds_read_b128 v[120:123], v24 offset:816
	ds_read_b128 v[124:127], v25
	ds_read_b128 v[128:131], v25 offset:128
	ds_read_b128 v[132:135], v25 offset:256
	ds_read_b128 v[136:139], v25 offset:384
	s_waitcnt lgkmcnt(7)
	v_mov_b32_e32 v30, v29
	s_waitcnt lgkmcnt(6)
	v_mov_b32_e32 v140, v39
	s_waitcnt lgkmcnt(3)
	v_fmac_f32_e32 v18, v126, v26
	v_fmac_f32_e32 v19, v127, v26
	v_fmac_f32_e32 v16, v124, v26
	v_fmac_f32_e32 v17, v125, v26
	v_fmac_f32_e32 v14, v126, v27
	v_fmac_f32_e32 v15, v127, v27
	v_fmac_f32_e32 v12, v124, v27
	v_fmac_f32_e32 v13, v125, v27
	v_fmac_f32_e32 v8, v124, v28
	v_fmac_f32_e32 v9, v125, v28
	v_fmac_f32_e32 v10, v126, v28
	v_fmac_f32_e32 v11, v127, v28
	v_fmac_f32_e32 v4, v124, v30
	v_fmac_f32_e32 v5, v125, v30
	v_fmac_f32_e32 v6, v126, v30
	v_fmac_f32_e32 v7, v127, v30
	v_mov_b32_e32 v142, v119
	s_waitcnt lgkmcnt(2)
	v_fmac_f32_e32 v18, v130, v36
	v_fmac_f32_e32 v19, v131, v36
	v_fmac_f32_e32 v16, v128, v36
	v_fmac_f32_e32 v17, v129, v36
	v_fmac_f32_e32 v14, v130, v37
	v_fmac_f32_e32 v15, v131, v37
	v_fmac_f32_e32 v12, v128, v37
	v_fmac_f32_e32 v13, v129, v37
	v_fmac_f32_e32 v10, v130, v38
	v_fmac_f32_e32 v11, v131, v38
	v_fmac_f32_e32 v8, v128, v38
	v_fmac_f32_e32 v9, v129, v38
	v_fmac_f32_e32 v6, v130, v140
	v_fmac_f32_e32 v7, v131, v140
	v_fmac_f32_e32 v4, v128, v140
	v_fmac_f32_e32 v5, v129, v140
	s_addk_i32 s16, 0x200
	v_mov_b32_e32 v144, v123
	s_waitcnt lgkmcnt(1)
	v_fmac_f32_e32 v18, v134, v116
	v_fmac_f32_e32 v19, v135, v116
	v_fmac_f32_e32 v16, v132, v116
	v_fmac_f32_e32 v17, v133, v116
	v_fmac_f32_e32 v14, v134, v117
	v_fmac_f32_e32 v15, v135, v117
	v_fmac_f32_e32 v12, v132, v117
	v_fmac_f32_e32 v13, v133, v117
	v_fmac_f32_e32 v10, v134, v118
	v_fmac_f32_e32 v11, v135, v118
	v_fmac_f32_e32 v8, v132, v118
	v_fmac_f32_e32 v9, v133, v118
	v_fmac_f32_e32 v6, v134, v142
	v_fmac_f32_e32 v7, v135, v142
	v_fmac_f32_e32 v4, v132, v142
	v_fmac_f32_e32 v5, v133, v142
	v_add_u32_e32 v24, 0x440, v24
	s_cmpk_lg_i32 s16, 0x800
	s_waitcnt lgkmcnt(0)
	v_fmac_f32_e32 v18, v138, v120
	v_fmac_f32_e32 v19, v139, v120
	v_fmac_f32_e32 v16, v136, v120
	v_fmac_f32_e32 v17, v137, v120
	v_fmac_f32_e32 v14, v138, v121
	v_fmac_f32_e32 v15, v139, v121
	v_fmac_f32_e32 v12, v136, v121
	v_fmac_f32_e32 v13, v137, v121
	v_fmac_f32_e32 v10, v138, v122
	v_fmac_f32_e32 v11, v139, v122
	v_fmac_f32_e32 v8, v136, v122
	v_fmac_f32_e32 v9, v137, v122
	v_fmac_f32_e32 v6, v138, v144
	v_fmac_f32_e32 v7, v139, v144
	v_fmac_f32_e32 v4, v136, v144
	v_fmac_f32_e32 v5, v137, v144
	s_cbranch_scc1 .LBB0_1489
	s_barrier
	global_load_dwordx4 v[28:31], v[92:93], off offset:1024
	global_load_dwordx4 v[24:27], v[66:67], off
	s_waitcnt vmcnt(3)
	v_cvt_f32_f16_sdwa v128, v32 dst_sel:DWORD dst_unused:UNUSED_PAD src0_sel:WORD_1
	v_cvt_f32_f16_e32 v32, v32
	v_cvt_f32_f16_e32 v129, v33
	v_cvt_f32_f16_sdwa v130, v34 dst_sel:DWORD dst_unused:UNUSED_PAD src0_sel:WORD_1
	v_cvt_f32_f16_e32 v133, v34
	ds_read_b128 v[36:39], v43 offset:14080
	ds_read_b128 v[116:119], v43 offset:14096
	ds_read_b128 v[120:123], v43 offset:18176
	ds_read_b128 v[124:127], v43 offset:18192
	v_cvt_f32_f16_sdwa v115, v33 dst_sel:DWORD dst_unused:UNUSED_PAD src0_sel:WORD_1
	v_cvt_f32_f16_sdwa v131, v35 dst_sel:DWORD dst_unused:UNUSED_PAD src0_sel:WORD_1
	v_cvt_f32_f16_e32 v132, v35
	v_sub_f32_e32 v32, v32, v0
	v_sub_f32_e32 v33, v128, v1
	v_sub_f32_e32 v34, v129, v2
	v_mul_f32_e32 v32, v88, v32
	v_mul_f32_e32 v33, v89, v33
	v_sub_f32_e32 v128, v133, v0
	v_sub_f32_e32 v129, v130, v1
	v_sub_f32_e32 v35, v115, v3
	v_sub_f32_e32 v130, v132, v2
	v_sub_f32_e32 v131, v131, v3
	v_mul_f32_e32 v128, v88, v128
	v_mul_f32_e32 v129, v89, v129
	s_waitcnt lgkmcnt(1)
	v_fma_f32 v32, v36, v32, v120
	v_fma_f32 v33, v37, v33, v121
	v_mul_f32_e32 v34, v90, v34
	v_mul_f32_e32 v35, v91, v35
	v_mul_f32_e32 v130, v90, v130
	v_mul_f32_e32 v131, v91, v131
	s_waitcnt lgkmcnt(0)
	v_fma_f32 v36, v116, v128, v124
	ds_write2_b32 v114, v32, v33 offset1:68
	v_fma_f32 v32, v117, v129, v125
	ds_write2_b32 v113, v36, v32 offset0:16 offset1:84
	v_fma_f32 v32, v38, v34, v122
	v_fma_f32 v33, v118, v130, v126
	v_fmac_f32_e32 v123, v39, v35
	v_fmac_f32_e32 v127, v119, v131
	ds_write2_b32 v114, v32, v123 offset0:136 offset1:204
	ds_write2_b32 v113, v33, v127 offset0:152 offset1:220
	s_waitcnt vmcnt(2)
	ds_write_b128 v96, v[20:23] offset:41984
	s_mov_b32 s16, 0
	v_mov_b32_e32 v20, v103
	s_waitcnt lgkmcnt(0)
	s_barrier
.LBB0_1491:
	v_add_u32_e32 v21, s16, v44
	ds_read_b128 v[32:35], v20
	ds_read_b128 v[36:39], v20 offset:272
	ds_read_b128 v[116:119], v20 offset:544
	ds_read_b128 v[120:123], v20 offset:816
	ds_read_b128 v[124:127], v21
	ds_read_b128 v[128:131], v21 offset:128
	ds_read_b128 v[132:135], v21 offset:256
	ds_read_b128 v[136:139], v21 offset:384
	s_waitcnt lgkmcnt(7)
	v_mov_b32_e32 v22, v35
	s_waitcnt lgkmcnt(6)
	v_mov_b32_e32 v140, v39
	s_waitcnt lgkmcnt(3)
	v_fmac_f32_e32 v18, v126, v32
	v_fmac_f32_e32 v19, v127, v32
	v_fmac_f32_e32 v16, v124, v32
	v_fmac_f32_e32 v17, v125, v32
	v_fmac_f32_e32 v14, v126, v33
	v_fmac_f32_e32 v15, v127, v33
	v_fmac_f32_e32 v12, v124, v33
	v_fmac_f32_e32 v13, v125, v33
	v_fmac_f32_e32 v8, v124, v34
	v_fmac_f32_e32 v9, v125, v34
	v_fmac_f32_e32 v10, v126, v34
	v_fmac_f32_e32 v11, v127, v34
	v_fmac_f32_e32 v4, v124, v22
	v_fmac_f32_e32 v5, v125, v22
	v_fmac_f32_e32 v6, v126, v22
	v_fmac_f32_e32 v7, v127, v22
	v_mov_b32_e32 v142, v119
	s_waitcnt lgkmcnt(2)
	v_fmac_f32_e32 v18, v130, v36
	v_fmac_f32_e32 v19, v131, v36
	v_fmac_f32_e32 v16, v128, v36
	v_fmac_f32_e32 v17, v129, v36
	v_fmac_f32_e32 v14, v130, v37
	v_fmac_f32_e32 v15, v131, v37
	v_fmac_f32_e32 v12, v128, v37
	v_fmac_f32_e32 v13, v129, v37
	v_fmac_f32_e32 v10, v130, v38
	v_fmac_f32_e32 v11, v131, v38
	v_fmac_f32_e32 v8, v128, v38
	v_fmac_f32_e32 v9, v129, v38
	v_fmac_f32_e32 v6, v130, v140
	v_fmac_f32_e32 v7, v131, v140
	v_fmac_f32_e32 v4, v128, v140
	v_fmac_f32_e32 v5, v129, v140
	s_addk_i32 s16, 0x200
	v_mov_b32_e32 v144, v123
	s_waitcnt lgkmcnt(1)
	v_fmac_f32_e32 v18, v134, v116
	v_fmac_f32_e32 v19, v135, v116
	v_fmac_f32_e32 v16, v132, v116
	v_fmac_f32_e32 v17, v133, v116
	v_fmac_f32_e32 v14, v134, v117
	v_fmac_f32_e32 v15, v135, v117
	v_fmac_f32_e32 v12, v132, v117
	v_fmac_f32_e32 v13, v133, v117
	v_fmac_f32_e32 v10, v134, v118
	v_fmac_f32_e32 v11, v135, v118
	v_fmac_f32_e32 v8, v132, v118
	v_fmac_f32_e32 v9, v133, v118
	v_fmac_f32_e32 v6, v134, v142
	v_fmac_f32_e32 v7, v135, v142
	v_fmac_f32_e32 v4, v132, v142
	v_fmac_f32_e32 v5, v133, v142
	v_add_u32_e32 v20, 0x440, v20
	s_cmpk_lg_i32 s16, 0x800
	s_waitcnt lgkmcnt(0)
	v_fmac_f32_e32 v18, v138, v120
	v_fmac_f32_e32 v19, v139, v120
	v_fmac_f32_e32 v16, v136, v120
	v_fmac_f32_e32 v17, v137, v120
	v_fmac_f32_e32 v14, v138, v121
	v_fmac_f32_e32 v15, v139, v121
	v_fmac_f32_e32 v12, v136, v121
	v_fmac_f32_e32 v13, v137, v121
	v_fmac_f32_e32 v10, v138, v122
	v_fmac_f32_e32 v11, v139, v122
	v_fmac_f32_e32 v8, v136, v122
	v_fmac_f32_e32 v9, v137, v122
	v_fmac_f32_e32 v6, v138, v144
	v_fmac_f32_e32 v7, v139, v144
	v_fmac_f32_e32 v4, v136, v144
	v_fmac_f32_e32 v5, v137, v144
	s_cbranch_scc1 .LBB0_1491
	s_barrier
	global_load_dwordx4 v[32:35], v[92:93], off offset:1152
	global_load_dwordx4 v[20:23], v[68:69], off
	s_waitcnt vmcnt(3)
	v_cvt_f32_f16_sdwa v128, v28 dst_sel:DWORD dst_unused:UNUSED_PAD src0_sel:WORD_1
	v_cvt_f32_f16_e32 v28, v28
	v_cvt_f32_f16_e32 v129, v29
	v_cvt_f32_f16_sdwa v130, v30 dst_sel:DWORD dst_unused:UNUSED_PAD src0_sel:WORD_1
	v_cvt_f32_f16_e32 v133, v30
	ds_read_b128 v[36:39], v43 offset:14336
	ds_read_b128 v[116:119], v43 offset:14352
	ds_read_b128 v[120:123], v43 offset:18432
	ds_read_b128 v[124:127], v43 offset:18448
	v_cvt_f32_f16_sdwa v115, v29 dst_sel:DWORD dst_unused:UNUSED_PAD src0_sel:WORD_1
	v_cvt_f32_f16_sdwa v131, v31 dst_sel:DWORD dst_unused:UNUSED_PAD src0_sel:WORD_1
	v_cvt_f32_f16_e32 v132, v31
	v_sub_f32_e32 v28, v28, v0
	v_sub_f32_e32 v29, v128, v1
	v_sub_f32_e32 v30, v129, v2
	v_mul_f32_e32 v28, v88, v28
	v_mul_f32_e32 v29, v89, v29
	v_sub_f32_e32 v128, v133, v0
	v_sub_f32_e32 v129, v130, v1
	v_sub_f32_e32 v31, v115, v3
	v_sub_f32_e32 v130, v132, v2
	v_sub_f32_e32 v131, v131, v3
	v_mul_f32_e32 v128, v88, v128
	v_mul_f32_e32 v129, v89, v129
	s_waitcnt lgkmcnt(1)
	v_fma_f32 v28, v36, v28, v120
	v_fma_f32 v29, v37, v29, v121
	v_mul_f32_e32 v30, v90, v30
	v_mul_f32_e32 v31, v91, v31
	v_mul_f32_e32 v130, v90, v130
	v_mul_f32_e32 v131, v91, v131
	s_waitcnt lgkmcnt(0)
	v_fma_f32 v36, v116, v128, v124
	ds_write2_b32 v114, v28, v29 offset1:68
	v_fma_f32 v28, v117, v129, v125
	ds_write2_b32 v113, v36, v28 offset0:16 offset1:84
	v_fma_f32 v28, v38, v30, v122
	v_fma_f32 v29, v118, v130, v126
	v_fmac_f32_e32 v123, v39, v31
	v_fmac_f32_e32 v127, v119, v131
	ds_write2_b32 v114, v28, v123 offset0:136 offset1:204
	ds_write2_b32 v113, v29, v127 offset0:152 offset1:220
	s_waitcnt vmcnt(2)
	ds_write_b128 v96, v[24:27] offset:41984
	s_mov_b32 s16, 0
	v_mov_b32_e32 v24, v103
	s_waitcnt lgkmcnt(0)
	s_barrier
.LBB0_1493:
	v_add_u32_e32 v25, s16, v44
	ds_read_b128 v[26:29], v24
	ds_read_b128 v[36:39], v24 offset:272
	ds_read_b128 v[116:119], v24 offset:544
	ds_read_b128 v[120:123], v24 offset:816
	ds_read_b128 v[124:127], v25
	ds_read_b128 v[128:131], v25 offset:128
	ds_read_b128 v[132:135], v25 offset:256
	ds_read_b128 v[136:139], v25 offset:384
	s_waitcnt lgkmcnt(7)
	v_mov_b32_e32 v30, v29
	s_waitcnt lgkmcnt(6)
	v_mov_b32_e32 v140, v39
	s_waitcnt lgkmcnt(3)
	v_fmac_f32_e32 v18, v126, v26
	v_fmac_f32_e32 v19, v127, v26
	v_fmac_f32_e32 v16, v124, v26
	v_fmac_f32_e32 v17, v125, v26
	v_fmac_f32_e32 v14, v126, v27
	v_fmac_f32_e32 v15, v127, v27
	v_fmac_f32_e32 v12, v124, v27
	v_fmac_f32_e32 v13, v125, v27
	v_fmac_f32_e32 v8, v124, v28
	v_fmac_f32_e32 v9, v125, v28
	v_fmac_f32_e32 v10, v126, v28
	v_fmac_f32_e32 v11, v127, v28
	v_fmac_f32_e32 v4, v124, v30
	v_fmac_f32_e32 v5, v125, v30
	v_fmac_f32_e32 v6, v126, v30
	v_fmac_f32_e32 v7, v127, v30
	v_mov_b32_e32 v142, v119
	s_waitcnt lgkmcnt(2)
	v_fmac_f32_e32 v18, v130, v36
	v_fmac_f32_e32 v19, v131, v36
	v_fmac_f32_e32 v16, v128, v36
	v_fmac_f32_e32 v17, v129, v36
	v_fmac_f32_e32 v14, v130, v37
	v_fmac_f32_e32 v15, v131, v37
	v_fmac_f32_e32 v12, v128, v37
	v_fmac_f32_e32 v13, v129, v37
	v_fmac_f32_e32 v10, v130, v38
	v_fmac_f32_e32 v11, v131, v38
	v_fmac_f32_e32 v8, v128, v38
	v_fmac_f32_e32 v9, v129, v38
	v_fmac_f32_e32 v6, v130, v140
	v_fmac_f32_e32 v7, v131, v140
	v_fmac_f32_e32 v4, v128, v140
	v_fmac_f32_e32 v5, v129, v140
	s_addk_i32 s16, 0x200
	v_mov_b32_e32 v144, v123
	s_waitcnt lgkmcnt(1)
	v_fmac_f32_e32 v18, v134, v116
	v_fmac_f32_e32 v19, v135, v116
	v_fmac_f32_e32 v16, v132, v116
	v_fmac_f32_e32 v17, v133, v116
	v_fmac_f32_e32 v14, v134, v117
	v_fmac_f32_e32 v15, v135, v117
	v_fmac_f32_e32 v12, v132, v117
	v_fmac_f32_e32 v13, v133, v117
	v_fmac_f32_e32 v10, v134, v118
	v_fmac_f32_e32 v11, v135, v118
	v_fmac_f32_e32 v8, v132, v118
	v_fmac_f32_e32 v9, v133, v118
	v_fmac_f32_e32 v6, v134, v142
	v_fmac_f32_e32 v7, v135, v142
	v_fmac_f32_e32 v4, v132, v142
	v_fmac_f32_e32 v5, v133, v142
	v_add_u32_e32 v24, 0x440, v24
	s_cmpk_lg_i32 s16, 0x800
	s_waitcnt lgkmcnt(0)
	v_fmac_f32_e32 v18, v138, v120
	v_fmac_f32_e32 v19, v139, v120
	v_fmac_f32_e32 v16, v136, v120
	v_fmac_f32_e32 v17, v137, v120
	v_fmac_f32_e32 v14, v138, v121
	v_fmac_f32_e32 v15, v139, v121
	v_fmac_f32_e32 v12, v136, v121
	v_fmac_f32_e32 v13, v137, v121
	v_fmac_f32_e32 v10, v138, v122
	v_fmac_f32_e32 v11, v139, v122
	v_fmac_f32_e32 v8, v136, v122
	v_fmac_f32_e32 v9, v137, v122
	v_fmac_f32_e32 v6, v138, v144
	v_fmac_f32_e32 v7, v139, v144
	v_fmac_f32_e32 v4, v136, v144
	v_fmac_f32_e32 v5, v137, v144
	s_cbranch_scc1 .LBB0_1493
	s_barrier
	global_load_dwordx4 v[28:31], v[92:93], off offset:1280
	global_load_dwordx4 v[24:27], v[70:71], off
	s_waitcnt vmcnt(3)
	v_cvt_f32_f16_sdwa v128, v32 dst_sel:DWORD dst_unused:UNUSED_PAD src0_sel:WORD_1
	v_cvt_f32_f16_e32 v32, v32
	v_cvt_f32_f16_e32 v129, v33
	v_cvt_f32_f16_sdwa v130, v34 dst_sel:DWORD dst_unused:UNUSED_PAD src0_sel:WORD_1
	v_cvt_f32_f16_e32 v133, v34
	ds_read_b128 v[36:39], v43 offset:14592
	ds_read_b128 v[116:119], v43 offset:14608
	ds_read_b128 v[120:123], v43 offset:18688
	ds_read_b128 v[124:127], v43 offset:18704
	v_cvt_f32_f16_sdwa v115, v33 dst_sel:DWORD dst_unused:UNUSED_PAD src0_sel:WORD_1
	v_cvt_f32_f16_sdwa v131, v35 dst_sel:DWORD dst_unused:UNUSED_PAD src0_sel:WORD_1
	v_cvt_f32_f16_e32 v132, v35
	v_sub_f32_e32 v32, v32, v0
	v_sub_f32_e32 v33, v128, v1
	v_sub_f32_e32 v34, v129, v2
	v_mul_f32_e32 v32, v88, v32
	v_mul_f32_e32 v33, v89, v33
	v_sub_f32_e32 v128, v133, v0
	v_sub_f32_e32 v129, v130, v1
	v_sub_f32_e32 v35, v115, v3
	v_sub_f32_e32 v130, v132, v2
	v_sub_f32_e32 v131, v131, v3
	v_mul_f32_e32 v128, v88, v128
	v_mul_f32_e32 v129, v89, v129
	s_waitcnt lgkmcnt(1)
	v_fma_f32 v32, v36, v32, v120
	v_fma_f32 v33, v37, v33, v121
	v_mul_f32_e32 v34, v90, v34
	v_mul_f32_e32 v35, v91, v35
	v_mul_f32_e32 v130, v90, v130
	v_mul_f32_e32 v131, v91, v131
	s_waitcnt lgkmcnt(0)
	v_fma_f32 v36, v116, v128, v124
	ds_write2_b32 v114, v32, v33 offset1:68
	v_fma_f32 v32, v117, v129, v125
	ds_write2_b32 v113, v36, v32 offset0:16 offset1:84
	v_fma_f32 v32, v38, v34, v122
	v_fma_f32 v33, v118, v130, v126
	v_fmac_f32_e32 v123, v39, v35
	v_fmac_f32_e32 v127, v119, v131
	ds_write2_b32 v114, v32, v123 offset0:136 offset1:204
	ds_write2_b32 v113, v33, v127 offset0:152 offset1:220
	s_waitcnt vmcnt(2)
	ds_write_b128 v96, v[20:23] offset:41984
	s_mov_b32 s16, 0
	v_mov_b32_e32 v20, v103
	s_waitcnt lgkmcnt(0)
	s_barrier
.LBB0_1495:
	v_add_u32_e32 v21, s16, v44
	ds_read_b128 v[32:35], v20
	ds_read_b128 v[36:39], v20 offset:272
	ds_read_b128 v[116:119], v20 offset:544
	ds_read_b128 v[120:123], v20 offset:816
	ds_read_b128 v[124:127], v21
	ds_read_b128 v[128:131], v21 offset:128
	ds_read_b128 v[132:135], v21 offset:256
	ds_read_b128 v[136:139], v21 offset:384
	s_waitcnt lgkmcnt(7)
	v_mov_b32_e32 v22, v35
	s_waitcnt lgkmcnt(6)
	v_mov_b32_e32 v140, v39
	s_waitcnt lgkmcnt(3)
	v_fmac_f32_e32 v18, v126, v32
	v_fmac_f32_e32 v19, v127, v32
	v_fmac_f32_e32 v16, v124, v32
	v_fmac_f32_e32 v17, v125, v32
	v_fmac_f32_e32 v14, v126, v33
	v_fmac_f32_e32 v15, v127, v33
	v_fmac_f32_e32 v12, v124, v33
	v_fmac_f32_e32 v13, v125, v33
	v_fmac_f32_e32 v8, v124, v34
	v_fmac_f32_e32 v9, v125, v34
	v_fmac_f32_e32 v10, v126, v34
	v_fmac_f32_e32 v11, v127, v34
	v_fmac_f32_e32 v4, v124, v22
	v_fmac_f32_e32 v5, v125, v22
	v_fmac_f32_e32 v6, v126, v22
	v_fmac_f32_e32 v7, v127, v22
	v_mov_b32_e32 v142, v119
	s_waitcnt lgkmcnt(2)
	v_fmac_f32_e32 v18, v130, v36
	v_fmac_f32_e32 v19, v131, v36
	v_fmac_f32_e32 v16, v128, v36
	v_fmac_f32_e32 v17, v129, v36
	v_fmac_f32_e32 v14, v130, v37
	v_fmac_f32_e32 v15, v131, v37
	v_fmac_f32_e32 v12, v128, v37
	v_fmac_f32_e32 v13, v129, v37
	v_fmac_f32_e32 v10, v130, v38
	v_fmac_f32_e32 v11, v131, v38
	v_fmac_f32_e32 v8, v128, v38
	v_fmac_f32_e32 v9, v129, v38
	v_fmac_f32_e32 v6, v130, v140
	v_fmac_f32_e32 v7, v131, v140
	v_fmac_f32_e32 v4, v128, v140
	v_fmac_f32_e32 v5, v129, v140
	s_addk_i32 s16, 0x200
	v_mov_b32_e32 v144, v123
	s_waitcnt lgkmcnt(1)
	v_fmac_f32_e32 v18, v134, v116
	v_fmac_f32_e32 v19, v135, v116
	v_fmac_f32_e32 v16, v132, v116
	v_fmac_f32_e32 v17, v133, v116
	v_fmac_f32_e32 v14, v134, v117
	v_fmac_f32_e32 v15, v135, v117
	v_fmac_f32_e32 v12, v132, v117
	v_fmac_f32_e32 v13, v133, v117
	v_fmac_f32_e32 v10, v134, v118
	v_fmac_f32_e32 v11, v135, v118
	v_fmac_f32_e32 v8, v132, v118
	v_fmac_f32_e32 v9, v133, v118
	v_fmac_f32_e32 v6, v134, v142
	v_fmac_f32_e32 v7, v135, v142
	v_fmac_f32_e32 v4, v132, v142
	v_fmac_f32_e32 v5, v133, v142
	v_add_u32_e32 v20, 0x440, v20
	s_cmpk_lg_i32 s16, 0x800
	s_waitcnt lgkmcnt(0)
	v_fmac_f32_e32 v18, v138, v120
	v_fmac_f32_e32 v19, v139, v120
	v_fmac_f32_e32 v16, v136, v120
	v_fmac_f32_e32 v17, v137, v120
	v_fmac_f32_e32 v14, v138, v121
	v_fmac_f32_e32 v15, v139, v121
	v_fmac_f32_e32 v12, v136, v121
	v_fmac_f32_e32 v13, v137, v121
	v_fmac_f32_e32 v10, v138, v122
	v_fmac_f32_e32 v11, v139, v122
	v_fmac_f32_e32 v8, v136, v122
	v_fmac_f32_e32 v9, v137, v122
	v_fmac_f32_e32 v6, v138, v144
	v_fmac_f32_e32 v7, v139, v144
	v_fmac_f32_e32 v4, v136, v144
	v_fmac_f32_e32 v5, v137, v144
	s_cbranch_scc1 .LBB0_1495
	s_barrier
	global_load_dwordx4 v[32:35], v[92:93], off offset:1408
	global_load_dwordx4 v[20:23], v[72:73], off
	s_waitcnt vmcnt(3)
	v_cvt_f32_f16_sdwa v128, v28 dst_sel:DWORD dst_unused:UNUSED_PAD src0_sel:WORD_1
	v_cvt_f32_f16_e32 v28, v28
	v_cvt_f32_f16_e32 v129, v29
	v_cvt_f32_f16_sdwa v130, v30 dst_sel:DWORD dst_unused:UNUSED_PAD src0_sel:WORD_1
	v_cvt_f32_f16_e32 v133, v30
	ds_read_b128 v[36:39], v43 offset:14848
	ds_read_b128 v[116:119], v43 offset:14864
	ds_read_b128 v[120:123], v43 offset:18944
	ds_read_b128 v[124:127], v43 offset:18960
	v_cvt_f32_f16_sdwa v115, v29 dst_sel:DWORD dst_unused:UNUSED_PAD src0_sel:WORD_1
	v_cvt_f32_f16_sdwa v131, v31 dst_sel:DWORD dst_unused:UNUSED_PAD src0_sel:WORD_1
	v_cvt_f32_f16_e32 v132, v31
	v_sub_f32_e32 v28, v28, v0
	v_sub_f32_e32 v29, v128, v1
	v_sub_f32_e32 v30, v129, v2
	v_mul_f32_e32 v28, v88, v28
	v_mul_f32_e32 v29, v89, v29
	v_sub_f32_e32 v128, v133, v0
	v_sub_f32_e32 v129, v130, v1
	v_sub_f32_e32 v31, v115, v3
	v_sub_f32_e32 v130, v132, v2
	v_sub_f32_e32 v131, v131, v3
	v_mul_f32_e32 v128, v88, v128
	v_mul_f32_e32 v129, v89, v129
	s_waitcnt lgkmcnt(1)
	v_fma_f32 v28, v36, v28, v120
	v_fma_f32 v29, v37, v29, v121
	v_mul_f32_e32 v30, v90, v30
	v_mul_f32_e32 v31, v91, v31
	v_mul_f32_e32 v130, v90, v130
	v_mul_f32_e32 v131, v91, v131
	s_waitcnt lgkmcnt(0)
	v_fma_f32 v36, v116, v128, v124
	ds_write2_b32 v114, v28, v29 offset1:68
	v_fma_f32 v28, v117, v129, v125
	ds_write2_b32 v113, v36, v28 offset0:16 offset1:84
	v_fma_f32 v28, v38, v30, v122
	v_fma_f32 v29, v118, v130, v126
	v_fmac_f32_e32 v123, v39, v31
	v_fmac_f32_e32 v127, v119, v131
	ds_write2_b32 v114, v28, v123 offset0:136 offset1:204
	ds_write2_b32 v113, v29, v127 offset0:152 offset1:220
	s_waitcnt vmcnt(2)
	ds_write_b128 v96, v[24:27] offset:41984
	s_mov_b32 s16, 0
	v_mov_b32_e32 v24, v103
	s_waitcnt lgkmcnt(0)
	s_barrier
.LBB0_1497:
	v_add_u32_e32 v25, s16, v44
	ds_read_b128 v[26:29], v24
	ds_read_b128 v[36:39], v24 offset:272
	ds_read_b128 v[116:119], v24 offset:544
	ds_read_b128 v[120:123], v24 offset:816
	ds_read_b128 v[124:127], v25
	ds_read_b128 v[128:131], v25 offset:128
	ds_read_b128 v[132:135], v25 offset:256
	ds_read_b128 v[136:139], v25 offset:384
	s_waitcnt lgkmcnt(7)
	v_mov_b32_e32 v30, v29
	s_waitcnt lgkmcnt(6)
	v_mov_b32_e32 v140, v39
	s_waitcnt lgkmcnt(3)
	v_fmac_f32_e32 v18, v126, v26
	v_fmac_f32_e32 v19, v127, v26
	v_fmac_f32_e32 v16, v124, v26
	v_fmac_f32_e32 v17, v125, v26
	v_fmac_f32_e32 v14, v126, v27
	v_fmac_f32_e32 v15, v127, v27
	v_fmac_f32_e32 v12, v124, v27
	v_fmac_f32_e32 v13, v125, v27
	v_fmac_f32_e32 v8, v124, v28
	v_fmac_f32_e32 v9, v125, v28
	v_fmac_f32_e32 v10, v126, v28
	v_fmac_f32_e32 v11, v127, v28
	v_fmac_f32_e32 v4, v124, v30
	v_fmac_f32_e32 v5, v125, v30
	v_fmac_f32_e32 v6, v126, v30
	v_fmac_f32_e32 v7, v127, v30
	v_mov_b32_e32 v142, v119
	s_waitcnt lgkmcnt(2)
	v_fmac_f32_e32 v18, v130, v36
	v_fmac_f32_e32 v19, v131, v36
	v_fmac_f32_e32 v16, v128, v36
	v_fmac_f32_e32 v17, v129, v36
	v_fmac_f32_e32 v14, v130, v37
	v_fmac_f32_e32 v15, v131, v37
	v_fmac_f32_e32 v12, v128, v37
	v_fmac_f32_e32 v13, v129, v37
	v_fmac_f32_e32 v10, v130, v38
	v_fmac_f32_e32 v11, v131, v38
	v_fmac_f32_e32 v8, v128, v38
	v_fmac_f32_e32 v9, v129, v38
	v_fmac_f32_e32 v6, v130, v140
	v_fmac_f32_e32 v7, v131, v140
	v_fmac_f32_e32 v4, v128, v140
	v_fmac_f32_e32 v5, v129, v140
	s_addk_i32 s16, 0x200
	v_mov_b32_e32 v144, v123
	s_waitcnt lgkmcnt(1)
	v_fmac_f32_e32 v18, v134, v116
	v_fmac_f32_e32 v19, v135, v116
	v_fmac_f32_e32 v16, v132, v116
	v_fmac_f32_e32 v17, v133, v116
	v_fmac_f32_e32 v14, v134, v117
	v_fmac_f32_e32 v15, v135, v117
	v_fmac_f32_e32 v12, v132, v117
	v_fmac_f32_e32 v13, v133, v117
	v_fmac_f32_e32 v10, v134, v118
	v_fmac_f32_e32 v11, v135, v118
	v_fmac_f32_e32 v8, v132, v118
	v_fmac_f32_e32 v9, v133, v118
	v_fmac_f32_e32 v6, v134, v142
	v_fmac_f32_e32 v7, v135, v142
	v_fmac_f32_e32 v4, v132, v142
	v_fmac_f32_e32 v5, v133, v142
	v_add_u32_e32 v24, 0x440, v24
	s_cmpk_lg_i32 s16, 0x800
	s_waitcnt lgkmcnt(0)
	v_fmac_f32_e32 v18, v138, v120
	v_fmac_f32_e32 v19, v139, v120
	v_fmac_f32_e32 v16, v136, v120
	v_fmac_f32_e32 v17, v137, v120
	v_fmac_f32_e32 v14, v138, v121
	v_fmac_f32_e32 v15, v139, v121
	v_fmac_f32_e32 v12, v136, v121
	v_fmac_f32_e32 v13, v137, v121
	v_fmac_f32_e32 v10, v138, v122
	v_fmac_f32_e32 v11, v139, v122
	v_fmac_f32_e32 v8, v136, v122
	v_fmac_f32_e32 v9, v137, v122
	v_fmac_f32_e32 v6, v138, v144
	v_fmac_f32_e32 v7, v139, v144
	v_fmac_f32_e32 v4, v136, v144
	v_fmac_f32_e32 v5, v137, v144
	s_cbranch_scc1 .LBB0_1497
	s_barrier
	global_load_dwordx4 v[28:31], v[92:93], off offset:1536
	global_load_dwordx4 v[24:27], v[74:75], off
	s_waitcnt vmcnt(3)
	v_cvt_f32_f16_sdwa v128, v32 dst_sel:DWORD dst_unused:UNUSED_PAD src0_sel:WORD_1
	v_cvt_f32_f16_e32 v32, v32
	v_cvt_f32_f16_e32 v129, v33
	v_cvt_f32_f16_sdwa v130, v34 dst_sel:DWORD dst_unused:UNUSED_PAD src0_sel:WORD_1
	v_cvt_f32_f16_e32 v133, v34
	ds_read_b128 v[36:39], v43 offset:15104
	ds_read_b128 v[116:119], v43 offset:15120
	ds_read_b128 v[120:123], v43 offset:19200
	ds_read_b128 v[124:127], v43 offset:19216
	v_cvt_f32_f16_sdwa v115, v33 dst_sel:DWORD dst_unused:UNUSED_PAD src0_sel:WORD_1
	v_cvt_f32_f16_sdwa v131, v35 dst_sel:DWORD dst_unused:UNUSED_PAD src0_sel:WORD_1
	v_cvt_f32_f16_e32 v132, v35
	v_sub_f32_e32 v32, v32, v0
	v_sub_f32_e32 v33, v128, v1
	v_sub_f32_e32 v34, v129, v2
	v_mul_f32_e32 v32, v88, v32
	v_mul_f32_e32 v33, v89, v33
	v_sub_f32_e32 v128, v133, v0
	v_sub_f32_e32 v129, v130, v1
	v_sub_f32_e32 v35, v115, v3
	v_sub_f32_e32 v130, v132, v2
	v_sub_f32_e32 v131, v131, v3
	v_mul_f32_e32 v128, v88, v128
	v_mul_f32_e32 v129, v89, v129
	s_waitcnt lgkmcnt(1)
	v_fma_f32 v32, v36, v32, v120
	v_fma_f32 v33, v37, v33, v121
	v_mul_f32_e32 v34, v90, v34
	v_mul_f32_e32 v35, v91, v35
	v_mul_f32_e32 v130, v90, v130
	v_mul_f32_e32 v131, v91, v131
	s_waitcnt lgkmcnt(0)
	v_fma_f32 v36, v116, v128, v124
	ds_write2_b32 v114, v32, v33 offset1:68
	v_fma_f32 v32, v117, v129, v125
	ds_write2_b32 v113, v36, v32 offset0:16 offset1:84
	v_fma_f32 v32, v38, v34, v122
	v_fma_f32 v33, v118, v130, v126
	v_fmac_f32_e32 v123, v39, v35
	v_fmac_f32_e32 v127, v119, v131
	ds_write2_b32 v114, v32, v123 offset0:136 offset1:204
	ds_write2_b32 v113, v33, v127 offset0:152 offset1:220
	s_waitcnt vmcnt(2)
	ds_write_b128 v96, v[20:23] offset:41984
	s_mov_b32 s16, 0
	v_mov_b32_e32 v20, v103
	s_waitcnt lgkmcnt(0)
	s_barrier
.LBB0_1499:
	v_add_u32_e32 v21, s16, v44
	ds_read_b128 v[32:35], v20
	ds_read_b128 v[36:39], v20 offset:272
	ds_read_b128 v[116:119], v20 offset:544
	ds_read_b128 v[120:123], v20 offset:816
	ds_read_b128 v[124:127], v21
	ds_read_b128 v[128:131], v21 offset:128
	ds_read_b128 v[132:135], v21 offset:256
	ds_read_b128 v[136:139], v21 offset:384
	s_waitcnt lgkmcnt(7)
	v_mov_b32_e32 v22, v35
	s_waitcnt lgkmcnt(6)
	v_mov_b32_e32 v140, v39
	s_waitcnt lgkmcnt(3)
	v_fmac_f32_e32 v18, v126, v32
	v_fmac_f32_e32 v19, v127, v32
	v_fmac_f32_e32 v16, v124, v32
	v_fmac_f32_e32 v17, v125, v32
	v_fmac_f32_e32 v14, v126, v33
	v_fmac_f32_e32 v15, v127, v33
	v_fmac_f32_e32 v12, v124, v33
	v_fmac_f32_e32 v13, v125, v33
	v_fmac_f32_e32 v8, v124, v34
	v_fmac_f32_e32 v9, v125, v34
	v_fmac_f32_e32 v10, v126, v34
	v_fmac_f32_e32 v11, v127, v34
	v_fmac_f32_e32 v4, v124, v22
	v_fmac_f32_e32 v5, v125, v22
	v_fmac_f32_e32 v6, v126, v22
	v_fmac_f32_e32 v7, v127, v22
	v_mov_b32_e32 v142, v119
	s_waitcnt lgkmcnt(2)
	v_fmac_f32_e32 v18, v130, v36
	v_fmac_f32_e32 v19, v131, v36
	v_fmac_f32_e32 v16, v128, v36
	v_fmac_f32_e32 v17, v129, v36
	v_fmac_f32_e32 v14, v130, v37
	v_fmac_f32_e32 v15, v131, v37
	v_fmac_f32_e32 v12, v128, v37
	v_fmac_f32_e32 v13, v129, v37
	v_fmac_f32_e32 v10, v130, v38
	v_fmac_f32_e32 v11, v131, v38
	v_fmac_f32_e32 v8, v128, v38
	v_fmac_f32_e32 v9, v129, v38
	v_fmac_f32_e32 v6, v130, v140
	v_fmac_f32_e32 v7, v131, v140
	v_fmac_f32_e32 v4, v128, v140
	v_fmac_f32_e32 v5, v129, v140
	s_addk_i32 s16, 0x200
	v_mov_b32_e32 v144, v123
	s_waitcnt lgkmcnt(1)
	v_fmac_f32_e32 v18, v134, v116
	v_fmac_f32_e32 v19, v135, v116
	v_fmac_f32_e32 v16, v132, v116
	v_fmac_f32_e32 v17, v133, v116
	v_fmac_f32_e32 v14, v134, v117
	v_fmac_f32_e32 v15, v135, v117
	v_fmac_f32_e32 v12, v132, v117
	v_fmac_f32_e32 v13, v133, v117
	v_fmac_f32_e32 v10, v134, v118
	v_fmac_f32_e32 v11, v135, v118
	v_fmac_f32_e32 v8, v132, v118
	v_fmac_f32_e32 v9, v133, v118
	v_fmac_f32_e32 v6, v134, v142
	v_fmac_f32_e32 v7, v135, v142
	v_fmac_f32_e32 v4, v132, v142
	v_fmac_f32_e32 v5, v133, v142
	v_add_u32_e32 v20, 0x440, v20
	s_cmpk_lg_i32 s16, 0x800
	s_waitcnt lgkmcnt(0)
	v_fmac_f32_e32 v18, v138, v120
	v_fmac_f32_e32 v19, v139, v120
	v_fmac_f32_e32 v16, v136, v120
	v_fmac_f32_e32 v17, v137, v120
	v_fmac_f32_e32 v14, v138, v121
	v_fmac_f32_e32 v15, v139, v121
	v_fmac_f32_e32 v12, v136, v121
	v_fmac_f32_e32 v13, v137, v121
	v_fmac_f32_e32 v10, v138, v122
	v_fmac_f32_e32 v11, v139, v122
	v_fmac_f32_e32 v8, v136, v122
	v_fmac_f32_e32 v9, v137, v122
	v_fmac_f32_e32 v6, v138, v144
	v_fmac_f32_e32 v7, v139, v144
	v_fmac_f32_e32 v4, v136, v144
	v_fmac_f32_e32 v5, v137, v144
	s_cbranch_scc1 .LBB0_1499
	s_barrier
	global_load_dwordx4 v[32:35], v[92:93], off offset:1664
	global_load_dwordx4 v[20:23], v[76:77], off
	s_waitcnt vmcnt(3)
	v_cvt_f32_f16_sdwa v128, v28 dst_sel:DWORD dst_unused:UNUSED_PAD src0_sel:WORD_1
	v_cvt_f32_f16_e32 v28, v28
	v_cvt_f32_f16_e32 v129, v29
	v_cvt_f32_f16_sdwa v130, v30 dst_sel:DWORD dst_unused:UNUSED_PAD src0_sel:WORD_1
	v_cvt_f32_f16_e32 v133, v30
	ds_read_b128 v[36:39], v43 offset:15360
	ds_read_b128 v[116:119], v43 offset:15376
	ds_read_b128 v[120:123], v43 offset:19456
	ds_read_b128 v[124:127], v43 offset:19472
	v_cvt_f32_f16_sdwa v115, v29 dst_sel:DWORD dst_unused:UNUSED_PAD src0_sel:WORD_1
	v_cvt_f32_f16_sdwa v131, v31 dst_sel:DWORD dst_unused:UNUSED_PAD src0_sel:WORD_1
	v_cvt_f32_f16_e32 v132, v31
	v_sub_f32_e32 v28, v28, v0
	v_sub_f32_e32 v29, v128, v1
	v_sub_f32_e32 v30, v129, v2
	v_mul_f32_e32 v28, v88, v28
	v_mul_f32_e32 v29, v89, v29
	v_sub_f32_e32 v128, v133, v0
	v_sub_f32_e32 v129, v130, v1
	v_sub_f32_e32 v31, v115, v3
	v_sub_f32_e32 v130, v132, v2
	v_sub_f32_e32 v131, v131, v3
	v_mul_f32_e32 v128, v88, v128
	v_mul_f32_e32 v129, v89, v129
	s_waitcnt lgkmcnt(1)
	v_fma_f32 v28, v36, v28, v120
	v_fma_f32 v29, v37, v29, v121
	v_mul_f32_e32 v30, v90, v30
	v_mul_f32_e32 v31, v91, v31
	v_mul_f32_e32 v130, v90, v130
	v_mul_f32_e32 v131, v91, v131
	s_waitcnt lgkmcnt(0)
	v_fma_f32 v36, v116, v128, v124
	ds_write2_b32 v114, v28, v29 offset1:68
	v_fma_f32 v28, v117, v129, v125
	ds_write2_b32 v113, v36, v28 offset0:16 offset1:84
	v_fma_f32 v28, v38, v30, v122
	v_fma_f32 v29, v118, v130, v126
	v_fmac_f32_e32 v123, v39, v31
	v_fmac_f32_e32 v127, v119, v131
	ds_write2_b32 v114, v28, v123 offset0:136 offset1:204
	ds_write2_b32 v113, v29, v127 offset0:152 offset1:220
	s_waitcnt vmcnt(2)
	ds_write_b128 v96, v[24:27] offset:41984
	s_mov_b32 s16, 0
	v_mov_b32_e32 v24, v103
	s_waitcnt lgkmcnt(0)
	s_barrier
.LBB0_1501:
	v_add_u32_e32 v25, s16, v44
	ds_read_b128 v[26:29], v24
	ds_read_b128 v[36:39], v24 offset:272
	ds_read_b128 v[116:119], v24 offset:544
	ds_read_b128 v[120:123], v24 offset:816
	ds_read_b128 v[124:127], v25
	ds_read_b128 v[128:131], v25 offset:128
	ds_read_b128 v[132:135], v25 offset:256
	ds_read_b128 v[136:139], v25 offset:384
	s_waitcnt lgkmcnt(7)
	v_mov_b32_e32 v30, v29
	s_waitcnt lgkmcnt(6)
	v_mov_b32_e32 v140, v39
	s_waitcnt lgkmcnt(3)
	v_fmac_f32_e32 v18, v126, v26
	v_fmac_f32_e32 v19, v127, v26
	v_fmac_f32_e32 v16, v124, v26
	v_fmac_f32_e32 v17, v125, v26
	v_fmac_f32_e32 v14, v126, v27
	v_fmac_f32_e32 v15, v127, v27
	v_fmac_f32_e32 v12, v124, v27
	v_fmac_f32_e32 v13, v125, v27
	v_fmac_f32_e32 v8, v124, v28
	v_fmac_f32_e32 v9, v125, v28
	v_fmac_f32_e32 v10, v126, v28
	v_fmac_f32_e32 v11, v127, v28
	v_fmac_f32_e32 v4, v124, v30
	v_fmac_f32_e32 v5, v125, v30
	v_fmac_f32_e32 v6, v126, v30
	v_fmac_f32_e32 v7, v127, v30
	v_mov_b32_e32 v142, v119
	s_waitcnt lgkmcnt(2)
	v_fmac_f32_e32 v18, v130, v36
	v_fmac_f32_e32 v19, v131, v36
	v_fmac_f32_e32 v16, v128, v36
	v_fmac_f32_e32 v17, v129, v36
	v_fmac_f32_e32 v14, v130, v37
	v_fmac_f32_e32 v15, v131, v37
	v_fmac_f32_e32 v12, v128, v37
	v_fmac_f32_e32 v13, v129, v37
	v_fmac_f32_e32 v10, v130, v38
	v_fmac_f32_e32 v11, v131, v38
	v_fmac_f32_e32 v8, v128, v38
	v_fmac_f32_e32 v9, v129, v38
	v_fmac_f32_e32 v6, v130, v140
	v_fmac_f32_e32 v7, v131, v140
	v_fmac_f32_e32 v4, v128, v140
	v_fmac_f32_e32 v5, v129, v140
	s_addk_i32 s16, 0x200
	v_mov_b32_e32 v144, v123
	s_waitcnt lgkmcnt(1)
	v_fmac_f32_e32 v18, v134, v116
	v_fmac_f32_e32 v19, v135, v116
	v_fmac_f32_e32 v16, v132, v116
	v_fmac_f32_e32 v17, v133, v116
	v_fmac_f32_e32 v14, v134, v117
	v_fmac_f32_e32 v15, v135, v117
	v_fmac_f32_e32 v12, v132, v117
	v_fmac_f32_e32 v13, v133, v117
	v_fmac_f32_e32 v10, v134, v118
	v_fmac_f32_e32 v11, v135, v118
	v_fmac_f32_e32 v8, v132, v118
	v_fmac_f32_e32 v9, v133, v118
	v_fmac_f32_e32 v6, v134, v142
	v_fmac_f32_e32 v7, v135, v142
	v_fmac_f32_e32 v4, v132, v142
	v_fmac_f32_e32 v5, v133, v142
	v_add_u32_e32 v24, 0x440, v24
	s_cmpk_lg_i32 s16, 0x800
	s_waitcnt lgkmcnt(0)
	v_fmac_f32_e32 v18, v138, v120
	v_fmac_f32_e32 v19, v139, v120
	v_fmac_f32_e32 v16, v136, v120
	v_fmac_f32_e32 v17, v137, v120
	v_fmac_f32_e32 v14, v138, v121
	v_fmac_f32_e32 v15, v139, v121
	v_fmac_f32_e32 v12, v136, v121
	v_fmac_f32_e32 v13, v137, v121
	v_fmac_f32_e32 v10, v138, v122
	v_fmac_f32_e32 v11, v139, v122
	v_fmac_f32_e32 v8, v136, v122
	v_fmac_f32_e32 v9, v137, v122
	v_fmac_f32_e32 v6, v138, v144
	v_fmac_f32_e32 v7, v139, v144
	v_fmac_f32_e32 v4, v136, v144
	v_fmac_f32_e32 v5, v137, v144
	s_cbranch_scc1 .LBB0_1501
	s_barrier
	global_load_dwordx4 v[28:31], v[92:93], off offset:1792
	global_load_dwordx4 v[24:27], v[78:79], off
	s_waitcnt vmcnt(3)
	v_cvt_f32_f16_sdwa v128, v32 dst_sel:DWORD dst_unused:UNUSED_PAD src0_sel:WORD_1
	v_cvt_f32_f16_e32 v32, v32
	v_cvt_f32_f16_e32 v129, v33
	v_cvt_f32_f16_sdwa v130, v34 dst_sel:DWORD dst_unused:UNUSED_PAD src0_sel:WORD_1
	v_cvt_f32_f16_e32 v133, v34
	ds_read_b128 v[36:39], v43 offset:15616
	ds_read_b128 v[116:119], v43 offset:15632
	ds_read_b128 v[120:123], v43 offset:19712
	ds_read_b128 v[124:127], v43 offset:19728
	v_cvt_f32_f16_sdwa v115, v33 dst_sel:DWORD dst_unused:UNUSED_PAD src0_sel:WORD_1
	v_cvt_f32_f16_sdwa v131, v35 dst_sel:DWORD dst_unused:UNUSED_PAD src0_sel:WORD_1
	v_cvt_f32_f16_e32 v132, v35
	v_sub_f32_e32 v32, v32, v0
	v_sub_f32_e32 v33, v128, v1
	v_sub_f32_e32 v34, v129, v2
	v_mul_f32_e32 v32, v88, v32
	v_mul_f32_e32 v33, v89, v33
	v_sub_f32_e32 v128, v133, v0
	v_sub_f32_e32 v129, v130, v1
	v_sub_f32_e32 v35, v115, v3
	v_sub_f32_e32 v130, v132, v2
	v_sub_f32_e32 v131, v131, v3
	v_mul_f32_e32 v128, v88, v128
	v_mul_f32_e32 v129, v89, v129
	s_waitcnt lgkmcnt(1)
	v_fma_f32 v32, v36, v32, v120
	v_fma_f32 v33, v37, v33, v121
	v_mul_f32_e32 v34, v90, v34
	v_mul_f32_e32 v35, v91, v35
	v_mul_f32_e32 v130, v90, v130
	v_mul_f32_e32 v131, v91, v131
	s_waitcnt lgkmcnt(0)
	v_fma_f32 v36, v116, v128, v124
	ds_write2_b32 v114, v32, v33 offset1:68
	v_fma_f32 v32, v117, v129, v125
	ds_write2_b32 v113, v36, v32 offset0:16 offset1:84
	v_fma_f32 v32, v38, v34, v122
	v_fma_f32 v33, v118, v130, v126
	v_fmac_f32_e32 v123, v39, v35
	v_fmac_f32_e32 v127, v119, v131
	ds_write2_b32 v114, v32, v123 offset0:136 offset1:204
	ds_write2_b32 v113, v33, v127 offset0:152 offset1:220
	s_waitcnt vmcnt(2)
	ds_write_b128 v96, v[20:23] offset:41984
	s_mov_b32 s16, 0
	v_mov_b32_e32 v20, v103
	s_waitcnt lgkmcnt(0)
	s_barrier
.LBB0_1503:
	v_add_u32_e32 v21, s16, v44
	ds_read_b128 v[32:35], v20
	ds_read_b128 v[36:39], v20 offset:272
	ds_read_b128 v[116:119], v20 offset:544
	ds_read_b128 v[120:123], v20 offset:816
	ds_read_b128 v[124:127], v21
	ds_read_b128 v[128:131], v21 offset:128
	ds_read_b128 v[132:135], v21 offset:256
	ds_read_b128 v[136:139], v21 offset:384
	s_waitcnt lgkmcnt(7)
	v_mov_b32_e32 v22, v35
	s_waitcnt lgkmcnt(6)
	v_mov_b32_e32 v140, v39
	s_waitcnt lgkmcnt(3)
	v_fmac_f32_e32 v18, v126, v32
	v_fmac_f32_e32 v19, v127, v32
	v_fmac_f32_e32 v16, v124, v32
	v_fmac_f32_e32 v17, v125, v32
	v_fmac_f32_e32 v14, v126, v33
	v_fmac_f32_e32 v15, v127, v33
	v_fmac_f32_e32 v12, v124, v33
	v_fmac_f32_e32 v13, v125, v33
	v_fmac_f32_e32 v8, v124, v34
	v_fmac_f32_e32 v9, v125, v34
	v_fmac_f32_e32 v10, v126, v34
	v_fmac_f32_e32 v11, v127, v34
	v_fmac_f32_e32 v4, v124, v22
	v_fmac_f32_e32 v5, v125, v22
	v_fmac_f32_e32 v6, v126, v22
	v_fmac_f32_e32 v7, v127, v22
	v_mov_b32_e32 v142, v119
	s_waitcnt lgkmcnt(2)
	v_fmac_f32_e32 v18, v130, v36
	v_fmac_f32_e32 v19, v131, v36
	v_fmac_f32_e32 v16, v128, v36
	v_fmac_f32_e32 v17, v129, v36
	v_fmac_f32_e32 v14, v130, v37
	v_fmac_f32_e32 v15, v131, v37
	v_fmac_f32_e32 v12, v128, v37
	v_fmac_f32_e32 v13, v129, v37
	v_fmac_f32_e32 v10, v130, v38
	v_fmac_f32_e32 v11, v131, v38
	v_fmac_f32_e32 v8, v128, v38
	v_fmac_f32_e32 v9, v129, v38
	v_fmac_f32_e32 v6, v130, v140
	v_fmac_f32_e32 v7, v131, v140
	v_fmac_f32_e32 v4, v128, v140
	v_fmac_f32_e32 v5, v129, v140
	s_addk_i32 s16, 0x200
	v_mov_b32_e32 v144, v123
	s_waitcnt lgkmcnt(1)
	v_fmac_f32_e32 v18, v134, v116
	v_fmac_f32_e32 v19, v135, v116
	v_fmac_f32_e32 v16, v132, v116
	v_fmac_f32_e32 v17, v133, v116
	v_fmac_f32_e32 v14, v134, v117
	v_fmac_f32_e32 v15, v135, v117
	v_fmac_f32_e32 v12, v132, v117
	v_fmac_f32_e32 v13, v133, v117
	v_fmac_f32_e32 v10, v134, v118
	v_fmac_f32_e32 v11, v135, v118
	v_fmac_f32_e32 v8, v132, v118
	v_fmac_f32_e32 v9, v133, v118
	v_fmac_f32_e32 v6, v134, v142
	v_fmac_f32_e32 v7, v135, v142
	v_fmac_f32_e32 v4, v132, v142
	v_fmac_f32_e32 v5, v133, v142
	v_add_u32_e32 v20, 0x440, v20
	s_cmpk_lg_i32 s16, 0x800
	s_waitcnt lgkmcnt(0)
	v_fmac_f32_e32 v18, v138, v120
	v_fmac_f32_e32 v19, v139, v120
	v_fmac_f32_e32 v16, v136, v120
	v_fmac_f32_e32 v17, v137, v120
	v_fmac_f32_e32 v14, v138, v121
	v_fmac_f32_e32 v15, v139, v121
	v_fmac_f32_e32 v12, v136, v121
	v_fmac_f32_e32 v13, v137, v121
	v_fmac_f32_e32 v10, v138, v122
	v_fmac_f32_e32 v11, v139, v122
	v_fmac_f32_e32 v8, v136, v122
	v_fmac_f32_e32 v9, v137, v122
	v_fmac_f32_e32 v6, v138, v144
	v_fmac_f32_e32 v7, v139, v144
	v_fmac_f32_e32 v4, v136, v144
	v_fmac_f32_e32 v5, v137, v144
	s_cbranch_scc1 .LBB0_1503
	s_barrier
	global_load_dwordx4 v[32:35], v[92:93], off offset:1920
	global_load_dwordx4 v[20:23], v[80:81], off
	s_waitcnt vmcnt(3)
	v_cvt_f32_f16_sdwa v93, v28 dst_sel:DWORD dst_unused:UNUSED_PAD src0_sel:WORD_1
	v_cvt_f32_f16_e32 v28, v28
	v_cvt_f32_f16_sdwa v92, v29 dst_sel:DWORD dst_unused:UNUSED_PAD src0_sel:WORD_1
	v_cvt_f32_f16_sdwa v128, v30 dst_sel:DWORD dst_unused:UNUSED_PAD src0_sel:WORD_1
	v_cvt_f32_f16_e32 v131, v30
	ds_read_b128 v[36:39], v43 offset:15872
	ds_read_b128 v[116:119], v43 offset:15888
	ds_read_b128 v[120:123], v43 offset:19968
	ds_read_b128 v[124:127], v43 offset:19984
	v_cvt_f32_f16_e32 v115, v29
	v_cvt_f32_f16_sdwa v129, v31 dst_sel:DWORD dst_unused:UNUSED_PAD src0_sel:WORD_1
	v_cvt_f32_f16_e32 v130, v31
	v_sub_f32_e32 v28, v28, v0
	v_sub_f32_e32 v29, v93, v1
	v_sub_f32_e32 v31, v92, v3
	v_mul_f32_e32 v28, v88, v28
	v_mul_f32_e32 v29, v89, v29
	v_sub_f32_e32 v92, v131, v0
	v_sub_f32_e32 v93, v128, v1
	v_sub_f32_e32 v30, v115, v2
	v_sub_f32_e32 v128, v130, v2
	v_sub_f32_e32 v129, v129, v3
	v_mul_f32_e32 v92, v88, v92
	v_mul_f32_e32 v93, v89, v93
	s_waitcnt lgkmcnt(1)
	v_fma_f32 v28, v36, v28, v120
	v_fma_f32 v29, v37, v29, v121
	v_mul_f32_e32 v30, v90, v30
	v_mul_f32_e32 v31, v91, v31
	v_mul_f32_e32 v128, v90, v128
	v_mul_f32_e32 v129, v91, v129
	s_waitcnt lgkmcnt(0)
	v_fma_f32 v36, v116, v92, v124
	ds_write2_b32 v114, v28, v29 offset1:68
	v_fma_f32 v28, v117, v93, v125
	ds_write2_b32 v113, v36, v28 offset0:16 offset1:84
	v_fma_f32 v28, v38, v30, v122
	v_fma_f32 v29, v118, v128, v126
	v_fmac_f32_e32 v123, v39, v31
	v_fmac_f32_e32 v127, v119, v129
	ds_write2_b32 v114, v28, v123 offset0:136 offset1:204
	ds_write2_b32 v113, v29, v127 offset0:152 offset1:220
	s_waitcnt vmcnt(2)
	ds_write_b128 v96, v[24:27] offset:41984
	s_mov_b32 s16, 0
	v_mov_b32_e32 v24, v103
	s_waitcnt lgkmcnt(0)
	s_barrier
.LBB0_1505:
	v_add_u32_e32 v25, s16, v44
	ds_read_b128 v[26:29], v24
	ds_read_b128 v[36:39], v24 offset:272
	ds_read_b128 v[116:119], v24 offset:544
	ds_read_b128 v[120:123], v24 offset:816
	ds_read_b128 v[124:127], v25
	ds_read_b128 v[128:131], v25 offset:128
	ds_read_b128 v[132:135], v25 offset:256
	ds_read_b128 v[136:139], v25 offset:384
	s_waitcnt lgkmcnt(7)
	v_mov_b32_e32 v30, v29
	s_waitcnt lgkmcnt(6)
	v_mov_b32_e32 v92, v39
	s_waitcnt lgkmcnt(3)
	v_fmac_f32_e32 v18, v126, v26
	v_fmac_f32_e32 v19, v127, v26
	v_fmac_f32_e32 v16, v124, v26
	v_fmac_f32_e32 v17, v125, v26
	v_fmac_f32_e32 v14, v126, v27
	v_fmac_f32_e32 v15, v127, v27
	v_fmac_f32_e32 v12, v124, v27
	v_fmac_f32_e32 v13, v125, v27
	v_fmac_f32_e32 v8, v124, v28
	v_fmac_f32_e32 v9, v125, v28
	v_fmac_f32_e32 v10, v126, v28
	v_fmac_f32_e32 v11, v127, v28
	v_fmac_f32_e32 v4, v124, v30
	v_fmac_f32_e32 v5, v125, v30
	v_fmac_f32_e32 v6, v126, v30
	v_fmac_f32_e32 v7, v127, v30
	v_mov_b32_e32 v140, v119
	s_waitcnt lgkmcnt(2)
	v_fmac_f32_e32 v18, v130, v36
	v_fmac_f32_e32 v19, v131, v36
	v_fmac_f32_e32 v16, v128, v36
	v_fmac_f32_e32 v17, v129, v36
	v_fmac_f32_e32 v14, v130, v37
	v_fmac_f32_e32 v15, v131, v37
	v_fmac_f32_e32 v12, v128, v37
	v_fmac_f32_e32 v13, v129, v37
	v_fmac_f32_e32 v10, v130, v38
	v_fmac_f32_e32 v11, v131, v38
	v_fmac_f32_e32 v8, v128, v38
	v_fmac_f32_e32 v9, v129, v38
	v_fmac_f32_e32 v6, v130, v92
	v_fmac_f32_e32 v7, v131, v92
	v_fmac_f32_e32 v4, v128, v92
	v_fmac_f32_e32 v5, v129, v92
	s_addk_i32 s16, 0x200
	v_mov_b32_e32 v142, v123
	s_waitcnt lgkmcnt(1)
	v_fmac_f32_e32 v18, v134, v116
	v_fmac_f32_e32 v19, v135, v116
	v_fmac_f32_e32 v16, v132, v116
	v_fmac_f32_e32 v17, v133, v116
	v_fmac_f32_e32 v14, v134, v117
	v_fmac_f32_e32 v15, v135, v117
	v_fmac_f32_e32 v12, v132, v117
	v_fmac_f32_e32 v13, v133, v117
	v_fmac_f32_e32 v10, v134, v118
	v_fmac_f32_e32 v11, v135, v118
	v_fmac_f32_e32 v8, v132, v118
	v_fmac_f32_e32 v9, v133, v118
	v_fmac_f32_e32 v6, v134, v140
	v_fmac_f32_e32 v7, v135, v140
	v_fmac_f32_e32 v4, v132, v140
	v_fmac_f32_e32 v5, v133, v140
	v_add_u32_e32 v24, 0x440, v24
	s_cmpk_lg_i32 s16, 0x800
	s_waitcnt lgkmcnt(0)
	v_fmac_f32_e32 v18, v138, v120
	v_fmac_f32_e32 v19, v139, v120
	v_fmac_f32_e32 v16, v136, v120
	v_fmac_f32_e32 v17, v137, v120
	v_fmac_f32_e32 v14, v138, v121
	v_fmac_f32_e32 v15, v139, v121
	v_fmac_f32_e32 v12, v136, v121
	v_fmac_f32_e32 v13, v137, v121
	v_fmac_f32_e32 v10, v138, v122
	v_fmac_f32_e32 v11, v139, v122
	v_fmac_f32_e32 v8, v136, v122
	v_fmac_f32_e32 v9, v137, v122
	v_fmac_f32_e32 v6, v138, v142
	v_fmac_f32_e32 v7, v139, v142
	v_fmac_f32_e32 v4, v136, v142
	v_fmac_f32_e32 v5, v137, v142
	s_cbranch_scc1 .LBB0_1505
	s_waitcnt vmcnt(1)
	v_cvt_f32_f16_sdwa v93, v32 dst_sel:DWORD dst_unused:UNUSED_PAD src0_sel:WORD_1
	v_cvt_f32_f16_e32 v32, v32
	v_cvt_f32_f16_sdwa v121, v34 dst_sel:DWORD dst_unused:UNUSED_PAD src0_sel:WORD_1
	v_cvt_f32_f16_e32 v123, v34
	s_barrier
	ds_read_b128 v[24:27], v43 offset:16128
	ds_read_b128 v[28:31], v43 offset:16144
	ds_read_b128 v[36:39], v43 offset:20224
	ds_read_b128 v[116:119], v43 offset:20240
	v_cvt_f32_f16_sdwa v92, v33 dst_sel:DWORD dst_unused:UNUSED_PAD src0_sel:WORD_1
	v_cvt_f32_f16_e32 v115, v33
	v_cvt_f32_f16_sdwa v120, v35 dst_sel:DWORD dst_unused:UNUSED_PAD src0_sel:WORD_1
	v_cvt_f32_f16_e32 v122, v35
	v_sub_f32_e32 v32, v32, v0
	v_sub_f32_e32 v33, v93, v1
	v_sub_f32_e32 v0, v123, v0
	v_sub_f32_e32 v1, v121, v1
	v_sub_f32_e32 v34, v115, v2
	v_sub_f32_e32 v35, v92, v3
	v_mul_f32_e32 v0, v88, v0
	v_mul_f32_e32 v1, v89, v1
	v_mul_f32_e32 v34, v90, v34
	v_mul_f32_e32 v35, v91, v35
	v_sub_f32_e32 v2, v122, v2
	v_sub_f32_e32 v3, v120, v3
	s_waitcnt lgkmcnt(0)
	v_fma_f32 v0, v28, v0, v116
	v_fma_f32 v1, v29, v1, v117
	v_mul_f32_e32 v32, v88, v32
	v_mul_f32_e32 v33, v89, v33
	v_mul_f32_e32 v2, v90, v2
	v_mul_f32_e32 v3, v91, v3
	ds_write2_b32 v113, v0, v1 offset0:16 offset1:84
	v_fma_f32 v0, v26, v34, v38
	v_fmac_f32_e32 v39, v27, v35
	v_fma_f32 v24, v24, v32, v36
	v_fma_f32 v25, v25, v33, v37
	v_fma_f32 v1, v30, v2, v118
	ds_write2_b32 v114, v0, v39 offset0:136 offset1:204
	v_fmac_f32_e32 v119, v31, v3
	s_mov_b32 s16, 0
	v_mov_b32_e32 v0, v103
	ds_write2_b32 v114, v24, v25 offset1:68
	ds_write2_b32 v113, v1, v119 offset0:152 offset1:220
	s_waitcnt vmcnt(0)
	ds_write_b128 v96, v[20:23] offset:41984
	s_waitcnt lgkmcnt(0)
	s_barrier
.LBB0_1507:
	v_add_u32_e32 v1, s16, v44
	ds_read_b128 v[20:23], v0
	ds_read_b128 v[24:27], v0 offset:272
	ds_read_b128 v[28:31], v0 offset:544
	ds_read_b128 v[32:35], v0 offset:816
	ds_read_b128 v[36:39], v1
	ds_read_b128 v[88:91], v1 offset:128
	ds_read_b128 v[114:117], v1 offset:256
	ds_read_b128 v[118:121], v1 offset:384
	s_waitcnt lgkmcnt(7)
	v_mov_b32_e32 v2, v23
	s_waitcnt lgkmcnt(6)
	v_mov_b32_e32 v92, v27
	s_waitcnt lgkmcnt(3)
	v_fmac_f32_e32 v18, v38, v20
	v_fmac_f32_e32 v19, v39, v20
	v_fmac_f32_e32 v16, v36, v20
	v_fmac_f32_e32 v17, v37, v20
	v_fmac_f32_e32 v14, v38, v21
	v_fmac_f32_e32 v15, v39, v21
	v_fmac_f32_e32 v12, v36, v21
	v_fmac_f32_e32 v13, v37, v21
	v_fmac_f32_e32 v8, v36, v22
	v_fmac_f32_e32 v9, v37, v22
	v_fmac_f32_e32 v10, v38, v22
	v_fmac_f32_e32 v11, v39, v22
	v_fmac_f32_e32 v4, v36, v2
	v_fmac_f32_e32 v5, v37, v2
	v_fma_f32 v3, v39, v2, v7
	v_fma_f32 v2, v38, v2, v6
	v_mov_b32_e32 v122, v31
	s_waitcnt lgkmcnt(2)
	v_fma_f32 v6, v90, v24, v18
	v_fma_f32 v7, v91, v24, v19
	v_fmac_f32_e32 v16, v88, v24
	v_fmac_f32_e32 v17, v89, v24
	v_fmac_f32_e32 v14, v90, v25
	v_fmac_f32_e32 v15, v91, v25
	v_fmac_f32_e32 v12, v88, v25
	v_fmac_f32_e32 v13, v89, v25
	v_fmac_f32_e32 v10, v90, v26
	v_fmac_f32_e32 v11, v91, v26
	v_fmac_f32_e32 v8, v88, v26
	v_fmac_f32_e32 v9, v89, v26
	v_fmac_f32_e32 v2, v90, v92
	v_fmac_f32_e32 v3, v91, v92
	v_fmac_f32_e32 v4, v88, v92
	v_fmac_f32_e32 v5, v89, v92
	s_addk_i32 s16, 0x200
	v_mov_b32_e32 v124, v35
	s_waitcnt lgkmcnt(1)
	v_fmac_f32_e32 v6, v116, v28
	v_fmac_f32_e32 v7, v117, v28
	v_fmac_f32_e32 v16, v114, v28
	v_fmac_f32_e32 v17, v115, v28
	v_fmac_f32_e32 v14, v116, v29
	v_fmac_f32_e32 v15, v117, v29
	v_fmac_f32_e32 v12, v114, v29
	v_fmac_f32_e32 v13, v115, v29
	v_fmac_f32_e32 v10, v116, v30
	v_fmac_f32_e32 v11, v117, v30
	v_fmac_f32_e32 v8, v114, v30
	v_fmac_f32_e32 v9, v115, v30
	v_fmac_f32_e32 v2, v116, v122
	v_fmac_f32_e32 v3, v117, v122
	v_fmac_f32_e32 v4, v114, v122
	v_fmac_f32_e32 v5, v115, v122
	v_add_u32_e32 v0, 0x440, v0
	s_cmpk_lg_i32 s16, 0x800
	s_waitcnt lgkmcnt(0)
	v_fma_f32 v18, v120, v32, v6
	v_fma_f32 v19, v121, v32, v7
	v_fmac_f32_e32 v16, v118, v32
	v_fmac_f32_e32 v17, v119, v32
	v_fmac_f32_e32 v14, v120, v33
	v_fmac_f32_e32 v15, v121, v33
	v_fmac_f32_e32 v12, v118, v33
	v_fmac_f32_e32 v13, v119, v33
	v_fmac_f32_e32 v10, v120, v34
	v_fmac_f32_e32 v11, v121, v34
	v_fmac_f32_e32 v8, v118, v34
	v_fmac_f32_e32 v9, v119, v34
	v_fma_f32 v6, v120, v124, v2
	v_fma_f32 v7, v121, v124, v3
	v_fmac_f32_e32 v4, v118, v124
	v_fmac_f32_e32 v5, v119, v124
	s_cbranch_scc1 .LBB0_1507
	s_barrier
	ds_write_b128 v107, v[16:19] offset:58752
	ds_write_b128 v107, v[12:15] offset:58880
	ds_write_b128 v107, v[8:11] offset:59008
	ds_write_b128 v107, v[4:7] offset:59136
	s_waitcnt lgkmcnt(0)
	s_barrier
	global_load_dwordx4 v[0:3], v[50:51], off offset:128
	ds_read_b128 v[4:7], v98 offset:58752
	ds_read_b128 v[8:11], v99 offset:8192
	ds_read_b128 v[12:15], v99 offset:16384
	ds_read_b128 v[16:19], v99 offset:24576
	v_add_u32_e32 v20, 0xc400, v100
	v_add_u32_e32 v21, 0xc408, v100
	s_waitcnt lgkmcnt(2)
	v_add_f32_e32 v4, v4, v8
	v_add_f32_e32 v5, v5, v9
	v_add_f32_e32 v6, v6, v10
	v_add_f32_e32 v7, v7, v11
	s_waitcnt lgkmcnt(1)
	v_add_f32_e32 v4, v12, v4
	v_add_f32_e32 v5, v13, v5
	v_add_f32_e32 v6, v14, v6
	v_add_f32_e32 v7, v15, v7
	s_waitcnt lgkmcnt(0)
	v_add_f32_e32 v4, v16, v4
	v_add_f32_e32 v5, v17, v5
	v_add_f32_e32 v6, v18, v6
	v_add_f32_e32 v7, v19, v7
	s_waitcnt vmcnt(0)
	v_add_f32_e32 v0, v0, v4
	v_add_f32_e32 v1, v1, v5
	v_add_f32_e32 v2, v6, v2
	v_add_f32_e32 v3, v7, v3
	ds_write2_b32 v20, v0, v1 offset1:1
	ds_write2_b32 v21, v2, v3 offset1:1
	s_waitcnt lgkmcnt(0)
	s_barrier
	s_and_saveexec_b64 s[36:37], s[6:7]
	s_cbranch_execz .LBB0_1510
	v_add_u32_e32 v0, 0xc400, v108
	v_add_u32_e32 v1, 0xc408, v108
	v_add_u32_e32 v2, 0xc410, v108
	v_add_u32_e32 v3, 0xc418, v108
	ds_read2_b32 v[34:35], v0 offset1:1
	ds_read2_b32 v[30:31], v1 offset1:1
	ds_read2_b32 v[22:23], v2 offset1:1
	ds_read2_b32 v[10:11], v3 offset1:1
	s_mov_b32 s16, 0xff61b1e6
	s_waitcnt lgkmcnt(3)
	v_max_f32_e32 v0, v34, v34
	v_max_f32_e32 v0, 0xff61b1e6, v0
	v_cmp_lt_f32_e32 vcc, s16, v34
	v_cmp_gt_f32_e64 s[16:17], v35, v0
	v_add_u32_e32 v2, 0xc420, v108
	ds_read2_b32 v[24:25], v2 offset1:1
	v_cndmask_b32_e64 v0, v0, v35, s[16:17]
	v_cndmask_b32_e64 v1, 0, 1, s[16:17]
	s_waitcnt lgkmcnt(3)
	v_cmp_gt_f32_e64 s[16:17], v30, v0
	v_add_u32_e32 v2, 0xc428, v108
	v_add_u32_e32 v3, 0xc430, v108
	v_cndmask_b32_e64 v0, v0, v30, s[16:17]
	v_cndmask_b32_e64 v1, v1, 2, s[16:17]
	v_cmp_gt_f32_e64 s[16:17], v31, v0
	v_add_u32_e32 v4, 0xc438, v108
	ds_read2_b32 v[32:33], v2 offset1:1
	ds_read2_b32 v[20:21], v3 offset1:1
	ds_read2_b32 v[6:7], v4 offset1:1
	v_cndmask_b32_e64 v0, v0, v31, s[16:17]
	v_cndmask_b32_e64 v1, v1, 3, s[16:17]
	s_waitcnt lgkmcnt(5)
	v_cmp_gt_f32_e64 s[16:17], v22, v0
	v_add_u32_e32 v2, 0xc440, v108
	ds_read2_b32 v[18:19], v2 offset1:1
	v_cndmask_b32_e64 v0, v0, v22, s[16:17]
	v_cndmask_b32_e64 v1, v1, 4, s[16:17]
	v_cmp_gt_f32_e64 s[16:17], v23, v0
	v_add_u32_e32 v2, 0xc448, v108
	v_add_u32_e32 v4, 0xc458, v108
	v_cndmask_b32_e64 v0, v0, v23, s[16:17]
	v_cndmask_b32_e64 v1, v1, 5, s[16:17]
	s_waitcnt lgkmcnt(5)
	v_cmp_gt_f32_e64 s[16:17], v10, v0
	v_add_u32_e32 v3, 0xc450, v108
	ds_read2_b32 v[28:29], v2 offset1:1
	ds_read2_b32 v[12:13], v3 offset1:1
	ds_read2_b32 v[4:5], v4 offset1:1
	v_cndmask_b32_e64 v0, v0, v10, s[16:17]
	v_cndmask_b32_e64 v1, v1, 6, s[16:17]
	v_cmp_gt_f32_e64 s[16:17], v11, v0
	v_add_u32_e32 v2, 0xc460, v108
	ds_read2_b32 v[14:15], v2 offset1:1
	v_cndmask_b32_e64 v0, v0, v11, s[16:17]
	v_cndmask_b32_e64 v1, v1, 7, s[16:17]
	s_waitcnt lgkmcnt(8)
	v_cmp_gt_f32_e64 s[16:17], v24, v0
	v_add_u32_e32 v2, 0xc468, v108
	v_add_u32_e32 v8, 0xc478, v108
	v_cndmask_b32_e64 v0, v0, v24, s[16:17]
	v_cndmask_b32_e64 v1, v1, 8, s[16:17]
	v_cmp_gt_f32_e64 s[16:17], v25, v0
	v_add_u32_e32 v3, 0xc470, v108
	ds_read2_b32 v[26:27], v2 offset1:1
	ds_read2_b32 v[16:17], v3 offset1:1
	ds_read2_b32 v[8:9], v8 offset1:1
	v_cndmask_b32_e64 v0, v0, v25, s[16:17]
	v_cndmask_b32_e64 v1, v1, 9, s[16:17]
	s_waitcnt lgkmcnt(10)
	v_cmp_gt_f32_e64 s[16:17], v32, v0
	s_nop 1
	v_cndmask_b32_e64 v0, v0, v32, s[16:17]
	v_cndmask_b32_e64 v1, v1, 10, s[16:17]
	v_cmp_gt_f32_e64 s[16:17], v33, v0
	s_nop 1
	v_cndmask_b32_e64 v0, v0, v33, s[16:17]
	v_cndmask_b32_e64 v1, v1, 11, s[16:17]
	s_waitcnt lgkmcnt(9)
	v_cmp_gt_f32_e64 s[16:17], v20, v0
	s_nop 1
	v_cndmask_b32_e64 v0, v0, v20, s[16:17]
	v_cndmask_b32_e64 v1, v1, 12, s[16:17]
	v_cmp_gt_f32_e64 s[16:17], v21, v0
	s_nop 1
	v_cndmask_b32_e64 v0, v0, v21, s[16:17]
	v_cndmask_b32_e64 v1, v1, 13, s[16:17]
	s_waitcnt lgkmcnt(8)
	v_cmp_gt_f32_e64 s[16:17], v6, v0
	s_nop 1
	v_cndmask_b32_e64 v0, v0, v6, s[16:17]
	v_cndmask_b32_e64 v1, v1, 14, s[16:17]
	v_cmp_gt_f32_e64 s[16:17], v7, v0
	s_nop 1
	v_cndmask_b32_e64 v0, v0, v7, s[16:17]
	v_cndmask_b32_e64 v1, v1, 15, s[16:17]
	s_waitcnt lgkmcnt(7)
	v_cmp_gt_f32_e64 s[16:17], v18, v0
	s_nop 1
	v_cndmask_b32_e64 v0, v0, v18, s[16:17]
	v_cndmask_b32_e64 v1, v1, 16, s[16:17]
	v_cmp_gt_f32_e64 s[16:17], v19, v0
	s_nop 1
	v_cndmask_b32_e64 v0, v0, v19, s[16:17]
	v_cndmask_b32_e64 v1, v1, 17, s[16:17]
	s_waitcnt lgkmcnt(6)
	v_cmp_gt_f32_e64 s[16:17], v28, v0
	s_nop 1
	v_cndmask_b32_e64 v0, v0, v28, s[16:17]
	v_cndmask_b32_e64 v1, v1, 18, s[16:17]
	v_cmp_gt_f32_e64 s[16:17], v29, v0
	s_nop 1
	v_cndmask_b32_e64 v0, v0, v29, s[16:17]
	v_cndmask_b32_e64 v1, v1, 19, s[16:17]
	s_waitcnt lgkmcnt(5)
	v_cmp_gt_f32_e64 s[16:17], v12, v0
	s_nop 1
	v_cndmask_b32_e64 v0, v0, v12, s[16:17]
	v_cndmask_b32_e64 v1, v1, 20, s[16:17]
	v_cmp_gt_f32_e64 s[16:17], v13, v0
	s_nop 1
	v_cndmask_b32_e64 v0, v0, v13, s[16:17]
	v_cndmask_b32_e64 v1, v1, 21, s[16:17]
	s_waitcnt lgkmcnt(4)
	v_cmp_gt_f32_e64 s[16:17], v4, v0
	s_nop 1
	v_cndmask_b32_e64 v0, v0, v4, s[16:17]
	v_cndmask_b32_e64 v1, v1, 22, s[16:17]
	v_cmp_gt_f32_e64 s[16:17], v5, v0
	s_nop 1
	v_cndmask_b32_e64 v0, v0, v5, s[16:17]
	v_cndmask_b32_e64 v1, v1, 23, s[16:17]
	s_waitcnt lgkmcnt(3)
	v_cmp_gt_f32_e64 s[16:17], v14, v0
	s_nop 1
	v_cndmask_b32_e64 v0, v0, v14, s[16:17]
	v_cndmask_b32_e64 v1, v1, 24, s[16:17]
	v_cmp_gt_f32_e64 s[16:17], v15, v0
	s_nop 1
	v_cndmask_b32_e64 v0, v0, v15, s[16:17]
	v_cndmask_b32_e64 v1, v1, 25, s[16:17]
	s_waitcnt lgkmcnt(2)
	v_cmp_gt_f32_e64 s[16:17], v26, v0
	s_nop 1
	v_cndmask_b32_e64 v0, v0, v26, s[16:17]
	v_cndmask_b32_e64 v1, v1, 26, s[16:17]
	v_cmp_gt_f32_e64 s[16:17], v27, v0
	s_nop 1
	v_cndmask_b32_e64 v0, v0, v27, s[16:17]
	v_cndmask_b32_e64 v1, v1, 27, s[16:17]
	s_waitcnt lgkmcnt(1)
	v_cmp_gt_f32_e64 s[16:17], v16, v0
	s_nop 1
	v_cndmask_b32_e64 v0, v0, v16, s[16:17]
	v_cndmask_b32_e64 v1, v1, 28, s[16:17]
	v_cmp_gt_f32_e64 s[16:17], v17, v0
	s_nop 1
	v_cndmask_b32_e64 v0, v0, v17, s[16:17]
	v_cndmask_b32_e64 v1, v1, 29, s[16:17]
	s_waitcnt lgkmcnt(0)
	v_cmp_gt_f32_e64 s[16:17], v8, v0
	s_nop 1
	v_cndmask_b32_e64 v0, v0, v8, s[16:17]
	v_cndmask_b32_e64 v1, v1, 30, s[16:17]
	v_cmp_gt_f32_e64 s[16:17], v9, v0
	s_nop 1
	v_cndmask_b32_e64 v36, v0, v9, s[16:17]
	v_cndmask_b32_e64 v0, v1, 31, s[16:17]
	v_cmp_ne_u32_e64 s[16:17], 0, v0
	v_lshlrev_b32_e64 v2, v0, 1
	s_and_b64 s[16:17], s[16:17], vcc
	v_cndmask_b32_e64 v1, v112, v34, s[16:17]
	v_and_b32_e32 v3, 2, v2
	v_cmp_eq_u32_e64 s[16:17], 0, v3
	v_cmp_gt_f32_e64 s[18:19], v35, v1
	s_and_b64 s[16:17], s[16:17], s[18:19]
	v_cndmask_b32_e64 v1, v1, v35, s[16:17]
	v_and_b32_e32 v37, 4, v2
	v_cndmask_b32_e64 v3, 0, 1, s[16:17]
	v_cmp_eq_u32_e64 s[16:17], 0, v37
	v_cmp_gt_f32_e64 s[18:19], v30, v1
	s_and_b64 s[16:17], s[16:17], s[18:19]
	v_cndmask_b32_e64 v1, v1, v30, s[16:17]
	v_and_b32_e32 v37, 8, v2
	v_cndmask_b32_e64 v3, v3, 2, s[16:17]
	v_cmp_eq_u32_e64 s[16:17], 0, v37
	v_cmp_gt_f32_e64 s[18:19], v31, v1
	s_and_b64 s[16:17], s[16:17], s[18:19]
	v_cndmask_b32_e64 v1, v1, v31, s[16:17]
	v_and_b32_e32 v37, 16, v2
	v_cndmask_b32_e64 v3, v3, 3, s[16:17]
	v_cmp_eq_u32_e64 s[16:17], 0, v37
	v_cmp_gt_f32_e64 s[18:19], v22, v1
	s_and_b64 s[16:17], s[16:17], s[18:19]
	v_cndmask_b32_e64 v1, v1, v22, s[16:17]
	v_and_b32_e32 v37, 32, v2
	v_cndmask_b32_e64 v3, v3, 4, s[16:17]
	v_cmp_eq_u32_e64 s[16:17], 0, v37
	v_cmp_gt_f32_e64 s[18:19], v23, v1
	s_and_b64 s[16:17], s[16:17], s[18:19]
	v_cndmask_b32_e64 v1, v1, v23, s[16:17]
	v_and_b32_e32 v37, 64, v2
	v_cndmask_b32_e64 v3, v3, 5, s[16:17]
	v_cmp_eq_u32_e64 s[16:17], 0, v37
	v_cmp_gt_f32_e64 s[18:19], v10, v1
	s_and_b64 s[16:17], s[16:17], s[18:19]
	v_cndmask_b32_e64 v1, v1, v10, s[16:17]
	v_and_b32_e32 v37, 0x80, v2
	v_cndmask_b32_e64 v3, v3, 6, s[16:17]
	v_cmp_eq_u32_e64 s[16:17], 0, v37
	v_cmp_gt_f32_e64 s[18:19], v11, v1
	s_and_b64 s[16:17], s[16:17], s[18:19]
	v_cndmask_b32_e64 v1, v1, v11, s[16:17]
	v_and_b32_e32 v37, 0x100, v2
	v_cndmask_b32_e64 v3, v3, 7, s[16:17]
	v_cmp_eq_u32_e64 s[16:17], 0, v37
	v_cmp_gt_f32_e64 s[18:19], v24, v1
	s_and_b64 s[16:17], s[16:17], s[18:19]
	v_cndmask_b32_e64 v1, v1, v24, s[16:17]
	v_and_b32_e32 v37, 0x200, v2
	v_cndmask_b32_e64 v3, v3, 8, s[16:17]
	v_cmp_eq_u32_e64 s[16:17], 0, v37
	v_cmp_gt_f32_e64 s[18:19], v25, v1
	s_and_b64 s[16:17], s[16:17], s[18:19]
	v_cndmask_b32_e64 v1, v1, v25, s[16:17]
	v_and_b32_e32 v37, 0x400, v2
	v_cndmask_b32_e64 v3, v3, 9, s[16:17]
	v_cmp_eq_u32_e64 s[16:17], 0, v37
	v_cmp_gt_f32_e64 s[18:19], v32, v1
	s_and_b64 s[16:17], s[16:17], s[18:19]
	v_cndmask_b32_e64 v1, v1, v32, s[16:17]
	v_and_b32_e32 v37, 0x800, v2
	v_cndmask_b32_e64 v3, v3, 10, s[16:17]
	v_cmp_eq_u32_e64 s[16:17], 0, v37
	v_cmp_gt_f32_e64 s[18:19], v33, v1
	s_and_b64 s[16:17], s[16:17], s[18:19]
	v_cndmask_b32_e64 v1, v1, v33, s[16:17]
	v_and_b32_e32 v37, 0x1000, v2
	v_cndmask_b32_e64 v3, v3, 11, s[16:17]
	v_cmp_eq_u32_e64 s[16:17], 0, v37
	v_cmp_gt_f32_e64 s[18:19], v20, v1
	s_and_b64 s[16:17], s[16:17], s[18:19]
	v_cndmask_b32_e64 v1, v1, v20, s[16:17]
	v_and_b32_e32 v37, 0x2000, v2
	v_cndmask_b32_e64 v3, v3, 12, s[16:17]
	v_cmp_eq_u32_e64 s[16:17], 0, v37
	v_cmp_gt_f32_e64 s[18:19], v21, v1
	s_and_b64 s[16:17], s[16:17], s[18:19]
	v_cndmask_b32_e64 v1, v1, v21, s[16:17]
	v_and_b32_e32 v37, 0x4000, v2
	v_cndmask_b32_e64 v3, v3, 13, s[16:17]
	v_cmp_eq_u32_e64 s[16:17], 0, v37
	v_cmp_gt_f32_e64 s[18:19], v6, v1
	s_and_b64 s[16:17], s[16:17], s[18:19]
	v_cndmask_b32_e64 v1, v1, v6, s[16:17]
	v_and_b32_e32 v37, 0x8000, v2
	v_cndmask_b32_e64 v3, v3, 14, s[16:17]
	v_cmp_eq_u32_e64 s[16:17], 0, v37
	v_cmp_gt_f32_e64 s[18:19], v7, v1
	s_and_b64 s[16:17], s[16:17], s[18:19]
	v_cndmask_b32_e64 v1, v1, v7, s[16:17]
	v_and_b32_e32 v37, 0x10000, v2
	v_cndmask_b32_e64 v3, v3, 15, s[16:17]
	v_cmp_eq_u32_e64 s[16:17], 0, v37
	v_cmp_gt_f32_e64 s[18:19], v18, v1
	s_and_b64 s[16:17], s[16:17], s[18:19]
	v_cndmask_b32_e64 v1, v1, v18, s[16:17]
	v_and_b32_e32 v37, 0x20000, v2
	v_cndmask_b32_e64 v3, v3, 16, s[16:17]
	v_cmp_eq_u32_e64 s[16:17], 0, v37
	v_cmp_gt_f32_e64 s[18:19], v19, v1
	s_and_b64 s[16:17], s[16:17], s[18:19]
	v_cndmask_b32_e64 v1, v1, v19, s[16:17]
	v_and_b32_e32 v37, 0x40000, v2
	v_cndmask_b32_e64 v3, v3, 17, s[16:17]
	v_cmp_eq_u32_e64 s[16:17], 0, v37
	v_cmp_gt_f32_e64 s[18:19], v28, v1
	s_and_b64 s[16:17], s[16:17], s[18:19]
	v_cndmask_b32_e64 v1, v1, v28, s[16:17]
	v_and_b32_e32 v37, 0x80000, v2
	v_cndmask_b32_e64 v3, v3, 18, s[16:17]
	v_cmp_eq_u32_e64 s[16:17], 0, v37
	v_cmp_gt_f32_e64 s[18:19], v29, v1
	s_and_b64 s[16:17], s[16:17], s[18:19]
	v_cndmask_b32_e64 v1, v1, v29, s[16:17]
	v_and_b32_e32 v37, 0x100000, v2
	v_cndmask_b32_e64 v3, v3, 19, s[16:17]
	v_cmp_eq_u32_e64 s[16:17], 0, v37
	v_cmp_gt_f32_e64 s[18:19], v12, v1
	s_and_b64 s[16:17], s[16:17], s[18:19]
	v_cndmask_b32_e64 v1, v1, v12, s[16:17]
	v_and_b32_e32 v37, 0x200000, v2
	v_cndmask_b32_e64 v3, v3, 20, s[16:17]
	v_cmp_eq_u32_e64 s[16:17], 0, v37
	v_cmp_gt_f32_e64 s[18:19], v13, v1
	s_and_b64 s[16:17], s[16:17], s[18:19]
	v_cndmask_b32_e64 v1, v1, v13, s[16:17]
	v_and_b32_e32 v37, 0x400000, v2
	v_cndmask_b32_e64 v3, v3, 21, s[16:17]
	v_cmp_eq_u32_e64 s[16:17], 0, v37
	v_cmp_gt_f32_e64 s[18:19], v4, v1
	s_and_b64 s[16:17], s[16:17], s[18:19]
	v_cndmask_b32_e64 v1, v1, v4, s[16:17]
	v_and_b32_e32 v37, 0x800000, v2
	v_cndmask_b32_e64 v3, v3, 22, s[16:17]
	v_cmp_eq_u32_e64 s[16:17], 0, v37
	v_cmp_gt_f32_e64 s[18:19], v5, v1
	s_and_b64 s[16:17], s[16:17], s[18:19]
	v_cndmask_b32_e64 v1, v1, v5, s[16:17]
	v_and_b32_e32 v37, 0x1000000, v2
	v_cndmask_b32_e64 v3, v3, 23, s[16:17]
	v_cmp_eq_u32_e64 s[16:17], 0, v37
	v_cmp_gt_f32_e64 s[18:19], v14, v1
	s_and_b64 s[16:17], s[16:17], s[18:19]
	v_cndmask_b32_e64 v1, v1, v14, s[16:17]
	v_and_b32_e32 v37, 0x2000000, v2
	v_cndmask_b32_e64 v3, v3, 24, s[16:17]
	v_cmp_eq_u32_e64 s[16:17], 0, v37
	v_cmp_gt_f32_e64 s[18:19], v15, v1
	s_and_b64 s[16:17], s[16:17], s[18:19]
	v_cndmask_b32_e64 v1, v1, v15, s[16:17]
	v_and_b32_e32 v37, 0x4000000, v2
	v_cndmask_b32_e64 v3, v3, 25, s[16:17]
	v_cmp_eq_u32_e64 s[16:17], 0, v37
	v_cmp_gt_f32_e64 s[18:19], v26, v1
	s_and_b64 s[16:17], s[16:17], s[18:19]
	v_cndmask_b32_e64 v1, v1, v26, s[16:17]
	v_and_b32_e32 v37, 0x8000000, v2
	v_cndmask_b32_e64 v3, v3, 26, s[16:17]
	v_cmp_eq_u32_e64 s[16:17], 0, v37
	v_cmp_gt_f32_e64 s[18:19], v27, v1
	s_and_b64 s[16:17], s[16:17], s[18:19]
	v_cndmask_b32_e64 v1, v1, v27, s[16:17]
	v_and_b32_e32 v37, 0x10000000, v2
	v_cndmask_b32_e64 v3, v3, 27, s[16:17]
	v_cmp_eq_u32_e64 s[16:17], 0, v37
	v_cmp_gt_f32_e64 s[18:19], v16, v1
	s_and_b64 s[16:17], s[16:17], s[18:19]
	v_cndmask_b32_e64 v1, v1, v16, s[16:17]
	v_and_b32_e32 v37, 0x20000000, v2
	v_cndmask_b32_e64 v3, v3, 28, s[16:17]
	v_cmp_eq_u32_e64 s[16:17], 0, v37
	v_cmp_gt_f32_e64 s[18:19], v17, v1
	s_and_b64 s[16:17], s[16:17], s[18:19]
	v_cndmask_b32_e64 v1, v1, v17, s[16:17]
	v_and_b32_e32 v37, 2.0, v2
	v_cndmask_b32_e64 v3, v3, 29, s[16:17]
	v_cmp_eq_u32_e64 s[16:17], 0, v37
	v_cmp_gt_f32_e64 s[18:19], v8, v1
	s_and_b64 s[16:17], s[16:17], s[18:19]
	v_cndmask_b32_e64 v1, v1, v8, s[16:17]
	v_cndmask_b32_e64 v3, v3, 30, s[16:17]
	v_cmp_ne_u32_e64 s[16:17], 31, v0
	v_cmp_gt_f32_e64 s[18:19], v9, v1
	s_and_b64 s[16:17], s[16:17], s[18:19]
	v_cndmask_b32_e64 v37, v1, v9, s[16:17]
	v_cndmask_b32_e64 v1, v3, 31, s[16:17]
	v_lshl_or_b32 v3, 1, v1, v2
	v_and_b32_e32 v2, 1, v3
	v_cmp_eq_u32_e64 s[16:17], 0, v2
	s_and_b64 s[16:17], s[16:17], vcc
	v_and_b32_e32 v38, 2, v3
	v_cndmask_b32_e64 v2, v112, v34, s[16:17]
	v_cmp_eq_u32_e64 s[16:17], 0, v38
	v_cmp_gt_f32_e64 s[18:19], v35, v2
	s_and_b64 s[16:17], s[16:17], s[18:19]
	v_cndmask_b32_e64 v2, v2, v35, s[16:17]
	v_and_b32_e32 v39, 4, v3
	v_cndmask_b32_e64 v38, 0, 1, s[16:17]
	v_cmp_eq_u32_e64 s[16:17], 0, v39
	v_cmp_gt_f32_e64 s[18:19], v30, v2
	s_and_b64 s[16:17], s[16:17], s[18:19]
	v_cndmask_b32_e64 v2, v2, v30, s[16:17]
	v_and_b32_e32 v39, 8, v3
	v_cndmask_b32_e64 v38, v38, 2, s[16:17]
	v_cmp_eq_u32_e64 s[16:17], 0, v39
	v_cmp_gt_f32_e64 s[18:19], v31, v2
	s_and_b64 s[16:17], s[16:17], s[18:19]
	v_cndmask_b32_e64 v2, v2, v31, s[16:17]
	v_and_b32_e32 v39, 16, v3
	v_cndmask_b32_e64 v38, v38, 3, s[16:17]
	v_cmp_eq_u32_e64 s[16:17], 0, v39
	v_cmp_gt_f32_e64 s[18:19], v22, v2
	s_and_b64 s[16:17], s[16:17], s[18:19]
	v_cndmask_b32_e64 v2, v2, v22, s[16:17]
	v_and_b32_e32 v39, 32, v3
	v_cndmask_b32_e64 v38, v38, 4, s[16:17]
	v_cmp_eq_u32_e64 s[16:17], 0, v39
	v_cmp_gt_f32_e64 s[18:19], v23, v2
	s_and_b64 s[16:17], s[16:17], s[18:19]
	v_cndmask_b32_e64 v2, v2, v23, s[16:17]
	v_and_b32_e32 v39, 64, v3
	v_cndmask_b32_e64 v38, v38, 5, s[16:17]
	v_cmp_eq_u32_e64 s[16:17], 0, v39
	v_cmp_gt_f32_e64 s[18:19], v10, v2
	s_and_b64 s[16:17], s[16:17], s[18:19]
	v_cndmask_b32_e64 v2, v2, v10, s[16:17]
	v_and_b32_e32 v39, 0x80, v3
	v_cndmask_b32_e64 v38, v38, 6, s[16:17]
	v_cmp_eq_u32_e64 s[16:17], 0, v39
	v_cmp_gt_f32_e64 s[18:19], v11, v2
	s_and_b64 s[16:17], s[16:17], s[18:19]
	v_cndmask_b32_e64 v2, v2, v11, s[16:17]
	v_and_b32_e32 v39, 0x100, v3
	v_cndmask_b32_e64 v38, v38, 7, s[16:17]
	v_cmp_eq_u32_e64 s[16:17], 0, v39
	v_cmp_gt_f32_e64 s[18:19], v24, v2
	s_and_b64 s[16:17], s[16:17], s[18:19]
	v_cndmask_b32_e64 v2, v2, v24, s[16:17]
	v_and_b32_e32 v39, 0x200, v3
	v_cndmask_b32_e64 v38, v38, 8, s[16:17]
	v_cmp_eq_u32_e64 s[16:17], 0, v39
	v_cmp_gt_f32_e64 s[18:19], v25, v2
	s_and_b64 s[16:17], s[16:17], s[18:19]
	v_cndmask_b32_e64 v2, v2, v25, s[16:17]
	v_and_b32_e32 v39, 0x400, v3
	v_cndmask_b32_e64 v38, v38, 9, s[16:17]
	v_cmp_eq_u32_e64 s[16:17], 0, v39
	v_cmp_gt_f32_e64 s[18:19], v32, v2
	s_and_b64 s[16:17], s[16:17], s[18:19]
	v_cndmask_b32_e64 v2, v2, v32, s[16:17]
	v_and_b32_e32 v39, 0x800, v3
	v_cndmask_b32_e64 v38, v38, 10, s[16:17]
	v_cmp_eq_u32_e64 s[16:17], 0, v39
	v_cmp_gt_f32_e64 s[18:19], v33, v2
	s_and_b64 s[16:17], s[16:17], s[18:19]
	v_cndmask_b32_e64 v2, v2, v33, s[16:17]
	v_and_b32_e32 v39, 0x1000, v3
	v_cndmask_b32_e64 v38, v38, 11, s[16:17]
	v_cmp_eq_u32_e64 s[16:17], 0, v39
	v_cmp_gt_f32_e64 s[18:19], v20, v2
	s_and_b64 s[16:17], s[16:17], s[18:19]
	v_cndmask_b32_e64 v2, v2, v20, s[16:17]
	v_and_b32_e32 v39, 0x2000, v3
	v_cndmask_b32_e64 v38, v38, 12, s[16:17]
	v_cmp_eq_u32_e64 s[16:17], 0, v39
	v_cmp_gt_f32_e64 s[18:19], v21, v2
	s_and_b64 s[16:17], s[16:17], s[18:19]
	v_cndmask_b32_e64 v2, v2, v21, s[16:17]
	v_and_b32_e32 v39, 0x4000, v3
	v_cndmask_b32_e64 v38, v38, 13, s[16:17]
	v_cmp_eq_u32_e64 s[16:17], 0, v39
	v_cmp_gt_f32_e64 s[18:19], v6, v2
	s_and_b64 s[16:17], s[16:17], s[18:19]
	v_cndmask_b32_e64 v2, v2, v6, s[16:17]
	v_and_b32_e32 v39, 0x8000, v3
	v_cndmask_b32_e64 v38, v38, 14, s[16:17]
	v_cmp_eq_u32_e64 s[16:17], 0, v39
	v_cmp_gt_f32_e64 s[18:19], v7, v2
	s_and_b64 s[16:17], s[16:17], s[18:19]
	v_cndmask_b32_e64 v2, v2, v7, s[16:17]
	v_and_b32_e32 v39, 0x10000, v3
	v_cndmask_b32_e64 v38, v38, 15, s[16:17]
	v_cmp_eq_u32_e64 s[16:17], 0, v39
	v_cmp_gt_f32_e64 s[18:19], v18, v2
	s_and_b64 s[16:17], s[16:17], s[18:19]
	v_cndmask_b32_e64 v2, v2, v18, s[16:17]
	v_and_b32_e32 v39, 0x20000, v3
	v_cndmask_b32_e64 v38, v38, 16, s[16:17]
	v_cmp_eq_u32_e64 s[16:17], 0, v39
	v_cmp_gt_f32_e64 s[18:19], v19, v2
	s_and_b64 s[16:17], s[16:17], s[18:19]
	v_cndmask_b32_e64 v2, v2, v19, s[16:17]
	v_and_b32_e32 v39, 0x40000, v3
	v_cndmask_b32_e64 v38, v38, 17, s[16:17]
	v_cmp_eq_u32_e64 s[16:17], 0, v39
	v_cmp_gt_f32_e64 s[18:19], v28, v2
	s_and_b64 s[16:17], s[16:17], s[18:19]
	v_cndmask_b32_e64 v2, v2, v28, s[16:17]
	v_and_b32_e32 v39, 0x80000, v3
	v_cndmask_b32_e64 v38, v38, 18, s[16:17]
	v_cmp_eq_u32_e64 s[16:17], 0, v39
	v_cmp_gt_f32_e64 s[18:19], v29, v2
	s_and_b64 s[16:17], s[16:17], s[18:19]
	v_cndmask_b32_e64 v2, v2, v29, s[16:17]
	v_and_b32_e32 v39, 0x100000, v3
	v_cndmask_b32_e64 v38, v38, 19, s[16:17]
	v_cmp_eq_u32_e64 s[16:17], 0, v39
	v_cmp_gt_f32_e64 s[18:19], v12, v2
	s_and_b64 s[16:17], s[16:17], s[18:19]
	v_cndmask_b32_e64 v2, v2, v12, s[16:17]
	v_and_b32_e32 v39, 0x200000, v3
	v_cndmask_b32_e64 v38, v38, 20, s[16:17]
	v_cmp_eq_u32_e64 s[16:17], 0, v39
	v_cmp_gt_f32_e64 s[18:19], v13, v2
	s_and_b64 s[16:17], s[16:17], s[18:19]
	v_cndmask_b32_e64 v2, v2, v13, s[16:17]
	v_and_b32_e32 v39, 0x400000, v3
	v_cndmask_b32_e64 v38, v38, 21, s[16:17]
	v_cmp_eq_u32_e64 s[16:17], 0, v39
	v_cmp_gt_f32_e64 s[18:19], v4, v2
	s_and_b64 s[16:17], s[16:17], s[18:19]
	v_cndmask_b32_e64 v2, v2, v4, s[16:17]
	v_and_b32_e32 v39, 0x800000, v3
	v_cndmask_b32_e64 v38, v38, 22, s[16:17]
	v_cmp_eq_u32_e64 s[16:17], 0, v39
	v_cmp_gt_f32_e64 s[18:19], v5, v2
	s_and_b64 s[16:17], s[16:17], s[18:19]
	v_cndmask_b32_e64 v2, v2, v5, s[16:17]
	v_and_b32_e32 v39, 0x1000000, v3
	v_cndmask_b32_e64 v38, v38, 23, s[16:17]
	v_cmp_eq_u32_e64 s[16:17], 0, v39
	v_cmp_gt_f32_e64 s[18:19], v14, v2
	s_and_b64 s[16:17], s[16:17], s[18:19]
	v_cndmask_b32_e64 v2, v2, v14, s[16:17]
	v_and_b32_e32 v39, 0x2000000, v3
	v_cndmask_b32_e64 v38, v38, 24, s[16:17]
	v_cmp_eq_u32_e64 s[16:17], 0, v39
	v_cmp_gt_f32_e64 s[18:19], v15, v2
	s_and_b64 s[16:17], s[16:17], s[18:19]
	v_cndmask_b32_e64 v2, v2, v15, s[16:17]
	v_and_b32_e32 v39, 0x4000000, v3
	v_cndmask_b32_e64 v38, v38, 25, s[16:17]
	v_cmp_eq_u32_e64 s[16:17], 0, v39
	v_cmp_gt_f32_e64 s[18:19], v26, v2
	s_and_b64 s[16:17], s[16:17], s[18:19]
	v_cndmask_b32_e64 v2, v2, v26, s[16:17]
	v_and_b32_e32 v39, 0x8000000, v3
	v_cndmask_b32_e64 v38, v38, 26, s[16:17]
	v_cmp_eq_u32_e64 s[16:17], 0, v39
	v_cmp_gt_f32_e64 s[18:19], v27, v2
	s_and_b64 s[16:17], s[16:17], s[18:19]
	v_cndmask_b32_e64 v2, v2, v27, s[16:17]
	v_and_b32_e32 v39, 0x10000000, v3
	v_cndmask_b32_e64 v38, v38, 27, s[16:17]
	v_cmp_eq_u32_e64 s[16:17], 0, v39
	v_cmp_gt_f32_e64 s[18:19], v16, v2
	s_and_b64 s[16:17], s[16:17], s[18:19]
	v_cndmask_b32_e64 v2, v2, v16, s[16:17]
	v_and_b32_e32 v39, 0x20000000, v3
	v_cndmask_b32_e64 v38, v38, 28, s[16:17]
	v_cmp_eq_u32_e64 s[16:17], 0, v39
	v_cmp_gt_f32_e64 s[18:19], v17, v2
	s_and_b64 s[16:17], s[16:17], s[18:19]
	v_cndmask_b32_e64 v2, v2, v17, s[16:17]
	v_and_b32_e32 v39, 2.0, v3
	v_cndmask_b32_e64 v38, v38, 29, s[16:17]
	v_cmp_eq_u32_e64 s[16:17], 0, v39
	v_cmp_gt_f32_e64 s[18:19], v8, v2
	s_and_b64 s[16:17], s[16:17], s[18:19]
	v_cndmask_b32_e64 v2, v2, v8, s[16:17]
	v_cndmask_b32_e64 v38, v38, 30, s[16:17]
	v_cmp_lt_i32_e64 s[16:17], -1, v3
	v_cmp_gt_f32_e64 s[18:19], v9, v2
	s_and_b64 s[16:17], s[16:17], s[18:19]
	v_cndmask_b32_e64 v39, v2, v9, s[16:17]
	v_cndmask_b32_e64 v2, v38, 31, s[16:17]
	v_lshlrev_b32_e64 v38, v2, 1
	v_bitop3_b32 v89, v38, 1, v3 bitop3:0xc8
	v_cmp_eq_u32_e64 s[16:17], 0, v89
	s_and_b64 vcc, s[16:17], vcc
	v_cndmask_b32_e32 v34, v112, v34, vcc
	v_bitop3_b32 v89, v38, 2, v3 bitop3:0xc8
	v_cmp_eq_u32_e32 vcc, 0, v89
	v_cmp_gt_f32_e64 s[16:17], v35, v34
	s_and_b64 vcc, vcc, s[16:17]
	v_cndmask_b32_e32 v34, v34, v35, vcc
	v_bitop3_b32 v89, v38, 4, v3 bitop3:0xc8
	v_cndmask_b32_e64 v35, 0, 1, vcc
	v_cmp_eq_u32_e32 vcc, 0, v89
	v_cmp_gt_f32_e64 s[16:17], v30, v34
	s_and_b64 vcc, vcc, s[16:17]
	v_cndmask_b32_e32 v30, v34, v30, vcc
	v_cndmask_b32_e64 v34, v35, 2, vcc
	v_bitop3_b32 v35, v38, 8, v3 bitop3:0xc8
	v_cmp_eq_u32_e32 vcc, 0, v35
	v_cmp_gt_f32_e64 s[16:17], v31, v30
	s_and_b64 vcc, vcc, s[16:17]
	v_cndmask_b32_e32 v30, v30, v31, vcc
	v_cndmask_b32_e64 v31, v34, 3, vcc
	v_bitop3_b32 v34, v38, 16, v3 bitop3:0xc8
	v_cmp_eq_u32_e32 vcc, 0, v34
	v_cmp_gt_f32_e64 s[16:17], v22, v30
	s_and_b64 vcc, vcc, s[16:17]
	v_cndmask_b32_e32 v22, v30, v22, vcc
	v_cndmask_b32_e64 v30, v31, 4, vcc
	v_bitop3_b32 v31, v38, 32, v3 bitop3:0xc8
	v_cmp_eq_u32_e32 vcc, 0, v31
	v_cmp_gt_f32_e64 s[16:17], v23, v22
	s_and_b64 vcc, vcc, s[16:17]
	v_cndmask_b32_e32 v22, v22, v23, vcc
	v_cndmask_b32_e64 v23, v30, 5, vcc
	v_bitop3_b32 v30, v38, 64, v3 bitop3:0xc8
	v_cmp_eq_u32_e32 vcc, 0, v30
	v_cmp_gt_f32_e64 s[16:17], v10, v22
	s_and_b64 vcc, vcc, s[16:17]
	s_movk_i32 s16, 0x80
	v_cndmask_b32_e32 v10, v22, v10, vcc
	v_cndmask_b32_e64 v22, v23, 6, vcc
	v_bitop3_b32 v23, v38, s16, v3 bitop3:0xc8
	v_cmp_eq_u32_e32 vcc, 0, v23
	v_cmp_gt_f32_e64 s[16:17], v11, v10
	s_and_b64 vcc, vcc, s[16:17]
	s_movk_i32 s16, 0x100
	v_cndmask_b32_e32 v10, v10, v11, vcc
	v_cndmask_b32_e64 v11, v22, 7, vcc
	v_bitop3_b32 v22, v38, s16, v3 bitop3:0xc8
	v_cmp_eq_u32_e32 vcc, 0, v22
	v_cmp_gt_f32_e64 s[16:17], v24, v10
	s_and_b64 vcc, vcc, s[16:17]
	s_movk_i32 s16, 0x200
	v_cndmask_b32_e32 v10, v10, v24, vcc
	v_bitop3_b32 v22, v38, s16, v3 bitop3:0xc8
	v_cndmask_b32_e64 v11, v11, 8, vcc
	v_cmp_eq_u32_e32 vcc, 0, v22
	v_cmp_gt_f32_e64 s[16:17], v25, v10
	s_and_b64 vcc, vcc, s[16:17]
	v_cndmask_b32_e32 v10, v10, v25, vcc
	v_bitop3_b32 v22, v38, s52, v3 bitop3:0xc8
	v_cndmask_b32_e64 v11, v11, 9, vcc
	v_cmp_eq_u32_e32 vcc, 0, v22
	v_cmp_gt_f32_e64 s[16:17], v32, v10
	s_and_b64 vcc, vcc, s[16:17]
	s_movk_i32 s16, 0x800
	v_cndmask_b32_e32 v10, v10, v32, vcc
	v_bitop3_b32 v22, v38, s16, v3 bitop3:0xc8
	v_cndmask_b32_e64 v11, v11, 10, vcc
	v_cmp_eq_u32_e32 vcc, 0, v22
	v_cmp_gt_f32_e64 s[16:17], v33, v10
	s_and_b64 vcc, vcc, s[16:17]
	s_movk_i32 s16, 0x1000
	v_cndmask_b32_e32 v10, v10, v33, vcc
	v_bitop3_b32 v22, v38, s16, v3 bitop3:0xc8
	v_cndmask_b32_e64 v11, v11, 11, vcc
	v_cmp_eq_u32_e32 vcc, 0, v22
	v_cmp_gt_f32_e64 s[16:17], v20, v10
	s_and_b64 vcc, vcc, s[16:17]
	s_movk_i32 s16, 0x2000
	v_cndmask_b32_e32 v10, v10, v20, vcc
	v_bitop3_b32 v20, v38, s16, v3 bitop3:0xc8
	v_cndmask_b32_e64 v11, v11, 12, vcc
	v_cmp_eq_u32_e32 vcc, 0, v20
	v_cmp_gt_f32_e64 s[16:17], v21, v10
	s_and_b64 vcc, vcc, s[16:17]
	s_movk_i32 s16, 0x4000
	v_cndmask_b32_e32 v10, v10, v21, vcc
	v_bitop3_b32 v20, v38, s16, v3 bitop3:0xc8
	v_cndmask_b32_e64 v11, v11, 13, vcc
	v_cmp_eq_u32_e32 vcc, 0, v20
	v_cmp_gt_f32_e64 s[16:17], v6, v10
	s_and_b64 vcc, vcc, s[16:17]
	s_mov_b32 s16, 0x8000
	v_cndmask_b32_e32 v6, v10, v6, vcc
	v_cndmask_b32_e64 v10, v11, 14, vcc
	v_bitop3_b32 v11, v38, s16, v3 bitop3:0xc8
	v_cmp_eq_u32_e32 vcc, 0, v11
	v_cmp_gt_f32_e64 s[16:17], v7, v6
	s_and_b64 vcc, vcc, s[16:17]
	s_mov_b32 s16, 0x10000
	v_cndmask_b32_e32 v6, v6, v7, vcc
	v_cndmask_b32_e64 v7, v10, 15, vcc
	v_bitop3_b32 v10, v38, s16, v3 bitop3:0xc8
	v_cmp_eq_u32_e32 vcc, 0, v10
	v_cmp_gt_f32_e64 s[16:17], v18, v6
	s_and_b64 vcc, vcc, s[16:17]
	s_mov_b32 s16, 0x20000
	v_cndmask_b32_e32 v6, v6, v18, vcc
	v_bitop3_b32 v10, v38, s16, v3 bitop3:0xc8
	v_cndmask_b32_e64 v7, v7, 16, vcc
	v_cmp_eq_u32_e32 vcc, 0, v10
	v_cmp_gt_f32_e64 s[16:17], v19, v6
	s_and_b64 vcc, vcc, s[16:17]
	s_mov_b32 s16, 0x40000
	v_cndmask_b32_e32 v6, v6, v19, vcc
	v_bitop3_b32 v10, v38, s16, v3 bitop3:0xc8
	v_cndmask_b32_e64 v7, v7, 17, vcc
	v_cmp_eq_u32_e32 vcc, 0, v10
	v_cmp_gt_f32_e64 s[16:17], v28, v6
	s_and_b64 vcc, vcc, s[16:17]
	s_mov_b32 s16, 0x80000
	v_cndmask_b32_e32 v6, v6, v28, vcc
	v_bitop3_b32 v10, v38, s16, v3 bitop3:0xc8
	v_cndmask_b32_e64 v7, v7, 18, vcc
	v_cmp_eq_u32_e32 vcc, 0, v10
	v_cmp_gt_f32_e64 s[16:17], v29, v6
	s_and_b64 vcc, vcc, s[16:17]
	s_mov_b32 s16, 0x100000
	v_cndmask_b32_e32 v6, v6, v29, vcc
	v_bitop3_b32 v10, v38, s16, v3 bitop3:0xc8
	v_cndmask_b32_e64 v7, v7, 19, vcc
	v_cmp_eq_u32_e32 vcc, 0, v10
	v_cmp_gt_f32_e64 s[16:17], v12, v6
	s_and_b64 vcc, vcc, s[16:17]
	s_mov_b32 s16, 0x200000
	v_cndmask_b32_e32 v6, v6, v12, vcc
	v_bitop3_b32 v10, v38, s16, v3 bitop3:0xc8
	v_cndmask_b32_e64 v7, v7, 20, vcc
	v_cmp_eq_u32_e32 vcc, 0, v10
	v_cmp_gt_f32_e64 s[16:17], v13, v6
	s_and_b64 vcc, vcc, s[16:17]
	s_mov_b32 s16, 0x400000
	v_cndmask_b32_e32 v6, v6, v13, vcc
	v_bitop3_b32 v10, v38, s16, v3 bitop3:0xc8
	v_cndmask_b32_e64 v7, v7, 21, vcc
	v_cmp_eq_u32_e32 vcc, 0, v10
	v_cmp_gt_f32_e64 s[16:17], v4, v6
	s_and_b64 vcc, vcc, s[16:17]
	s_mov_b32 s16, 0x800000
	v_cndmask_b32_e32 v4, v6, v4, vcc
	v_cndmask_b32_e64 v6, v7, 22, vcc
	v_bitop3_b32 v7, v38, s16, v3 bitop3:0xc8
	v_cmp_eq_u32_e32 vcc, 0, v7
	v_cmp_gt_f32_e64 s[16:17], v5, v4
	s_and_b64 vcc, vcc, s[16:17]
	s_mov_b32 s16, 0x1000000
	v_cndmask_b32_e32 v4, v4, v5, vcc
	v_cndmask_b32_e64 v5, v6, 23, vcc
	v_bitop3_b32 v6, v38, s16, v3 bitop3:0xc8
	v_cmp_eq_u32_e32 vcc, 0, v6
	v_cmp_gt_f32_e64 s[16:17], v14, v4
	s_and_b64 vcc, vcc, s[16:17]
	v_cndmask_b32_e32 v4, v4, v14, vcc
	v_bitop3_b32 v6, v38, s61, v3 bitop3:0xc8
	v_cndmask_b32_e64 v5, v5, 24, vcc
	v_cmp_eq_u32_e32 vcc, 0, v6
	v_cmp_gt_f32_e64 s[16:17], v15, v4
	s_and_b64 vcc, vcc, s[16:17]
	v_cndmask_b32_e32 v4, v4, v15, vcc
	v_bitop3_b32 v6, v38, s62, v3 bitop3:0xc8
	v_cndmask_b32_e64 v5, v5, 25, vcc
	v_cmp_eq_u32_e32 vcc, 0, v6
	v_cmp_gt_f32_e64 s[16:17], v26, v4
	s_and_b64 vcc, vcc, s[16:17]
	v_cndmask_b32_e32 v4, v4, v26, vcc
	v_bitop3_b32 v6, v38, s63, v3 bitop3:0xc8
	v_cndmask_b32_e64 v5, v5, 26, vcc
	v_cmp_eq_u32_e32 vcc, 0, v6
	v_cmp_gt_f32_e64 s[16:17], v27, v4
	s_and_b64 vcc, vcc, s[16:17]
	v_cndmask_b32_e32 v4, v4, v27, vcc
	v_bitop3_b32 v6, v38, s64, v3 bitop3:0xc8
	v_cndmask_b32_e64 v5, v5, 27, vcc
	v_cmp_eq_u32_e32 vcc, 0, v6
	v_cmp_gt_f32_e64 s[16:17], v16, v4
	s_and_b64 vcc, vcc, s[16:17]
	v_cndmask_b32_e32 v4, v4, v16, vcc
	v_bitop3_b32 v6, v38, s65, v3 bitop3:0xc8
	v_cndmask_b32_e64 v5, v5, 28, vcc
	v_cmp_eq_u32_e32 vcc, 0, v6
	v_cmp_gt_f32_e64 s[16:17], v17, v4
	s_and_b64 vcc, vcc, s[16:17]
	v_or_b32_e32 v88, v38, v3
	v_cndmask_b32_e32 v4, v4, v17, vcc
	v_bitop3_b32 v3, v38, 2.0, v3 bitop3:0xc8
	v_cndmask_b32_e64 v5, v5, 29, vcc
	v_cmp_eq_u32_e32 vcc, 0, v3
	v_cmp_gt_f32_e64 s[16:17], v8, v4
	s_and_b64 vcc, vcc, s[16:17]
	v_cndmask_b32_e32 v3, v4, v8, vcc
	v_cndmask_b32_e64 v4, v5, 30, vcc
	v_cmp_lt_i32_e32 vcc, -1, v88
	v_cmp_gt_f32_e64 s[16:17], v9, v3
	s_and_b64 vcc, vcc, s[16:17]
	v_cndmask_b32_e32 v5, v3, v9, vcc
	v_cndmask_b32_e64 v3, v4, 31, vcc
	v_sub_f32_e32 v4, v36, v36
	v_mul_f32_e32 v4, 0x3fb8aa3b, v4
	v_exp_f32_e32 v10, v4
	v_sub_f32_e32 v4, v37, v36
	v_mul_f32_e32 v4, 0x3fb8aa3b, v4
	v_exp_f32_e32 v11, v4
	v_sub_f32_e32 v4, v39, v36
	v_mul_f32_e32 v4, 0x3fb8aa3b, v4
	v_exp_f32_e32 v12, v4
	v_sub_f32_e32 v4, v5, v36
	v_mul_f32_e32 v4, 0x3fb8aa3b, v4
	v_exp_f32_e32 v13, v4
	v_add_f32_e32 v4, 0, v10
	v_add_f32_e32 v4, v4, v11
	v_add_f32_e32 v4, v4, v12
	v_add_f32_e32 v14, v4, v13
	v_div_scale_f32 v15, s[16:17], v14, v14, v10
	v_rcp_f32_e32 v16, v15
	v_lshl_add_u32 v4, s66, 8, v94
	v_ashrrev_i32_e32 v5, 31, v4
	v_lshlrev_b64 v[6:7], 2, v[4:5]
	v_fma_f32 v5, -v15, v16, 1.0
	v_fmac_f32_e32 v16, v5, v16
	v_div_scale_f32 v5, vcc, v10, v14, v10
	v_mul_f32_e32 v17, v5, v16
	v_fma_f32 v18, -v15, v17, v5
	v_fmac_f32_e32 v17, v18, v16
	v_fma_f32 v5, -v15, v17, v5
	v_div_fmas_f32 v5, v5, v16, v17
	v_div_fixup_f32 v5, v5, v14, v10
	v_div_scale_f32 v10, s[16:17], v14, v14, v11
	v_rcp_f32_e32 v15, v10
	v_lshl_add_u64 v[8:9], s[20:21], 0, v[6:7]
	v_lshl_add_u64 v[6:7], s[22:23], 0, v[6:7]
	global_store_dword v[6:7], v5, off
	v_or_b32_e32 v6, 1, v4
	v_fma_f32 v4, -v10, v15, 1.0
	v_lshl_add_u32 v5, v0, 2, 0
	v_fmac_f32_e32 v15, v4, v15
	v_div_scale_f32 v4, vcc, v11, v14, v11
	ds_add_u32 v5, v109 offset:58624
	v_mul_f32_e32 v5, v4, v15
	v_fma_f32 v16, -v10, v5, v4
	v_fmac_f32_e32 v5, v16, v15
	v_fma_f32 v4, -v10, v5, v4
	v_div_fmas_f32 v4, v4, v15, v5
	v_div_scale_f32 v5, s[16:17], v14, v14, v12
	v_rcp_f32_e32 v15, v5
	v_ashrrev_i32_e32 v7, 31, v6
	v_div_fixup_f32 v4, v4, v14, v11
	v_lshl_add_u64 v[10:11], v[6:7], 2, s[22:23]
	v_lshl_add_u32 v6, v1, 2, 0
	ds_add_u32 v6, v109 offset:58624
	v_fma_f32 v6, -v5, v15, 1.0
	v_fmac_f32_e32 v15, v6, v15
	v_div_scale_f32 v6, vcc, v12, v14, v12
	v_mul_f32_e32 v7, v6, v15
	v_fma_f32 v16, -v5, v7, v6
	v_fmac_f32_e32 v7, v16, v15
	v_fma_f32 v5, -v5, v7, v6
	v_div_scale_f32 v6, s[16:17], v14, v14, v13
	v_div_fmas_f32 v5, v5, v15, v7
	v_rcp_f32_e32 v7, v6
	v_div_fixup_f32 v5, v5, v14, v12
	v_lshl_add_u32 v12, v2, 2, 0
	ds_add_u32 v12, v109 offset:58624
	global_store_dwordx4 v[8:9], v[0:3], off
	s_nop 1
	v_fma_f32 v0, -v6, v7, 1.0
	v_fmac_f32_e32 v7, v0, v7
	v_div_scale_f32 v0, vcc, v13, v14, v13
	v_mul_f32_e32 v1, v0, v7
	v_fma_f32 v2, -v6, v1, v0
	v_fmac_f32_e32 v1, v2, v7
	v_fma_f32 v0, -v6, v1, v0
	v_div_fmas_f32 v0, v0, v7, v1
	v_div_fixup_f32 v6, v0, v14, v13
	global_store_dwordx3 v[10:11], v[4:6], off
	v_lshl_add_u32 v0, v3, 2, 0
	ds_add_u32 v0, v109 offset:58624

.LBB0_2361:
	v_ashrrev_i32_e32 v19, 31, v17
	v_mov_b32_e32 v18, v17
	v_ashrrev_i32_e32 v25, 31, v16
	v_mov_b32_e32 v24, v16
	v_lshlrev_b64 v[24:25], 2, v[24:25]
	v_lshlrev_b64 v[28:29], 2, v[18:19]
	v_lshl_add_u64 v[26:27], s[42:43], 0, v[24:25]
	v_lshl_add_u64 v[18:19], s[42:43], 0, v[28:29]
	global_load_dword v21, v[26:27], off
	s_nop 0
	global_load_dword v18, v[18:19], off
	v_lshl_add_u64 v[26:27], v[24:25], 0, s[30:31]
	v_lshl_add_u64 v[30:31], s[68:69], 0, v[26:27]
	v_lshl_add_u64 v[26:27], s[70:71], 0, v[26:27]
	v_add_u32_e32 v20, -2, v20
	s_add_i32 s33, s33, 4
	v_cmp_eq_u32_e32 vcc, 0, v20
	s_or_b64 s[46:47], vcc, s[46:47]
	s_waitcnt vmcnt(0)
	ds_write2st64_b32 v22, v21, v18 offset1:8
	v_lshl_add_u64 v[18:19], v[28:29], 0, s[30:31]
	v_lshl_add_u64 v[32:33], s[68:69], 0, v[18:19]
	global_load_dword v21, v[30:31], off
	global_load_dword v23, v[32:33], off
	v_lshl_add_u64 v[18:19], s[70:71], 0, v[18:19]
	s_waitcnt vmcnt(1)
	ds_write_b32 v22, v21 offset:4096
	global_load_dword v32, v[26:27], off
	global_load_dword v36, v[18:19], off
	v_lshl_add_u64 v[18:19], s[40:41], 0, v[24:25]
	v_lshl_add_u64 v[26:27], s[40:41], 0, v[28:29]
	v_lshl_add_u64 v[24:25], s[38:39], 0, v[24:25]
	global_load_dword v18, v[18:19], off
	s_nop 0
	global_load_dword v19, v[26:27], off
	v_lshl_add_u64 v[26:27], s[38:39], 0, v[28:29]
	global_load_dword v37, v[24:25], off
	global_load_dword v38, v[26:27], off
	v_add_u32_e32 v24, 0x400, v16
	v_add_u32_e32 v26, 0x400, v17
	v_ashrrev_i32_e32 v25, 31, v24
	v_ashrrev_i32_e32 v27, 31, v26
	v_lshlrev_b64 v[24:25], 2, v[24:25]
	v_lshl_add_u64 v[28:29], s[42:43], 0, v[24:25]
	v_lshlrev_b64 v[26:27], 2, v[26:27]
	v_lshl_add_u64 v[30:31], s[42:43], 0, v[26:27]
	global_load_dword v28, v[28:29], off
	s_nop 0
	global_load_dword v29, v[30:31], off
	v_add_u32_e32 v30, 0x1400, v17
	v_ashrrev_i32_e32 v31, 31, v30
	v_lshlrev_b64 v[30:31], 2, v[30:31]
	v_lshl_add_u64 v[34:35], s[68:69], 0, v[30:31]
	v_lshl_add_u64 v[30:31], s[70:71], 0, v[30:31]
	v_add_u32_e32 v21, 0x2000, v22
	v_add_u32_e32 v17, 0x800, v17
	s_waitcnt vmcnt(1)
	ds_write2st64_b32 v22, v28, v23 offset0:16 offset1:24
	s_waitcnt vmcnt(0)
	ds_write2st64_b32 v22, v29, v32 offset0:24 offset1:32
	v_add_u32_e32 v28, 0x1400, v16
	v_ashrrev_i32_e32 v29, 31, v28
	v_lshlrev_b64 v[28:29], 2, v[28:29]
	v_lshl_add_u64 v[32:33], s[68:69], 0, v[28:29]
	global_load_dword v23, v[32:33], off
	s_nop 0
	global_load_dword v32, v[34:35], off
	v_add_f32_e32 v18, 1.0, v18
	v_add_f32_e32 v19, 1.0, v19
	v_lshl_add_u64 v[28:29], s[70:71], 0, v[28:29]
	v_add_u32_e32 v16, 0x800, v16
	s_waitcnt vmcnt(1)
	ds_write2st64_b32 v22, v23, v36 offset0:32 offset1:40
	s_waitcnt vmcnt(0)
	ds_write2st64_b32 v22, v32, v18 offset0:40 offset1:48
	global_load_dword v18, v[28:29], off
	global_load_dword v23, v[30:31], off
	v_lshl_add_u64 v[28:29], s[40:41], 0, v[26:27]
	v_lshl_add_u64 v[26:27], s[38:39], 0, v[26:27]
	s_waitcnt vmcnt(1)
	ds_write2st64_b32 v22, v18, v19 offset0:48 offset1:56
	s_waitcnt vmcnt(0)
	ds_write2st64_b32 v22, v23, v37 offset0:56 offset1:64
	v_lshl_add_u64 v[18:19], s[40:41], 0, v[24:25]
	global_load_dword v18, v[18:19], off
	s_nop 0
	global_load_dword v19, v[28:29], off
	v_lshl_add_u64 v[24:25], s[38:39], 0, v[24:25]
	s_waitcnt vmcnt(0)
	v_add_f32_e32 v18, 1.0, v18
	v_add_f32_e32 v19, 1.0, v19
	ds_write2st64_b32 v22, v18, v38 offset0:64 offset1:72
	global_load_dword v18, v[24:25], off
	global_load_dword v23, v[26:27], off
	s_waitcnt vmcnt(1)
	ds_write2st64_b32 v22, v19, v18 offset0:72 offset1:80
	s_waitcnt vmcnt(0)
	ds_write_b32 v22, v23 offset:22528
	v_mov_b32_e32 v18, s33
	v_mov_b32_e32 v22, v21
	s_andn2_b64 exec, exec, s[46:47]
	s_cbranch_execnz .LBB0_2361
	s_or_b64 exec, exec, s[46:47]
	v_lshlrev_b32_e32 v18, 9, v18
	s_or_b64 exec, exec, s[44:45]
	s_and_saveexec_b64 s[44:45], s[12:13]
	s_cbranch_execz .LBB0_2365
	s_branch .LBB0_2364

.LBB0_2415:
	v_add_u32_e32 v1, s16, v44
	ds_read_b128 v[20:23], v0
	ds_read_b128 v[24:27], v0 offset:272
	ds_read_b128 v[28:31], v0 offset:544
	ds_read_b128 v[32:35], v0 offset:816
	ds_read_b128 v[36:39], v1
	ds_read_b128 v[88:91], v1 offset:128
	ds_read_b128 v[114:117], v1 offset:256
	ds_read_b128 v[118:121], v1 offset:384
	s_waitcnt lgkmcnt(7)
	v_mov_b32_e32 v2, v23
	s_waitcnt lgkmcnt(6)
	v_mov_b32_e32 v92, v27
	s_waitcnt lgkmcnt(3)
	v_fmac_f32_e32 v18, v38, v20
	v_fmac_f32_e32 v19, v39, v20
	v_fmac_f32_e32 v16, v36, v20
	v_fmac_f32_e32 v17, v37, v20
	v_fmac_f32_e32 v14, v38, v21
	v_fmac_f32_e32 v15, v39, v21
	v_fmac_f32_e32 v12, v36, v21
	v_fmac_f32_e32 v13, v37, v21
	v_fmac_f32_e32 v8, v36, v22
	v_fmac_f32_e32 v9, v37, v22
	v_fmac_f32_e32 v10, v38, v22
	v_fmac_f32_e32 v11, v39, v22
	v_fmac_f32_e32 v4, v36, v2
	v_fmac_f32_e32 v5, v37, v2
	v_fma_f32 v3, v39, v2, v7
	v_fma_f32 v2, v38, v2, v6
	v_mov_b32_e32 v122, v31
	s_waitcnt lgkmcnt(2)
	v_fma_f32 v6, v90, v24, v18
	v_fma_f32 v7, v91, v24, v19
	v_fmac_f32_e32 v16, v88, v24
	v_fmac_f32_e32 v17, v89, v24
	v_fmac_f32_e32 v14, v90, v25
	v_fmac_f32_e32 v15, v91, v25
	v_fmac_f32_e32 v12, v88, v25
	v_fmac_f32_e32 v13, v89, v25
	v_fmac_f32_e32 v10, v90, v26
	v_fmac_f32_e32 v11, v91, v26
	v_fmac_f32_e32 v8, v88, v26
	v_fmac_f32_e32 v9, v89, v26
	v_fmac_f32_e32 v2, v90, v92
	v_fmac_f32_e32 v3, v91, v92
	v_fmac_f32_e32 v4, v88, v92
	v_fmac_f32_e32 v5, v89, v92
	s_addk_i32 s16, 0x200
	v_mov_b32_e32 v124, v35
	s_waitcnt lgkmcnt(1)
	v_fmac_f32_e32 v6, v116, v28
	v_fmac_f32_e32 v7, v117, v28
	v_fmac_f32_e32 v16, v114, v28
	v_fmac_f32_e32 v17, v115, v28
	v_fmac_f32_e32 v14, v116, v29
	v_fmac_f32_e32 v15, v117, v29
	v_fmac_f32_e32 v12, v114, v29
	v_fmac_f32_e32 v13, v115, v29
	v_fmac_f32_e32 v10, v116, v30
	v_fmac_f32_e32 v11, v117, v30
	v_fmac_f32_e32 v8, v114, v30
	v_fmac_f32_e32 v9, v115, v30
	v_fmac_f32_e32 v2, v116, v122
	v_fmac_f32_e32 v3, v117, v122
	v_fmac_f32_e32 v4, v114, v122
	v_fmac_f32_e32 v5, v115, v122
	v_add_u32_e32 v0, 0x440, v0
	s_cmpk_lg_i32 s16, 0x800
	s_waitcnt lgkmcnt(0)
	v_fma_f32 v18, v120, v32, v6
	v_fma_f32 v19, v121, v32, v7
	v_fmac_f32_e32 v16, v118, v32
	v_fmac_f32_e32 v17, v119, v32
	v_fmac_f32_e32 v14, v120, v33
	v_fmac_f32_e32 v15, v121, v33
	v_fmac_f32_e32 v12, v118, v33
	v_fmac_f32_e32 v13, v119, v33
	v_fmac_f32_e32 v10, v120, v34
	v_fmac_f32_e32 v11, v121, v34
	v_fmac_f32_e32 v8, v118, v34
	v_fmac_f32_e32 v9, v119, v34
	v_fma_f32 v6, v120, v124, v2
	v_fma_f32 v7, v121, v124, v3
	v_fmac_f32_e32 v4, v118, v124
	v_fmac_f32_e32 v5, v119, v124
	s_cbranch_scc1 .LBB0_2415
	s_barrier
	ds_write_b128 v107, v[16:19] offset:58752
	ds_write_b128 v107, v[12:15] offset:58880
	ds_write_b128 v107, v[8:11] offset:59008
	ds_write_b128 v107, v[4:7] offset:59136
	s_waitcnt lgkmcnt(0)
	s_barrier
	global_load_dwordx4 v[0:3], v[50:51], off offset:256
	ds_read_b128 v[4:7], v98 offset:58752
	ds_read_b128 v[8:11], v99 offset:8192
	ds_read_b128 v[12:15], v99 offset:16384
	ds_read_b128 v[16:19], v99 offset:24576
	v_add_u32_e32 v20, 0xc400, v100
	v_add_u32_e32 v21, 0xc408, v100
	s_waitcnt lgkmcnt(2)
	v_add_f32_e32 v4, v4, v8
	v_add_f32_e32 v5, v5, v9
	v_add_f32_e32 v6, v6, v10
	v_add_f32_e32 v7, v7, v11
	s_waitcnt lgkmcnt(1)
	v_add_f32_e32 v4, v12, v4
	v_add_f32_e32 v5, v13, v5
	v_add_f32_e32 v6, v14, v6
	v_add_f32_e32 v7, v15, v7
	s_waitcnt lgkmcnt(0)
	v_add_f32_e32 v4, v16, v4
	v_add_f32_e32 v5, v17, v5
	v_add_f32_e32 v6, v18, v6
	v_add_f32_e32 v7, v19, v7
	s_waitcnt vmcnt(0)
	v_add_f32_e32 v0, v0, v4
	v_add_f32_e32 v1, v1, v5
	v_add_f32_e32 v2, v6, v2
	v_add_f32_e32 v3, v7, v3
	ds_write2_b32 v20, v0, v1 offset1:1
	ds_write2_b32 v21, v2, v3 offset1:1
	s_waitcnt lgkmcnt(0)
	s_barrier
	s_and_saveexec_b64 s[36:37], s[6:7]
	s_cbranch_execz .LBB0_2418
	v_add_u32_e32 v0, 0xc400, v108
	v_add_u32_e32 v1, 0xc408, v108
	v_add_u32_e32 v2, 0xc410, v108
	v_add_u32_e32 v3, 0xc418, v108
	ds_read2_b32 v[34:35], v0 offset1:1
	ds_read2_b32 v[30:31], v1 offset1:1
	ds_read2_b32 v[22:23], v2 offset1:1
	ds_read2_b32 v[10:11], v3 offset1:1
	s_mov_b32 s16, 0xff61b1e6
	s_waitcnt lgkmcnt(3)
	v_max_f32_e32 v0, v34, v34
	v_max_f32_e32 v0, 0xff61b1e6, v0
	v_cmp_lt_f32_e32 vcc, s16, v34
	v_cmp_gt_f32_e64 s[16:17], v35, v0
	v_add_u32_e32 v2, 0xc420, v108
	ds_read2_b32 v[24:25], v2 offset1:1
	v_cndmask_b32_e64 v0, v0, v35, s[16:17]
	v_cndmask_b32_e64 v1, 0, 1, s[16:17]
	s_waitcnt lgkmcnt(3)
	v_cmp_gt_f32_e64 s[16:17], v30, v0
	v_add_u32_e32 v2, 0xc428, v108
	v_add_u32_e32 v3, 0xc430, v108
	v_cndmask_b32_e64 v0, v0, v30, s[16:17]
	v_cndmask_b32_e64 v1, v1, 2, s[16:17]
	v_cmp_gt_f32_e64 s[16:17], v31, v0
	v_add_u32_e32 v4, 0xc438, v108
	ds_read2_b32 v[32:33], v2 offset1:1
	ds_read2_b32 v[20:21], v3 offset1:1
	ds_read2_b32 v[6:7], v4 offset1:1
	v_cndmask_b32_e64 v0, v0, v31, s[16:17]
	v_cndmask_b32_e64 v1, v1, 3, s[16:17]
	s_waitcnt lgkmcnt(5)
	v_cmp_gt_f32_e64 s[16:17], v22, v0
	v_add_u32_e32 v2, 0xc440, v108
	ds_read2_b32 v[18:19], v2 offset1:1
	v_cndmask_b32_e64 v0, v0, v22, s[16:17]
	v_cndmask_b32_e64 v1, v1, 4, s[16:17]
	v_cmp_gt_f32_e64 s[16:17], v23, v0
	v_add_u32_e32 v2, 0xc448, v108
	v_add_u32_e32 v4, 0xc458, v108
	v_cndmask_b32_e64 v0, v0, v23, s[16:17]
	v_cndmask_b32_e64 v1, v1, 5, s[16:17]
	s_waitcnt lgkmcnt(5)
	v_cmp_gt_f32_e64 s[16:17], v10, v0
	v_add_u32_e32 v3, 0xc450, v108
	ds_read2_b32 v[28:29], v2 offset1:1
	ds_read2_b32 v[12:13], v3 offset1:1
	ds_read2_b32 v[4:5], v4 offset1:1
	v_cndmask_b32_e64 v0, v0, v10, s[16:17]
	v_cndmask_b32_e64 v1, v1, 6, s[16:17]
	v_cmp_gt_f32_e64 s[16:17], v11, v0
	v_add_u32_e32 v2, 0xc460, v108
	ds_read2_b32 v[14:15], v2 offset1:1
	v_cndmask_b32_e64 v0, v0, v11, s[16:17]
	v_cndmask_b32_e64 v1, v1, 7, s[16:17]
	s_waitcnt lgkmcnt(8)
	v_cmp_gt_f32_e64 s[16:17], v24, v0
	v_add_u32_e32 v2, 0xc468, v108
	v_add_u32_e32 v8, 0xc478, v108
	v_cndmask_b32_e64 v0, v0, v24, s[16:17]
	v_cndmask_b32_e64 v1, v1, 8, s[16:17]
	v_cmp_gt_f32_e64 s[16:17], v25, v0
	v_add_u32_e32 v3, 0xc470, v108
	ds_read2_b32 v[26:27], v2 offset1:1
	ds_read2_b32 v[16:17], v3 offset1:1
	ds_read2_b32 v[8:9], v8 offset1:1
	v_cndmask_b32_e64 v0, v0, v25, s[16:17]
	v_cndmask_b32_e64 v1, v1, 9, s[16:17]
	s_waitcnt lgkmcnt(10)
	v_cmp_gt_f32_e64 s[16:17], v32, v0
	s_nop 1
	v_cndmask_b32_e64 v0, v0, v32, s[16:17]
	v_cndmask_b32_e64 v1, v1, 10, s[16:17]
	v_cmp_gt_f32_e64 s[16:17], v33, v0
	s_nop 1
	v_cndmask_b32_e64 v0, v0, v33, s[16:17]
	v_cndmask_b32_e64 v1, v1, 11, s[16:17]
	s_waitcnt lgkmcnt(9)
	v_cmp_gt_f32_e64 s[16:17], v20, v0
	s_nop 1
	v_cndmask_b32_e64 v0, v0, v20, s[16:17]
	v_cndmask_b32_e64 v1, v1, 12, s[16:17]
	v_cmp_gt_f32_e64 s[16:17], v21, v0
	s_nop 1
	v_cndmask_b32_e64 v0, v0, v21, s[16:17]
	v_cndmask_b32_e64 v1, v1, 13, s[16:17]
	s_waitcnt lgkmcnt(8)
	v_cmp_gt_f32_e64 s[16:17], v6, v0
	s_nop 1
	v_cndmask_b32_e64 v0, v0, v6, s[16:17]
	v_cndmask_b32_e64 v1, v1, 14, s[16:17]
	v_cmp_gt_f32_e64 s[16:17], v7, v0
	s_nop 1
	v_cndmask_b32_e64 v0, v0, v7, s[16:17]
	v_cndmask_b32_e64 v1, v1, 15, s[16:17]
	s_waitcnt lgkmcnt(7)
	v_cmp_gt_f32_e64 s[16:17], v18, v0
	s_nop 1
	v_cndmask_b32_e64 v0, v0, v18, s[16:17]
	v_cndmask_b32_e64 v1, v1, 16, s[16:17]
	v_cmp_gt_f32_e64 s[16:17], v19, v0
	s_nop 1
	v_cndmask_b32_e64 v0, v0, v19, s[16:17]
	v_cndmask_b32_e64 v1, v1, 17, s[16:17]
	s_waitcnt lgkmcnt(6)
	v_cmp_gt_f32_e64 s[16:17], v28, v0
	s_nop 1
	v_cndmask_b32_e64 v0, v0, v28, s[16:17]
	v_cndmask_b32_e64 v1, v1, 18, s[16:17]
	v_cmp_gt_f32_e64 s[16:17], v29, v0
	s_nop 1
	v_cndmask_b32_e64 v0, v0, v29, s[16:17]
	v_cndmask_b32_e64 v1, v1, 19, s[16:17]
	s_waitcnt lgkmcnt(5)
	v_cmp_gt_f32_e64 s[16:17], v12, v0
	s_nop 1
	v_cndmask_b32_e64 v0, v0, v12, s[16:17]
	v_cndmask_b32_e64 v1, v1, 20, s[16:17]
	v_cmp_gt_f32_e64 s[16:17], v13, v0
	s_nop 1
	v_cndmask_b32_e64 v0, v0, v13, s[16:17]
	v_cndmask_b32_e64 v1, v1, 21, s[16:17]
	s_waitcnt lgkmcnt(4)
	v_cmp_gt_f32_e64 s[16:17], v4, v0
	s_nop 1
	v_cndmask_b32_e64 v0, v0, v4, s[16:17]
	v_cndmask_b32_e64 v1, v1, 22, s[16:17]
	v_cmp_gt_f32_e64 s[16:17], v5, v0
	s_nop 1
	v_cndmask_b32_e64 v0, v0, v5, s[16:17]
	v_cndmask_b32_e64 v1, v1, 23, s[16:17]
	s_waitcnt lgkmcnt(3)
	v_cmp_gt_f32_e64 s[16:17], v14, v0
	s_nop 1
	v_cndmask_b32_e64 v0, v0, v14, s[16:17]
	v_cndmask_b32_e64 v1, v1, 24, s[16:17]
	v_cmp_gt_f32_e64 s[16:17], v15, v0
	s_nop 1
	v_cndmask_b32_e64 v0, v0, v15, s[16:17]
	v_cndmask_b32_e64 v1, v1, 25, s[16:17]
	s_waitcnt lgkmcnt(2)
	v_cmp_gt_f32_e64 s[16:17], v26, v0
	s_nop 1
	v_cndmask_b32_e64 v0, v0, v26, s[16:17]
	v_cndmask_b32_e64 v1, v1, 26, s[16:17]
	v_cmp_gt_f32_e64 s[16:17], v27, v0
	s_nop 1
	v_cndmask_b32_e64 v0, v0, v27, s[16:17]
	v_cndmask_b32_e64 v1, v1, 27, s[16:17]
	s_waitcnt lgkmcnt(1)
	v_cmp_gt_f32_e64 s[16:17], v16, v0
	s_nop 1
	v_cndmask_b32_e64 v0, v0, v16, s[16:17]
	v_cndmask_b32_e64 v1, v1, 28, s[16:17]
	v_cmp_gt_f32_e64 s[16:17], v17, v0
	s_nop 1
	v_cndmask_b32_e64 v0, v0, v17, s[16:17]
	v_cndmask_b32_e64 v1, v1, 29, s[16:17]
	s_waitcnt lgkmcnt(0)
	v_cmp_gt_f32_e64 s[16:17], v8, v0
	s_nop 1
	v_cndmask_b32_e64 v0, v0, v8, s[16:17]
	v_cndmask_b32_e64 v1, v1, 30, s[16:17]
	v_cmp_gt_f32_e64 s[16:17], v9, v0
	s_nop 1
	v_cndmask_b32_e64 v36, v0, v9, s[16:17]
	v_cndmask_b32_e64 v0, v1, 31, s[16:17]
	v_cmp_ne_u32_e64 s[16:17], 0, v0
	v_lshlrev_b32_e64 v2, v0, 1
	s_and_b64 s[16:17], s[16:17], vcc
	v_cndmask_b32_e64 v1, v112, v34, s[16:17]
	v_and_b32_e32 v3, 2, v2
	v_cmp_eq_u32_e64 s[16:17], 0, v3
	v_cmp_gt_f32_e64 s[18:19], v35, v1
	s_and_b64 s[16:17], s[16:17], s[18:19]
	v_cndmask_b32_e64 v1, v1, v35, s[16:17]
	v_and_b32_e32 v37, 4, v2
	v_cndmask_b32_e64 v3, 0, 1, s[16:17]
	v_cmp_eq_u32_e64 s[16:17], 0, v37
	v_cmp_gt_f32_e64 s[18:19], v30, v1
	s_and_b64 s[16:17], s[16:17], s[18:19]
	v_cndmask_b32_e64 v1, v1, v30, s[16:17]
	v_and_b32_e32 v37, 8, v2
	v_cndmask_b32_e64 v3, v3, 2, s[16:17]
	v_cmp_eq_u32_e64 s[16:17], 0, v37
	v_cmp_gt_f32_e64 s[18:19], v31, v1
	s_and_b64 s[16:17], s[16:17], s[18:19]
	v_cndmask_b32_e64 v1, v1, v31, s[16:17]
	v_and_b32_e32 v37, 16, v2
	v_cndmask_b32_e64 v3, v3, 3, s[16:17]
	v_cmp_eq_u32_e64 s[16:17], 0, v37
	v_cmp_gt_f32_e64 s[18:19], v22, v1
	s_and_b64 s[16:17], s[16:17], s[18:19]
	v_cndmask_b32_e64 v1, v1, v22, s[16:17]
	v_and_b32_e32 v37, 32, v2
	v_cndmask_b32_e64 v3, v3, 4, s[16:17]
	v_cmp_eq_u32_e64 s[16:17], 0, v37
	v_cmp_gt_f32_e64 s[18:19], v23, v1
	s_and_b64 s[16:17], s[16:17], s[18:19]
	v_cndmask_b32_e64 v1, v1, v23, s[16:17]
	v_and_b32_e32 v37, 64, v2
	v_cndmask_b32_e64 v3, v3, 5, s[16:17]
	v_cmp_eq_u32_e64 s[16:17], 0, v37
	v_cmp_gt_f32_e64 s[18:19], v10, v1
	s_and_b64 s[16:17], s[16:17], s[18:19]
	v_cndmask_b32_e64 v1, v1, v10, s[16:17]
	v_and_b32_e32 v37, 0x80, v2
	v_cndmask_b32_e64 v3, v3, 6, s[16:17]
	v_cmp_eq_u32_e64 s[16:17], 0, v37
	v_cmp_gt_f32_e64 s[18:19], v11, v1
	s_and_b64 s[16:17], s[16:17], s[18:19]
	v_cndmask_b32_e64 v1, v1, v11, s[16:17]
	v_and_b32_e32 v37, 0x100, v2
	v_cndmask_b32_e64 v3, v3, 7, s[16:17]
	v_cmp_eq_u32_e64 s[16:17], 0, v37
	v_cmp_gt_f32_e64 s[18:19], v24, v1
	s_and_b64 s[16:17], s[16:17], s[18:19]
	v_cndmask_b32_e64 v1, v1, v24, s[16:17]
	v_and_b32_e32 v37, 0x200, v2
	v_cndmask_b32_e64 v3, v3, 8, s[16:17]
	v_cmp_eq_u32_e64 s[16:17], 0, v37
	v_cmp_gt_f32_e64 s[18:19], v25, v1
	s_and_b64 s[16:17], s[16:17], s[18:19]
	v_cndmask_b32_e64 v1, v1, v25, s[16:17]
	v_and_b32_e32 v37, 0x400, v2
	v_cndmask_b32_e64 v3, v3, 9, s[16:17]
	v_cmp_eq_u32_e64 s[16:17], 0, v37
	v_cmp_gt_f32_e64 s[18:19], v32, v1
	s_and_b64 s[16:17], s[16:17], s[18:19]
	v_cndmask_b32_e64 v1, v1, v32, s[16:17]
	v_and_b32_e32 v37, 0x800, v2
	v_cndmask_b32_e64 v3, v3, 10, s[16:17]
	v_cmp_eq_u32_e64 s[16:17], 0, v37
	v_cmp_gt_f32_e64 s[18:19], v33, v1
	s_and_b64 s[16:17], s[16:17], s[18:19]
	v_cndmask_b32_e64 v1, v1, v33, s[16:17]
	v_and_b32_e32 v37, 0x1000, v2
	v_cndmask_b32_e64 v3, v3, 11, s[16:17]
	v_cmp_eq_u32_e64 s[16:17], 0, v37
	v_cmp_gt_f32_e64 s[18:19], v20, v1
	s_and_b64 s[16:17], s[16:17], s[18:19]
	v_cndmask_b32_e64 v1, v1, v20, s[16:17]
	v_and_b32_e32 v37, 0x2000, v2
	v_cndmask_b32_e64 v3, v3, 12, s[16:17]
	v_cmp_eq_u32_e64 s[16:17], 0, v37
	v_cmp_gt_f32_e64 s[18:19], v21, v1
	s_and_b64 s[16:17], s[16:17], s[18:19]
	v_cndmask_b32_e64 v1, v1, v21, s[16:17]
	v_and_b32_e32 v37, 0x4000, v2
	v_cndmask_b32_e64 v3, v3, 13, s[16:17]
	v_cmp_eq_u32_e64 s[16:17], 0, v37
	v_cmp_gt_f32_e64 s[18:19], v6, v1
	s_and_b64 s[16:17], s[16:17], s[18:19]
	v_cndmask_b32_e64 v1, v1, v6, s[16:17]
	v_and_b32_e32 v37, 0x8000, v2
	v_cndmask_b32_e64 v3, v3, 14, s[16:17]
	v_cmp_eq_u32_e64 s[16:17], 0, v37
	v_cmp_gt_f32_e64 s[18:19], v7, v1
	s_and_b64 s[16:17], s[16:17], s[18:19]
	v_cndmask_b32_e64 v1, v1, v7, s[16:17]
	v_and_b32_e32 v37, 0x10000, v2
	v_cndmask_b32_e64 v3, v3, 15, s[16:17]
	v_cmp_eq_u32_e64 s[16:17], 0, v37
	v_cmp_gt_f32_e64 s[18:19], v18, v1
	s_and_b64 s[16:17], s[16:17], s[18:19]
	v_cndmask_b32_e64 v1, v1, v18, s[16:17]
	v_and_b32_e32 v37, 0x20000, v2
	v_cndmask_b32_e64 v3, v3, 16, s[16:17]
	v_cmp_eq_u32_e64 s[16:17], 0, v37
	v_cmp_gt_f32_e64 s[18:19], v19, v1
	s_and_b64 s[16:17], s[16:17], s[18:19]
	v_cndmask_b32_e64 v1, v1, v19, s[16:17]
	v_and_b32_e32 v37, 0x40000, v2
	v_cndmask_b32_e64 v3, v3, 17, s[16:17]
	v_cmp_eq_u32_e64 s[16:17], 0, v37
	v_cmp_gt_f32_e64 s[18:19], v28, v1
	s_and_b64 s[16:17], s[16:17], s[18:19]
	v_cndmask_b32_e64 v1, v1, v28, s[16:17]
	v_and_b32_e32 v37, 0x80000, v2
	v_cndmask_b32_e64 v3, v3, 18, s[16:17]
	v_cmp_eq_u32_e64 s[16:17], 0, v37
	v_cmp_gt_f32_e64 s[18:19], v29, v1
	s_and_b64 s[16:17], s[16:17], s[18:19]
	v_cndmask_b32_e64 v1, v1, v29, s[16:17]
	v_and_b32_e32 v37, 0x100000, v2
	v_cndmask_b32_e64 v3, v3, 19, s[16:17]
	v_cmp_eq_u32_e64 s[16:17], 0, v37
	v_cmp_gt_f32_e64 s[18:19], v12, v1
	s_and_b64 s[16:17], s[16:17], s[18:19]
	v_cndmask_b32_e64 v1, v1, v12, s[16:17]
	v_and_b32_e32 v37, 0x200000, v2
	v_cndmask_b32_e64 v3, v3, 20, s[16:17]
	v_cmp_eq_u32_e64 s[16:17], 0, v37
	v_cmp_gt_f32_e64 s[18:19], v13, v1
	s_and_b64 s[16:17], s[16:17], s[18:19]
	v_cndmask_b32_e64 v1, v1, v13, s[16:17]
	v_and_b32_e32 v37, 0x400000, v2
	v_cndmask_b32_e64 v3, v3, 21, s[16:17]
	v_cmp_eq_u32_e64 s[16:17], 0, v37
	v_cmp_gt_f32_e64 s[18:19], v4, v1
	s_and_b64 s[16:17], s[16:17], s[18:19]
	v_cndmask_b32_e64 v1, v1, v4, s[16:17]
	v_and_b32_e32 v37, 0x800000, v2
	v_cndmask_b32_e64 v3, v3, 22, s[16:17]
	v_cmp_eq_u32_e64 s[16:17], 0, v37
	v_cmp_gt_f32_e64 s[18:19], v5, v1
	s_and_b64 s[16:17], s[16:17], s[18:19]
	v_cndmask_b32_e64 v1, v1, v5, s[16:17]
	v_and_b32_e32 v37, 0x1000000, v2
	v_cndmask_b32_e64 v3, v3, 23, s[16:17]
	v_cmp_eq_u32_e64 s[16:17], 0, v37
	v_cmp_gt_f32_e64 s[18:19], v14, v1
	s_and_b64 s[16:17], s[16:17], s[18:19]
	v_cndmask_b32_e64 v1, v1, v14, s[16:17]
	v_and_b32_e32 v37, 0x2000000, v2
	v_cndmask_b32_e64 v3, v3, 24, s[16:17]
	v_cmp_eq_u32_e64 s[16:17], 0, v37
	v_cmp_gt_f32_e64 s[18:19], v15, v1
	s_and_b64 s[16:17], s[16:17], s[18:19]
	v_cndmask_b32_e64 v1, v1, v15, s[16:17]
	v_and_b32_e32 v37, 0x4000000, v2
	v_cndmask_b32_e64 v3, v3, 25, s[16:17]
	v_cmp_eq_u32_e64 s[16:17], 0, v37
	v_cmp_gt_f32_e64 s[18:19], v26, v1
	s_and_b64 s[16:17], s[16:17], s[18:19]
	v_cndmask_b32_e64 v1, v1, v26, s[16:17]
	v_and_b32_e32 v37, 0x8000000, v2
	v_cndmask_b32_e64 v3, v3, 26, s[16:17]
	v_cmp_eq_u32_e64 s[16:17], 0, v37
	v_cmp_gt_f32_e64 s[18:19], v27, v1
	s_and_b64 s[16:17], s[16:17], s[18:19]
	v_cndmask_b32_e64 v1, v1, v27, s[16:17]
	v_and_b32_e32 v37, 0x10000000, v2
	v_cndmask_b32_e64 v3, v3, 27, s[16:17]
	v_cmp_eq_u32_e64 s[16:17], 0, v37
	v_cmp_gt_f32_e64 s[18:19], v16, v1
	s_and_b64 s[16:17], s[16:17], s[18:19]
	v_cndmask_b32_e64 v1, v1, v16, s[16:17]
	v_and_b32_e32 v37, 0x20000000, v2
	v_cndmask_b32_e64 v3, v3, 28, s[16:17]
	v_cmp_eq_u32_e64 s[16:17], 0, v37
	v_cmp_gt_f32_e64 s[18:19], v17, v1
	s_and_b64 s[16:17], s[16:17], s[18:19]
	v_cndmask_b32_e64 v1, v1, v17, s[16:17]
	v_and_b32_e32 v37, 2.0, v2
	v_cndmask_b32_e64 v3, v3, 29, s[16:17]
	v_cmp_eq_u32_e64 s[16:17], 0, v37
	v_cmp_gt_f32_e64 s[18:19], v8, v1
	s_and_b64 s[16:17], s[16:17], s[18:19]
	v_cndmask_b32_e64 v1, v1, v8, s[16:17]
	v_cndmask_b32_e64 v3, v3, 30, s[16:17]
	v_cmp_ne_u32_e64 s[16:17], 31, v0
	v_cmp_gt_f32_e64 s[18:19], v9, v1
	s_and_b64 s[16:17], s[16:17], s[18:19]
	v_cndmask_b32_e64 v37, v1, v9, s[16:17]
	v_cndmask_b32_e64 v1, v3, 31, s[16:17]
	v_lshl_or_b32 v3, 1, v1, v2
	v_and_b32_e32 v2, 1, v3
	v_cmp_eq_u32_e64 s[16:17], 0, v2
	s_and_b64 s[16:17], s[16:17], vcc
	v_and_b32_e32 v38, 2, v3
	v_cndmask_b32_e64 v2, v112, v34, s[16:17]
	v_cmp_eq_u32_e64 s[16:17], 0, v38
	v_cmp_gt_f32_e64 s[18:19], v35, v2
	s_and_b64 s[16:17], s[16:17], s[18:19]
	v_cndmask_b32_e64 v2, v2, v35, s[16:17]
	v_and_b32_e32 v39, 4, v3
	v_cndmask_b32_e64 v38, 0, 1, s[16:17]
	v_cmp_eq_u32_e64 s[16:17], 0, v39
	v_cmp_gt_f32_e64 s[18:19], v30, v2
	s_and_b64 s[16:17], s[16:17], s[18:19]
	v_cndmask_b32_e64 v2, v2, v30, s[16:17]
	v_and_b32_e32 v39, 8, v3
	v_cndmask_b32_e64 v38, v38, 2, s[16:17]
	v_cmp_eq_u32_e64 s[16:17], 0, v39
	v_cmp_gt_f32_e64 s[18:19], v31, v2
	s_and_b64 s[16:17], s[16:17], s[18:19]
	v_cndmask_b32_e64 v2, v2, v31, s[16:17]
	v_and_b32_e32 v39, 16, v3
	v_cndmask_b32_e64 v38, v38, 3, s[16:17]
	v_cmp_eq_u32_e64 s[16:17], 0, v39
	v_cmp_gt_f32_e64 s[18:19], v22, v2
	s_and_b64 s[16:17], s[16:17], s[18:19]
	v_cndmask_b32_e64 v2, v2, v22, s[16:17]
	v_and_b32_e32 v39, 32, v3
	v_cndmask_b32_e64 v38, v38, 4, s[16:17]
	v_cmp_eq_u32_e64 s[16:17], 0, v39
	v_cmp_gt_f32_e64 s[18:19], v23, v2
	s_and_b64 s[16:17], s[16:17], s[18:19]
	v_cndmask_b32_e64 v2, v2, v23, s[16:17]
	v_and_b32_e32 v39, 64, v3
	v_cndmask_b32_e64 v38, v38, 5, s[16:17]
	v_cmp_eq_u32_e64 s[16:17], 0, v39
	v_cmp_gt_f32_e64 s[18:19], v10, v2
	s_and_b64 s[16:17], s[16:17], s[18:19]
	v_cndmask_b32_e64 v2, v2, v10, s[16:17]
	v_and_b32_e32 v39, 0x80, v3
	v_cndmask_b32_e64 v38, v38, 6, s[16:17]
	v_cmp_eq_u32_e64 s[16:17], 0, v39
	v_cmp_gt_f32_e64 s[18:19], v11, v2
	s_and_b64 s[16:17], s[16:17], s[18:19]
	v_cndmask_b32_e64 v2, v2, v11, s[16:17]
	v_and_b32_e32 v39, 0x100, v3
	v_cndmask_b32_e64 v38, v38, 7, s[16:17]
	v_cmp_eq_u32_e64 s[16:17], 0, v39
	v_cmp_gt_f32_e64 s[18:19], v24, v2
	s_and_b64 s[16:17], s[16:17], s[18:19]
	v_cndmask_b32_e64 v2, v2, v24, s[16:17]
	v_and_b32_e32 v39, 0x200, v3
	v_cndmask_b32_e64 v38, v38, 8, s[16:17]
	v_cmp_eq_u32_e64 s[16:17], 0, v39
	v_cmp_gt_f32_e64 s[18:19], v25, v2
	s_and_b64 s[16:17], s[16:17], s[18:19]
	v_cndmask_b32_e64 v2, v2, v25, s[16:17]
	v_and_b32_e32 v39, 0x400, v3
	v_cndmask_b32_e64 v38, v38, 9, s[16:17]
	v_cmp_eq_u32_e64 s[16:17], 0, v39
	v_cmp_gt_f32_e64 s[18:19], v32, v2
	s_and_b64 s[16:17], s[16:17], s[18:19]
	v_cndmask_b32_e64 v2, v2, v32, s[16:17]
	v_and_b32_e32 v39, 0x800, v3
	v_cndmask_b32_e64 v38, v38, 10, s[16:17]
	v_cmp_eq_u32_e64 s[16:17], 0, v39
	v_cmp_gt_f32_e64 s[18:19], v33, v2
	s_and_b64 s[16:17], s[16:17], s[18:19]
	v_cndmask_b32_e64 v2, v2, v33, s[16:17]
	v_and_b32_e32 v39, 0x1000, v3
	v_cndmask_b32_e64 v38, v38, 11, s[16:17]
	v_cmp_eq_u32_e64 s[16:17], 0, v39
	v_cmp_gt_f32_e64 s[18:19], v20, v2
	s_and_b64 s[16:17], s[16:17], s[18:19]
	v_cndmask_b32_e64 v2, v2, v20, s[16:17]
	v_and_b32_e32 v39, 0x2000, v3
	v_cndmask_b32_e64 v38, v38, 12, s[16:17]
	v_cmp_eq_u32_e64 s[16:17], 0, v39
	v_cmp_gt_f32_e64 s[18:19], v21, v2
	s_and_b64 s[16:17], s[16:17], s[18:19]
	v_cndmask_b32_e64 v2, v2, v21, s[16:17]
	v_and_b32_e32 v39, 0x4000, v3
	v_cndmask_b32_e64 v38, v38, 13, s[16:17]
	v_cmp_eq_u32_e64 s[16:17], 0, v39
	v_cmp_gt_f32_e64 s[18:19], v6, v2
	s_and_b64 s[16:17], s[16:17], s[18:19]
	v_cndmask_b32_e64 v2, v2, v6, s[16:17]
	v_and_b32_e32 v39, 0x8000, v3
	v_cndmask_b32_e64 v38, v38, 14, s[16:17]
	v_cmp_eq_u32_e64 s[16:17], 0, v39
	v_cmp_gt_f32_e64 s[18:19], v7, v2
	s_and_b64 s[16:17], s[16:17], s[18:19]
	v_cndmask_b32_e64 v2, v2, v7, s[16:17]
	v_and_b32_e32 v39, 0x10000, v3
	v_cndmask_b32_e64 v38, v38, 15, s[16:17]
	v_cmp_eq_u32_e64 s[16:17], 0, v39
	v_cmp_gt_f32_e64 s[18:19], v18, v2
	s_and_b64 s[16:17], s[16:17], s[18:19]
	v_cndmask_b32_e64 v2, v2, v18, s[16:17]
	v_and_b32_e32 v39, 0x20000, v3
	v_cndmask_b32_e64 v38, v38, 16, s[16:17]
	v_cmp_eq_u32_e64 s[16:17], 0, v39
	v_cmp_gt_f32_e64 s[18:19], v19, v2
	s_and_b64 s[16:17], s[16:17], s[18:19]
	v_cndmask_b32_e64 v2, v2, v19, s[16:17]
	v_and_b32_e32 v39, 0x40000, v3
	v_cndmask_b32_e64 v38, v38, 17, s[16:17]
	v_cmp_eq_u32_e64 s[16:17], 0, v39
	v_cmp_gt_f32_e64 s[18:19], v28, v2
	s_and_b64 s[16:17], s[16:17], s[18:19]
	v_cndmask_b32_e64 v2, v2, v28, s[16:17]
	v_and_b32_e32 v39, 0x80000, v3
	v_cndmask_b32_e64 v38, v38, 18, s[16:17]
	v_cmp_eq_u32_e64 s[16:17], 0, v39
	v_cmp_gt_f32_e64 s[18:19], v29, v2
	s_and_b64 s[16:17], s[16:17], s[18:19]
	v_cndmask_b32_e64 v2, v2, v29, s[16:17]
	v_and_b32_e32 v39, 0x100000, v3
	v_cndmask_b32_e64 v38, v38, 19, s[16:17]
	v_cmp_eq_u32_e64 s[16:17], 0, v39
	v_cmp_gt_f32_e64 s[18:19], v12, v2
	s_and_b64 s[16:17], s[16:17], s[18:19]
	v_cndmask_b32_e64 v2, v2, v12, s[16:17]
	v_and_b32_e32 v39, 0x200000, v3
	v_cndmask_b32_e64 v38, v38, 20, s[16:17]
	v_cmp_eq_u32_e64 s[16:17], 0, v39
	v_cmp_gt_f32_e64 s[18:19], v13, v2
	s_and_b64 s[16:17], s[16:17], s[18:19]
	v_cndmask_b32_e64 v2, v2, v13, s[16:17]
	v_and_b32_e32 v39, 0x400000, v3
	v_cndmask_b32_e64 v38, v38, 21, s[16:17]
	v_cmp_eq_u32_e64 s[16:17], 0, v39
	v_cmp_gt_f32_e64 s[18:19], v4, v2
	s_and_b64 s[16:17], s[16:17], s[18:19]
	v_cndmask_b32_e64 v2, v2, v4, s[16:17]
	v_and_b32_e32 v39, 0x800000, v3
	v_cndmask_b32_e64 v38, v38, 22, s[16:17]
	v_cmp_eq_u32_e64 s[16:17], 0, v39
	v_cmp_gt_f32_e64 s[18:19], v5, v2
	s_and_b64 s[16:17], s[16:17], s[18:19]
	v_cndmask_b32_e64 v2, v2, v5, s[16:17]
	v_and_b32_e32 v39, 0x1000000, v3
	v_cndmask_b32_e64 v38, v38, 23, s[16:17]
	v_cmp_eq_u32_e64 s[16:17], 0, v39
	v_cmp_gt_f32_e64 s[18:19], v14, v2
	s_and_b64 s[16:17], s[16:17], s[18:19]
	v_cndmask_b32_e64 v2, v2, v14, s[16:17]
	v_and_b32_e32 v39, 0x2000000, v3
	v_cndmask_b32_e64 v38, v38, 24, s[16:17]
	v_cmp_eq_u32_e64 s[16:17], 0, v39
	v_cmp_gt_f32_e64 s[18:19], v15, v2
	s_and_b64 s[16:17], s[16:17], s[18:19]
	v_cndmask_b32_e64 v2, v2, v15, s[16:17]
	v_and_b32_e32 v39, 0x4000000, v3
	v_cndmask_b32_e64 v38, v38, 25, s[16:17]
	v_cmp_eq_u32_e64 s[16:17], 0, v39
	v_cmp_gt_f32_e64 s[18:19], v26, v2
	s_and_b64 s[16:17], s[16:17], s[18:19]
	v_cndmask_b32_e64 v2, v2, v26, s[16:17]
	v_and_b32_e32 v39, 0x8000000, v3
	v_cndmask_b32_e64 v38, v38, 26, s[16:17]
	v_cmp_eq_u32_e64 s[16:17], 0, v39
	v_cmp_gt_f32_e64 s[18:19], v27, v2
	s_and_b64 s[16:17], s[16:17], s[18:19]
	v_cndmask_b32_e64 v2, v2, v27, s[16:17]
	v_and_b32_e32 v39, 0x10000000, v3
	v_cndmask_b32_e64 v38, v38, 27, s[16:17]
	v_cmp_eq_u32_e64 s[16:17], 0, v39
	v_cmp_gt_f32_e64 s[18:19], v16, v2
	s_and_b64 s[16:17], s[16:17], s[18:19]
	v_cndmask_b32_e64 v2, v2, v16, s[16:17]
	v_and_b32_e32 v39, 0x20000000, v3
	v_cndmask_b32_e64 v38, v38, 28, s[16:17]
	v_cmp_eq_u32_e64 s[16:17], 0, v39
	v_cmp_gt_f32_e64 s[18:19], v17, v2
	s_and_b64 s[16:17], s[16:17], s[18:19]
	v_cndmask_b32_e64 v2, v2, v17, s[16:17]
	v_and_b32_e32 v39, 2.0, v3
	v_cndmask_b32_e64 v38, v38, 29, s[16:17]
	v_cmp_eq_u32_e64 s[16:17], 0, v39
	v_cmp_gt_f32_e64 s[18:19], v8, v2
	s_and_b64 s[16:17], s[16:17], s[18:19]
	v_cndmask_b32_e64 v2, v2, v8, s[16:17]
	v_cndmask_b32_e64 v38, v38, 30, s[16:17]
	v_cmp_lt_i32_e64 s[16:17], -1, v3
	v_cmp_gt_f32_e64 s[18:19], v9, v2
	s_and_b64 s[16:17], s[16:17], s[18:19]
	v_cndmask_b32_e64 v39, v2, v9, s[16:17]
	v_cndmask_b32_e64 v2, v38, 31, s[16:17]
	v_lshlrev_b32_e64 v38, v2, 1
	v_bitop3_b32 v89, v38, 1, v3 bitop3:0xc8
	v_cmp_eq_u32_e64 s[16:17], 0, v89
	s_and_b64 vcc, s[16:17], vcc
	v_cndmask_b32_e32 v34, v112, v34, vcc
	v_bitop3_b32 v89, v38, 2, v3 bitop3:0xc8
	v_cmp_eq_u32_e32 vcc, 0, v89
	v_cmp_gt_f32_e64 s[16:17], v35, v34
	s_and_b64 vcc, vcc, s[16:17]
	v_cndmask_b32_e32 v34, v34, v35, vcc
	v_bitop3_b32 v89, v38, 4, v3 bitop3:0xc8
	v_cndmask_b32_e64 v35, 0, 1, vcc
	v_cmp_eq_u32_e32 vcc, 0, v89
	v_cmp_gt_f32_e64 s[16:17], v30, v34
	s_and_b64 vcc, vcc, s[16:17]
	v_cndmask_b32_e32 v30, v34, v30, vcc
	v_cndmask_b32_e64 v34, v35, 2, vcc
	v_bitop3_b32 v35, v38, 8, v3 bitop3:0xc8
	v_cmp_eq_u32_e32 vcc, 0, v35
	v_cmp_gt_f32_e64 s[16:17], v31, v30
	s_and_b64 vcc, vcc, s[16:17]
	v_cndmask_b32_e32 v30, v30, v31, vcc
	v_cndmask_b32_e64 v31, v34, 3, vcc
	v_bitop3_b32 v34, v38, 16, v3 bitop3:0xc8
	v_cmp_eq_u32_e32 vcc, 0, v34
	v_cmp_gt_f32_e64 s[16:17], v22, v30
	s_and_b64 vcc, vcc, s[16:17]
	v_cndmask_b32_e32 v22, v30, v22, vcc
	v_cndmask_b32_e64 v30, v31, 4, vcc
	v_bitop3_b32 v31, v38, 32, v3 bitop3:0xc8
	v_cmp_eq_u32_e32 vcc, 0, v31
	v_cmp_gt_f32_e64 s[16:17], v23, v22
	s_and_b64 vcc, vcc, s[16:17]
	v_cndmask_b32_e32 v22, v22, v23, vcc
	v_cndmask_b32_e64 v23, v30, 5, vcc
	v_bitop3_b32 v30, v38, 64, v3 bitop3:0xc8
	v_cmp_eq_u32_e32 vcc, 0, v30
	v_cmp_gt_f32_e64 s[16:17], v10, v22
	s_and_b64 vcc, vcc, s[16:17]
	s_movk_i32 s16, 0x80
	v_cndmask_b32_e32 v10, v22, v10, vcc
	v_cndmask_b32_e64 v22, v23, 6, vcc
	v_bitop3_b32 v23, v38, s16, v3 bitop3:0xc8
	v_cmp_eq_u32_e32 vcc, 0, v23
	v_cmp_gt_f32_e64 s[16:17], v11, v10
	s_and_b64 vcc, vcc, s[16:17]
	s_movk_i32 s16, 0x100
	v_cndmask_b32_e32 v10, v10, v11, vcc
	v_cndmask_b32_e64 v11, v22, 7, vcc
	v_bitop3_b32 v22, v38, s16, v3 bitop3:0xc8
	v_cmp_eq_u32_e32 vcc, 0, v22
	v_cmp_gt_f32_e64 s[16:17], v24, v10
	s_and_b64 vcc, vcc, s[16:17]
	s_movk_i32 s16, 0x200
	v_cndmask_b32_e32 v10, v10, v24, vcc
	v_bitop3_b32 v22, v38, s16, v3 bitop3:0xc8
	v_cndmask_b32_e64 v11, v11, 8, vcc
	v_cmp_eq_u32_e32 vcc, 0, v22
	v_cmp_gt_f32_e64 s[16:17], v25, v10
	s_and_b64 vcc, vcc, s[16:17]
	v_cndmask_b32_e32 v10, v10, v25, vcc
	v_bitop3_b32 v22, v38, s52, v3 bitop3:0xc8
	v_cndmask_b32_e64 v11, v11, 9, vcc
	v_cmp_eq_u32_e32 vcc, 0, v22
	v_cmp_gt_f32_e64 s[16:17], v32, v10
	s_and_b64 vcc, vcc, s[16:17]
	s_movk_i32 s16, 0x800
	v_cndmask_b32_e32 v10, v10, v32, vcc
	v_bitop3_b32 v22, v38, s16, v3 bitop3:0xc8
	v_cndmask_b32_e64 v11, v11, 10, vcc
	v_cmp_eq_u32_e32 vcc, 0, v22
	v_cmp_gt_f32_e64 s[16:17], v33, v10
	s_and_b64 vcc, vcc, s[16:17]
	s_movk_i32 s16, 0x1000
	v_cndmask_b32_e32 v10, v10, v33, vcc
	v_bitop3_b32 v22, v38, s16, v3 bitop3:0xc8
	v_cndmask_b32_e64 v11, v11, 11, vcc
	v_cmp_eq_u32_e32 vcc, 0, v22
	v_cmp_gt_f32_e64 s[16:17], v20, v10
	s_and_b64 vcc, vcc, s[16:17]
	s_movk_i32 s16, 0x2000
	v_cndmask_b32_e32 v10, v10, v20, vcc
	v_bitop3_b32 v20, v38, s16, v3 bitop3:0xc8
	v_cndmask_b32_e64 v11, v11, 12, vcc
	v_cmp_eq_u32_e32 vcc, 0, v20
	v_cmp_gt_f32_e64 s[16:17], v21, v10
	s_and_b64 vcc, vcc, s[16:17]
	s_movk_i32 s16, 0x4000
	v_cndmask_b32_e32 v10, v10, v21, vcc
	v_bitop3_b32 v20, v38, s16, v3 bitop3:0xc8
	v_cndmask_b32_e64 v11, v11, 13, vcc
	v_cmp_eq_u32_e32 vcc, 0, v20
	v_cmp_gt_f32_e64 s[16:17], v6, v10
	s_and_b64 vcc, vcc, s[16:17]
	s_mov_b32 s16, 0x8000
	v_cndmask_b32_e32 v6, v10, v6, vcc
	v_cndmask_b32_e64 v10, v11, 14, vcc
	v_bitop3_b32 v11, v38, s16, v3 bitop3:0xc8
	v_cmp_eq_u32_e32 vcc, 0, v11
	v_cmp_gt_f32_e64 s[16:17], v7, v6
	s_and_b64 vcc, vcc, s[16:17]
	s_mov_b32 s16, 0x10000
	v_cndmask_b32_e32 v6, v6, v7, vcc
	v_cndmask_b32_e64 v7, v10, 15, vcc
	v_bitop3_b32 v10, v38, s16, v3 bitop3:0xc8
	v_cmp_eq_u32_e32 vcc, 0, v10
	v_cmp_gt_f32_e64 s[16:17], v18, v6
	s_and_b64 vcc, vcc, s[16:17]
	s_mov_b32 s16, 0x20000
	v_cndmask_b32_e32 v6, v6, v18, vcc
	v_bitop3_b32 v10, v38, s16, v3 bitop3:0xc8
	v_cndmask_b32_e64 v7, v7, 16, vcc
	v_cmp_eq_u32_e32 vcc, 0, v10
	v_cmp_gt_f32_e64 s[16:17], v19, v6
	s_and_b64 vcc, vcc, s[16:17]
	s_mov_b32 s16, 0x40000
	v_cndmask_b32_e32 v6, v6, v19, vcc
	v_bitop3_b32 v10, v38, s16, v3 bitop3:0xc8
	v_cndmask_b32_e64 v7, v7, 17, vcc
	v_cmp_eq_u32_e32 vcc, 0, v10
	v_cmp_gt_f32_e64 s[16:17], v28, v6
	s_and_b64 vcc, vcc, s[16:17]
	s_mov_b32 s16, 0x80000
	v_cndmask_b32_e32 v6, v6, v28, vcc
	v_bitop3_b32 v10, v38, s16, v3 bitop3:0xc8
	v_cndmask_b32_e64 v7, v7, 18, vcc
	v_cmp_eq_u32_e32 vcc, 0, v10
	v_cmp_gt_f32_e64 s[16:17], v29, v6
	s_and_b64 vcc, vcc, s[16:17]
	s_mov_b32 s16, 0x100000
	v_cndmask_b32_e32 v6, v6, v29, vcc
	v_bitop3_b32 v10, v38, s16, v3 bitop3:0xc8
	v_cndmask_b32_e64 v7, v7, 19, vcc
	v_cmp_eq_u32_e32 vcc, 0, v10
	v_cmp_gt_f32_e64 s[16:17], v12, v6
	s_and_b64 vcc, vcc, s[16:17]
	s_mov_b32 s16, 0x200000
	v_cndmask_b32_e32 v6, v6, v12, vcc
	v_bitop3_b32 v10, v38, s16, v3 bitop3:0xc8
	v_cndmask_b32_e64 v7, v7, 20, vcc
	v_cmp_eq_u32_e32 vcc, 0, v10
	v_cmp_gt_f32_e64 s[16:17], v13, v6
	s_and_b64 vcc, vcc, s[16:17]
	s_mov_b32 s16, 0x400000
	v_cndmask_b32_e32 v6, v6, v13, vcc
	v_bitop3_b32 v10, v38, s16, v3 bitop3:0xc8
	v_cndmask_b32_e64 v7, v7, 21, vcc
	v_cmp_eq_u32_e32 vcc, 0, v10
	v_cmp_gt_f32_e64 s[16:17], v4, v6
	s_and_b64 vcc, vcc, s[16:17]
	s_mov_b32 s16, 0x800000
	v_cndmask_b32_e32 v4, v6, v4, vcc
	v_cndmask_b32_e64 v6, v7, 22, vcc
	v_bitop3_b32 v7, v38, s16, v3 bitop3:0xc8
	v_cmp_eq_u32_e32 vcc, 0, v7
	v_cmp_gt_f32_e64 s[16:17], v5, v4
	s_and_b64 vcc, vcc, s[16:17]
	s_mov_b32 s16, 0x1000000
	v_cndmask_b32_e32 v4, v4, v5, vcc
	v_cndmask_b32_e64 v5, v6, 23, vcc
	v_bitop3_b32 v6, v38, s16, v3 bitop3:0xc8
	v_cmp_eq_u32_e32 vcc, 0, v6
	v_cmp_gt_f32_e64 s[16:17], v14, v4
	s_and_b64 vcc, vcc, s[16:17]
	v_cndmask_b32_e32 v4, v4, v14, vcc
	v_bitop3_b32 v6, v38, s61, v3 bitop3:0xc8
	v_cndmask_b32_e64 v5, v5, 24, vcc
	v_cmp_eq_u32_e32 vcc, 0, v6
	v_cmp_gt_f32_e64 s[16:17], v15, v4
	s_and_b64 vcc, vcc, s[16:17]
	v_cndmask_b32_e32 v4, v4, v15, vcc
	v_bitop3_b32 v6, v38, s62, v3 bitop3:0xc8
	v_cndmask_b32_e64 v5, v5, 25, vcc
	v_cmp_eq_u32_e32 vcc, 0, v6
	v_cmp_gt_f32_e64 s[16:17], v26, v4
	s_and_b64 vcc, vcc, s[16:17]
	v_cndmask_b32_e32 v4, v4, v26, vcc
	v_bitop3_b32 v6, v38, s63, v3 bitop3:0xc8
	v_cndmask_b32_e64 v5, v5, 26, vcc
	v_cmp_eq_u32_e32 vcc, 0, v6
	v_cmp_gt_f32_e64 s[16:17], v27, v4
	s_and_b64 vcc, vcc, s[16:17]
	v_cndmask_b32_e32 v4, v4, v27, vcc
	v_bitop3_b32 v6, v38, s64, v3 bitop3:0xc8
	v_cndmask_b32_e64 v5, v5, 27, vcc
	v_cmp_eq_u32_e32 vcc, 0, v6
	v_cmp_gt_f32_e64 s[16:17], v16, v4
	s_and_b64 vcc, vcc, s[16:17]
	v_cndmask_b32_e32 v4, v4, v16, vcc
	v_bitop3_b32 v6, v38, s65, v3 bitop3:0xc8
	v_cndmask_b32_e64 v5, v5, 28, vcc
	v_cmp_eq_u32_e32 vcc, 0, v6
	v_cmp_gt_f32_e64 s[16:17], v17, v4
	s_and_b64 vcc, vcc, s[16:17]
	v_or_b32_e32 v88, v38, v3
	v_cndmask_b32_e32 v4, v4, v17, vcc
	v_bitop3_b32 v3, v38, 2.0, v3 bitop3:0xc8
	v_cndmask_b32_e64 v5, v5, 29, vcc
	v_cmp_eq_u32_e32 vcc, 0, v3
	v_cmp_gt_f32_e64 s[16:17], v8, v4
	s_and_b64 vcc, vcc, s[16:17]
	v_cndmask_b32_e32 v3, v4, v8, vcc
	v_cndmask_b32_e64 v4, v5, 30, vcc
	v_cmp_lt_i32_e32 vcc, -1, v88
	v_cmp_gt_f32_e64 s[16:17], v9, v3
	s_and_b64 vcc, vcc, s[16:17]
	v_cndmask_b32_e32 v5, v3, v9, vcc
	v_cndmask_b32_e64 v3, v4, 31, vcc
	v_sub_f32_e32 v4, v36, v36
	v_mul_f32_e32 v4, 0x3fb8aa3b, v4
	v_exp_f32_e32 v10, v4
	v_sub_f32_e32 v4, v37, v36
	v_mul_f32_e32 v4, 0x3fb8aa3b, v4
	v_exp_f32_e32 v11, v4
	v_sub_f32_e32 v4, v39, v36
	v_mul_f32_e32 v4, 0x3fb8aa3b, v4
	v_exp_f32_e32 v12, v4
	v_sub_f32_e32 v4, v5, v36
	v_mul_f32_e32 v4, 0x3fb8aa3b, v4
	v_exp_f32_e32 v13, v4
	v_add_f32_e32 v4, 0, v10
	v_add_f32_e32 v4, v4, v11
	v_add_f32_e32 v4, v4, v12
	v_add_f32_e32 v14, v4, v13
	v_div_scale_f32 v15, s[16:17], v14, v14, v10
	v_rcp_f32_e32 v16, v15
	v_lshl_add_u32 v4, s66, 8, v94
	v_ashrrev_i32_e32 v5, 31, v4
	v_lshlrev_b64 v[6:7], 2, v[4:5]
	v_fma_f32 v5, -v15, v16, 1.0
	v_fmac_f32_e32 v16, v5, v16
	v_div_scale_f32 v5, vcc, v10, v14, v10
	v_mul_f32_e32 v17, v5, v16
	v_fma_f32 v18, -v15, v17, v5
	v_fmac_f32_e32 v17, v18, v16
	v_fma_f32 v5, -v15, v17, v5
	v_div_fmas_f32 v5, v5, v16, v17
	v_div_fixup_f32 v5, v5, v14, v10
	v_div_scale_f32 v10, s[16:17], v14, v14, v11
	v_rcp_f32_e32 v15, v10
	v_lshl_add_u64 v[8:9], s[20:21], 0, v[6:7]
	v_lshl_add_u64 v[6:7], s[22:23], 0, v[6:7]
	global_store_dword v[6:7], v5, off
	v_or_b32_e32 v6, 1, v4
	v_fma_f32 v4, -v10, v15, 1.0
	v_lshl_add_u32 v5, v0, 2, 0
	v_fmac_f32_e32 v15, v4, v15
	v_div_scale_f32 v4, vcc, v11, v14, v11
	ds_add_u32 v5, v109 offset:58624
	v_mul_f32_e32 v5, v4, v15
	v_fma_f32 v16, -v10, v5, v4
	v_fmac_f32_e32 v5, v16, v15
	v_fma_f32 v4, -v10, v5, v4
	v_div_fmas_f32 v4, v4, v15, v5
	v_div_scale_f32 v5, s[16:17], v14, v14, v12
	v_rcp_f32_e32 v15, v5
	v_ashrrev_i32_e32 v7, 31, v6
	v_div_fixup_f32 v4, v4, v14, v11
	v_lshl_add_u64 v[10:11], v[6:7], 2, s[22:23]
	v_lshl_add_u32 v6, v1, 2, 0
	ds_add_u32 v6, v109 offset:58624
	v_fma_f32 v6, -v5, v15, 1.0
	v_fmac_f32_e32 v15, v6, v15
	v_div_scale_f32 v6, vcc, v12, v14, v12
	v_mul_f32_e32 v7, v6, v15
	v_fma_f32 v16, -v5, v7, v6
	v_fmac_f32_e32 v7, v16, v15
	v_fma_f32 v5, -v5, v7, v6
	v_div_scale_f32 v6, s[16:17], v14, v14, v13
	v_div_fmas_f32 v5, v5, v15, v7
	v_rcp_f32_e32 v7, v6
	v_div_fixup_f32 v5, v5, v14, v12
	v_lshl_add_u32 v12, v2, 2, 0
	ds_add_u32 v12, v109 offset:58624
	global_store_dwordx4 v[8:9], v[0:3], off
	s_nop 1
	v_fma_f32 v0, -v6, v7, 1.0
	v_fmac_f32_e32 v7, v0, v7
	v_div_scale_f32 v0, vcc, v13, v14, v13
	v_mul_f32_e32 v1, v0, v7
	v_fma_f32 v2, -v6, v1, v0
	v_fmac_f32_e32 v1, v2, v7
	v_fma_f32 v0, -v6, v1, v0
	v_div_fmas_f32 v0, v0, v7, v1
	v_div_fixup_f32 v6, v0, v14, v13
	global_store_dwordx3 v[10:11], v[4:6], off
	v_lshl_add_u32 v0, v3, 2, 0
	ds_add_u32 v0, v109 offset:58624

.LBB0_3308:
	v_ashrrev_i32_e32 v19, 31, v17
	v_mov_b32_e32 v18, v17
	v_ashrrev_i32_e32 v25, 31, v16
	v_mov_b32_e32 v24, v16
	v_lshlrev_b64 v[24:25], 2, v[24:25]
	v_lshlrev_b64 v[28:29], 2, v[18:19]
	v_lshl_add_u64 v[26:27], s[42:43], 0, v[24:25]
	v_lshl_add_u64 v[18:19], s[42:43], 0, v[28:29]
	global_load_dword v21, v[26:27], off
	s_nop 0
	global_load_dword v18, v[18:19], off
	v_lshl_add_u64 v[26:27], v[24:25], 0, s[30:31]
	v_lshl_add_u64 v[30:31], s[76:77], 0, v[26:27]
	v_lshl_add_u64 v[26:27], s[78:79], 0, v[26:27]
	v_add_u32_e32 v20, -2, v20
	s_add_i32 s33, s33, 4
	v_cmp_eq_u32_e32 vcc, 0, v20
	s_or_b64 s[46:47], vcc, s[46:47]
	s_waitcnt vmcnt(0)
	ds_write2st64_b32 v22, v21, v18 offset1:8
	v_lshl_add_u64 v[18:19], v[28:29], 0, s[30:31]
	v_lshl_add_u64 v[32:33], s[76:77], 0, v[18:19]
	global_load_dword v21, v[30:31], off
	global_load_dword v23, v[32:33], off
	v_lshl_add_u64 v[18:19], s[78:79], 0, v[18:19]
	s_waitcnt vmcnt(1)
	ds_write_b32 v22, v21 offset:4096
	global_load_dword v32, v[26:27], off
	global_load_dword v36, v[18:19], off
	v_lshl_add_u64 v[18:19], s[40:41], 0, v[24:25]
	v_lshl_add_u64 v[26:27], s[40:41], 0, v[28:29]
	v_lshl_add_u64 v[24:25], s[38:39], 0, v[24:25]
	global_load_dword v18, v[18:19], off
	s_nop 0
	global_load_dword v19, v[26:27], off
	v_lshl_add_u64 v[26:27], s[38:39], 0, v[28:29]
	global_load_dword v37, v[24:25], off
	global_load_dword v38, v[26:27], off
	v_add_u32_e32 v24, 0x400, v16
	v_add_u32_e32 v26, 0x400, v17
	v_ashrrev_i32_e32 v25, 31, v24
	v_ashrrev_i32_e32 v27, 31, v26
	v_lshlrev_b64 v[24:25], 2, v[24:25]
	v_lshl_add_u64 v[28:29], s[42:43], 0, v[24:25]
	v_lshlrev_b64 v[26:27], 2, v[26:27]
	v_lshl_add_u64 v[30:31], s[42:43], 0, v[26:27]
	global_load_dword v28, v[28:29], off
	s_nop 0
	global_load_dword v29, v[30:31], off
	v_add_u32_e32 v30, 0x1c00, v17
	v_ashrrev_i32_e32 v31, 31, v30
	v_lshlrev_b64 v[30:31], 2, v[30:31]
	v_lshl_add_u64 v[34:35], s[76:77], 0, v[30:31]
	v_lshl_add_u64 v[30:31], s[78:79], 0, v[30:31]
	v_add_u32_e32 v21, 0x2000, v22
	v_add_u32_e32 v17, 0x800, v17
	s_waitcnt vmcnt(1)
	ds_write2st64_b32 v22, v28, v23 offset0:16 offset1:24
	s_waitcnt vmcnt(0)
	ds_write2st64_b32 v22, v29, v32 offset0:24 offset1:32
	v_add_u32_e32 v28, 0x1c00, v16
	v_ashrrev_i32_e32 v29, 31, v28
	v_lshlrev_b64 v[28:29], 2, v[28:29]
	v_lshl_add_u64 v[32:33], s[76:77], 0, v[28:29]
	global_load_dword v23, v[32:33], off
	s_nop 0
	global_load_dword v32, v[34:35], off
	v_add_f32_e32 v18, 1.0, v18
	v_add_f32_e32 v19, 1.0, v19
	v_lshl_add_u64 v[28:29], s[78:79], 0, v[28:29]
	v_add_u32_e32 v16, 0x800, v16
	s_waitcnt vmcnt(1)
	ds_write2st64_b32 v22, v23, v36 offset0:32 offset1:40
	s_waitcnt vmcnt(0)
	ds_write2st64_b32 v22, v32, v18 offset0:40 offset1:48
	global_load_dword v18, v[28:29], off
	global_load_dword v23, v[30:31], off
	v_lshl_add_u64 v[28:29], s[40:41], 0, v[26:27]
	v_lshl_add_u64 v[26:27], s[38:39], 0, v[26:27]
	s_waitcnt vmcnt(1)
	ds_write2st64_b32 v22, v18, v19 offset0:48 offset1:56
	s_waitcnt vmcnt(0)
	ds_write2st64_b32 v22, v23, v37 offset0:56 offset1:64
	v_lshl_add_u64 v[18:19], s[40:41], 0, v[24:25]
	global_load_dword v18, v[18:19], off
	s_nop 0
	global_load_dword v19, v[28:29], off
	v_lshl_add_u64 v[24:25], s[38:39], 0, v[24:25]
	s_waitcnt vmcnt(0)
	v_add_f32_e32 v18, 1.0, v18
	v_add_f32_e32 v19, 1.0, v19
	ds_write2st64_b32 v22, v18, v38 offset0:64 offset1:72
	global_load_dword v18, v[24:25], off
	global_load_dword v23, v[26:27], off
	s_waitcnt vmcnt(1)
	ds_write2st64_b32 v22, v19, v18 offset0:72 offset1:80
	s_waitcnt vmcnt(0)
	ds_write_b32 v22, v23 offset:22528
	v_mov_b32_e32 v18, s33
	v_mov_b32_e32 v22, v21
	s_andn2_b64 exec, exec, s[46:47]
	s_cbranch_execnz .LBB0_3308
	s_or_b64 exec, exec, s[46:47]
	v_lshlrev_b32_e32 v18, 9, v18
	s_or_b64 exec, exec, s[44:45]
	s_and_saveexec_b64 s[44:45], s[12:13]
	s_cbranch_execz .LBB0_3312
	s_branch .LBB0_3311

.LBB0_3311:
	v_ashrrev_i32_e32 v21, 31, v17
	v_mov_b32_e32 v20, v17
	v_ashrrev_i32_e32 v17, 31, v16
	v_lshlrev_b64 v[16:17], 2, v[16:17]
	v_lshl_add_u64 v[22:23], s[42:43], 0, v[16:17]
	v_lshlrev_b64 v[20:21], 2, v[20:21]
	v_lshl_add_u64 v[24:25], s[42:43], 0, v[20:21]
	global_load_dword v19, v[22:23], off
	s_nop 0
	global_load_dword v22, v[24:25], off
	v_lshl_add_u32 v28, v18, 2, v95
	v_readlane_b32 s68, v253, 27
	v_readlane_b32 s76, v253, 35
	v_readlane_b32 s77, v253, 36
	v_readlane_b32 s78, v253, 37
	v_readlane_b32 s79, v253, 38
	v_readlane_b32 s69, v253, 28
	v_readlane_b32 s70, v253, 29
	v_readlane_b32 s71, v253, 30
	v_readlane_b32 s72, v253, 31
	v_readlane_b32 s73, v253, 32
	v_readlane_b32 s74, v253, 33
	v_readlane_b32 s75, v253, 34
	v_readlane_b32 s80, v253, 39
	v_readlane_b32 s81, v253, 40
	v_readlane_b32 s82, v253, 41
	v_readlane_b32 s83, v253, 42
	s_waitcnt vmcnt(0)
	ds_write2st64_b32 v28, v19, v22 offset1:8
	v_lshl_add_u64 v[22:23], v[16:17], 0, s[30:31]
	v_lshl_add_u64 v[18:19], v[20:21], 0, s[30:31]
	v_lshl_add_u64 v[24:25], s[76:77], 0, v[22:23]
	v_lshl_add_u64 v[26:27], s[76:77], 0, v[18:19]
	global_load_dword v24, v[24:25], off
	s_nop 0
	global_load_dword v25, v[26:27], off
	v_lshl_add_u64 v[22:23], s[78:79], 0, v[22:23]
	v_lshl_add_u64 v[18:19], s[78:79], 0, v[18:19]
	s_waitcnt vmcnt(0)
	ds_write2st64_b32 v28, v24, v25 offset0:16 offset1:24
	global_load_dword v22, v[22:23], off
	s_nop 0
	global_load_dword v18, v[18:19], off
	s_waitcnt vmcnt(0)
	ds_write2st64_b32 v28, v22, v18 offset0:32 offset1:40
	v_lshl_add_u64 v[18:19], s[40:41], 0, v[16:17]
	v_lshl_add_u64 v[22:23], s[40:41], 0, v[20:21]
	global_load_dword v18, v[18:19], off
	s_nop 0
	global_load_dword v19, v[22:23], off
	v_lshl_add_u64 v[16:17], s[38:39], 0, v[16:17]
	s_waitcnt vmcnt(0)
	v_add_f32_e32 v18, 1.0, v18
	v_add_f32_e32 v19, 1.0, v19
	ds_write2st64_b32 v28, v18, v19 offset0:48 offset1:56
	v_lshl_add_u64 v[18:19], s[38:39], 0, v[20:21]
	global_load_dword v16, v[16:17], off
	s_nop 0
	global_load_dword v17, v[18:19], off
	s_waitcnt vmcnt(0)
	ds_write2st64_b32 v28, v16, v17 offset0:64 offset1:72

.LBB0_3327:
	v_cvt_f32_f16_sdwa v117, v24 dst_sel:DWORD dst_unused:UNUSED_PAD src0_sel:WORD_1
	v_cvt_f32_f16_sdwa v119, v25 dst_sel:DWORD dst_unused:UNUSED_PAD src0_sel:WORD_1
	v_cvt_f32_f16_e32 v116, v24
	v_cvt_f32_f16_e32 v118, v25
	v_lshlrev_b32_e32 v122, 16, v22
	v_and_b32_e32 v123, 0xffff0000, v22
	v_lshlrev_b32_e32 v124, 16, v23
	v_and_b32_e32 v125, 0xffff0000, v23
	ds_read_b128 v[22:25], v110
	v_cvt_f32_f16_sdwa v37, v34 dst_sel:DWORD dst_unused:UNUSED_PAD src0_sel:WORD_1
	v_cvt_f32_f16_sdwa v39, v35 dst_sel:DWORD dst_unused:UNUSED_PAD src0_sel:WORD_1
	v_cvt_f32_f16_e32 v36, v34
	v_cvt_f32_f16_e32 v38, v35
	v_cvt_f32_f16_sdwa v89, v32 dst_sel:DWORD dst_unused:UNUSED_PAD src0_sel:WORD_1
	v_cvt_f32_f16_sdwa v91, v33 dst_sel:DWORD dst_unused:UNUSED_PAD src0_sel:WORD_1
	v_cvt_f32_f16_e32 v88, v32
	v_cvt_f32_f16_e32 v90, v33
	v_cvt_f32_f16_sdwa v93, v28 dst_sel:DWORD dst_unused:UNUSED_PAD src0_sel:WORD_1
	v_cvt_f32_f16_sdwa v115, v29 dst_sel:DWORD dst_unused:UNUSED_PAD src0_sel:WORD_1
	v_cvt_f32_f16_e32 v92, v28
	v_cvt_f32_f16_e32 v114, v29
	v_lshlrev_b32_e32 v28, 16, v30
	v_and_b32_e32 v29, 0xffff0000, v30
	v_lshlrev_b32_e32 v30, 16, v31
	v_and_b32_e32 v31, 0xffff0000, v31
	ds_read_b128 v[32:35], v110 offset:1024
	v_lshlrev_b32_e32 v126, 16, v20
	v_and_b32_e32 v127, 0xffff0000, v20
	v_lshlrev_b32_e32 v128, 16, v21
	v_and_b32_e32 v129, 0xffff0000, v21
	s_waitcnt lgkmcnt(1)
	v_mul_f32_e32 v20, v24, v30
	v_mul_f32_e32 v21, v25, v31
	v_mul_f32_e32 v22, v22, v28
	v_mul_f32_e32 v23, v23, v29
	v_fma_f32 v30, v38, s34, v20
	v_fma_f32 v31, v39, s34, v21
	v_fma_f32 v28, v36, s34, v22
	v_fma_f32 v29, v37, s34, v23
	v_add_f32_e32 v21, v30, v31
	v_add_f32_e32 v20, v28, v29
	v_lshlrev_b32_e32 v120, 16, v26
	v_and_b32_e32 v121, 0xffff0000, v26
	v_lshlrev_b32_e32 v26, 16, v27
	v_and_b32_e32 v27, 0xffff0000, v27
	v_add_f32_e32 v20, v20, v21
	v_add_f32_e32 v36, 0, v20
	s_waitcnt lgkmcnt(0)
	v_mul_f32_e32 v20, v34, v26
	v_mul_f32_e32 v21, v35, v27
	v_mul_f32_e32 v24, v32, v120
	v_mul_f32_e32 v25, v33, v121
	v_fma_f32 v22, v90, s34, v20
	v_fma_f32 v23, v91, s34, v21
	v_fma_f32 v20, v88, s34, v24
	v_fma_f32 v21, v89, s34, v25
	ds_read_b128 v[24:27], v110 offset:2048
	v_add_f32_e32 v32, v20, v21
	v_add_f32_e32 v33, v22, v23
	v_add_f32_e32 v32, v32, v33
	v_add_f32_e32 v88, v36, v32
	ds_read_b128 v[36:39], v110 offset:3072
	s_waitcnt lgkmcnt(1)
	v_mul_f32_e32 v26, v26, v124
	v_mul_f32_e32 v27, v27, v125
	v_mul_f32_e32 v24, v24, v122
	v_mul_f32_e32 v25, v25, v123
	v_fma_f32 v34, v114, s34, v26
	v_fma_f32 v35, v115, s34, v27
	v_fma_f32 v32, v92, s34, v24
	v_fma_f32 v33, v93, s34, v25
	v_add_f32_e32 v25, v34, v35
	v_add_f32_e32 v24, v32, v33
	v_add_f32_e32 v24, v24, v25
	v_add_f32_e32 v88, v88, v24
	s_waitcnt lgkmcnt(0)
	v_mul_f32_e32 v24, v38, v128
	v_mul_f32_e32 v25, v39, v129
	v_mul_f32_e32 v36, v36, v126
	v_mul_f32_e32 v37, v37, v127
	v_fma_f32 v26, v118, s34, v24
	v_fma_f32 v27, v119, s34, v25
	v_fma_f32 v24, v116, s34, v36
	v_fma_f32 v25, v117, s34, v37
	v_add_f32_e32 v37, v26, v27
	v_add_f32_e32 v36, v24, v25
	v_add_f32_e32 v36, v36, v37
	v_add_f32_e32 v36, v88, v36
	s_add_i32 s33, s33, s53
	s_add_i32 s36, s33, s96
	v_add_f32_dpp v36, v36, v36 quad_perm:[1,0,3,2] row_mask:0xf bank_mask:0xf bound_ctrl:1
	s_ashr_i32 s37, s36, 31
	s_nop 0
	v_add_f32_dpp v36, v36, v36 quad_perm:[2,3,0,1] row_mask:0xf bank_mask:0xf bound_ctrl:1
	s_nop 1
	v_add_f32_dpp v36, v36, v36 row_half_mirror row_mask:0xf bank_mask:0xf bound_ctrl:1
	s_nop 1
	v_add_f32_dpp v36, v36, v36 row_mirror row_mask:0xf bank_mask:0xf bound_ctrl:1
	v_mov_b32_e32 v37, v36
	s_nop 1
	v_permlane16_swap_b32_e32 v36, v37
	v_add_f32_e32 v36, v36, v37
	v_mov_b32_e32 v37, v36
	s_nop 1
	v_permlane32_swap_b32_e32 v36, v37
	v_add_f32_e32 v36, v36, v37
	v_fmac_f32_e32 v31, 0xba800000, v36
	v_fmac_f32_e32 v29, 0xba800000, v36
	v_fmamk_f32 v30, v36, 0xba800000, v30
	v_fmamk_f32 v28, v36, 0xba800000, v28
	v_mul_f32_e32 v37, v29, v29
	v_mul_f32_e32 v38, v31, v31
	v_fmac_f32_e32 v37, v28, v28
	v_fmac_f32_e32 v38, v30, v30
	v_fmac_f32_e32 v23, 0xba800000, v36
	v_fmac_f32_e32 v21, 0xba800000, v36
	v_add_f32_e32 v37, v37, v38
	v_fmamk_f32 v22, v36, 0xba800000, v22
	v_fmamk_f32 v20, v36, 0xba800000, v20
	v_mul_f32_e32 v38, v21, v21
	v_mul_f32_e32 v39, v23, v23
	v_fmac_f32_e32 v38, v20, v20
	v_fmac_f32_e32 v39, v22, v22
	v_add_f32_e32 v38, v38, v39
	v_fmac_f32_e32 v35, 0xba800000, v36
	v_fmac_f32_e32 v33, 0xba800000, v36
	v_add_f32_e32 v37, v37, v38
	v_fmamk_f32 v34, v36, 0xba800000, v34
	v_fmamk_f32 v32, v36, 0xba800000, v32
	v_mul_f32_e32 v38, v33, v33
	v_mul_f32_e32 v39, v35, v35
	v_fmac_f32_e32 v38, v32, v32
	v_fmac_f32_e32 v39, v34, v34
	v_add_f32_e32 v38, v38, v39
	v_fmac_f32_e32 v27, 0xba800000, v36
	v_fmac_f32_e32 v25, 0xba800000, v36
	v_add_f32_e32 v37, v38, v37
	v_fmamk_f32 v26, v36, 0xba800000, v26
	v_fmamk_f32 v24, v36, 0xba800000, v24
	v_mul_f32_e32 v36, v25, v25
	v_mul_f32_e32 v38, v27, v27
	v_fmac_f32_e32 v36, v24, v24
	v_fmac_f32_e32 v38, v26, v26
	v_add_f32_e32 v36, v36, v38
	v_add_f32_e32 v36, v36, v37
	s_nop 1
	v_add_f32_dpp v36, v36, v36 quad_perm:[1,0,3,2] row_mask:0xf bank_mask:0xf bound_ctrl:1
	s_nop 1
	v_add_f32_dpp v36, v36, v36 quad_perm:[2,3,0,1] row_mask:0xf bank_mask:0xf bound_ctrl:1
	s_nop 1
	v_add_f32_dpp v36, v36, v36 row_half_mirror row_mask:0xf bank_mask:0xf bound_ctrl:1
	s_nop 1
	v_add_f32_dpp v36, v36, v36 row_mirror row_mask:0xf bank_mask:0xf bound_ctrl:1
	v_mov_b32_e32 v37, v36
	s_nop 1
	v_permlane16_swap_b32_e32 v36, v37
	v_add_f32_e32 v36, v36, v37
	v_mov_b32_e32 v37, v36
	s_nop 1
	v_permlane32_swap_b32_e32 v36, v37
	v_add_f32_e32 v36, v36, v37
	v_fmamk_f32 v36, v36, 0x3a800000, v104
	v_mul_f32_e32 v37, 0x4f800000, v36
	v_cmp_gt_f32_e32 vcc, s59, v36
	s_nop 1
	v_cndmask_b32_e32 v36, v36, v37, vcc
	v_sqrt_f32_e32 v37, v36
	s_nop 0
	v_add_u32_e32 v38, -1, v37
	v_fma_f32 v39, -v38, v37, v36
	v_cmp_ge_f32_e64 s[16:17], 0, v39
	v_add_u32_e32 v39, 1, v37
	s_nop 0
	v_cndmask_b32_e64 v38, v37, v38, s[16:17]
	v_fma_f32 v37, -v39, v37, v36
	v_cmp_lt_f32_e64 s[16:17], 0, v37
	s_nop 1
	v_cndmask_b32_e64 v37, v38, v39, s[16:17]
	v_mul_f32_e32 v38, 0x37800000, v37
	v_cndmask_b32_e32 v37, v37, v38, vcc
	v_cmp_class_f32_e32 vcc, v36, v105
	s_nop 1
	v_cndmask_b32_e32 v36, v37, v36, vcc
	v_div_scale_f32 v37, s[16:17], v36, v36, 1.0
	v_rcp_f32_e32 v38, v37
	s_lshl_b64 s[16:17], s[36:37], 11
	v_fma_f32 v39, -v37, v38, 1.0
	v_fmac_f32_e32 v38, v39, v38
	v_div_scale_f32 v39, vcc, 1.0, v36, 1.0
	v_mul_f32_e32 v88, v39, v38
	v_fma_f32 v89, -v37, v88, v39
	v_fmac_f32_e32 v88, v89, v38
	v_fma_f32 v37, -v37, v88, v39
	v_div_fmas_f32 v37, v37, v38, v88
	v_div_fixup_f32 v92, v37, v36, 1.0
	ds_read_b128 v[36:39], v110 offset:4096
	ds_read_b128 v[88:91], v110 offset:8192
	v_mul_f32_e32 v118, v30, v92
	v_mul_f32_e32 v119, v31, v92
	v_mul_f32_e32 v120, v28, v92
	v_mul_f32_e32 v121, v29, v92
	ds_read_b128 v[28:31], v110 offset:5120
	ds_read_b128 v[114:117], v110 offset:9216
	s_waitcnt lgkmcnt(2)
	v_fma_f32 v38, v38, v118, v90
	v_fma_f32 v39, v39, v119, v91
	v_fma_f32 v36, v36, v120, v88
	v_fma_f32 v37, v37, v121, v89
	v_cvt_pk_f16_f32 v89, v38, v39
	v_cvt_f32_f16_e32 v93, v89
	v_cvt_pk_f16_f32 v88, v36, v37
	v_cvt_f32_f16_sdwa v113, v89 dst_sel:DWORD dst_unused:UNUSED_PAD src0_sel:WORD_1
	v_cvt_f32_f16_e32 v118, v88
	v_mul_f32_e32 v22, v22, v92
	v_mul_f32_e32 v23, v23, v92
	v_mul_f32_e32 v20, v20, v92
	v_mul_f32_e32 v21, v21, v92
	s_waitcnt lgkmcnt(0)
	v_fma_f32 v22, v30, v22, v116
	v_fma_f32 v23, v31, v23, v117
	v_fma_f32 v20, v28, v20, v114
	v_fma_f32 v21, v29, v21, v115
	v_cvt_pk_f16_f32 v91, v22, v23
	v_cvt_pk_f16_f32 v90, v20, v21
	ds_read_b128 v[20:23], v110 offset:6144
	ds_read_b128 v[28:31], v110 offset:10240
	v_mul_f32_e32 v114, v34, v92
	v_mul_f32_e32 v115, v35, v92
	v_mul_f32_e32 v116, v32, v92
	v_mul_f32_e32 v117, v33, v92
	ds_read_b128 v[32:35], v110 offset:7168
	ds_read_b128 v[36:39], v110 offset:11264
	v_cvt_f32_f16_sdwa v119, v88 dst_sel:DWORD dst_unused:UNUSED_PAD src0_sel:WORD_1
	s_waitcnt lgkmcnt(2)
	v_fma_f32 v20, v20, v116, v28
	v_fma_f32 v21, v21, v117, v29
	v_fma_f32 v22, v22, v114, v30
	v_fma_f32 v23, v23, v115, v31
	v_cvt_f32_f16_e32 v120, v91
	v_cvt_f32_f16_sdwa v121, v91 dst_sel:DWORD dst_unused:UNUSED_PAD src0_sel:WORD_1
	v_cvt_f32_f16_e32 v122, v90
	v_cvt_f32_f16_sdwa v123, v90 dst_sel:DWORD dst_unused:UNUSED_PAD src0_sel:WORD_1
	v_cvt_pk_f16_f32 v115, v22, v23
	v_cvt_pk_f16_f32 v114, v20, v21
	v_mul_f32_e32 v20, v26, v92
	v_mul_f32_e32 v21, v27, v92
	v_mul_f32_e32 v22, v24, v92
	v_mul_f32_e32 v23, v25, v92
	s_waitcnt lgkmcnt(0)
	v_fma_f32 v20, v20, v34, v38
	v_fma_f32 v21, v21, v35, v39
	v_fma_f32 v22, v22, v32, v36
	v_fma_f32 v23, v23, v33, v37
	v_cvt_f32_f16_e32 v28, v115
	v_cvt_f32_f16_sdwa v29, v115 dst_sel:DWORD dst_unused:UNUSED_PAD src0_sel:WORD_1
	v_cvt_f32_f16_e32 v30, v114
	v_cvt_f32_f16_sdwa v31, v114 dst_sel:DWORD dst_unused:UNUSED_PAD src0_sel:WORD_1
	v_cvt_pk_f16_f32 v39, v20, v21
	v_cvt_pk_f16_f32 v38, v22, v23
	v_cvt_f32_f16_e32 v20, v39
	v_cvt_f32_f16_sdwa v21, v39 dst_sel:DWORD dst_unused:UNUSED_PAD src0_sel:WORD_1
	v_cvt_f32_f16_e32 v22, v38
	v_cvt_f32_f16_sdwa v23, v38 dst_sel:DWORD dst_unused:UNUSED_PAD src0_sel:WORD_1
	v_add_f32_e32 v24, v118, v119
	v_add_f32_e32 v25, v93, v113
	v_add_f32_e32 v24, v24, v25
	v_add_f32_e32 v25, v122, v123
	v_add_f32_e32 v26, v120, v121
	v_add_f32_e32 v24, 0, v24
	v_add_f32_e32 v25, v25, v26
	v_add_f32_e32 v24, v25, v24
	v_add_f32_e32 v25, v30, v31
	v_add_f32_e32 v26, v28, v29
	v_add_f32_e32 v25, v25, v26
	v_add_f32_e32 v22, v22, v23
	v_add_f32_e32 v20, v20, v21
	v_add_f32_e32 v24, v25, v24
	v_add_f32_e32 v20, v22, v20
	v_add_f32_e32 v20, v20, v24
	s_nop 1
	v_add_f32_dpp v20, v20, v20 quad_perm:[1,0,3,2] row_mask:0xf bank_mask:0xf bound_ctrl:1
	s_nop 1
	v_add_f32_dpp v20, v20, v20 quad_perm:[2,3,0,1] row_mask:0xf bank_mask:0xf bound_ctrl:1
	s_nop 1
	v_add_f32_dpp v20, v20, v20 row_half_mirror row_mask:0xf bank_mask:0xf bound_ctrl:1
	s_nop 1
	v_add_f32_dpp v20, v20, v20 row_mirror row_mask:0xf bank_mask:0xf bound_ctrl:1
	v_mov_b32_e32 v21, v20
	s_nop 1
	v_permlane16_swap_b32_e32 v20, v21
	v_add_f32_e32 v20, v20, v21
	v_mov_b32_e32 v21, v20
	s_nop 1
	v_permlane32_swap_b32_e32 v20, v21
	v_add_f32_e32 v37, v20, v21
	v_fma_mix_f32 v33, v37, s58, v89 op_sel:[0,0,1] op_sel_hi:[0,0,1]
	v_fma_mix_f32 v35, v37, s58, v88 op_sel:[0,0,1] op_sel_hi:[0,0,1]
	v_fma_mix_f32 v32, v37, s58, v89 op_sel_hi:[0,0,1]
	v_fma_mix_f32 v34, v37, s58, v88 op_sel_hi:[0,0,1]
	v_mul_f32_e32 v20, v35, v35
	v_mul_f32_e32 v21, v33, v33
	v_fmac_f32_e32 v20, v34, v34
	v_fmac_f32_e32 v21, v32, v32
	v_fma_mix_f32 v29, v37, s58, v91 op_sel:[0,0,1] op_sel_hi:[0,0,1]
	v_fma_mix_f32 v31, v37, s58, v90 op_sel:[0,0,1] op_sel_hi:[0,0,1]
	v_add_f32_e32 v20, v20, v21
	v_fma_mix_f32 v28, v37, s58, v91 op_sel_hi:[0,0,1]
	v_fma_mix_f32 v30, v37, s58, v90 op_sel_hi:[0,0,1]
	v_mul_f32_e32 v21, v31, v31
	v_mul_f32_e32 v22, v29, v29
	v_fmac_f32_e32 v21, v30, v30
	v_fmac_f32_e32 v22, v28, v28
	v_add_f32_e32 v21, v21, v22
	v_fma_mix_f32 v25, v37, s58, v115 op_sel:[0,0,1] op_sel_hi:[0,0,1]
	v_fma_mix_f32 v27, v37, s58, v114 op_sel:[0,0,1] op_sel_hi:[0,0,1]
	v_add_f32_e32 v20, v20, v21
	v_fma_mix_f32 v24, v37, s58, v115 op_sel_hi:[0,0,1]
	v_fma_mix_f32 v26, v37, s58, v114 op_sel_hi:[0,0,1]
	v_mul_f32_e32 v21, v27, v27
	v_mul_f32_e32 v22, v25, v25
	v_fmac_f32_e32 v21, v26, v26
	v_fmac_f32_e32 v22, v24, v24
	v_add_f32_e32 v21, v21, v22
	v_add_f32_e32 v36, v21, v20
	v_fma_mix_f32 v21, v37, s58, v39 op_sel:[0,0,1] op_sel_hi:[0,0,1]
	v_fma_mix_f32 v23, v37, s58, v38 op_sel:[0,0,1] op_sel_hi:[0,0,1]
	v_fma_mix_f32 v20, v37, s58, v39 op_sel_hi:[0,0,1]
	v_fma_mix_f32 v22, v37, s58, v38 op_sel_hi:[0,0,1]
	v_mul_f32_e32 v92, v23, v23
	v_mul_f32_e32 v93, v21, v21
	v_fmac_f32_e32 v92, v22, v22
	v_fmac_f32_e32 v93, v20, v20
	v_add_f32_e32 v92, v92, v93
	v_add_f32_e32 v36, v92, v36
	s_nop 1
	v_add_f32_dpp v36, v36, v36 quad_perm:[1,0,3,2] row_mask:0xf bank_mask:0xf bound_ctrl:1
	s_nop 1
	v_add_f32_dpp v36, v36, v36 quad_perm:[2,3,0,1] row_mask:0xf bank_mask:0xf bound_ctrl:1
	s_nop 1
	v_add_f32_dpp v36, v36, v36 row_half_mirror row_mask:0xf bank_mask:0xf bound_ctrl:1
	s_nop 1
	v_add_f32_dpp v36, v36, v36 row_mirror row_mask:0xf bank_mask:0xf bound_ctrl:1
	v_mov_b32_e32 v92, v36
	s_nop 1
	v_permlane16_swap_b32_e32 v36, v92
	v_add_f32_e32 v36, v36, v92
	v_mov_b32_e32 v92, v36
	s_nop 1
	v_permlane32_swap_b32_e32 v36, v92
	v_add_f32_e32 v36, v36, v92
	v_fmamk_f32 v36, v36, 0x3a800000, v104
	v_mul_f32_e32 v92, 0x4f800000, v36
	v_cmp_gt_f32_e32 vcc, s59, v36
	s_nop 1
	v_cndmask_b32_e32 v36, v36, v92, vcc
	v_sqrt_f32_e32 v113, v36
	v_lshl_add_u64 v[92:93], v[82:83], 0, s[16:17]
	global_store_dwordx2 v[92:93], v[88:89], off
	global_store_dwordx2 v[92:93], v[90:91], off offset:512
	global_store_dwordx2 v[92:93], v[114:115], off offset:1024
	global_store_dwordx2 v[92:93], v[38:39], off offset:1536
	v_add_u32_e32 v88, -1, v113
	v_fma_f32 v89, -v88, v113, v36
	v_cmp_ge_f32_e64 s[16:17], 0, v89
	v_add_u32_e32 v89, 1, v113
	s_nop 0
	v_cndmask_b32_e64 v88, v113, v88, s[16:17]
	v_fma_f32 v113, -v89, v113, v36
	v_cmp_lt_f32_e64 s[16:17], 0, v113
	s_nop 1
	v_cndmask_b32_e64 v88, v88, v89, s[16:17]
	v_mul_f32_e32 v89, 0x37800000, v88
	v_cndmask_b32_e32 v88, v88, v89, vcc
	v_cmp_class_f32_e32 vcc, v36, v105
	s_nop 1
	v_cndmask_b32_e32 v36, v88, v36, vcc
	v_div_scale_f32 v88, s[16:17], v36, v36, 1.0
	v_rcp_f32_e32 v89, v88
	s_nop 0
	v_fma_f32 v38, -v88, v89, 1.0
	v_fmac_f32_e32 v89, v38, v89
	v_div_scale_f32 v38, vcc, 1.0, v36, 1.0
	v_mul_f32_e32 v39, v38, v89
	v_fma_f32 v90, -v88, v39, v38
	v_fmac_f32_e32 v39, v90, v89
	v_fma_f32 v38, -v88, v39, v38
	v_div_fmas_f32 v38, v38, v89, v39
	v_div_fixup_f32 v36, v38, v36, 1.0
	s_and_saveexec_b64 s[16:17], s[2:3]
	s_cbranch_execz .LBB0_3319
	s_lshl_b32 s33, s33, 3
	s_add_i32 s33, s33, 0
	v_mul_f32_e32 v38, 0x3a800000, v37
	v_mov_b32_e32 v39, v36
	v_mov_b32_e32 v37, s33
	ds_write_b64 v37, v[38:39] offset:20480
	s_branch .LBB0_3319
.LBB0_3329:
	s_waitcnt vmcnt(0)
	s_barrier
	s_waitcnt vmcnt(0)
	buffer_inv sc1
	s_waitcnt vmcnt(0)
	s_and_saveexec_b64 s[16:17], s[4:5]
	ds_write_b32 v95, v45 offset:58624
	s_or_b64 exec, exec, s[16:17]
	v_add_u32_e32 v0, s96, v42
	v_ashrrev_i32_e32 v1, 31, v0
	v_lshlrev_b64 v[0:1], 11, v[0:1]
	v_lshl_add_u64 v[92:93], v[46:47], 0, v[0:1]
	global_load_dwordx4 v[30:33], v[92:93], off
	global_load_dwordx4 v[34:37], v[48:49], off
	global_load_dwordx4 v[20:23], v[52:53], off
	global_load_dwordx4 v[24:27], v[92:93], off offset:128
	ds_read_b64 v[38:39], v106 offset:20480
	ds_read_b128 v[116:119], v43 offset:12288
	ds_read_b128 v[120:123], v43 offset:12304
	ds_read_b128 v[124:127], v43 offset:16384
	ds_read_b128 v[128:131], v43 offset:16400
	v_add_u32_e32 v114, 0x6000, v97
	v_mov_b32_e32 v4, 0
	s_waitcnt lgkmcnt(4)
	v_mov_b32_e32 v0, v38
	v_mov_b32_e32 v1, v38
	v_mov_b32_e32 v2, v38
	v_mov_b32_e32 v3, v38
	v_mov_b32_e32 v88, v39
	v_mov_b32_e32 v89, v39
	v_mov_b32_e32 v90, v39
	v_mov_b32_e32 v91, v39
	v_add_u32_e32 v113, 0x6400, v97
	s_mov_b32 s16, 0
	v_mov_b32_e32 v28, v103
	v_mov_b32_e32 v5, v4
	v_mov_b32_e32 v6, v4
	v_mov_b32_e32 v7, v4
	v_mov_b32_e32 v8, v4
	v_mov_b32_e32 v9, v4
	v_mov_b32_e32 v10, v4
	v_mov_b32_e32 v11, v4
	v_mov_b32_e32 v12, v4
	v_mov_b32_e32 v13, v4
	v_mov_b32_e32 v14, v4
	v_mov_b32_e32 v15, v4
	v_mov_b32_e32 v16, v4
	v_mov_b32_e32 v17, v4
	v_mov_b32_e32 v18, v4
	s_waitcnt vmcnt(3)
	v_cvt_f32_f16_sdwa v19, v31 dst_sel:DWORD dst_unused:UNUSED_PAD src0_sel:WORD_1
	v_cvt_f32_f16_e32 v29, v31
	v_cvt_f32_f16_sdwa v31, v30 dst_sel:DWORD dst_unused:UNUSED_PAD src0_sel:WORD_1
	v_cvt_f32_f16_e32 v30, v30
	v_cvt_f32_f16_sdwa v115, v33 dst_sel:DWORD dst_unused:UNUSED_PAD src0_sel:WORD_1
	v_cvt_f32_f16_e32 v134, v33
	v_cvt_f32_f16_sdwa v133, v32 dst_sel:DWORD dst_unused:UNUSED_PAD src0_sel:WORD_1
	v_cvt_f32_f16_e32 v132, v32
	v_sub_f32_e32 v30, v30, v38
	v_sub_f32_e32 v31, v31, v38
	v_sub_f32_e32 v32, v29, v38
	v_sub_f32_e32 v33, v19, v38
	v_sub_f32_e32 v132, v132, v38
	v_sub_f32_e32 v133, v133, v38
	v_sub_f32_e32 v134, v134, v38
	v_sub_f32_e32 v135, v115, v38
	v_mul_f32_e32 v30, v39, v30
	v_mul_f32_e32 v31, v39, v31
	v_mul_f32_e32 v32, v39, v32
	v_mul_f32_e32 v33, v39, v33
	v_mul_f32_e32 v134, v39, v134
	v_mul_f32_e32 v135, v39, v135
	v_mul_f32_e32 v38, v39, v132
	v_mul_f32_e32 v39, v39, v133
	s_waitcnt lgkmcnt(1)
	v_fma_f32 v19, v116, v30, v124
	v_fma_f32 v30, v117, v31, v125
	s_waitcnt lgkmcnt(0)
	v_fma_f32 v29, v120, v38, v128
	v_fma_f32 v31, v121, v39, v129
	v_fma_f32 v32, v118, v32, v126
	v_fma_f32 v38, v122, v134, v130
	v_fmac_f32_e32 v127, v119, v33
	v_fmac_f32_e32 v131, v123, v135
	ds_write2_b32 v114, v19, v30 offset1:68
	ds_write2_b32 v113, v29, v31 offset0:16 offset1:84
	ds_write2_b32 v114, v32, v127 offset0:136 offset1:204
	ds_write2_b32 v113, v38, v131 offset0:152 offset1:220
	s_waitcnt vmcnt(2)
	ds_write_b128 v96, v[34:37] offset:41984
	v_mov_b32_e32 v19, v4
	s_waitcnt lgkmcnt(0)
	s_barrier

.LBB0_3362:
	v_add_u32_e32 v1, s16, v44
	ds_read_b128 v[20:23], v0
	ds_read_b128 v[24:27], v0 offset:272
	ds_read_b128 v[28:31], v0 offset:544
	ds_read_b128 v[32:35], v0 offset:816
	ds_read_b128 v[36:39], v1
	ds_read_b128 v[88:91], v1 offset:128
	ds_read_b128 v[114:117], v1 offset:256
	ds_read_b128 v[118:121], v1 offset:384
	s_waitcnt lgkmcnt(7)
	v_mov_b32_e32 v2, v23
	s_waitcnt lgkmcnt(6)
	v_mov_b32_e32 v92, v27
	s_waitcnt lgkmcnt(3)
	v_fmac_f32_e32 v18, v38, v20
	v_fmac_f32_e32 v19, v39, v20
	v_fmac_f32_e32 v16, v36, v20
	v_fmac_f32_e32 v17, v37, v20
	v_fmac_f32_e32 v14, v38, v21
	v_fmac_f32_e32 v15, v39, v21
	v_fmac_f32_e32 v12, v36, v21
	v_fmac_f32_e32 v13, v37, v21
	v_fmac_f32_e32 v8, v36, v22
	v_fmac_f32_e32 v9, v37, v22
	v_fmac_f32_e32 v10, v38, v22
	v_fmac_f32_e32 v11, v39, v22
	v_fmac_f32_e32 v4, v36, v2
	v_fmac_f32_e32 v5, v37, v2
	v_fma_f32 v3, v39, v2, v7
	v_fma_f32 v2, v38, v2, v6
	v_mov_b32_e32 v122, v31
	s_waitcnt lgkmcnt(2)
	v_fma_f32 v6, v90, v24, v18
	v_fma_f32 v7, v91, v24, v19
	v_fmac_f32_e32 v16, v88, v24
	v_fmac_f32_e32 v17, v89, v24
	v_fmac_f32_e32 v14, v90, v25
	v_fmac_f32_e32 v15, v91, v25
	v_fmac_f32_e32 v12, v88, v25
	v_fmac_f32_e32 v13, v89, v25
	v_fmac_f32_e32 v10, v90, v26
	v_fmac_f32_e32 v11, v91, v26
	v_fmac_f32_e32 v8, v88, v26
	v_fmac_f32_e32 v9, v89, v26
	v_fmac_f32_e32 v2, v90, v92
	v_fmac_f32_e32 v3, v91, v92
	v_fmac_f32_e32 v4, v88, v92
	v_fmac_f32_e32 v5, v89, v92
	s_addk_i32 s16, 0x200
	v_mov_b32_e32 v124, v35
	s_waitcnt lgkmcnt(1)
	v_fmac_f32_e32 v6, v116, v28
	v_fmac_f32_e32 v7, v117, v28
	v_fmac_f32_e32 v16, v114, v28
	v_fmac_f32_e32 v17, v115, v28
	v_fmac_f32_e32 v14, v116, v29
	v_fmac_f32_e32 v15, v117, v29
	v_fmac_f32_e32 v12, v114, v29
	v_fmac_f32_e32 v13, v115, v29
	v_fmac_f32_e32 v10, v116, v30
	v_fmac_f32_e32 v11, v117, v30
	v_fmac_f32_e32 v8, v114, v30
	v_fmac_f32_e32 v9, v115, v30
	v_fmac_f32_e32 v2, v116, v122
	v_fmac_f32_e32 v3, v117, v122
	v_fmac_f32_e32 v4, v114, v122
	v_fmac_f32_e32 v5, v115, v122
	v_add_u32_e32 v0, 0x440, v0
	s_cmpk_lg_i32 s16, 0x800
	s_waitcnt lgkmcnt(0)
	v_fma_f32 v18, v120, v32, v6
	v_fma_f32 v19, v121, v32, v7
	v_fmac_f32_e32 v16, v118, v32
	v_fmac_f32_e32 v17, v119, v32
	v_fmac_f32_e32 v14, v120, v33
	v_fmac_f32_e32 v15, v121, v33
	v_fmac_f32_e32 v12, v118, v33
	v_fmac_f32_e32 v13, v119, v33
	v_fmac_f32_e32 v10, v120, v34
	v_fmac_f32_e32 v11, v121, v34
	v_fmac_f32_e32 v8, v118, v34
	v_fmac_f32_e32 v9, v119, v34
	v_fma_f32 v6, v120, v124, v2
	v_fma_f32 v7, v121, v124, v3
	v_fmac_f32_e32 v4, v118, v124
	v_fmac_f32_e32 v5, v119, v124
	s_cbranch_scc1 .LBB0_3362
	s_barrier
	ds_write_b128 v107, v[16:19] offset:58752
	ds_write_b128 v107, v[12:15] offset:58880
	ds_write_b128 v107, v[8:11] offset:59008
	ds_write_b128 v107, v[4:7] offset:59136
	s_waitcnt lgkmcnt(0)
	s_barrier
	global_load_dwordx4 v[0:3], v[50:51], off offset:384
	ds_read_b128 v[4:7], v98 offset:58752
	ds_read_b128 v[8:11], v99 offset:8192
	ds_read_b128 v[12:15], v99 offset:16384
	ds_read_b128 v[16:19], v99 offset:24576
	v_add_u32_e32 v20, 0xc400, v100
	v_add_u32_e32 v21, 0xc408, v100
	s_waitcnt lgkmcnt(2)
	v_add_f32_e32 v4, v4, v8
	v_add_f32_e32 v5, v5, v9
	v_add_f32_e32 v6, v6, v10
	v_add_f32_e32 v7, v7, v11
	s_waitcnt lgkmcnt(1)
	v_add_f32_e32 v4, v12, v4
	v_add_f32_e32 v5, v13, v5
	v_add_f32_e32 v6, v14, v6
	v_add_f32_e32 v7, v15, v7
	s_waitcnt lgkmcnt(0)
	v_add_f32_e32 v4, v16, v4
	v_add_f32_e32 v5, v17, v5
	v_add_f32_e32 v6, v18, v6
	v_add_f32_e32 v7, v19, v7
	s_waitcnt vmcnt(0)
	v_add_f32_e32 v0, v0, v4
	v_add_f32_e32 v1, v1, v5
	v_add_f32_e32 v2, v6, v2
	v_add_f32_e32 v3, v7, v3
	ds_write2_b32 v20, v0, v1 offset1:1
	ds_write2_b32 v21, v2, v3 offset1:1
	s_waitcnt lgkmcnt(0)
	s_barrier
	s_and_saveexec_b64 s[36:37], s[6:7]
	s_cbranch_execz .LBB0_3365
	v_add_u32_e32 v0, 0xc400, v108
	v_add_u32_e32 v1, 0xc408, v108
	v_add_u32_e32 v2, 0xc410, v108
	v_add_u32_e32 v3, 0xc418, v108
	ds_read2_b32 v[34:35], v0 offset1:1
	ds_read2_b32 v[28:29], v1 offset1:1
	ds_read2_b32 v[18:19], v2 offset1:1
	ds_read2_b32 v[8:9], v3 offset1:1
	s_mov_b32 s16, 0xff61b1e6
	s_waitcnt lgkmcnt(3)
	v_max_f32_e32 v0, v34, v34
	v_max_f32_e32 v0, 0xff61b1e6, v0
	v_cmp_lt_f32_e32 vcc, s16, v34
	v_cmp_gt_f32_e64 s[16:17], v35, v0
	v_add_u32_e32 v2, 0xc420, v108
	ds_read2_b32 v[20:21], v2 offset1:1
	v_cndmask_b32_e64 v0, v0, v35, s[16:17]
	v_cndmask_b32_e64 v1, 0, 1, s[16:17]
	s_waitcnt lgkmcnt(3)
	v_cmp_gt_f32_e64 s[16:17], v28, v0
	v_add_u32_e32 v2, 0xc428, v108
	v_add_u32_e32 v4, 0xc438, v108
	v_cndmask_b32_e64 v0, v0, v28, s[16:17]
	v_cndmask_b32_e64 v1, v1, 2, s[16:17]
	v_cmp_gt_f32_e64 s[16:17], v29, v0
	v_add_u32_e32 v3, 0xc430, v108
	ds_read2_b32 v[30:31], v2 offset1:1
	ds_read2_b32 v[16:17], v3 offset1:1
	ds_read2_b32 v[4:5], v4 offset1:1
	v_cndmask_b32_e64 v0, v0, v29, s[16:17]
	v_cndmask_b32_e64 v1, v1, 3, s[16:17]
	s_waitcnt lgkmcnt(5)
	v_cmp_gt_f32_e64 s[16:17], v18, v0
	v_add_u32_e32 v2, 0xc440, v108
	ds_read2_b32 v[12:13], v2 offset1:1
	v_cndmask_b32_e64 v0, v0, v18, s[16:17]
	v_cndmask_b32_e64 v1, v1, 4, s[16:17]
	v_cmp_gt_f32_e64 s[16:17], v19, v0
	v_add_u32_e32 v2, 0xc448, v108
	v_add_u32_e32 v6, 0xc458, v108
	v_cndmask_b32_e64 v0, v0, v19, s[16:17]
	v_cndmask_b32_e64 v1, v1, 5, s[16:17]
	s_waitcnt lgkmcnt(5)
	v_cmp_gt_f32_e64 s[16:17], v8, v0
	v_add_u32_e32 v3, 0xc450, v108
	ds_read2_b32 v[26:27], v2 offset1:1
	ds_read2_b32 v[14:15], v3 offset1:1
	ds_read2_b32 v[6:7], v6 offset1:1
	v_cndmask_b32_e64 v0, v0, v8, s[16:17]
	v_cndmask_b32_e64 v1, v1, 6, s[16:17]
	v_cmp_gt_f32_e64 s[16:17], v9, v0
	v_add_u32_e32 v2, 0xc460, v108
	ds_read2_b32 v[22:23], v2 offset1:1
	v_cndmask_b32_e64 v0, v0, v9, s[16:17]
	v_cndmask_b32_e64 v1, v1, 7, s[16:17]
	s_waitcnt lgkmcnt(8)
	v_cmp_gt_f32_e64 s[16:17], v20, v0
	v_add_u32_e32 v2, 0xc468, v108
	v_add_u32_e32 v10, 0xc478, v108
	v_cndmask_b32_e64 v0, v0, v20, s[16:17]
	v_cndmask_b32_e64 v1, v1, 8, s[16:17]
	v_cmp_gt_f32_e64 s[16:17], v21, v0
	v_add_u32_e32 v3, 0xc470, v108
	ds_read2_b32 v[32:33], v2 offset1:1
	ds_read2_b32 v[24:25], v3 offset1:1
	ds_read2_b32 v[10:11], v10 offset1:1
	v_cndmask_b32_e64 v0, v0, v21, s[16:17]
	v_cndmask_b32_e64 v1, v1, 9, s[16:17]
	s_waitcnt lgkmcnt(10)
	v_cmp_gt_f32_e64 s[16:17], v30, v0
	s_nop 1
	v_cndmask_b32_e64 v0, v0, v30, s[16:17]
	v_cndmask_b32_e64 v1, v1, 10, s[16:17]
	v_cmp_gt_f32_e64 s[16:17], v31, v0
	s_nop 1
	v_cndmask_b32_e64 v0, v0, v31, s[16:17]
	v_cndmask_b32_e64 v1, v1, 11, s[16:17]
	s_waitcnt lgkmcnt(9)
	v_cmp_gt_f32_e64 s[16:17], v16, v0
	s_nop 1
	v_cndmask_b32_e64 v0, v0, v16, s[16:17]
	v_cndmask_b32_e64 v1, v1, 12, s[16:17]
	v_cmp_gt_f32_e64 s[16:17], v17, v0
	s_nop 1
	v_cndmask_b32_e64 v0, v0, v17, s[16:17]
	v_cndmask_b32_e64 v1, v1, 13, s[16:17]
	s_waitcnt lgkmcnt(8)
	v_cmp_gt_f32_e64 s[16:17], v4, v0
	s_nop 1
	v_cndmask_b32_e64 v0, v0, v4, s[16:17]
	v_cndmask_b32_e64 v1, v1, 14, s[16:17]
	v_cmp_gt_f32_e64 s[16:17], v5, v0
	s_nop 1
	v_cndmask_b32_e64 v0, v0, v5, s[16:17]
	v_cndmask_b32_e64 v1, v1, 15, s[16:17]
	s_waitcnt lgkmcnt(7)
	v_cmp_gt_f32_e64 s[16:17], v12, v0
	s_nop 1
	v_cndmask_b32_e64 v0, v0, v12, s[16:17]
	v_cndmask_b32_e64 v1, v1, 16, s[16:17]
	v_cmp_gt_f32_e64 s[16:17], v13, v0
	s_nop 1
	v_cndmask_b32_e64 v0, v0, v13, s[16:17]
	v_cndmask_b32_e64 v1, v1, 17, s[16:17]
	s_waitcnt lgkmcnt(6)
	v_cmp_gt_f32_e64 s[16:17], v26, v0
	s_nop 1
	v_cndmask_b32_e64 v0, v0, v26, s[16:17]
	v_cndmask_b32_e64 v1, v1, 18, s[16:17]
	v_cmp_gt_f32_e64 s[16:17], v27, v0
	s_nop 1
	v_cndmask_b32_e64 v0, v0, v27, s[16:17]
	v_cndmask_b32_e64 v1, v1, 19, s[16:17]
	s_waitcnt lgkmcnt(5)
	v_cmp_gt_f32_e64 s[16:17], v14, v0
	s_nop 1
	v_cndmask_b32_e64 v0, v0, v14, s[16:17]
	v_cndmask_b32_e64 v1, v1, 20, s[16:17]
	v_cmp_gt_f32_e64 s[16:17], v15, v0
	s_nop 1
	v_cndmask_b32_e64 v0, v0, v15, s[16:17]
	v_cndmask_b32_e64 v1, v1, 21, s[16:17]
	s_waitcnt lgkmcnt(4)
	v_cmp_gt_f32_e64 s[16:17], v6, v0
	s_nop 1
	v_cndmask_b32_e64 v0, v0, v6, s[16:17]
	v_cndmask_b32_e64 v1, v1, 22, s[16:17]
	v_cmp_gt_f32_e64 s[16:17], v7, v0
	s_nop 1
	v_cndmask_b32_e64 v0, v0, v7, s[16:17]
	v_cndmask_b32_e64 v1, v1, 23, s[16:17]
	s_waitcnt lgkmcnt(3)
	v_cmp_gt_f32_e64 s[16:17], v22, v0
	s_nop 1
	v_cndmask_b32_e64 v0, v0, v22, s[16:17]
	v_cndmask_b32_e64 v1, v1, 24, s[16:17]
	v_cmp_gt_f32_e64 s[16:17], v23, v0
	s_nop 1
	v_cndmask_b32_e64 v0, v0, v23, s[16:17]
	v_cndmask_b32_e64 v1, v1, 25, s[16:17]
	s_waitcnt lgkmcnt(2)
	v_cmp_gt_f32_e64 s[16:17], v32, v0
	s_nop 1
	v_cndmask_b32_e64 v0, v0, v32, s[16:17]
	v_cndmask_b32_e64 v1, v1, 26, s[16:17]
	v_cmp_gt_f32_e64 s[16:17], v33, v0
	s_nop 1
	v_cndmask_b32_e64 v0, v0, v33, s[16:17]
	v_cndmask_b32_e64 v1, v1, 27, s[16:17]
	s_waitcnt lgkmcnt(1)
	v_cmp_gt_f32_e64 s[16:17], v24, v0
	s_nop 1
	v_cndmask_b32_e64 v0, v0, v24, s[16:17]
	v_cndmask_b32_e64 v1, v1, 28, s[16:17]
	v_cmp_gt_f32_e64 s[16:17], v25, v0
	s_nop 1
	v_cndmask_b32_e64 v0, v0, v25, s[16:17]
	v_cndmask_b32_e64 v1, v1, 29, s[16:17]
	s_waitcnt lgkmcnt(0)
	v_cmp_gt_f32_e64 s[16:17], v10, v0
	s_nop 1
	v_cndmask_b32_e64 v0, v0, v10, s[16:17]
	v_cndmask_b32_e64 v1, v1, 30, s[16:17]
	v_cmp_gt_f32_e64 s[16:17], v11, v0
	s_nop 1
	v_cndmask_b32_e64 v36, v0, v11, s[16:17]
	v_cndmask_b32_e64 v0, v1, 31, s[16:17]
	v_cmp_ne_u32_e64 s[16:17], 0, v0
	v_lshlrev_b32_e64 v2, v0, 1
	s_and_b64 s[16:17], s[16:17], vcc
	v_cndmask_b32_e64 v1, v112, v34, s[16:17]
	v_and_b32_e32 v3, 2, v2
	v_cmp_eq_u32_e64 s[16:17], 0, v3
	v_cmp_gt_f32_e64 s[18:19], v35, v1
	s_and_b64 s[16:17], s[16:17], s[18:19]
	v_cndmask_b32_e64 v1, v1, v35, s[16:17]
	v_and_b32_e32 v37, 4, v2
	v_cndmask_b32_e64 v3, 0, 1, s[16:17]
	v_cmp_eq_u32_e64 s[16:17], 0, v37
	v_cmp_gt_f32_e64 s[18:19], v28, v1
	s_and_b64 s[16:17], s[16:17], s[18:19]
	v_cndmask_b32_e64 v1, v1, v28, s[16:17]
	v_and_b32_e32 v37, 8, v2
	v_cndmask_b32_e64 v3, v3, 2, s[16:17]
	v_cmp_eq_u32_e64 s[16:17], 0, v37
	v_cmp_gt_f32_e64 s[18:19], v29, v1
	s_and_b64 s[16:17], s[16:17], s[18:19]
	v_cndmask_b32_e64 v1, v1, v29, s[16:17]
	v_and_b32_e32 v37, 16, v2
	v_cndmask_b32_e64 v3, v3, 3, s[16:17]
	v_cmp_eq_u32_e64 s[16:17], 0, v37
	v_cmp_gt_f32_e64 s[18:19], v18, v1
	s_and_b64 s[16:17], s[16:17], s[18:19]
	v_cndmask_b32_e64 v1, v1, v18, s[16:17]
	v_and_b32_e32 v37, 32, v2
	v_cndmask_b32_e64 v3, v3, 4, s[16:17]
	v_cmp_eq_u32_e64 s[16:17], 0, v37
	v_cmp_gt_f32_e64 s[18:19], v19, v1
	s_and_b64 s[16:17], s[16:17], s[18:19]
	v_cndmask_b32_e64 v1, v1, v19, s[16:17]
	v_and_b32_e32 v37, 64, v2
	v_cndmask_b32_e64 v3, v3, 5, s[16:17]
	v_cmp_eq_u32_e64 s[16:17], 0, v37
	v_cmp_gt_f32_e64 s[18:19], v8, v1
	s_and_b64 s[16:17], s[16:17], s[18:19]
	v_cndmask_b32_e64 v1, v1, v8, s[16:17]
	v_and_b32_e32 v37, 0x80, v2
	v_cndmask_b32_e64 v3, v3, 6, s[16:17]
	v_cmp_eq_u32_e64 s[16:17], 0, v37
	v_cmp_gt_f32_e64 s[18:19], v9, v1
	s_and_b64 s[16:17], s[16:17], s[18:19]
	v_cndmask_b32_e64 v1, v1, v9, s[16:17]
	v_and_b32_e32 v37, 0x100, v2
	v_cndmask_b32_e64 v3, v3, 7, s[16:17]
	v_cmp_eq_u32_e64 s[16:17], 0, v37
	v_cmp_gt_f32_e64 s[18:19], v20, v1
	s_and_b64 s[16:17], s[16:17], s[18:19]
	v_cndmask_b32_e64 v1, v1, v20, s[16:17]
	v_and_b32_e32 v37, 0x200, v2
	v_cndmask_b32_e64 v3, v3, 8, s[16:17]
	v_cmp_eq_u32_e64 s[16:17], 0, v37
	v_cmp_gt_f32_e64 s[18:19], v21, v1
	s_and_b64 s[16:17], s[16:17], s[18:19]
	v_cndmask_b32_e64 v1, v1, v21, s[16:17]
	v_and_b32_e32 v37, 0x400, v2
	v_cndmask_b32_e64 v3, v3, 9, s[16:17]
	v_cmp_eq_u32_e64 s[16:17], 0, v37
	v_cmp_gt_f32_e64 s[18:19], v30, v1
	s_and_b64 s[16:17], s[16:17], s[18:19]
	v_cndmask_b32_e64 v1, v1, v30, s[16:17]
	v_and_b32_e32 v37, 0x800, v2
	v_cndmask_b32_e64 v3, v3, 10, s[16:17]
	v_cmp_eq_u32_e64 s[16:17], 0, v37
	v_cmp_gt_f32_e64 s[18:19], v31, v1
	s_and_b64 s[16:17], s[16:17], s[18:19]
	v_cndmask_b32_e64 v1, v1, v31, s[16:17]
	v_and_b32_e32 v37, 0x1000, v2
	v_cndmask_b32_e64 v3, v3, 11, s[16:17]
	v_cmp_eq_u32_e64 s[16:17], 0, v37
	v_cmp_gt_f32_e64 s[18:19], v16, v1
	s_and_b64 s[16:17], s[16:17], s[18:19]
	v_cndmask_b32_e64 v1, v1, v16, s[16:17]
	v_and_b32_e32 v37, 0x2000, v2
	v_cndmask_b32_e64 v3, v3, 12, s[16:17]
	v_cmp_eq_u32_e64 s[16:17], 0, v37
	v_cmp_gt_f32_e64 s[18:19], v17, v1
	s_and_b64 s[16:17], s[16:17], s[18:19]
	v_cndmask_b32_e64 v1, v1, v17, s[16:17]
	v_and_b32_e32 v37, 0x4000, v2
	v_cndmask_b32_e64 v3, v3, 13, s[16:17]
	v_cmp_eq_u32_e64 s[16:17], 0, v37
	v_cmp_gt_f32_e64 s[18:19], v4, v1
	s_and_b64 s[16:17], s[16:17], s[18:19]
	v_cndmask_b32_e64 v1, v1, v4, s[16:17]
	v_and_b32_e32 v37, 0x8000, v2
	v_cndmask_b32_e64 v3, v3, 14, s[16:17]
	v_cmp_eq_u32_e64 s[16:17], 0, v37
	v_cmp_gt_f32_e64 s[18:19], v5, v1
	s_and_b64 s[16:17], s[16:17], s[18:19]
	v_cndmask_b32_e64 v1, v1, v5, s[16:17]
	v_and_b32_e32 v37, 0x10000, v2
	v_cndmask_b32_e64 v3, v3, 15, s[16:17]
	v_cmp_eq_u32_e64 s[16:17], 0, v37
	v_cmp_gt_f32_e64 s[18:19], v12, v1
	s_and_b64 s[16:17], s[16:17], s[18:19]
	v_cndmask_b32_e64 v1, v1, v12, s[16:17]
	v_and_b32_e32 v37, 0x20000, v2
	v_cndmask_b32_e64 v3, v3, 16, s[16:17]
	v_cmp_eq_u32_e64 s[16:17], 0, v37
	v_cmp_gt_f32_e64 s[18:19], v13, v1
	s_and_b64 s[16:17], s[16:17], s[18:19]
	v_cndmask_b32_e64 v1, v1, v13, s[16:17]
	v_and_b32_e32 v37, 0x40000, v2
	v_cndmask_b32_e64 v3, v3, 17, s[16:17]
	v_cmp_eq_u32_e64 s[16:17], 0, v37
	v_cmp_gt_f32_e64 s[18:19], v26, v1
	s_and_b64 s[16:17], s[16:17], s[18:19]
	v_cndmask_b32_e64 v1, v1, v26, s[16:17]
	v_and_b32_e32 v37, 0x80000, v2
	v_cndmask_b32_e64 v3, v3, 18, s[16:17]
	v_cmp_eq_u32_e64 s[16:17], 0, v37
	v_cmp_gt_f32_e64 s[18:19], v27, v1
	s_and_b64 s[16:17], s[16:17], s[18:19]
	v_cndmask_b32_e64 v1, v1, v27, s[16:17]
	v_and_b32_e32 v37, 0x100000, v2
	v_cndmask_b32_e64 v3, v3, 19, s[16:17]
	v_cmp_eq_u32_e64 s[16:17], 0, v37
	v_cmp_gt_f32_e64 s[18:19], v14, v1
	s_and_b64 s[16:17], s[16:17], s[18:19]
	v_cndmask_b32_e64 v1, v1, v14, s[16:17]
	v_and_b32_e32 v37, 0x200000, v2
	v_cndmask_b32_e64 v3, v3, 20, s[16:17]
	v_cmp_eq_u32_e64 s[16:17], 0, v37
	v_cmp_gt_f32_e64 s[18:19], v15, v1
	s_and_b64 s[16:17], s[16:17], s[18:19]
	v_cndmask_b32_e64 v1, v1, v15, s[16:17]
	v_and_b32_e32 v37, 0x400000, v2
	v_cndmask_b32_e64 v3, v3, 21, s[16:17]
	v_cmp_eq_u32_e64 s[16:17], 0, v37
	v_cmp_gt_f32_e64 s[18:19], v6, v1
	s_and_b64 s[16:17], s[16:17], s[18:19]
	v_cndmask_b32_e64 v1, v1, v6, s[16:17]
	v_and_b32_e32 v37, 0x800000, v2
	v_cndmask_b32_e64 v3, v3, 22, s[16:17]
	v_cmp_eq_u32_e64 s[16:17], 0, v37
	v_cmp_gt_f32_e64 s[18:19], v7, v1
	s_and_b64 s[16:17], s[16:17], s[18:19]
	v_cndmask_b32_e64 v1, v1, v7, s[16:17]
	v_and_b32_e32 v37, 0x1000000, v2
	v_cndmask_b32_e64 v3, v3, 23, s[16:17]
	v_cmp_eq_u32_e64 s[16:17], 0, v37
	v_cmp_gt_f32_e64 s[18:19], v22, v1
	s_and_b64 s[16:17], s[16:17], s[18:19]
	v_cndmask_b32_e64 v1, v1, v22, s[16:17]
	v_and_b32_e32 v37, 0x2000000, v2
	v_cndmask_b32_e64 v3, v3, 24, s[16:17]
	v_cmp_eq_u32_e64 s[16:17], 0, v37
	v_cmp_gt_f32_e64 s[18:19], v23, v1
	s_and_b64 s[16:17], s[16:17], s[18:19]
	v_cndmask_b32_e64 v1, v1, v23, s[16:17]
	v_and_b32_e32 v37, 0x4000000, v2
	v_cndmask_b32_e64 v3, v3, 25, s[16:17]
	v_cmp_eq_u32_e64 s[16:17], 0, v37
	v_cmp_gt_f32_e64 s[18:19], v32, v1
	s_and_b64 s[16:17], s[16:17], s[18:19]
	v_cndmask_b32_e64 v1, v1, v32, s[16:17]
	v_and_b32_e32 v37, 0x8000000, v2
	v_cndmask_b32_e64 v3, v3, 26, s[16:17]
	v_cmp_eq_u32_e64 s[16:17], 0, v37
	v_cmp_gt_f32_e64 s[18:19], v33, v1
	s_and_b64 s[16:17], s[16:17], s[18:19]
	v_cndmask_b32_e64 v1, v1, v33, s[16:17]
	v_and_b32_e32 v37, 0x10000000, v2
	v_cndmask_b32_e64 v3, v3, 27, s[16:17]
	v_cmp_eq_u32_e64 s[16:17], 0, v37
	v_cmp_gt_f32_e64 s[18:19], v24, v1
	s_and_b64 s[16:17], s[16:17], s[18:19]
	v_cndmask_b32_e64 v1, v1, v24, s[16:17]
	v_and_b32_e32 v37, 0x20000000, v2
	v_cndmask_b32_e64 v3, v3, 28, s[16:17]
	v_cmp_eq_u32_e64 s[16:17], 0, v37
	v_cmp_gt_f32_e64 s[18:19], v25, v1
	s_and_b64 s[16:17], s[16:17], s[18:19]
	v_cndmask_b32_e64 v1, v1, v25, s[16:17]
	v_and_b32_e32 v37, 2.0, v2
	v_cndmask_b32_e64 v3, v3, 29, s[16:17]
	v_cmp_eq_u32_e64 s[16:17], 0, v37
	v_cmp_gt_f32_e64 s[18:19], v10, v1
	s_and_b64 s[16:17], s[16:17], s[18:19]
	v_cndmask_b32_e64 v1, v1, v10, s[16:17]
	v_cndmask_b32_e64 v3, v3, 30, s[16:17]
	v_cmp_ne_u32_e64 s[16:17], 31, v0
	v_cmp_gt_f32_e64 s[18:19], v11, v1
	s_and_b64 s[16:17], s[16:17], s[18:19]
	v_cndmask_b32_e64 v37, v1, v11, s[16:17]
	v_cndmask_b32_e64 v1, v3, 31, s[16:17]
	v_lshl_or_b32 v3, 1, v1, v2
	v_and_b32_e32 v2, 1, v3
	v_cmp_eq_u32_e64 s[16:17], 0, v2
	s_and_b64 s[16:17], s[16:17], vcc
	v_and_b32_e32 v38, 2, v3
	v_cndmask_b32_e64 v2, v112, v34, s[16:17]
	v_cmp_eq_u32_e64 s[16:17], 0, v38
	v_cmp_gt_f32_e64 s[18:19], v35, v2
	s_and_b64 s[16:17], s[16:17], s[18:19]
	v_cndmask_b32_e64 v2, v2, v35, s[16:17]
	v_and_b32_e32 v39, 4, v3
	v_cndmask_b32_e64 v38, 0, 1, s[16:17]
	v_cmp_eq_u32_e64 s[16:17], 0, v39
	v_cmp_gt_f32_e64 s[18:19], v28, v2
	s_and_b64 s[16:17], s[16:17], s[18:19]
	v_cndmask_b32_e64 v2, v2, v28, s[16:17]
	v_and_b32_e32 v39, 8, v3
	v_cndmask_b32_e64 v38, v38, 2, s[16:17]
	v_cmp_eq_u32_e64 s[16:17], 0, v39
	v_cmp_gt_f32_e64 s[18:19], v29, v2
	s_and_b64 s[16:17], s[16:17], s[18:19]
	v_cndmask_b32_e64 v2, v2, v29, s[16:17]
	v_and_b32_e32 v39, 16, v3
	v_cndmask_b32_e64 v38, v38, 3, s[16:17]
	v_cmp_eq_u32_e64 s[16:17], 0, v39
	v_cmp_gt_f32_e64 s[18:19], v18, v2
	s_and_b64 s[16:17], s[16:17], s[18:19]
	v_cndmask_b32_e64 v2, v2, v18, s[16:17]
	v_and_b32_e32 v39, 32, v3
	v_cndmask_b32_e64 v38, v38, 4, s[16:17]
	v_cmp_eq_u32_e64 s[16:17], 0, v39
	v_cmp_gt_f32_e64 s[18:19], v19, v2
	s_and_b64 s[16:17], s[16:17], s[18:19]
	v_cndmask_b32_e64 v2, v2, v19, s[16:17]
	v_and_b32_e32 v39, 64, v3
	v_cndmask_b32_e64 v38, v38, 5, s[16:17]
	v_cmp_eq_u32_e64 s[16:17], 0, v39
	v_cmp_gt_f32_e64 s[18:19], v8, v2
	s_and_b64 s[16:17], s[16:17], s[18:19]
	v_cndmask_b32_e64 v2, v2, v8, s[16:17]
	v_and_b32_e32 v39, 0x80, v3
	v_cndmask_b32_e64 v38, v38, 6, s[16:17]
	v_cmp_eq_u32_e64 s[16:17], 0, v39
	v_cmp_gt_f32_e64 s[18:19], v9, v2
	s_and_b64 s[16:17], s[16:17], s[18:19]
	v_cndmask_b32_e64 v2, v2, v9, s[16:17]
	v_and_b32_e32 v39, 0x100, v3
	v_cndmask_b32_e64 v38, v38, 7, s[16:17]
	v_cmp_eq_u32_e64 s[16:17], 0, v39
	v_cmp_gt_f32_e64 s[18:19], v20, v2
	s_and_b64 s[16:17], s[16:17], s[18:19]
	v_cndmask_b32_e64 v2, v2, v20, s[16:17]
	v_and_b32_e32 v39, 0x200, v3
	v_cndmask_b32_e64 v38, v38, 8, s[16:17]
	v_cmp_eq_u32_e64 s[16:17], 0, v39
	v_cmp_gt_f32_e64 s[18:19], v21, v2
	s_and_b64 s[16:17], s[16:17], s[18:19]
	v_cndmask_b32_e64 v2, v2, v21, s[16:17]
	v_and_b32_e32 v39, 0x400, v3
	v_cndmask_b32_e64 v38, v38, 9, s[16:17]
	v_cmp_eq_u32_e64 s[16:17], 0, v39
	v_cmp_gt_f32_e64 s[18:19], v30, v2
	s_and_b64 s[16:17], s[16:17], s[18:19]
	v_cndmask_b32_e64 v2, v2, v30, s[16:17]
	v_and_b32_e32 v39, 0x800, v3
	v_cndmask_b32_e64 v38, v38, 10, s[16:17]
	v_cmp_eq_u32_e64 s[16:17], 0, v39
	v_cmp_gt_f32_e64 s[18:19], v31, v2
	s_and_b64 s[16:17], s[16:17], s[18:19]
	v_cndmask_b32_e64 v2, v2, v31, s[16:17]
	v_and_b32_e32 v39, 0x1000, v3
	v_cndmask_b32_e64 v38, v38, 11, s[16:17]
	v_cmp_eq_u32_e64 s[16:17], 0, v39
	v_cmp_gt_f32_e64 s[18:19], v16, v2
	s_and_b64 s[16:17], s[16:17], s[18:19]
	v_cndmask_b32_e64 v2, v2, v16, s[16:17]
	v_and_b32_e32 v39, 0x2000, v3
	v_cndmask_b32_e64 v38, v38, 12, s[16:17]
	v_cmp_eq_u32_e64 s[16:17], 0, v39
	v_cmp_gt_f32_e64 s[18:19], v17, v2
	s_and_b64 s[16:17], s[16:17], s[18:19]
	v_cndmask_b32_e64 v2, v2, v17, s[16:17]
	v_and_b32_e32 v39, 0x4000, v3
	v_cndmask_b32_e64 v38, v38, 13, s[16:17]
	v_cmp_eq_u32_e64 s[16:17], 0, v39
	v_cmp_gt_f32_e64 s[18:19], v4, v2
	s_and_b64 s[16:17], s[16:17], s[18:19]
	v_cndmask_b32_e64 v2, v2, v4, s[16:17]
	v_and_b32_e32 v39, 0x8000, v3
	v_cndmask_b32_e64 v38, v38, 14, s[16:17]
	v_cmp_eq_u32_e64 s[16:17], 0, v39
	v_cmp_gt_f32_e64 s[18:19], v5, v2
	s_and_b64 s[16:17], s[16:17], s[18:19]
	v_cndmask_b32_e64 v2, v2, v5, s[16:17]
	v_and_b32_e32 v39, 0x10000, v3
	v_cndmask_b32_e64 v38, v38, 15, s[16:17]
	v_cmp_eq_u32_e64 s[16:17], 0, v39
	v_cmp_gt_f32_e64 s[18:19], v12, v2
	s_and_b64 s[16:17], s[16:17], s[18:19]
	v_cndmask_b32_e64 v2, v2, v12, s[16:17]
	v_and_b32_e32 v39, 0x20000, v3
	v_cndmask_b32_e64 v38, v38, 16, s[16:17]
	v_cmp_eq_u32_e64 s[16:17], 0, v39
	v_cmp_gt_f32_e64 s[18:19], v13, v2
	s_and_b64 s[16:17], s[16:17], s[18:19]
	v_cndmask_b32_e64 v2, v2, v13, s[16:17]
	v_and_b32_e32 v39, 0x40000, v3
	v_cndmask_b32_e64 v38, v38, 17, s[16:17]
	v_cmp_eq_u32_e64 s[16:17], 0, v39
	v_cmp_gt_f32_e64 s[18:19], v26, v2
	s_and_b64 s[16:17], s[16:17], s[18:19]
	v_cndmask_b32_e64 v2, v2, v26, s[16:17]
	v_and_b32_e32 v39, 0x80000, v3
	v_cndmask_b32_e64 v38, v38, 18, s[16:17]
	v_cmp_eq_u32_e64 s[16:17], 0, v39
	v_cmp_gt_f32_e64 s[18:19], v27, v2
	s_and_b64 s[16:17], s[16:17], s[18:19]
	v_cndmask_b32_e64 v2, v2, v27, s[16:17]
	v_and_b32_e32 v39, 0x100000, v3
	v_cndmask_b32_e64 v38, v38, 19, s[16:17]
	v_cmp_eq_u32_e64 s[16:17], 0, v39
	v_cmp_gt_f32_e64 s[18:19], v14, v2
	s_and_b64 s[16:17], s[16:17], s[18:19]
	v_cndmask_b32_e64 v2, v2, v14, s[16:17]
	v_and_b32_e32 v39, 0x200000, v3
	v_cndmask_b32_e64 v38, v38, 20, s[16:17]
	v_cmp_eq_u32_e64 s[16:17], 0, v39
	v_cmp_gt_f32_e64 s[18:19], v15, v2
	s_and_b64 s[16:17], s[16:17], s[18:19]
	v_cndmask_b32_e64 v2, v2, v15, s[16:17]
	v_and_b32_e32 v39, 0x400000, v3
	v_cndmask_b32_e64 v38, v38, 21, s[16:17]
	v_cmp_eq_u32_e64 s[16:17], 0, v39
	v_cmp_gt_f32_e64 s[18:19], v6, v2
	s_and_b64 s[16:17], s[16:17], s[18:19]
	v_cndmask_b32_e64 v2, v2, v6, s[16:17]
	v_and_b32_e32 v39, 0x800000, v3
	v_cndmask_b32_e64 v38, v38, 22, s[16:17]
	v_cmp_eq_u32_e64 s[16:17], 0, v39
	v_cmp_gt_f32_e64 s[18:19], v7, v2
	s_and_b64 s[16:17], s[16:17], s[18:19]
	v_cndmask_b32_e64 v2, v2, v7, s[16:17]
	v_and_b32_e32 v39, 0x1000000, v3
	v_cndmask_b32_e64 v38, v38, 23, s[16:17]
	v_cmp_eq_u32_e64 s[16:17], 0, v39
	v_cmp_gt_f32_e64 s[18:19], v22, v2
	s_and_b64 s[16:17], s[16:17], s[18:19]
	v_cndmask_b32_e64 v2, v2, v22, s[16:17]
	v_and_b32_e32 v39, 0x2000000, v3
	v_cndmask_b32_e64 v38, v38, 24, s[16:17]
	v_cmp_eq_u32_e64 s[16:17], 0, v39
	v_cmp_gt_f32_e64 s[18:19], v23, v2
	s_and_b64 s[16:17], s[16:17], s[18:19]
	v_cndmask_b32_e64 v2, v2, v23, s[16:17]
	v_and_b32_e32 v39, 0x4000000, v3
	v_cndmask_b32_e64 v38, v38, 25, s[16:17]
	v_cmp_eq_u32_e64 s[16:17], 0, v39
	v_cmp_gt_f32_e64 s[18:19], v32, v2
	s_and_b64 s[16:17], s[16:17], s[18:19]
	v_cndmask_b32_e64 v2, v2, v32, s[16:17]
	v_and_b32_e32 v39, 0x8000000, v3
	v_cndmask_b32_e64 v38, v38, 26, s[16:17]
	v_cmp_eq_u32_e64 s[16:17], 0, v39
	v_cmp_gt_f32_e64 s[18:19], v33, v2
	s_and_b64 s[16:17], s[16:17], s[18:19]
	v_cndmask_b32_e64 v2, v2, v33, s[16:17]
	v_and_b32_e32 v39, 0x10000000, v3
	v_cndmask_b32_e64 v38, v38, 27, s[16:17]
	v_cmp_eq_u32_e64 s[16:17], 0, v39
	v_cmp_gt_f32_e64 s[18:19], v24, v2
	s_and_b64 s[16:17], s[16:17], s[18:19]
	v_cndmask_b32_e64 v2, v2, v24, s[16:17]
	v_and_b32_e32 v39, 0x20000000, v3
	v_cndmask_b32_e64 v38, v38, 28, s[16:17]
	v_cmp_eq_u32_e64 s[16:17], 0, v39
	v_cmp_gt_f32_e64 s[18:19], v25, v2
	s_and_b64 s[16:17], s[16:17], s[18:19]
	v_cndmask_b32_e64 v2, v2, v25, s[16:17]
	v_and_b32_e32 v39, 2.0, v3
	v_cndmask_b32_e64 v38, v38, 29, s[16:17]
	v_cmp_eq_u32_e64 s[16:17], 0, v39
	v_cmp_gt_f32_e64 s[18:19], v10, v2
	s_and_b64 s[16:17], s[16:17], s[18:19]
	v_cndmask_b32_e64 v2, v2, v10, s[16:17]
	v_cndmask_b32_e64 v38, v38, 30, s[16:17]
	v_cmp_lt_i32_e64 s[16:17], -1, v3
	v_cmp_gt_f32_e64 s[18:19], v11, v2
	s_and_b64 s[16:17], s[16:17], s[18:19]
	v_cndmask_b32_e64 v39, v2, v11, s[16:17]
	v_cndmask_b32_e64 v2, v38, 31, s[16:17]
	v_lshlrev_b32_e64 v38, v2, 1
	v_bitop3_b32 v89, v38, 1, v3 bitop3:0xc8
	v_cmp_eq_u32_e64 s[16:17], 0, v89
	s_and_b64 vcc, s[16:17], vcc
	v_cndmask_b32_e32 v34, v112, v34, vcc
	v_bitop3_b32 v89, v38, 2, v3 bitop3:0xc8
	v_cmp_eq_u32_e32 vcc, 0, v89
	v_cmp_gt_f32_e64 s[16:17], v35, v34
	s_and_b64 vcc, vcc, s[16:17]
	v_cndmask_b32_e32 v34, v34, v35, vcc
	v_bitop3_b32 v89, v38, 4, v3 bitop3:0xc8
	v_cndmask_b32_e64 v35, 0, 1, vcc
	v_cmp_eq_u32_e32 vcc, 0, v89
	v_cmp_gt_f32_e64 s[16:17], v28, v34
	s_and_b64 vcc, vcc, s[16:17]
	v_cndmask_b32_e32 v28, v34, v28, vcc
	v_cndmask_b32_e64 v34, v35, 2, vcc
	v_bitop3_b32 v35, v38, 8, v3 bitop3:0xc8
	v_cmp_eq_u32_e32 vcc, 0, v35
	v_cmp_gt_f32_e64 s[16:17], v29, v28
	s_and_b64 vcc, vcc, s[16:17]
	v_cndmask_b32_e32 v28, v28, v29, vcc
	v_cndmask_b32_e64 v29, v34, 3, vcc
	v_bitop3_b32 v34, v38, 16, v3 bitop3:0xc8
	v_cmp_eq_u32_e32 vcc, 0, v34
	v_cmp_gt_f32_e64 s[16:17], v18, v28
	s_and_b64 vcc, vcc, s[16:17]
	v_cndmask_b32_e32 v18, v28, v18, vcc
	v_cndmask_b32_e64 v28, v29, 4, vcc
	v_bitop3_b32 v29, v38, 32, v3 bitop3:0xc8
	v_cmp_eq_u32_e32 vcc, 0, v29
	v_cmp_gt_f32_e64 s[16:17], v19, v18
	s_and_b64 vcc, vcc, s[16:17]
	v_cndmask_b32_e32 v18, v18, v19, vcc
	v_cndmask_b32_e64 v19, v28, 5, vcc
	v_bitop3_b32 v28, v38, 64, v3 bitop3:0xc8
	v_cmp_eq_u32_e32 vcc, 0, v28
	v_cmp_gt_f32_e64 s[16:17], v8, v18
	s_and_b64 vcc, vcc, s[16:17]
	s_movk_i32 s16, 0x80
	v_cndmask_b32_e32 v8, v18, v8, vcc
	v_cndmask_b32_e64 v18, v19, 6, vcc
	v_bitop3_b32 v19, v38, s16, v3 bitop3:0xc8
	v_cmp_eq_u32_e32 vcc, 0, v19
	v_cmp_gt_f32_e64 s[16:17], v9, v8
	s_and_b64 vcc, vcc, s[16:17]
	s_movk_i32 s16, 0x100
	v_cndmask_b32_e32 v8, v8, v9, vcc
	v_cndmask_b32_e64 v9, v18, 7, vcc
	v_bitop3_b32 v18, v38, s16, v3 bitop3:0xc8
	v_cmp_eq_u32_e32 vcc, 0, v18
	v_cmp_gt_f32_e64 s[16:17], v20, v8
	s_and_b64 vcc, vcc, s[16:17]
	s_movk_i32 s16, 0x200
	v_cndmask_b32_e32 v8, v8, v20, vcc
	v_bitop3_b32 v18, v38, s16, v3 bitop3:0xc8
	v_cndmask_b32_e64 v9, v9, 8, vcc
	v_cmp_eq_u32_e32 vcc, 0, v18
	v_cmp_gt_f32_e64 s[16:17], v21, v8
	s_and_b64 vcc, vcc, s[16:17]
	v_cndmask_b32_e32 v8, v8, v21, vcc
	v_bitop3_b32 v18, v38, s52, v3 bitop3:0xc8
	v_cndmask_b32_e64 v9, v9, 9, vcc
	v_cmp_eq_u32_e32 vcc, 0, v18
	v_cmp_gt_f32_e64 s[16:17], v30, v8
	s_and_b64 vcc, vcc, s[16:17]
	s_movk_i32 s16, 0x800
	v_cndmask_b32_e32 v8, v8, v30, vcc
	v_bitop3_b32 v18, v38, s16, v3 bitop3:0xc8
	v_cndmask_b32_e64 v9, v9, 10, vcc
	v_cmp_eq_u32_e32 vcc, 0, v18
	v_cmp_gt_f32_e64 s[16:17], v31, v8
	s_and_b64 vcc, vcc, s[16:17]
	s_movk_i32 s16, 0x1000
	v_cndmask_b32_e32 v8, v8, v31, vcc
	v_bitop3_b32 v18, v38, s16, v3 bitop3:0xc8
	v_cndmask_b32_e64 v9, v9, 11, vcc
	v_cmp_eq_u32_e32 vcc, 0, v18
	v_cmp_gt_f32_e64 s[16:17], v16, v8
	s_and_b64 vcc, vcc, s[16:17]
	s_movk_i32 s16, 0x2000
	v_cndmask_b32_e32 v8, v8, v16, vcc
	v_bitop3_b32 v16, v38, s16, v3 bitop3:0xc8
	v_cndmask_b32_e64 v9, v9, 12, vcc
	v_cmp_eq_u32_e32 vcc, 0, v16
	v_cmp_gt_f32_e64 s[16:17], v17, v8
	s_and_b64 vcc, vcc, s[16:17]
	s_movk_i32 s16, 0x4000
	v_cndmask_b32_e32 v8, v8, v17, vcc
	v_bitop3_b32 v16, v38, s16, v3 bitop3:0xc8
	v_cndmask_b32_e64 v9, v9, 13, vcc
	v_cmp_eq_u32_e32 vcc, 0, v16
	v_cmp_gt_f32_e64 s[16:17], v4, v8
	s_and_b64 vcc, vcc, s[16:17]
	s_mov_b32 s16, 0x8000
	v_cndmask_b32_e32 v4, v8, v4, vcc
	v_cndmask_b32_e64 v8, v9, 14, vcc
	v_bitop3_b32 v9, v38, s16, v3 bitop3:0xc8
	v_cmp_eq_u32_e32 vcc, 0, v9
	v_cmp_gt_f32_e64 s[16:17], v5, v4
	s_and_b64 vcc, vcc, s[16:17]
	s_mov_b32 s16, 0x10000
	v_cndmask_b32_e32 v4, v4, v5, vcc
	v_cndmask_b32_e64 v5, v8, 15, vcc
	v_bitop3_b32 v8, v38, s16, v3 bitop3:0xc8
	v_cmp_eq_u32_e32 vcc, 0, v8
	v_cmp_gt_f32_e64 s[16:17], v12, v4
	s_and_b64 vcc, vcc, s[16:17]
	s_mov_b32 s16, 0x20000
	v_cndmask_b32_e32 v4, v4, v12, vcc
	v_bitop3_b32 v8, v38, s16, v3 bitop3:0xc8
	v_cndmask_b32_e64 v5, v5, 16, vcc
	v_cmp_eq_u32_e32 vcc, 0, v8
	v_cmp_gt_f32_e64 s[16:17], v13, v4
	s_and_b64 vcc, vcc, s[16:17]
	s_mov_b32 s16, 0x40000
	v_cndmask_b32_e32 v4, v4, v13, vcc
	v_bitop3_b32 v8, v38, s16, v3 bitop3:0xc8
	v_cndmask_b32_e64 v5, v5, 17, vcc
	v_cmp_eq_u32_e32 vcc, 0, v8
	v_cmp_gt_f32_e64 s[16:17], v26, v4
	s_and_b64 vcc, vcc, s[16:17]
	v_cndmask_b32_e32 v4, v4, v26, vcc
	v_bitop3_b32 v8, v38, s61, v3 bitop3:0xc8
	v_cndmask_b32_e64 v5, v5, 18, vcc
	v_cmp_eq_u32_e32 vcc, 0, v8
	v_cmp_gt_f32_e64 s[16:17], v27, v4
	s_and_b64 vcc, vcc, s[16:17]
	v_cndmask_b32_e32 v4, v4, v27, vcc
	v_bitop3_b32 v8, v38, s62, v3 bitop3:0xc8
	v_cndmask_b32_e64 v5, v5, 19, vcc
	v_cmp_eq_u32_e32 vcc, 0, v8
	v_cmp_gt_f32_e64 s[16:17], v14, v4
	s_and_b64 vcc, vcc, s[16:17]
	v_cndmask_b32_e32 v4, v4, v14, vcc
	v_bitop3_b32 v8, v38, s63, v3 bitop3:0xc8
	v_cndmask_b32_e64 v5, v5, 20, vcc
	v_cmp_eq_u32_e32 vcc, 0, v8
	v_cmp_gt_f32_e64 s[16:17], v15, v4
	s_and_b64 vcc, vcc, s[16:17]
	v_cndmask_b32_e32 v4, v4, v15, vcc
	v_bitop3_b32 v8, v38, s64, v3 bitop3:0xc8
	v_cndmask_b32_e64 v5, v5, 21, vcc
	v_cmp_eq_u32_e32 vcc, 0, v8
	v_cmp_gt_f32_e64 s[16:17], v6, v4
	s_and_b64 vcc, vcc, s[16:17]
	v_cndmask_b32_e32 v4, v4, v6, vcc
	v_bitop3_b32 v6, v38, s65, v3 bitop3:0xc8
	v_cndmask_b32_e64 v5, v5, 22, vcc
	v_cmp_eq_u32_e32 vcc, 0, v6
	v_cmp_gt_f32_e64 s[16:17], v7, v4
	s_and_b64 vcc, vcc, s[16:17]
	v_cndmask_b32_e32 v4, v4, v7, vcc
	v_bitop3_b32 v6, v38, s66, v3 bitop3:0xc8
	v_cndmask_b32_e64 v5, v5, 23, vcc
	v_cmp_eq_u32_e32 vcc, 0, v6
	v_cmp_gt_f32_e64 s[16:17], v22, v4
	s_and_b64 vcc, vcc, s[16:17]
	v_cndmask_b32_e32 v4, v4, v22, vcc
	v_bitop3_b32 v6, v38, s67, v3 bitop3:0xc8
	v_cndmask_b32_e64 v5, v5, 24, vcc
	v_cmp_eq_u32_e32 vcc, 0, v6
	v_cmp_gt_f32_e64 s[16:17], v23, v4
	s_and_b64 vcc, vcc, s[16:17]
	v_cndmask_b32_e32 v4, v4, v23, vcc
	v_bitop3_b32 v6, v38, s84, v3 bitop3:0xc8
	v_cndmask_b32_e64 v5, v5, 25, vcc
	v_cmp_eq_u32_e32 vcc, 0, v6
	v_cmp_gt_f32_e64 s[16:17], v32, v4
	s_and_b64 vcc, vcc, s[16:17]
	v_cndmask_b32_e32 v4, v4, v32, vcc
	v_bitop3_b32 v6, v38, s85, v3 bitop3:0xc8
	v_cndmask_b32_e64 v5, v5, 26, vcc
	v_cmp_eq_u32_e32 vcc, 0, v6
	v_cmp_gt_f32_e64 s[16:17], v33, v4
	s_and_b64 vcc, vcc, s[16:17]
	v_cndmask_b32_e32 v4, v4, v33, vcc
	v_bitop3_b32 v6, v38, s86, v3 bitop3:0xc8
	v_cndmask_b32_e64 v5, v5, 27, vcc
	v_cmp_eq_u32_e32 vcc, 0, v6
	v_cmp_gt_f32_e64 s[16:17], v24, v4
	s_and_b64 vcc, vcc, s[16:17]
	v_cndmask_b32_e32 v4, v4, v24, vcc
	v_bitop3_b32 v6, v38, s87, v3 bitop3:0xc8
	v_cndmask_b32_e64 v5, v5, 28, vcc
	v_cmp_eq_u32_e32 vcc, 0, v6
	v_cmp_gt_f32_e64 s[16:17], v25, v4
	s_and_b64 vcc, vcc, s[16:17]
	v_or_b32_e32 v88, v38, v3
	v_cndmask_b32_e32 v4, v4, v25, vcc
	v_bitop3_b32 v3, v38, 2.0, v3 bitop3:0xc8
	v_cndmask_b32_e64 v5, v5, 29, vcc
	v_cmp_eq_u32_e32 vcc, 0, v3
	v_cmp_gt_f32_e64 s[16:17], v10, v4
	s_and_b64 vcc, vcc, s[16:17]
	v_cndmask_b32_e32 v3, v4, v10, vcc
	v_cndmask_b32_e64 v4, v5, 30, vcc
	v_cmp_lt_i32_e32 vcc, -1, v88
	v_cmp_gt_f32_e64 s[16:17], v11, v3
	s_and_b64 vcc, vcc, s[16:17]
	v_cndmask_b32_e32 v5, v3, v11, vcc
	v_cndmask_b32_e64 v3, v4, 31, vcc
	v_sub_f32_e32 v4, v36, v36
	v_mul_f32_e32 v4, 0x3fb8aa3b, v4
	v_exp_f32_e32 v10, v4
	v_sub_f32_e32 v4, v37, v36
	v_mul_f32_e32 v4, 0x3fb8aa3b, v4
	v_exp_f32_e32 v11, v4
	v_sub_f32_e32 v4, v39, v36
	v_mul_f32_e32 v4, 0x3fb8aa3b, v4
	v_exp_f32_e32 v12, v4
	v_sub_f32_e32 v4, v5, v36
	v_mul_f32_e32 v4, 0x3fb8aa3b, v4
	v_exp_f32_e32 v13, v4
	v_add_f32_e32 v4, 0, v10
	v_add_f32_e32 v4, v4, v11
	v_add_f32_e32 v4, v4, v12
	v_add_f32_e32 v14, v4, v13
	v_div_scale_f32 v15, s[16:17], v14, v14, v10
	v_rcp_f32_e32 v16, v15
	v_lshl_add_u32 v4, s91, 8, v94
	v_ashrrev_i32_e32 v5, 31, v4
	v_lshlrev_b64 v[6:7], 2, v[4:5]
	v_fma_f32 v5, -v15, v16, 1.0
	v_fmac_f32_e32 v16, v5, v16
	v_div_scale_f32 v5, vcc, v10, v14, v10
	v_mul_f32_e32 v17, v5, v16
	v_fma_f32 v18, -v15, v17, v5
	v_fmac_f32_e32 v17, v18, v16
	v_fma_f32 v5, -v15, v17, v5
	v_div_fmas_f32 v5, v5, v16, v17
	v_div_fixup_f32 v5, v5, v14, v10
	v_div_scale_f32 v10, s[16:17], v14, v14, v11
	v_rcp_f32_e32 v15, v10
	v_lshl_add_u64 v[8:9], s[20:21], 0, v[6:7]
	v_lshl_add_u64 v[6:7], s[22:23], 0, v[6:7]
	global_store_dword v[6:7], v5, off
	v_or_b32_e32 v6, 1, v4
	v_fma_f32 v4, -v10, v15, 1.0
	v_lshl_add_u32 v5, v0, 2, 0
	v_fmac_f32_e32 v15, v4, v15
	v_div_scale_f32 v4, vcc, v11, v14, v11
	ds_add_u32 v5, v109 offset:58624
	v_mul_f32_e32 v5, v4, v15
	v_fma_f32 v16, -v10, v5, v4
	v_fmac_f32_e32 v5, v16, v15
	v_fma_f32 v4, -v10, v5, v4
	v_div_fmas_f32 v4, v4, v15, v5
	v_div_scale_f32 v5, s[16:17], v14, v14, v12
	v_rcp_f32_e32 v15, v5
	v_ashrrev_i32_e32 v7, 31, v6
	v_div_fixup_f32 v4, v4, v14, v11
	v_lshl_add_u64 v[10:11], v[6:7], 2, s[22:23]
	v_lshl_add_u32 v6, v1, 2, 0
	ds_add_u32 v6, v109 offset:58624
	v_fma_f32 v6, -v5, v15, 1.0
	v_fmac_f32_e32 v15, v6, v15
	v_div_scale_f32 v6, vcc, v12, v14, v12
	v_mul_f32_e32 v7, v6, v15
	v_fma_f32 v16, -v5, v7, v6
	v_fmac_f32_e32 v7, v16, v15
	v_fma_f32 v5, -v5, v7, v6
	v_div_scale_f32 v6, s[16:17], v14, v14, v13
	v_div_fmas_f32 v5, v5, v15, v7
	v_rcp_f32_e32 v7, v6
	v_div_fixup_f32 v5, v5, v14, v12
	v_lshl_add_u32 v12, v2, 2, 0
	ds_add_u32 v12, v109 offset:58624
	global_store_dwordx4 v[8:9], v[0:3], off
	s_nop 1
	v_fma_f32 v0, -v6, v7, 1.0
	v_fmac_f32_e32 v7, v0, v7
	v_div_scale_f32 v0, vcc, v13, v14, v13
	v_mul_f32_e32 v1, v0, v7
	v_fma_f32 v2, -v6, v1, v0
	v_fmac_f32_e32 v1, v2, v7
	v_fma_f32 v0, -v6, v1, v0
	v_div_fmas_f32 v0, v0, v7, v1
	v_div_fixup_f32 v6, v0, v14, v13
	global_store_dwordx3 v[10:11], v[4:6], off
	v_lshl_add_u32 v0, v3, 2, 0
	ds_add_u32 v0, v109 offset:58624
